# v33 with the mid-burst s_setprio 0 / s_setprio 1 pairs between the two 16-MFMA groups of every GEMM phase removed (priority 1 held through the 32-MFMA burst)
# baseline (speedup 1.0000x reference)
; #define PG8_STAGE(bufoff, gbase, voff) do { _Pragma("unroll") for (int _i = 0; _i < 2; ++_i) \
;         __builtin_amdgcn_global_load_lds((const unsigned*)((const char*)(gbase) + (voff)[_i]), (LAS unsigned*)(lds + (bufoff) + ldsw + _i * 8192), 16, 0, 0); } while (0)
; #define PG8_LDA(dst, b, h) do { _Pragma("unroll") for (int m = 0; m < 4; ++m) _Pragma("unroll") for (int k = 0; k < 2; ++k) dst[m][k] = *(const LAS bf16x8*)(lds + PG8_SA(b, h) + aoff + m * 2048 + k * 1024); } while (0)
; #define PG8_LDB(dst, b, h) do { _Pragma("unroll") for (int n = 0; n < 2; ++n) _Pragma("unroll") for (int k = 0; k < 2; ++k) dst[n][k] = *(const LAS bf16x8*)(lds + PG8_SB(b, h) + boff + n * 2048 + k * 1024); } while (0)
; #define PG8_MMA(ai, bj, At, Bt) do { __builtin_amdgcn_s_setprio(1); _Pragma("unroll") for (int m = 0; m < 4; ++m) _Pragma("unroll") for (int n = 0; n < 2; ++n) _Pragma("unroll") for (int k = 0; k < 2; ++k) \
;         acc[ai][bj][m][n] = __builtin_amdgcn_mfma_f32_16x16x32_bf16(Bt[n][k], At[m][k], acc[ai][bj][m][n], 0, 0, 0); __builtin_amdgcn_s_setprio(0); } while (0)
; #define PG8_WAIT_V(n) asm volatile("s_waitcnt vmcnt(" #n ")" ::: "memory")
; #define PG8_WAIT_L(n) asm volatile("s_waitcnt lgkmcnt(" #n ")" ::: "memory")
; #define PG8_BAR __builtin_amdgcn_s_barrier()
; #define PG8_SCHED __builtin_amdgcn_sched_barrier(0)
; template <class Epi, class Sched>
; __device__ __forceinline__ void gemm_phase(LAS unsigned char* lds, const int tid, const char* Abase, const int K, const Sched& S, const Epi& E) {
;     ...
;             PG8_LDB(B0, 0, 0); PG8_LDB(B1, 0, 1); PG8_SCHED; PG8_LDA(At, 0, 0); PG8_STAGE(PG8_SA(1, 1), a1, vc[1]);
;             PG8_WAIT_V(8); PG8_WAIT_L(0); PG8_BAR; PG8_MMA(0, 0, At, B0); PG8_MMA(0, 1, At, B1); PG8_BAR; PG8_SCHED;
;             PG8_LDA(At, 0, 1); PG8_STAGE(PG8_SB(0, 0), b2, voffB); PG8_STAGE(PG8_SB(0, 1), b2 + hstep, voffB); PG8_STAGE(PG8_SA(0, 0), a2, w2[0]);
;             PG8_WAIT_V(8); PG8_WAIT_L(0); PG8_BAR; PG8_MMA(1, 0, At, B0); PG8_MMA(1, 1, At, B1); PG8_BAR; PG8_SCHED;
.LBB0_347:
	s_add_u32 s16, s12, 0x80
	s_addc_u32 s17, s13, 0
	s_and_b64 s[14:15], s[14:15], exec
	s_cselect_b32 s17, s31, s17
	s_cselect_b32 s16, s30, s16
	s_cselect_b32 s15, s61, s18
	s_cselect_b32 s14, s60, s7
	s_add_i32 s20, 0, 0x10000
	v_add_u32_e32 v145, s20, v147
	s_add_i32 s27, 0, 0x14000
	ds_read_b128 v[150:153], v145
	ds_read_b128 v[154:157], v145 offset:1024
	ds_read_b128 v[158:161], v145 offset:2048
	ds_read_b128 v[162:165], v145 offset:3072
	v_add_u32_e32 v145, s27, v147
	ds_read_b128 v[166:169], v145
	ds_read_b128 v[170:173], v145 offset:1024
	ds_read_b128 v[174:177], v145 offset:2048
	ds_read_b128 v[178:181], v145 offset:3072
	v_lshl_add_u64 v[186:187], s[12:13], 0, v[116:117]
	s_add_i32 m0, s71, 0xc000
	ds_read_b128 v[182:185], v148
	ds_read_b128 v[202:205], v148 offset:1024
	ds_read_b128 v[206:209], v148 offset:2048
	ds_read_b128 v[214:217], v148 offset:3072
	ds_read_b128 v[218:221], v148 offset:4096
	ds_read_b128 v[222:225], v148 offset:5120
	ds_read_b128 v[226:229], v148 offset:6144
	ds_read_b128 v[230:233], v148 offset:7168
	global_load_lds_dwordx4 v[186:187], off
	v_lshl_add_u64 v[186:187], s[12:13], 0, v[138:139]
	s_add_i32 m0, s71, 0xe000
	s_nop 0
	global_load_lds_dwordx4 v[186:187], off
	s_waitcnt vmcnt(8)
	s_waitcnt lgkmcnt(0)
	s_barrier
	s_setprio 1
	s_waitcnt lgkmcnt(0)
	v_mfma_f32_16x16x32_bf16 v[130:133], v[150:153], v[182:185], v[130:133]
	v_mfma_f32_16x16x32_bf16 v[126:129], v[158:161], v[182:185], v[126:129]
	v_mfma_f32_16x16x32_bf16 v[110:113], v[150:153], v[206:209], v[110:113]
	v_mfma_f32_16x16x32_bf16 v[106:109], v[158:161], v[206:209], v[106:109]
	v_mfma_f32_16x16x32_bf16 v[94:97], v[150:153], v[218:221], v[94:97]
	v_mfma_f32_16x16x32_bf16 v[90:93], v[158:161], v[218:221], v[90:93]
	v_mfma_f32_16x16x32_bf16 v[78:81], v[150:153], v[226:229], v[78:81]
	v_mfma_f32_16x16x32_bf16 v[74:77], v[158:161], v[226:229], v[74:77]
	v_mfma_f32_16x16x32_bf16 v[130:133], v[154:157], v[202:205], v[130:133]
	v_mfma_f32_16x16x32_bf16 v[126:129], v[162:165], v[202:205], v[126:129]
	v_mfma_f32_16x16x32_bf16 v[110:113], v[154:157], v[214:217], v[110:113]
	v_mfma_f32_16x16x32_bf16 v[106:109], v[162:165], v[214:217], v[106:109]
	v_mfma_f32_16x16x32_bf16 v[94:97], v[154:157], v[222:225], v[94:97]
	v_mfma_f32_16x16x32_bf16 v[90:93], v[162:165], v[222:225], v[90:93]
	v_mfma_f32_16x16x32_bf16 v[78:81], v[154:157], v[230:233], v[78:81]
	v_mfma_f32_16x16x32_bf16 v[74:77], v[162:165], v[230:233], v[74:77]
	v_mfma_f32_16x16x32_bf16 v[122:125], v[166:169], v[182:185], v[122:125]
	v_mfma_f32_16x16x32_bf16 v[118:121], v[174:177], v[182:185], v[118:121]
	v_mfma_f32_16x16x32_bf16 v[102:105], v[166:169], v[206:209], v[102:105]
	v_mfma_f32_16x16x32_bf16 v[98:101], v[174:177], v[206:209], v[98:101]
	v_mfma_f32_16x16x32_bf16 v[86:89], v[166:169], v[218:221], v[86:89]
	v_mfma_f32_16x16x32_bf16 v[82:85], v[174:177], v[218:221], v[82:85]
	v_mfma_f32_16x16x32_bf16 v[70:73], v[166:169], v[226:229], v[70:73]
	v_mfma_f32_16x16x32_bf16 v[66:69], v[174:177], v[226:229], v[66:69]
	v_mfma_f32_16x16x32_bf16 v[122:125], v[170:173], v[202:205], v[122:125]
	v_mfma_f32_16x16x32_bf16 v[118:121], v[178:181], v[202:205], v[118:121]
	v_mfma_f32_16x16x32_bf16 v[102:105], v[170:173], v[214:217], v[102:105]
	v_mfma_f32_16x16x32_bf16 v[98:101], v[178:181], v[214:217], v[98:101]
	v_mfma_f32_16x16x32_bf16 v[86:89], v[170:173], v[222:225], v[86:89]
	v_mfma_f32_16x16x32_bf16 v[82:85], v[178:181], v[222:225], v[82:85]
	v_mfma_f32_16x16x32_bf16 v[70:73], v[170:173], v[230:233], v[70:73]
	v_mfma_f32_16x16x32_bf16 v[66:69], v[178:181], v[230:233], v[66:69]
	s_setprio 0
	s_barrier
	s_add_i32 s20, s20, s70
	v_lshl_add_u64 v[186:187], s[14:15], 0, v[134:135]
	s_mov_b32 m0, s20
	ds_read_b128 v[182:185], v148 offset:16384
	ds_read_b128 v[202:205], v148 offset:17408
	ds_read_b128 v[206:209], v148 offset:18432
	ds_read_b128 v[214:217], v148 offset:19456
	ds_read_b128 v[218:221], v148 offset:20480
	ds_read_b128 v[222:225], v148 offset:21504
	ds_read_b128 v[226:229], v148 offset:22528
	ds_read_b128 v[230:233], v148 offset:23552
	global_load_lds_dwordx4 v[186:187], off
	s_add_i32 m0, s20, 0x2000
	s_add_u32 s20, s14, 0x40000
	v_lshl_add_u64 v[190:191], s[14:15], 0, v[136:137]
	s_addc_u32 s21, s15, 0
	s_add_i32 s27, s27, s70
	global_load_lds_dwordx4 v[190:191], off
	v_lshl_add_u64 v[192:193], s[20:21], 0, v[134:135]
	s_mov_b32 m0, s27
	v_mov_b32_e32 v145, v1
	global_load_lds_dwordx4 v[192:193], off
	v_lshl_add_u64 v[192:193], s[20:21], 0, v[136:137]
	s_add_i32 m0, s27, 0x2000
	s_nop 0
	global_load_lds_dwordx4 v[192:193], off
	s_mov_b32 m0, s71
	v_lshl_add_u64 v[192:193], s[16:17], 0, v[0:1]
	global_load_lds_dwordx4 v0, s[16:17]
	s_mov_b32 m0, s72
	s_nop 0
	global_load_lds_dwordx4 v144, s[16:17]
	s_waitcnt vmcnt(8)
	s_waitcnt lgkmcnt(0)
	v_lshl_add_u64 v[144:145], s[16:17], 0, v[144:145]
	s_barrier
; #define PG8_STAGE(bufoff, gbase, voff) do { _Pragma("unroll") for (int _i = 0; _i < 2; ++_i) \
;         __builtin_amdgcn_global_load_lds((const unsigned*)((const char*)(gbase) + (voff)[_i]), (LAS unsigned*)(lds + (bufoff) + ldsw + _i * 8192), 16, 0, 0); } while (0)
; #define PG8_LDA(dst, b, h) do { _Pragma("unroll") for (int m = 0; m < 4; ++m) _Pragma("unroll") for (int k = 0; k < 2; ++k) dst[m][k] = *(const LAS bf16x8*)(lds + PG8_SA(b, h) + aoff + m * 2048 + k * 1024); } while (0)
; #define PG8_LDB(dst, b, h) do { _Pragma("unroll") for (int n = 0; n < 2; ++n) _Pragma("unroll") for (int k = 0; k < 2; ++k) dst[n][k] = *(const LAS bf16x8*)(lds + PG8_SB(b, h) + boff + n * 2048 + k * 1024); } while (0)
; #define PG8_MMA(ai, bj, At, Bt) do { __builtin_amdgcn_s_setprio(1); _Pragma("unroll") for (int m = 0; m < 4; ++m) _Pragma("unroll") for (int n = 0; n < 2; ++n) _Pragma("unroll") for (int k = 0; k < 2; ++k) \
;         acc[ai][bj][m][n] = __builtin_amdgcn_mfma_f32_16x16x32_bf16(Bt[n][k], At[m][k], acc[ai][bj][m][n], 0, 0, 0); __builtin_amdgcn_s_setprio(0); } while (0)
; #define PG8_WAIT_V(n) asm volatile("s_waitcnt vmcnt(" #n ")" ::: "memory")
; #define PG8_WAIT_L(n) asm volatile("s_waitcnt lgkmcnt(" #n ")" ::: "memory")
; #define PG8_BAR __builtin_amdgcn_s_barrier()
; #define PG8_SCHED __builtin_amdgcn_sched_barrier(0)
; template <class Epi, class Sched>
; __device__ __forceinline__ void gemm_phase(LAS unsigned char* lds, const int tid, const char* Abase, const int K, const Sched& S, const Epi& E) {
;     ...
;             PG8_WAIT_V(8); PG8_WAIT_L(0); PG8_BAR; PG8_MMA(1, 0, At, B0); PG8_MMA(1, 1, At, B1); PG8_BAR; PG8_SCHED;
;             PG8_LDB(B0, 1, 0); PG8_LDB(B1, 1, 1); PG8_SCHED; PG8_LDA(At, 1, 0); PG8_STAGE(PG8_SA(0, 1), a2, w2[1]);
;             PG8_WAIT_V(8); PG8_WAIT_L(0); PG8_BAR; PG8_MMA(0, 0, At, B0); PG8_MMA(0, 1, At, B1); PG8_BAR; PG8_SCHED;
	s_setprio 1
	s_waitcnt lgkmcnt(0)
	v_mfma_f32_16x16x32_bf16 v[62:65], v[150:153], v[182:185], v[62:65]
	v_mfma_f32_16x16x32_bf16 v[58:61], v[158:161], v[182:185], v[58:61]
	v_mfma_f32_16x16x32_bf16 v[46:49], v[150:153], v[206:209], v[46:49]
	v_mfma_f32_16x16x32_bf16 v[42:45], v[158:161], v[206:209], v[42:45]
	v_mfma_f32_16x16x32_bf16 v[30:33], v[150:153], v[218:221], v[30:33]
	v_mfma_f32_16x16x32_bf16 v[26:29], v[158:161], v[218:221], v[26:29]
	v_mfma_f32_16x16x32_bf16 v[14:17], v[150:153], v[226:229], v[14:17]
	v_mfma_f32_16x16x32_bf16 v[10:13], v[158:161], v[226:229], v[10:13]
	v_mfma_f32_16x16x32_bf16 v[62:65], v[154:157], v[202:205], v[62:65]
	v_mfma_f32_16x16x32_bf16 v[58:61], v[162:165], v[202:205], v[58:61]
	v_mfma_f32_16x16x32_bf16 v[46:49], v[154:157], v[214:217], v[46:49]
	v_mfma_f32_16x16x32_bf16 v[42:45], v[162:165], v[214:217], v[42:45]
	v_mfma_f32_16x16x32_bf16 v[30:33], v[154:157], v[222:225], v[30:33]
	v_mfma_f32_16x16x32_bf16 v[26:29], v[162:165], v[222:225], v[26:29]
	v_mfma_f32_16x16x32_bf16 v[14:17], v[154:157], v[230:233], v[14:17]
	v_mfma_f32_16x16x32_bf16 v[10:13], v[162:165], v[230:233], v[10:13]
	v_mfma_f32_16x16x32_bf16 v[54:57], v[166:169], v[182:185], v[54:57]
	v_mfma_f32_16x16x32_bf16 v[50:53], v[174:177], v[182:185], v[50:53]
	v_mfma_f32_16x16x32_bf16 v[38:41], v[166:169], v[206:209], v[38:41]
	v_mfma_f32_16x16x32_bf16 v[34:37], v[174:177], v[206:209], v[34:37]
	v_mfma_f32_16x16x32_bf16 v[22:25], v[166:169], v[218:221], v[22:25]
	v_mfma_f32_16x16x32_bf16 v[18:21], v[174:177], v[218:221], v[18:21]
	v_mfma_f32_16x16x32_bf16 v[6:9], v[166:169], v[226:229], v[6:9]
	v_mfma_f32_16x16x32_bf16 v[2:5], v[174:177], v[226:229], v[2:5]
	v_mfma_f32_16x16x32_bf16 v[54:57], v[170:173], v[202:205], v[54:57]
	v_mfma_f32_16x16x32_bf16 v[50:53], v[178:181], v[202:205], v[50:53]
	v_mfma_f32_16x16x32_bf16 v[38:41], v[170:173], v[214:217], v[38:41]
	v_mfma_f32_16x16x32_bf16 v[34:37], v[178:181], v[214:217], v[34:37]
	v_mfma_f32_16x16x32_bf16 v[22:25], v[170:173], v[222:225], v[22:25]
	v_mfma_f32_16x16x32_bf16 v[18:21], v[178:181], v[222:225], v[18:21]
	v_mfma_f32_16x16x32_bf16 v[6:9], v[170:173], v[230:233], v[6:9]
	v_mfma_f32_16x16x32_bf16 v[2:5], v[178:181], v[230:233], v[2:5]
	s_setprio 0
	s_barrier
	s_add_i32 s20, 0, 0x18000
	v_add_u32_e32 v0, s20, v147
	s_add_i32 s21, 0, 0x1c000
	ds_read_b128 v[150:153], v0
	ds_read_b128 v[154:157], v0 offset:1024
	ds_read_b128 v[158:161], v0 offset:2048
	ds_read_b128 v[162:165], v0 offset:3072
	v_add_u32_e32 v0, s21, v147
	ds_read_b128 v[166:169], v0
	ds_read_b128 v[170:173], v0 offset:1024
	ds_read_b128 v[174:177], v0 offset:2048
	ds_read_b128 v[178:181], v0 offset:3072
	s_mov_b32 m0, s73
	v_lshl_add_u64 v[142:143], s[16:17], 0, v[142:143]
	ds_read_b128 v[182:185], v148 offset:32768
	ds_read_b128 v[202:205], v148 offset:33792
	ds_read_b128 v[206:209], v148 offset:34816
	ds_read_b128 v[214:217], v148 offset:35840
	ds_read_b128 v[218:221], v148 offset:36864
	ds_read_b128 v[222:225], v148 offset:37888
	ds_read_b128 v[226:229], v148 offset:38912
	ds_read_b128 v[230:233], v148 offset:39936
	global_load_lds_dwordx4 v[142:143], off
	v_lshl_add_u64 v[140:141], s[16:17], 0, v[140:141]
	s_mov_b32 m0, s90
	s_nop 0
	global_load_lds_dwordx4 v[140:141], off
	s_waitcnt vmcnt(8)
	s_waitcnt lgkmcnt(0)
	s_barrier
	s_setprio 1
	s_waitcnt lgkmcnt(0)
	v_mfma_f32_16x16x32_bf16 v[130:133], v[150:153], v[182:185], v[130:133]
	v_mfma_f32_16x16x32_bf16 v[126:129], v[158:161], v[182:185], v[126:129]
	v_mfma_f32_16x16x32_bf16 v[110:113], v[150:153], v[206:209], v[110:113]
	v_mfma_f32_16x16x32_bf16 v[106:109], v[158:161], v[206:209], v[106:109]
	v_mfma_f32_16x16x32_bf16 v[94:97], v[150:153], v[218:221], v[94:97]
	v_mfma_f32_16x16x32_bf16 v[90:93], v[158:161], v[218:221], v[90:93]
	v_mfma_f32_16x16x32_bf16 v[78:81], v[150:153], v[226:229], v[78:81]
	v_mfma_f32_16x16x32_bf16 v[74:77], v[158:161], v[226:229], v[74:77]
	v_mfma_f32_16x16x32_bf16 v[130:133], v[154:157], v[202:205], v[130:133]
	v_mfma_f32_16x16x32_bf16 v[126:129], v[162:165], v[202:205], v[126:129]
	v_mfma_f32_16x16x32_bf16 v[110:113], v[154:157], v[214:217], v[110:113]
	v_mfma_f32_16x16x32_bf16 v[106:109], v[162:165], v[214:217], v[106:109]
	v_mfma_f32_16x16x32_bf16 v[94:97], v[154:157], v[222:225], v[94:97]
	v_mfma_f32_16x16x32_bf16 v[90:93], v[162:165], v[222:225], v[90:93]
	v_mfma_f32_16x16x32_bf16 v[78:81], v[154:157], v[230:233], v[78:81]
	v_mfma_f32_16x16x32_bf16 v[74:77], v[162:165], v[230:233], v[74:77]
	v_mfma_f32_16x16x32_bf16 v[122:125], v[166:169], v[182:185], v[122:125]
	v_mfma_f32_16x16x32_bf16 v[118:121], v[174:177], v[182:185], v[118:121]
	v_mfma_f32_16x16x32_bf16 v[102:105], v[166:169], v[206:209], v[102:105]
	v_mfma_f32_16x16x32_bf16 v[98:101], v[174:177], v[206:209], v[98:101]
	v_mfma_f32_16x16x32_bf16 v[86:89], v[166:169], v[218:221], v[86:89]
	v_mfma_f32_16x16x32_bf16 v[82:85], v[174:177], v[218:221], v[82:85]
	v_mfma_f32_16x16x32_bf16 v[70:73], v[166:169], v[226:229], v[70:73]
	v_mfma_f32_16x16x32_bf16 v[66:69], v[174:177], v[226:229], v[66:69]
	v_mfma_f32_16x16x32_bf16 v[122:125], v[170:173], v[202:205], v[122:125]
	v_mfma_f32_16x16x32_bf16 v[118:121], v[178:181], v[202:205], v[118:121]
	v_mfma_f32_16x16x32_bf16 v[102:105], v[170:173], v[214:217], v[102:105]
	v_mfma_f32_16x16x32_bf16 v[98:101], v[178:181], v[214:217], v[98:101]
	v_mfma_f32_16x16x32_bf16 v[86:89], v[170:173], v[222:225], v[86:89]
	v_mfma_f32_16x16x32_bf16 v[82:85], v[178:181], v[222:225], v[82:85]
	v_mfma_f32_16x16x32_bf16 v[70:73], v[170:173], v[230:233], v[70:73]
	v_mfma_f32_16x16x32_bf16 v[66:69], v[178:181], v[230:233], v[66:69]
	s_setprio 0
	s_barrier
; #define PG8_STAGE(bufoff, gbase, voff) do { _Pragma("unroll") for (int _i = 0; _i < 2; ++_i) \
;         __builtin_amdgcn_global_load_lds((const unsigned*)((const char*)(gbase) + (voff)[_i]), (LAS unsigned*)(lds + (bufoff) + ldsw + _i * 8192), 16, 0, 0); } while (0)
; #define PG8_LDA(dst, b, h) do { _Pragma("unroll") for (int m = 0; m < 4; ++m) _Pragma("unroll") for (int k = 0; k < 2; ++k) dst[m][k] = *(const LAS bf16x8*)(lds + PG8_SA(b, h) + aoff + m * 2048 + k * 1024); } while (0)
; #define PG8_MMA(ai, bj, At, Bt) do { __builtin_amdgcn_s_setprio(1); _Pragma("unroll") for (int m = 0; m < 4; ++m) _Pragma("unroll") for (int n = 0; n < 2; ++n) _Pragma("unroll") for (int k = 0; k < 2; ++k) \
;         acc[ai][bj][m][n] = __builtin_amdgcn_mfma_f32_16x16x32_bf16(Bt[n][k], At[m][k], acc[ai][bj][m][n], 0, 0, 0); __builtin_amdgcn_s_setprio(0); } while (0)
; #define PG8_WAIT_V(n) asm volatile("s_waitcnt vmcnt(" #n ")" ::: "memory")
; #define PG8_WAIT_L(n) asm volatile("s_waitcnt lgkmcnt(" #n ")" ::: "memory")
; #define PG8_BAR __builtin_amdgcn_s_barrier()
; #define PG8_SCHED __builtin_amdgcn_sched_barrier(0)
; template <class Epi, class Sched>
; __device__ __forceinline__ void gemm_phase(LAS unsigned char* lds, const int tid, const char* Abase, const int K, const Sched& S, const Epi& E) {
;     ...
;             PG8_LDA(At, 1, 1); PG8_STAGE(PG8_SB(1, 0), b3, voffB); PG8_STAGE(PG8_SB(1, 1), b3 + hstep, voffB); PG8_STAGE(PG8_SA(1, 0), a3, w2[0]);
;             PG8_WAIT_V(8); PG8_WAIT_L(0); PG8_BAR; PG8_MMA(1, 0, At, B0); PG8_MMA(1, 1, At, B1); PG8_BAR; PG8_SCHED;
;         }
	s_add_i32 s16, s20, s70
	v_lshl_add_u64 v[186:187], v[186:187], 0, s[24:25]
	s_mov_b32 m0, s16
	ds_read_b128 v[140:143], v148 offset:49152
	ds_read_b128 v[182:185], v148 offset:50176
	ds_read_b128 v[202:205], v148 offset:51200
	ds_read_b128 v[206:209], v148 offset:52224
	ds_read_b128 v[214:217], v148 offset:53248
	ds_read_b128 v[218:221], v148 offset:54272
	ds_read_b128 v[222:225], v148 offset:55296
	ds_read_b128 v[226:229], v148 offset:56320
	global_load_lds_dwordx4 v[186:187], off
	s_add_i32 m0, s16, 0x2000
	s_add_u32 s14, s14, 0x40080
	v_lshl_add_u64 v[186:187], v[190:191], 0, s[24:25]
	s_addc_u32 s15, s15, 0
	s_add_i32 s16, s21, s70
	global_load_lds_dwordx4 v[186:187], off
	v_lshl_add_u64 v[186:187], s[14:15], 0, v[134:135]
	s_mov_b32 m0, s16
	v_lshl_add_u64 v[144:145], v[144:145], 0, s[24:25]
	global_load_lds_dwordx4 v[186:187], off
	v_lshl_add_u64 v[186:187], s[14:15], 0, v[136:137]
	s_add_i32 m0, s16, 0x2000
	s_nop 0
	global_load_lds_dwordx4 v[186:187], off
	v_lshl_add_u64 v[186:187], v[192:193], 0, s[24:25]
	s_mov_b32 m0, s2
	s_nop 0
	global_load_lds_dwordx4 v[186:187], off
	s_mov_b32 m0, s33
	s_nop 0
	global_load_lds_dwordx4 v[144:145], off
	s_waitcnt vmcnt(8)
	s_waitcnt lgkmcnt(0)
	s_barrier
	s_setprio 1
	s_waitcnt lgkmcnt(0)
	v_mfma_f32_16x16x32_bf16 v[62:65], v[150:153], v[140:143], v[62:65]
	v_mfma_f32_16x16x32_bf16 v[58:61], v[158:161], v[140:143], v[58:61]
	v_mfma_f32_16x16x32_bf16 v[46:49], v[150:153], v[202:205], v[46:49]
	v_mfma_f32_16x16x32_bf16 v[42:45], v[158:161], v[202:205], v[42:45]
	v_mfma_f32_16x16x32_bf16 v[30:33], v[150:153], v[214:217], v[30:33]
	v_mfma_f32_16x16x32_bf16 v[26:29], v[158:161], v[214:217], v[26:29]
	v_mfma_f32_16x16x32_bf16 v[14:17], v[150:153], v[222:225], v[14:17]
	v_mfma_f32_16x16x32_bf16 v[10:13], v[158:161], v[222:225], v[10:13]
	v_mfma_f32_16x16x32_bf16 v[62:65], v[154:157], v[182:185], v[62:65]
	v_mfma_f32_16x16x32_bf16 v[58:61], v[162:165], v[182:185], v[58:61]
	v_mfma_f32_16x16x32_bf16 v[46:49], v[154:157], v[206:209], v[46:49]
	v_mfma_f32_16x16x32_bf16 v[42:45], v[162:165], v[206:209], v[42:45]
	v_mfma_f32_16x16x32_bf16 v[30:33], v[154:157], v[218:221], v[30:33]
	v_mfma_f32_16x16x32_bf16 v[26:29], v[162:165], v[218:221], v[26:29]
	v_mfma_f32_16x16x32_bf16 v[14:17], v[154:157], v[226:229], v[14:17]
	v_mfma_f32_16x16x32_bf16 v[10:13], v[162:165], v[226:229], v[10:13]
	v_mfma_f32_16x16x32_bf16 v[54:57], v[166:169], v[140:143], v[54:57]
	v_mfma_f32_16x16x32_bf16 v[50:53], v[174:177], v[140:143], v[50:53]
	v_mfma_f32_16x16x32_bf16 v[38:41], v[166:169], v[202:205], v[38:41]
	v_mfma_f32_16x16x32_bf16 v[34:37], v[174:177], v[202:205], v[34:37]
	v_mfma_f32_16x16x32_bf16 v[22:25], v[166:169], v[214:217], v[22:25]
	v_mfma_f32_16x16x32_bf16 v[18:21], v[174:177], v[214:217], v[18:21]
	v_mfma_f32_16x16x32_bf16 v[6:9], v[166:169], v[222:225], v[6:9]
	v_mfma_f32_16x16x32_bf16 v[2:5], v[174:177], v[222:225], v[2:5]
	v_mfma_f32_16x16x32_bf16 v[54:57], v[170:173], v[182:185], v[54:57]
	v_mfma_f32_16x16x32_bf16 v[50:53], v[178:181], v[182:185], v[50:53]
	v_mfma_f32_16x16x32_bf16 v[38:41], v[170:173], v[206:209], v[38:41]
	v_mfma_f32_16x16x32_bf16 v[34:37], v[178:181], v[206:209], v[34:37]
	v_mfma_f32_16x16x32_bf16 v[22:25], v[170:173], v[218:221], v[22:25]
	v_mfma_f32_16x16x32_bf16 v[18:21], v[178:181], v[218:221], v[18:21]
	v_mfma_f32_16x16x32_bf16 v[6:9], v[170:173], v[226:229], v[6:9]
	v_mfma_f32_16x16x32_bf16 v[2:5], v[178:181], v[226:229], v[2:5]
	s_setprio 0
	s_barrier
	s_add_i32 s19, s19, 2
	s_add_u32 s7, s7, 0x100
	s_addc_u32 s18, s18, 0
	s_add_u32 s12, s12, 0x100
	s_addc_u32 s13, s13, 0
	s_cmp_gt_u32 s19, 13
	s_cbranch_scc1 .LBB0_350

; #define PG8_STAGE(bufoff, gbase, voff) do { _Pragma("unroll") for (int _i = 0; _i < 2; ++_i) \
;         __builtin_amdgcn_global_load_lds((const unsigned*)((const char*)(gbase) + (voff)[_i]), (LAS unsigned*)(lds + (bufoff) + ldsw + _i * 8192), 16, 0, 0); } while (0)
; #define PG8_LDA(dst, b, h) do { _Pragma("unroll") for (int m = 0; m < 4; ++m) _Pragma("unroll") for (int k = 0; k < 2; ++k) dst[m][k] = *(const LAS bf16x8*)(lds + PG8_SA(b, h) + aoff + m * 2048 + k * 1024); } while (0)
; #define PG8_LDB(dst, b, h) do { _Pragma("unroll") for (int n = 0; n < 2; ++n) _Pragma("unroll") for (int k = 0; k < 2; ++k) dst[n][k] = *(const LAS bf16x8*)(lds + PG8_SB(b, h) + boff + n * 2048 + k * 1024); } while (0)
; #define PG8_WAIT_V(n) asm volatile("s_waitcnt vmcnt(" #n ")" ::: "memory")
; template <class Epi, class Sched>
; __device__ __forceinline__ void gemm_phase(LAS unsigned char* lds, const int tid, const char* Abase, const int K, const Sched& S, const Epi& E) {
;     ...
;           if (has_next) { PG8_AOFFS(vn, nxt); nB = S.b_tile(nxt); *vslot = (u32x4){vn[0][0], vn[0][1], vn[1][0], vn[1][1]}; }
;           else *vslot = (u32x4){vc[0][0], vc[0][1], vc[1][0], vc[1][1]}; }
;         for (int t = 0; t < nt; t += 2) {
;             if constexpr (Epi::MID) { if (t == (nt >> 1)) E.mid(acc, ui, wr, fr, lds); }
;             const bool last = (t == nt - 2);
;             const char* a1 = Abase + (size_t)(t + 1) * kstep;
;             const char* a2 = last ? Abase : Abase + (size_t)(t + 2) * kstep; const char* b2 = last ? nB : cB + (size_t)(t + 2) * kstep;
;             const char* a3 = a2 + kstep; const char* b3 = b2 + kstep;
;             unsigned w2[2][2];
;             if (last) { const u32x4 q = *vslot; w2[0][0] = q.x; w2[0][1] = q.y; w2[1][0] = q.z; w2[1][1] = q.w; }
;             else { w2[0][0] = vc[0][0]; w2[0][1] = vc[0][1]; w2[1][0] = vc[1][0]; w2[1][1] = vc[1][1]; }
;             PG8_LDB(B0, 0, 0); PG8_LDB(B1, 0, 1); PG8_SCHED; PG8_LDA(At, 0, 0); PG8_STAGE(PG8_SA(1, 1), a1, vc[1]);
;             PG8_WAIT_V(8); PG8_WAIT_L(0); PG8_BAR; PG8_MMA(0, 0, At, B0); PG8_MMA(0, 1, At, B1); PG8_BAR; PG8_SCHED;
;             PG8_LDA(At, 0, 1); PG8_STAGE(PG8_SB(0, 0), b2, voffB); PG8_STAGE(PG8_SB(0, 1), b2 + hstep, voffB); PG8_STAGE(PG8_SA(0, 0), a2, w2[0]);
;             PG8_WAIT_V(8); PG8_WAIT_L(0); PG8_BAR; PG8_MMA(1, 0, At, B0); PG8_MMA(1, 1, At, B1); PG8_BAR; PG8_SCHED;
.LBB0_654:
	s_add_i32 s65, 0, 0x10000
	s_add_i32 s48, 0, 0x14000
	ds_write_b128 v250, v[6:9]
	v_add_u32_e32 v0, s65, v252
	v_add_u32_e32 v10, s48, v252
	ds_read_b128 v[12:15], v0
	ds_read_b128 v[16:19], v0 offset:1024
	ds_read_b128 v[20:23], v0 offset:2048
	ds_read_b128 v[24:27], v0 offset:3072
	ds_read_b128 v[28:31], v10
	ds_read_b128 v[32:35], v10 offset:1024
	ds_read_b128 v[36:39], v10 offset:2048
	ds_read_b128 v[40:43], v10 offset:3072
	v_mov_b32_e32 v212, 1
	s_add_i32 s7, s51, 0xc000
	s_mov_b32 m0, s7
	s_add_i32 s12, s51, 0xe000
	ds_read_b128 v[6:9], v150
	ds_read_b128 v[44:47], v150 offset:1024
	ds_read_b128 v[48:51], v150 offset:2048
	ds_read_b128 v[52:55], v150 offset:3072
	ds_read_b128 v[56:59], v150 offset:4096
	ds_read_b128 v[60:63], v150 offset:5120
	ds_read_b128 v[64:67], v150 offset:6144
	ds_read_b128 v[68:71], v150 offset:7168
	global_load_lds_dwordx4 v4, s[30:31]
	s_mov_b32 m0, s12
	s_nop 0
	global_load_lds_dwordx4 v5, s[30:31]
	s_waitcnt vmcnt(8)
	s_waitcnt lgkmcnt(0)
	s_barrier
	s_setprio 1
	s_waitcnt lgkmcnt(0)
	v_mfma_f32_16x16x32_bf16 v[72:75], v[12:15], v[6:9], 0
	v_mfma_f32_16x16x32_bf16 v[76:79], v[20:23], v[6:9], 0
	v_mfma_f32_16x16x32_bf16 v[80:83], v[12:15], v[48:51], 0
	v_mfma_f32_16x16x32_bf16 v[84:87], v[20:23], v[48:51], 0
	v_mfma_f32_16x16x32_bf16 v[88:91], v[12:15], v[56:59], 0
	v_mfma_f32_16x16x32_bf16 v[92:95], v[20:23], v[56:59], 0
	v_mfma_f32_16x16x32_bf16 v[96:99], v[12:15], v[64:67], 0
	v_mfma_f32_16x16x32_bf16 v[100:103], v[20:23], v[64:67], 0
	v_mfma_f32_16x16x32_bf16 v[72:75], v[16:19], v[44:47], v[72:75]
	v_mfma_f32_16x16x32_bf16 v[76:79], v[24:27], v[44:47], v[76:79]
	v_mfma_f32_16x16x32_bf16 v[80:83], v[16:19], v[52:55], v[80:83]
	v_mfma_f32_16x16x32_bf16 v[84:87], v[24:27], v[52:55], v[84:87]
	v_mfma_f32_16x16x32_bf16 v[88:91], v[16:19], v[60:63], v[88:91]
	v_mfma_f32_16x16x32_bf16 v[92:95], v[24:27], v[60:63], v[92:95]
	v_mfma_f32_16x16x32_bf16 v[96:99], v[16:19], v[68:71], v[96:99]
	v_mfma_f32_16x16x32_bf16 v[100:103], v[24:27], v[68:71], v[100:103]
	v_mfma_f32_16x16x32_bf16 v[104:107], v[28:31], v[6:9], 0
	v_mfma_f32_16x16x32_bf16 v[6:9], v[36:39], v[6:9], 0
	v_mfma_f32_16x16x32_bf16 v[104:107], v[32:35], v[44:47], v[104:107]
	v_mfma_f32_16x16x32_bf16 v[44:47], v[40:43], v[44:47], v[6:9]
	v_mfma_f32_16x16x32_bf16 v[6:9], v[28:31], v[48:51], 0
	v_mfma_f32_16x16x32_bf16 v[108:111], v[32:35], v[52:55], v[6:9]
	v_mfma_f32_16x16x32_bf16 v[6:9], v[36:39], v[48:51], 0
	v_mfma_f32_16x16x32_bf16 v[48:51], v[40:43], v[52:55], v[6:9]
	v_mfma_f32_16x16x32_bf16 v[6:9], v[28:31], v[56:59], 0
	v_mfma_f32_16x16x32_bf16 v[52:55], v[32:35], v[60:63], v[6:9]
	v_mfma_f32_16x16x32_bf16 v[6:9], v[36:39], v[56:59], 0
	v_mfma_f32_16x16x32_bf16 v[56:59], v[40:43], v[60:63], v[6:9]
	v_mfma_f32_16x16x32_bf16 v[6:9], v[28:31], v[64:67], 0
	v_mfma_f32_16x16x32_bf16 v[60:63], v[32:35], v[68:71], v[6:9]
	v_mfma_f32_16x16x32_bf16 v[6:9], v[36:39], v[64:67], 0
	v_mfma_f32_16x16x32_bf16 v[64:67], v[40:43], v[68:71], v[6:9]
	s_setprio 0
	s_barrier
	s_nop 4
	v_lshl_add_u64 v[6:7], s[14:15], 0, v[130:131]
	s_mov_b64 s[66:67], 0x100
	s_add_i32 s65, s65, s50
	v_lshl_add_u64 v[8:9], v[6:7], 0, s[66:67]
	s_mov_b32 m0, s65
	ds_read_b128 v[68:71], v150 offset:16384
	ds_read_b128 v[112:115], v150 offset:17408
	ds_read_b128 v[116:119], v150 offset:18432
	ds_read_b128 v[120:123], v150 offset:19456
	ds_read_b128 v[124:127], v150 offset:20480
	ds_read_b128 v[134:137], v150 offset:21504
	ds_read_b128 v[138:141], v150 offset:22528
	ds_read_b128 v[142:145], v150 offset:23552
	global_load_lds_dwordx4 v[8:9], off
	v_lshl_add_u64 v[8:9], s[14:15], 0, v[132:133]
	s_add_i32 s13, s65, 0x2000
	v_lshl_add_u64 v[128:129], v[8:9], 0, s[66:67]
	s_add_u32 s66, s14, 0x18100
	s_mov_b32 m0, s13
	s_addc_u32 s67, s15, 0
	s_add_i32 s48, s48, s50
	global_load_lds_dwordx4 v[128:129], off
	v_lshl_add_u64 v[128:129], s[66:67], 0, v[130:131]
	s_mov_b32 m0, s48
	s_add_i32 s49, s48, 0x2000
	global_load_lds_dwordx4 v[128:129], off
	v_lshl_add_u64 v[128:129], s[66:67], 0, v[132:133]
	s_mov_b32 m0, s49
	s_nop 0
	global_load_lds_dwordx4 v[128:129], off
	s_mov_b32 m0, s51
	s_nop 0
	global_load_lds_dwordx4 v2, s[36:37]
	s_mov_b32 m0, s52
	s_nop 0
	global_load_lds_dwordx4 v3, s[36:37]
	s_waitcnt vmcnt(8)
	s_waitcnt lgkmcnt(0)
	s_barrier
	s_setprio 1
	s_waitcnt lgkmcnt(0)
	v_mfma_f32_16x16x32_bf16 v[152:155], v[12:15], v[68:71], 0
	v_mfma_f32_16x16x32_bf16 v[160:163], v[12:15], v[116:119], 0
	v_mfma_f32_16x16x32_bf16 v[168:171], v[12:15], v[124:127], 0
	v_mfma_f32_16x16x32_bf16 v[12:15], v[12:15], v[138:141], 0
	v_mfma_f32_16x16x32_bf16 v[152:155], v[16:19], v[112:115], v[152:155]
	v_mfma_f32_16x16x32_bf16 v[156:159], v[20:23], v[68:71], 0
	v_mfma_f32_16x16x32_bf16 v[160:163], v[16:19], v[120:123], v[160:163]
	v_mfma_f32_16x16x32_bf16 v[164:167], v[20:23], v[116:119], 0
	v_mfma_f32_16x16x32_bf16 v[168:171], v[16:19], v[134:137], v[168:171]
	v_mfma_f32_16x16x32_bf16 v[172:175], v[20:23], v[124:127], 0
	v_mfma_f32_16x16x32_bf16 v[14:17], v[16:19], v[142:145], v[12:15]
	v_mfma_f32_16x16x32_bf16 v[18:21], v[20:23], v[138:141], 0
	v_mfma_f32_16x16x32_bf16 v[18:21], v[24:27], v[142:145], v[18:21]
	v_mfma_f32_16x16x32_bf16 v[156:159], v[24:27], v[112:115], v[156:159]
	v_mfma_f32_16x16x32_bf16 v[164:167], v[24:27], v[120:123], v[164:167]
	v_mfma_f32_16x16x32_bf16 v[172:175], v[24:27], v[134:137], v[172:175]
	v_mfma_f32_16x16x32_bf16 v[22:25], v[28:31], v[68:71], 0
	v_mfma_f32_16x16x32_bf16 v[68:71], v[36:39], v[68:71], 0
	v_mfma_f32_16x16x32_bf16 v[22:25], v[32:35], v[112:115], v[22:25]
	v_mfma_f32_16x16x32_bf16 v[68:71], v[40:43], v[112:115], v[68:71]
	v_mfma_f32_16x16x32_bf16 v[112:115], v[28:31], v[116:119], 0
	v_mfma_f32_16x16x32_bf16 v[116:119], v[36:39], v[116:119], 0
	v_mfma_f32_16x16x32_bf16 v[112:115], v[32:35], v[120:123], v[112:115]
	v_mfma_f32_16x16x32_bf16 v[116:119], v[40:43], v[120:123], v[116:119]
	v_mfma_f32_16x16x32_bf16 v[120:123], v[28:31], v[124:127], 0
	v_mfma_f32_16x16x32_bf16 v[26:29], v[28:31], v[138:141], 0
	v_mfma_f32_16x16x32_bf16 v[120:123], v[32:35], v[134:137], v[120:123]
	v_mfma_f32_16x16x32_bf16 v[124:127], v[36:39], v[124:127], 0
	v_mfma_f32_16x16x32_bf16 v[26:29], v[32:35], v[142:145], v[26:29]
	v_mfma_f32_16x16x32_bf16 v[30:33], v[36:39], v[138:141], 0
	v_mfma_f32_16x16x32_bf16 v[124:127], v[40:43], v[134:137], v[124:127]
	v_mfma_f32_16x16x32_bf16 v[30:33], v[40:43], v[142:145], v[30:33]
	s_setprio 0
	s_barrier
; #define PG8_STAGE(bufoff, gbase, voff) do { _Pragma("unroll") for (int _i = 0; _i < 2; ++_i) \
;         __builtin_amdgcn_global_load_lds((const unsigned*)((const char*)(gbase) + (voff)[_i]), (LAS unsigned*)(lds + (bufoff) + ldsw + _i * 8192), 16, 0, 0); } while (0)
; #define PG8_LDA(dst, b, h) do { _Pragma("unroll") for (int m = 0; m < 4; ++m) _Pragma("unroll") for (int k = 0; k < 2; ++k) dst[m][k] = *(const LAS bf16x8*)(lds + PG8_SA(b, h) + aoff + m * 2048 + k * 1024); } while (0)
; #define PG8_LDB(dst, b, h) do { _Pragma("unroll") for (int n = 0; n < 2; ++n) _Pragma("unroll") for (int k = 0; k < 2; ++k) dst[n][k] = *(const LAS bf16x8*)(lds + PG8_SB(b, h) + boff + n * 2048 + k * 1024); } while (0)
; #define PG8_MMA(ai, bj, At, Bt) do { __builtin_amdgcn_s_setprio(1); _Pragma("unroll") for (int m = 0; m < 4; ++m) _Pragma("unroll") for (int n = 0; n < 2; ++n) _Pragma("unroll") for (int k = 0; k < 2; ++k) \
;         acc[ai][bj][m][n] = __builtin_amdgcn_mfma_f32_16x16x32_bf16(Bt[n][k], At[m][k], acc[ai][bj][m][n], 0, 0, 0); __builtin_amdgcn_s_setprio(0); } while (0)
; #define PG8_WAIT_V(n) asm volatile("s_waitcnt vmcnt(" #n ")" ::: "memory")
; #define PG8_WAIT_L(n) asm volatile("s_waitcnt lgkmcnt(" #n ")" ::: "memory")
; #define PG8_BAR __builtin_amdgcn_s_barrier()
; #define PG8_SCHED __builtin_amdgcn_sched_barrier(0)
; template <class Epi, class Sched>
; __device__ __forceinline__ void gemm_phase(LAS unsigned char* lds, const int tid, const char* Abase, const int K, const Sched& S, const Epi& E) {
;     ...
;             PG8_LDB(B0, 1, 0); PG8_LDB(B1, 1, 1); PG8_SCHED; PG8_LDA(At, 1, 0); PG8_STAGE(PG8_SA(0, 1), a2, w2[1]);
;             PG8_WAIT_V(8); PG8_WAIT_L(0); PG8_BAR; PG8_MMA(0, 0, At, B0); PG8_MMA(0, 1, At, B1); PG8_BAR; PG8_SCHED;
;             PG8_LDA(At, 1, 1); PG8_STAGE(PG8_SB(1, 0), b3, voffB); PG8_STAGE(PG8_SB(1, 1), b3 + hstep, voffB); PG8_STAGE(PG8_SA(1, 0), a3, w2[0]);
;             PG8_WAIT_V(8); PG8_WAIT_L(0); PG8_BAR; PG8_MMA(1, 0, At, B0); PG8_MMA(1, 1, At, B1); PG8_BAR; PG8_SCHED;
	s_add_i32 s67, 0, 0x18000
	s_add_i32 s64, 0, 0x1c000
	v_add_u32_e32 v11, s67, v252
	v_add_u32_e32 v12, s64, v252
	ds_read_b128 v[34:37], v11
	ds_read_b128 v[38:41], v11 offset:1024
	ds_read_b128 v[134:137], v11 offset:2048
	ds_read_b128 v[138:141], v11 offset:3072
	ds_read_b128 v[142:145], v12
	ds_read_b128 v[176:179], v12 offset:1024
	ds_read_b128 v[180:183], v12 offset:2048
	ds_read_b128 v[184:187], v12 offset:3072
	s_mov_b32 m0, s53
	ds_read_b128 v[202:205], v150 offset:32768
	ds_read_b128 v[206:209], v150 offset:33792
	ds_read_b128 v[214:217], v150 offset:34816
	ds_read_b128 v[218:221], v150 offset:35840
	ds_read_b128 v[222:225], v150 offset:36864
	ds_read_b128 v[226:229], v150 offset:37888
	ds_read_b128 v[230:233], v150 offset:38912
	ds_read_b128 v[234:237], v150 offset:39936
	global_load_lds_dwordx4 v4, s[36:37]
	s_mov_b32 m0, s54
	s_nop 0
	global_load_lds_dwordx4 v5, s[36:37]
	s_waitcnt vmcnt(8)
	s_waitcnt lgkmcnt(0)
	s_barrier
	s_setprio 1
	s_waitcnt lgkmcnt(0)
	v_mfma_f32_16x16x32_bf16 v[72:75], v[34:37], v[202:205], v[72:75]
	v_mfma_f32_16x16x32_bf16 v[76:79], v[134:137], v[202:205], v[76:79]
	v_mfma_f32_16x16x32_bf16 v[80:83], v[34:37], v[214:217], v[80:83]
	v_mfma_f32_16x16x32_bf16 v[84:87], v[134:137], v[214:217], v[84:87]
	v_mfma_f32_16x16x32_bf16 v[88:91], v[34:37], v[222:225], v[88:91]
	v_mfma_f32_16x16x32_bf16 v[92:95], v[134:137], v[222:225], v[92:95]
	v_mfma_f32_16x16x32_bf16 v[96:99], v[34:37], v[230:233], v[96:99]
	v_mfma_f32_16x16x32_bf16 v[100:103], v[134:137], v[230:233], v[100:103]
	v_mfma_f32_16x16x32_bf16 v[72:75], v[38:41], v[206:209], v[72:75]
	v_mfma_f32_16x16x32_bf16 v[76:79], v[138:141], v[206:209], v[76:79]
	v_mfma_f32_16x16x32_bf16 v[80:83], v[38:41], v[218:221], v[80:83]
	v_mfma_f32_16x16x32_bf16 v[84:87], v[138:141], v[218:221], v[84:87]
	v_mfma_f32_16x16x32_bf16 v[88:91], v[38:41], v[226:229], v[88:91]
	v_mfma_f32_16x16x32_bf16 v[92:95], v[138:141], v[226:229], v[92:95]
	v_mfma_f32_16x16x32_bf16 v[96:99], v[38:41], v[234:237], v[96:99]
	v_mfma_f32_16x16x32_bf16 v[100:103], v[138:141], v[234:237], v[100:103]
	v_mfma_f32_16x16x32_bf16 v[104:107], v[142:145], v[202:205], v[104:107]
	v_mfma_f32_16x16x32_bf16 v[42:45], v[180:183], v[202:205], v[44:47]
	v_mfma_f32_16x16x32_bf16 v[108:111], v[142:145], v[214:217], v[108:111]
	v_mfma_f32_16x16x32_bf16 v[46:49], v[180:183], v[214:217], v[48:51]
	v_mfma_f32_16x16x32_bf16 v[50:53], v[142:145], v[222:225], v[52:55]
	v_mfma_f32_16x16x32_bf16 v[54:57], v[180:183], v[222:225], v[56:59]
	v_mfma_f32_16x16x32_bf16 v[58:61], v[142:145], v[230:233], v[60:63]
	v_mfma_f32_16x16x32_bf16 v[62:65], v[180:183], v[230:233], v[64:67]
	v_mfma_f32_16x16x32_bf16 v[104:107], v[176:179], v[206:209], v[104:107]
	v_mfma_f32_16x16x32_bf16 v[42:45], v[184:187], v[206:209], v[42:45]
	v_mfma_f32_16x16x32_bf16 v[108:111], v[176:179], v[218:221], v[108:111]
	v_mfma_f32_16x16x32_bf16 v[46:49], v[184:187], v[218:221], v[46:49]
	v_mfma_f32_16x16x32_bf16 v[50:53], v[176:179], v[226:229], v[50:53]
	v_mfma_f32_16x16x32_bf16 v[54:57], v[184:187], v[226:229], v[54:57]
	v_mfma_f32_16x16x32_bf16 v[58:61], v[176:179], v[234:237], v[58:61]
	v_mfma_f32_16x16x32_bf16 v[62:65], v[184:187], v[234:237], v[62:65]
	s_setprio 0
	s_barrier
	s_mov_b64 s[68:69], 0x180
	s_add_i32 s67, s67, s50
	v_lshl_add_u64 v[66:67], v[6:7], 0, s[68:69]
	s_mov_b32 m0, s67
	s_add_i32 s63, s67, 0x2000
	ds_read_b128 v[202:205], v150 offset:49152
	ds_read_b128 v[206:209], v150 offset:50176
	ds_read_b128 v[214:217], v150 offset:51200
	ds_read_b128 v[218:221], v150 offset:52224
	ds_read_b128 v[222:225], v150 offset:53248
	ds_read_b128 v[226:229], v150 offset:54272
	ds_read_b128 v[230:233], v150 offset:55296
	ds_read_b128 v[234:237], v150 offset:56320
	global_load_lds_dwordx4 v[66:67], off
	v_lshl_add_u64 v[66:67], v[8:9], 0, s[68:69]
	s_add_u32 s68, s14, 0x18180
	s_mov_b32 m0, s63
	s_addc_u32 s69, s15, 0
	s_add_i32 s64, s64, s50
	global_load_lds_dwordx4 v[66:67], off
	v_lshl_add_u64 v[66:67], s[68:69], 0, v[130:131]
	s_mov_b32 m0, s64
	s_add_i32 s66, s64, 0x2000
	global_load_lds_dwordx4 v[66:67], off
	v_lshl_add_u64 v[66:67], s[68:69], 0, v[132:133]
	s_mov_b32 m0, s66
	s_nop 0
	global_load_lds_dwordx4 v[66:67], off
	s_mov_b32 m0, s58
	s_nop 0
	global_load_lds_dwordx4 v2, s[38:39]
	s_mov_b32 m0, s59
	s_nop 0
	global_load_lds_dwordx4 v3, s[38:39]
	s_waitcnt vmcnt(8)
	s_waitcnt lgkmcnt(0)
	s_barrier
	s_setprio 1
	s_waitcnt lgkmcnt(0)
	v_mfma_f32_16x16x32_bf16 v[14:17], v[34:37], v[230:233], v[14:17]
	v_mfma_f32_16x16x32_bf16 v[18:21], v[134:137], v[230:233], v[18:21]
	v_mfma_f32_16x16x32_bf16 v[152:155], v[34:37], v[202:205], v[152:155]
	v_mfma_f32_16x16x32_bf16 v[156:159], v[134:137], v[202:205], v[156:159]
	v_mfma_f32_16x16x32_bf16 v[160:163], v[34:37], v[214:217], v[160:163]
	v_mfma_f32_16x16x32_bf16 v[164:167], v[134:137], v[214:217], v[164:167]
	v_mfma_f32_16x16x32_bf16 v[168:171], v[34:37], v[222:225], v[168:171]
	v_mfma_f32_16x16x32_bf16 v[172:175], v[134:137], v[222:225], v[172:175]
	v_mfma_f32_16x16x32_bf16 v[14:17], v[38:41], v[234:237], v[14:17]
	v_mfma_f32_16x16x32_bf16 v[18:21], v[138:141], v[234:237], v[18:21]
	v_mfma_f32_16x16x32_bf16 v[152:155], v[38:41], v[206:209], v[152:155]
	v_mfma_f32_16x16x32_bf16 v[156:159], v[138:141], v[206:209], v[156:159]
	v_mfma_f32_16x16x32_bf16 v[160:163], v[38:41], v[218:221], v[160:163]
	v_mfma_f32_16x16x32_bf16 v[164:167], v[138:141], v[218:221], v[164:167]
	v_mfma_f32_16x16x32_bf16 v[168:171], v[38:41], v[226:229], v[168:171]
	v_mfma_f32_16x16x32_bf16 v[172:175], v[138:141], v[226:229], v[172:175]
	v_mfma_f32_16x16x32_bf16 v[22:25], v[142:145], v[202:205], v[22:25]
	v_mfma_f32_16x16x32_bf16 v[34:37], v[180:183], v[202:205], v[68:71]
	v_mfma_f32_16x16x32_bf16 v[38:41], v[142:145], v[214:217], v[112:115]
	v_mfma_f32_16x16x32_bf16 v[66:69], v[180:183], v[214:217], v[116:119]
	v_mfma_f32_16x16x32_bf16 v[112:115], v[142:145], v[222:225], v[120:123]
	v_mfma_f32_16x16x32_bf16 v[116:119], v[180:183], v[222:225], v[124:127]
	v_mfma_f32_16x16x32_bf16 v[26:29], v[142:145], v[230:233], v[26:29]
	v_mfma_f32_16x16x32_bf16 v[30:33], v[180:183], v[230:233], v[30:33]
	v_mfma_f32_16x16x32_bf16 v[22:25], v[176:179], v[206:209], v[22:25]
	v_mfma_f32_16x16x32_bf16 v[34:37], v[184:187], v[206:209], v[34:37]
	v_mfma_f32_16x16x32_bf16 v[38:41], v[176:179], v[218:221], v[38:41]
	v_mfma_f32_16x16x32_bf16 v[66:69], v[184:187], v[218:221], v[66:69]
	v_mfma_f32_16x16x32_bf16 v[112:115], v[176:179], v[226:229], v[112:115]
	v_mfma_f32_16x16x32_bf16 v[116:119], v[184:187], v[226:229], v[116:119]
	v_mfma_f32_16x16x32_bf16 v[26:29], v[176:179], v[234:237], v[26:29]
	v_mfma_f32_16x16x32_bf16 v[30:33], v[184:187], v[234:237], v[30:33]
	s_setprio 0
	s_barrier
; #define PG8_STAGE(bufoff, gbase, voff) do { _Pragma("unroll") for (int _i = 0; _i < 2; ++_i) \
;         __builtin_amdgcn_global_load_lds((const unsigned*)((const char*)(gbase) + (voff)[_i]), (LAS unsigned*)(lds + (bufoff) + ldsw + _i * 8192), 16, 0, 0); } while (0)
; #define PG8_LDA(dst, b, h) do { _Pragma("unroll") for (int m = 0; m < 4; ++m) _Pragma("unroll") for (int k = 0; k < 2; ++k) dst[m][k] = *(const LAS bf16x8*)(lds + PG8_SA(b, h) + aoff + m * 2048 + k * 1024); } while (0)
; #define PG8_LDB(dst, b, h) do { _Pragma("unroll") for (int n = 0; n < 2; ++n) _Pragma("unroll") for (int k = 0; k < 2; ++k) dst[n][k] = *(const LAS bf16x8*)(lds + PG8_SB(b, h) + boff + n * 2048 + k * 1024); } while (0)
; #define PG8_MMA(ai, bj, At, Bt) do { __builtin_amdgcn_s_setprio(1); _Pragma("unroll") for (int m = 0; m < 4; ++m) _Pragma("unroll") for (int n = 0; n < 2; ++n) _Pragma("unroll") for (int k = 0; k < 2; ++k) \
;         acc[ai][bj][m][n] = __builtin_amdgcn_mfma_f32_16x16x32_bf16(Bt[n][k], At[m][k], acc[ai][bj][m][n], 0, 0, 0); __builtin_amdgcn_s_setprio(0); } while (0)
; #define PG8_WAIT_V(n) asm volatile("s_waitcnt vmcnt(" #n ")" ::: "memory")
; #define PG8_WAIT_L(n) asm volatile("s_waitcnt lgkmcnt(" #n ")" ::: "memory")
; #define PG8_BAR __builtin_amdgcn_s_barrier()
; #define PG8_SCHED __builtin_amdgcn_sched_barrier(0)
; template <class Epi, class Sched>
; __device__ __forceinline__ void gemm_phase(LAS unsigned char* lds, const int tid, const char* Abase, const int K, const Sched& S, const Epi& E) {
;     ...
;             PG8_LDB(B0, 0, 0); PG8_LDB(B1, 0, 1); PG8_SCHED; PG8_LDA(At, 0, 0); PG8_STAGE(PG8_SA(1, 1), a1, vc[1]);
;             PG8_WAIT_V(8); PG8_WAIT_L(0); PG8_BAR; PG8_MMA(0, 0, At, B0); PG8_MMA(0, 1, At, B1); PG8_BAR; PG8_SCHED;
;             PG8_LDA(At, 0, 1); PG8_STAGE(PG8_SB(0, 0), b2, voffB); PG8_STAGE(PG8_SB(0, 1), b2 + hstep, voffB); PG8_STAGE(PG8_SA(0, 0), a2, w2[0]);
;             PG8_WAIT_V(8); PG8_WAIT_L(0); PG8_BAR; PG8_MMA(1, 0, At, B0); PG8_MMA(1, 1, At, B1); PG8_BAR; PG8_SCHED;
	ds_read_b128 v[120:123], v0
	ds_read_b128 v[124:127], v0 offset:1024
	ds_read_b128 v[134:137], v0 offset:2048
	ds_read_b128 v[138:141], v0 offset:3072
	ds_read_b128 v[142:145], v10
	ds_read_b128 v[176:179], v10 offset:1024
	ds_read_b128 v[180:183], v10 offset:2048
	ds_read_b128 v[184:187], v10 offset:3072
	s_mov_b32 m0, s7
	ds_read_b128 v[202:205], v150
	ds_read_b128 v[206:209], v150 offset:1024
	ds_read_b128 v[214:217], v150 offset:2048
	ds_read_b128 v[218:221], v150 offset:3072
	ds_read_b128 v[222:225], v150 offset:4096
	ds_read_b128 v[226:229], v150 offset:5120
	ds_read_b128 v[230:233], v150 offset:6144
	ds_read_b128 v[234:237], v150 offset:7168
	global_load_lds_dwordx4 v4, s[38:39]
	s_mov_b32 m0, s12
	s_nop 0
	global_load_lds_dwordx4 v5, s[38:39]
	s_waitcnt vmcnt(8)
	s_waitcnt lgkmcnt(0)
	s_barrier
	s_setprio 1
	s_waitcnt lgkmcnt(0)
	v_mfma_f32_16x16x32_bf16 v[70:73], v[120:123], v[202:205], v[72:75]
	v_mfma_f32_16x16x32_bf16 v[74:77], v[134:137], v[202:205], v[76:79]
	v_mfma_f32_16x16x32_bf16 v[78:81], v[120:123], v[214:217], v[80:83]
	v_mfma_f32_16x16x32_bf16 v[82:85], v[134:137], v[214:217], v[84:87]
	v_mfma_f32_16x16x32_bf16 v[86:89], v[120:123], v[222:225], v[88:91]
	v_mfma_f32_16x16x32_bf16 v[90:93], v[134:137], v[222:225], v[92:95]
	v_mfma_f32_16x16x32_bf16 v[94:97], v[120:123], v[230:233], v[96:99]
	v_mfma_f32_16x16x32_bf16 v[98:101], v[134:137], v[230:233], v[100:103]
	v_mfma_f32_16x16x32_bf16 v[70:73], v[124:127], v[206:209], v[70:73]
	v_mfma_f32_16x16x32_bf16 v[74:77], v[138:141], v[206:209], v[74:77]
	v_mfma_f32_16x16x32_bf16 v[78:81], v[124:127], v[218:221], v[78:81]
	v_mfma_f32_16x16x32_bf16 v[82:85], v[138:141], v[218:221], v[82:85]
	v_mfma_f32_16x16x32_bf16 v[86:89], v[124:127], v[226:229], v[86:89]
	v_mfma_f32_16x16x32_bf16 v[90:93], v[138:141], v[226:229], v[90:93]
	v_mfma_f32_16x16x32_bf16 v[94:97], v[124:127], v[234:237], v[94:97]
	v_mfma_f32_16x16x32_bf16 v[98:101], v[138:141], v[234:237], v[98:101]
	v_mfma_f32_16x16x32_bf16 v[102:105], v[142:145], v[202:205], v[104:107]
	v_mfma_f32_16x16x32_bf16 v[42:45], v[180:183], v[202:205], v[42:45]
	v_mfma_f32_16x16x32_bf16 v[106:109], v[142:145], v[214:217], v[108:111]
	v_mfma_f32_16x16x32_bf16 v[46:49], v[180:183], v[214:217], v[46:49]
	v_mfma_f32_16x16x32_bf16 v[50:53], v[142:145], v[222:225], v[50:53]
	v_mfma_f32_16x16x32_bf16 v[54:57], v[180:183], v[222:225], v[54:57]
	v_mfma_f32_16x16x32_bf16 v[58:61], v[142:145], v[230:233], v[58:61]
	v_mfma_f32_16x16x32_bf16 v[62:65], v[180:183], v[230:233], v[62:65]
	v_mfma_f32_16x16x32_bf16 v[102:105], v[176:179], v[206:209], v[102:105]
	v_mfma_f32_16x16x32_bf16 v[42:45], v[184:187], v[206:209], v[42:45]
	v_mfma_f32_16x16x32_bf16 v[106:109], v[176:179], v[218:221], v[106:109]
	v_mfma_f32_16x16x32_bf16 v[46:49], v[184:187], v[218:221], v[46:49]
	v_mfma_f32_16x16x32_bf16 v[50:53], v[176:179], v[226:229], v[50:53]
	v_mfma_f32_16x16x32_bf16 v[54:57], v[184:187], v[226:229], v[54:57]
	v_mfma_f32_16x16x32_bf16 v[58:61], v[176:179], v[234:237], v[58:61]
	v_mfma_f32_16x16x32_bf16 v[62:65], v[184:187], v[234:237], v[62:65]
	s_setprio 0
	s_barrier
	s_mov_b64 s[68:69], 0x200
	s_mov_b32 m0, s65
	v_lshl_add_u64 v[110:111], v[6:7], 0, s[68:69]
	ds_read_b128 v[202:205], v150 offset:16384
	ds_read_b128 v[206:209], v150 offset:17408
	ds_read_b128 v[214:217], v150 offset:18432
	ds_read_b128 v[218:221], v150 offset:19456
	ds_read_b128 v[222:225], v150 offset:20480
	ds_read_b128 v[226:229], v150 offset:21504
	ds_read_b128 v[230:233], v150 offset:22528
	ds_read_b128 v[234:237], v150 offset:23552
	global_load_lds_dwordx4 v[110:111], off
	v_lshl_add_u64 v[110:111], v[8:9], 0, s[68:69]
	s_add_u32 s68, s14, 0x18200
	s_mov_b32 m0, s13
	s_addc_u32 s69, s15, 0
	global_load_lds_dwordx4 v[110:111], off
	v_lshl_add_u64 v[110:111], s[68:69], 0, v[130:131]
	s_mov_b32 m0, s48
	s_nop 0
	global_load_lds_dwordx4 v[110:111], off
	v_lshl_add_u64 v[110:111], s[68:69], 0, v[132:133]
	s_mov_b32 m0, s49
	s_nop 0
	global_load_lds_dwordx4 v[110:111], off
	s_mov_b32 m0, s51
	s_nop 0
	global_load_lds_dwordx4 v2, s[40:41]
	s_mov_b32 m0, s52
	s_nop 0
	global_load_lds_dwordx4 v3, s[40:41]
	s_waitcnt vmcnt(8)
	s_waitcnt lgkmcnt(0)
	s_barrier
	s_setprio 1
	s_waitcnt lgkmcnt(0)
	v_mfma_f32_16x16x32_bf16 v[14:17], v[120:123], v[230:233], v[14:17]
	v_mfma_f32_16x16x32_bf16 v[18:21], v[134:137], v[230:233], v[18:21]
	v_mfma_f32_16x16x32_bf16 v[152:155], v[120:123], v[202:205], v[152:155]
	v_mfma_f32_16x16x32_bf16 v[156:159], v[134:137], v[202:205], v[156:159]
	v_mfma_f32_16x16x32_bf16 v[160:163], v[120:123], v[214:217], v[160:163]
	v_mfma_f32_16x16x32_bf16 v[164:167], v[134:137], v[214:217], v[164:167]
	v_mfma_f32_16x16x32_bf16 v[168:171], v[120:123], v[222:225], v[168:171]
	v_mfma_f32_16x16x32_bf16 v[172:175], v[134:137], v[222:225], v[172:175]
	v_mfma_f32_16x16x32_bf16 v[14:17], v[124:127], v[234:237], v[14:17]
	v_mfma_f32_16x16x32_bf16 v[18:21], v[138:141], v[234:237], v[18:21]
	v_mfma_f32_16x16x32_bf16 v[152:155], v[124:127], v[206:209], v[152:155]
	v_mfma_f32_16x16x32_bf16 v[156:159], v[138:141], v[206:209], v[156:159]
	v_mfma_f32_16x16x32_bf16 v[160:163], v[124:127], v[218:221], v[160:163]
	v_mfma_f32_16x16x32_bf16 v[164:167], v[138:141], v[218:221], v[164:167]
	v_mfma_f32_16x16x32_bf16 v[168:171], v[124:127], v[226:229], v[168:171]
	v_mfma_f32_16x16x32_bf16 v[172:175], v[138:141], v[226:229], v[172:175]
	v_mfma_f32_16x16x32_bf16 v[22:25], v[142:145], v[202:205], v[22:25]
	v_mfma_f32_16x16x32_bf16 v[34:37], v[180:183], v[202:205], v[34:37]
	v_mfma_f32_16x16x32_bf16 v[38:41], v[142:145], v[214:217], v[38:41]
	v_mfma_f32_16x16x32_bf16 v[66:69], v[180:183], v[214:217], v[66:69]
	v_mfma_f32_16x16x32_bf16 v[110:113], v[142:145], v[222:225], v[112:115]
	v_mfma_f32_16x16x32_bf16 v[114:117], v[180:183], v[222:225], v[116:119]
	v_mfma_f32_16x16x32_bf16 v[26:29], v[142:145], v[230:233], v[26:29]
	v_mfma_f32_16x16x32_bf16 v[30:33], v[180:183], v[230:233], v[30:33]
	v_mfma_f32_16x16x32_bf16 v[22:25], v[176:179], v[206:209], v[22:25]
	v_mfma_f32_16x16x32_bf16 v[34:37], v[184:187], v[206:209], v[34:37]
	v_mfma_f32_16x16x32_bf16 v[38:41], v[176:179], v[218:221], v[38:41]
	v_mfma_f32_16x16x32_bf16 v[66:69], v[184:187], v[218:221], v[66:69]
	v_mfma_f32_16x16x32_bf16 v[110:113], v[176:179], v[226:229], v[110:113]
	v_mfma_f32_16x16x32_bf16 v[114:117], v[184:187], v[226:229], v[114:117]
	v_mfma_f32_16x16x32_bf16 v[26:29], v[176:179], v[234:237], v[26:29]
	v_mfma_f32_16x16x32_bf16 v[30:33], v[184:187], v[234:237], v[30:33]
	s_setprio 0
	s_barrier
; #define PG8_STAGE(bufoff, gbase, voff) do { _Pragma("unroll") for (int _i = 0; _i < 2; ++_i) \
;         __builtin_amdgcn_global_load_lds((const unsigned*)((const char*)(gbase) + (voff)[_i]), (LAS unsigned*)(lds + (bufoff) + ldsw + _i * 8192), 16, 0, 0); } while (0)
; #define PG8_LDA(dst, b, h) do { _Pragma("unroll") for (int m = 0; m < 4; ++m) _Pragma("unroll") for (int k = 0; k < 2; ++k) dst[m][k] = *(const LAS bf16x8*)(lds + PG8_SA(b, h) + aoff + m * 2048 + k * 1024); } while (0)
; #define PG8_LDB(dst, b, h) do { _Pragma("unroll") for (int n = 0; n < 2; ++n) _Pragma("unroll") for (int k = 0; k < 2; ++k) dst[n][k] = *(const LAS bf16x8*)(lds + PG8_SB(b, h) + boff + n * 2048 + k * 1024); } while (0)
; #define PG8_MMA(ai, bj, At, Bt) do { __builtin_amdgcn_s_setprio(1); _Pragma("unroll") for (int m = 0; m < 4; ++m) _Pragma("unroll") for (int n = 0; n < 2; ++n) _Pragma("unroll") for (int k = 0; k < 2; ++k) \
;         acc[ai][bj][m][n] = __builtin_amdgcn_mfma_f32_16x16x32_bf16(Bt[n][k], At[m][k], acc[ai][bj][m][n], 0, 0, 0); __builtin_amdgcn_s_setprio(0); } while (0)
; #define PG8_WAIT_V(n) asm volatile("s_waitcnt vmcnt(" #n ")" ::: "memory")
; #define PG8_WAIT_L(n) asm volatile("s_waitcnt lgkmcnt(" #n ")" ::: "memory")
; #define PG8_BAR __builtin_amdgcn_s_barrier()
; #define PG8_SCHED __builtin_amdgcn_sched_barrier(0)
; template <class Epi, class Sched>
; __device__ __forceinline__ void gemm_phase(LAS unsigned char* lds, const int tid, const char* Abase, const int K, const Sched& S, const Epi& E) {
;     ...
;             PG8_LDB(B0, 1, 0); PG8_LDB(B1, 1, 1); PG8_SCHED; PG8_LDA(At, 1, 0); PG8_STAGE(PG8_SA(0, 1), a2, w2[1]);
;             PG8_WAIT_V(8); PG8_WAIT_L(0); PG8_BAR; PG8_MMA(0, 0, At, B0); PG8_MMA(0, 1, At, B1); PG8_BAR; PG8_SCHED;
;             PG8_LDA(At, 1, 1); PG8_STAGE(PG8_SB(1, 0), b3, voffB); PG8_STAGE(PG8_SB(1, 1), b3 + hstep, voffB); PG8_STAGE(PG8_SA(1, 0), a3, w2[0]);
;             PG8_WAIT_V(8); PG8_WAIT_L(0); PG8_BAR; PG8_MMA(1, 0, At, B0); PG8_MMA(1, 1, At, B1); PG8_BAR; PG8_SCHED;
	ds_read_b128 v[118:121], v11
	ds_read_b128 v[122:125], v11 offset:1024
	ds_read_b128 v[126:129], v11 offset:2048
	ds_read_b128 v[134:137], v11 offset:3072
	ds_read_b128 v[138:141], v12
	ds_read_b128 v[142:145], v12 offset:1024
	ds_read_b128 v[176:179], v12 offset:2048
	ds_read_b128 v[180:183], v12 offset:3072
	s_mov_b32 m0, s53
	ds_read_b128 v[184:187], v150 offset:32768
	ds_read_b128 v[202:205], v150 offset:33792
	ds_read_b128 v[206:209], v150 offset:34816
	ds_read_b128 v[214:217], v150 offset:35840
	ds_read_b128 v[218:221], v150 offset:36864
	ds_read_b128 v[222:225], v150 offset:37888
	ds_read_b128 v[226:229], v150 offset:38912
	ds_read_b128 v[230:233], v150 offset:39936
	global_load_lds_dwordx4 v4, s[40:41]
	s_mov_b32 m0, s54
	s_nop 0
	global_load_lds_dwordx4 v5, s[40:41]
	s_waitcnt vmcnt(8)
	s_waitcnt lgkmcnt(0)
	s_barrier
	s_setprio 1
	s_waitcnt lgkmcnt(0)
	v_mfma_f32_16x16x32_bf16 v[70:73], v[118:121], v[184:187], v[70:73]
	v_mfma_f32_16x16x32_bf16 v[74:77], v[126:129], v[184:187], v[74:77]
	v_mfma_f32_16x16x32_bf16 v[78:81], v[118:121], v[206:209], v[78:81]
	v_mfma_f32_16x16x32_bf16 v[82:85], v[126:129], v[206:209], v[82:85]
	v_mfma_f32_16x16x32_bf16 v[86:89], v[118:121], v[218:221], v[86:89]
	v_mfma_f32_16x16x32_bf16 v[90:93], v[126:129], v[218:221], v[90:93]
	v_mfma_f32_16x16x32_bf16 v[94:97], v[118:121], v[226:229], v[94:97]
	v_mfma_f32_16x16x32_bf16 v[98:101], v[126:129], v[226:229], v[98:101]
	v_mfma_f32_16x16x32_bf16 v[70:73], v[122:125], v[202:205], v[70:73]
	v_mfma_f32_16x16x32_bf16 v[74:77], v[134:137], v[202:205], v[74:77]
	v_mfma_f32_16x16x32_bf16 v[78:81], v[122:125], v[214:217], v[78:81]
	v_mfma_f32_16x16x32_bf16 v[82:85], v[134:137], v[214:217], v[82:85]
	v_mfma_f32_16x16x32_bf16 v[86:89], v[122:125], v[222:225], v[86:89]
	v_mfma_f32_16x16x32_bf16 v[90:93], v[134:137], v[222:225], v[90:93]
	v_mfma_f32_16x16x32_bf16 v[94:97], v[122:125], v[230:233], v[94:97]
	v_mfma_f32_16x16x32_bf16 v[98:101], v[134:137], v[230:233], v[98:101]
	v_mfma_f32_16x16x32_bf16 v[102:105], v[138:141], v[184:187], v[102:105]
	v_mfma_f32_16x16x32_bf16 v[42:45], v[176:179], v[184:187], v[42:45]
	v_mfma_f32_16x16x32_bf16 v[106:109], v[138:141], v[206:209], v[106:109]
	v_mfma_f32_16x16x32_bf16 v[46:49], v[176:179], v[206:209], v[46:49]
	v_mfma_f32_16x16x32_bf16 v[50:53], v[138:141], v[218:221], v[50:53]
	v_mfma_f32_16x16x32_bf16 v[54:57], v[176:179], v[218:221], v[54:57]
	v_mfma_f32_16x16x32_bf16 v[58:61], v[138:141], v[226:229], v[58:61]
	v_mfma_f32_16x16x32_bf16 v[62:65], v[176:179], v[226:229], v[62:65]
	v_mfma_f32_16x16x32_bf16 v[102:105], v[142:145], v[202:205], v[102:105]
	v_mfma_f32_16x16x32_bf16 v[42:45], v[180:183], v[202:205], v[42:45]
	v_mfma_f32_16x16x32_bf16 v[106:109], v[142:145], v[214:217], v[106:109]
	v_mfma_f32_16x16x32_bf16 v[46:49], v[180:183], v[214:217], v[46:49]
	v_mfma_f32_16x16x32_bf16 v[50:53], v[142:145], v[222:225], v[50:53]
	v_mfma_f32_16x16x32_bf16 v[54:57], v[180:183], v[222:225], v[54:57]
	v_mfma_f32_16x16x32_bf16 v[58:61], v[142:145], v[230:233], v[58:61]
	v_mfma_f32_16x16x32_bf16 v[62:65], v[180:183], v[230:233], v[62:65]
	s_setprio 0
	s_barrier
	s_mov_b64 s[68:69], 0x280
	s_mov_b32 m0, s67
	v_lshl_add_u64 v[6:7], v[6:7], 0, s[68:69]
	s_add_u32 s14, s14, 0x18280
	ds_read_b128 v[184:187], v150 offset:49152
	ds_read_b128 v[202:205], v150 offset:50176
	ds_read_b128 v[206:209], v150 offset:51200
	ds_read_b128 v[214:217], v150 offset:52224
	ds_read_b128 v[218:221], v150 offset:53248
	ds_read_b128 v[222:225], v150 offset:54272
	ds_read_b128 v[226:229], v150 offset:55296
	ds_read_b128 v[230:233], v150 offset:56320
	global_load_lds_dwordx4 v[6:7], off
	v_lshl_add_u64 v[6:7], v[8:9], 0, s[68:69]
	s_mov_b32 m0, s63
	s_addc_u32 s15, s15, 0
	global_load_lds_dwordx4 v[6:7], off
	v_lshl_add_u64 v[6:7], s[14:15], 0, v[130:131]
	s_mov_b32 m0, s64
	s_nop 0
	global_load_lds_dwordx4 v[6:7], off
	v_lshl_add_u64 v[6:7], s[14:15], 0, v[132:133]
	s_mov_b32 m0, s66
	s_nop 0
	global_load_lds_dwordx4 v[6:7], off
	s_mov_b32 m0, s58
	s_nop 0
	global_load_lds_dwordx4 v2, s[42:43]
	s_mov_b32 m0, s59
	s_nop 0
	global_load_lds_dwordx4 v3, s[42:43]
	s_waitcnt vmcnt(8)
	s_waitcnt lgkmcnt(0)
	s_barrier
	s_setprio 1
	s_waitcnt lgkmcnt(0)
	v_mfma_f32_16x16x32_bf16 v[6:9], v[118:121], v[184:187], v[152:155]
	v_mfma_f32_16x16x32_bf16 v[14:17], v[118:121], v[226:229], v[14:17]
	v_mfma_f32_16x16x32_bf16 v[18:21], v[126:129], v[226:229], v[18:21]
	v_mfma_f32_16x16x32_bf16 v[6:9], v[122:125], v[202:205], v[6:9]
	v_mfma_f32_16x16x32_bf16 v[152:155], v[126:129], v[184:187], v[156:159]
	v_mfma_f32_16x16x32_bf16 v[156:159], v[118:121], v[206:209], v[160:163]
	v_mfma_f32_16x16x32_bf16 v[160:163], v[126:129], v[206:209], v[164:167]
	v_mfma_f32_16x16x32_bf16 v[164:167], v[118:121], v[218:221], v[168:171]
	v_mfma_f32_16x16x32_bf16 v[168:171], v[126:129], v[218:221], v[172:175]
	v_mfma_f32_16x16x32_bf16 v[14:17], v[122:125], v[230:233], v[14:17]
	v_mfma_f32_16x16x32_bf16 v[18:21], v[134:137], v[230:233], v[18:21]
	v_mfma_f32_16x16x32_bf16 v[152:155], v[134:137], v[202:205], v[152:155]
	v_mfma_f32_16x16x32_bf16 v[156:159], v[122:125], v[214:217], v[156:159]
	v_mfma_f32_16x16x32_bf16 v[160:163], v[134:137], v[214:217], v[160:163]
	v_mfma_f32_16x16x32_bf16 v[164:167], v[122:125], v[222:225], v[164:167]
	v_mfma_f32_16x16x32_bf16 v[168:171], v[134:137], v[222:225], v[168:171]
	v_mfma_f32_16x16x32_bf16 v[22:25], v[138:141], v[184:187], v[22:25]
	v_mfma_f32_16x16x32_bf16 v[34:37], v[176:179], v[184:187], v[34:37]
	v_mfma_f32_16x16x32_bf16 v[38:41], v[138:141], v[206:209], v[38:41]
	v_mfma_f32_16x16x32_bf16 v[66:69], v[176:179], v[206:209], v[66:69]
	v_mfma_f32_16x16x32_bf16 v[110:113], v[138:141], v[218:221], v[110:113]
	v_mfma_f32_16x16x32_bf16 v[114:117], v[176:179], v[218:221], v[114:117]
	v_mfma_f32_16x16x32_bf16 v[26:29], v[138:141], v[226:229], v[26:29]
	v_mfma_f32_16x16x32_bf16 v[30:33], v[176:179], v[226:229], v[30:33]
	v_mfma_f32_16x16x32_bf16 v[22:25], v[142:145], v[202:205], v[22:25]
	v_mfma_f32_16x16x32_bf16 v[34:37], v[180:183], v[202:205], v[34:37]
	v_mfma_f32_16x16x32_bf16 v[38:41], v[142:145], v[214:217], v[38:41]
	v_mfma_f32_16x16x32_bf16 v[66:69], v[180:183], v[214:217], v[66:69]
	v_mfma_f32_16x16x32_bf16 v[110:113], v[142:145], v[222:225], v[110:113]
	v_mfma_f32_16x16x32_bf16 v[114:117], v[180:183], v[222:225], v[114:117]
	v_mfma_f32_16x16x32_bf16 v[26:29], v[142:145], v[230:233], v[26:29]
	v_mfma_f32_16x16x32_bf16 v[30:33], v[180:183], v[230:233], v[30:33]
	s_setprio 0
	s_barrier
; #define PG8_STAGE(bufoff, gbase, voff) do { _Pragma("unroll") for (int _i = 0; _i < 2; ++_i) \
;         __builtin_amdgcn_global_load_lds((const unsigned*)((const char*)(gbase) + (voff)[_i]), (LAS unsigned*)(lds + (bufoff) + ldsw + _i * 8192), 16, 0, 0); } while (0)
; #define PG8_LDA(dst, b, h) do { _Pragma("unroll") for (int m = 0; m < 4; ++m) _Pragma("unroll") for (int k = 0; k < 2; ++k) dst[m][k] = *(const LAS bf16x8*)(lds + PG8_SA(b, h) + aoff + m * 2048 + k * 1024); } while (0)
; #define PG8_LDB(dst, b, h) do { _Pragma("unroll") for (int n = 0; n < 2; ++n) _Pragma("unroll") for (int k = 0; k < 2; ++k) dst[n][k] = *(const LAS bf16x8*)(lds + PG8_SB(b, h) + boff + n * 2048 + k * 1024); } while (0)
; #define PG8_MMA(ai, bj, At, Bt) do { __builtin_amdgcn_s_setprio(1); _Pragma("unroll") for (int m = 0; m < 4; ++m) _Pragma("unroll") for (int n = 0; n < 2; ++n) _Pragma("unroll") for (int k = 0; k < 2; ++k) \
;         acc[ai][bj][m][n] = __builtin_amdgcn_mfma_f32_16x16x32_bf16(Bt[n][k], At[m][k], acc[ai][bj][m][n], 0, 0, 0); __builtin_amdgcn_s_setprio(0); } while (0)
; #define PG8_WAIT_V(n) asm volatile("s_waitcnt vmcnt(" #n ")" ::: "memory")
; #define PG8_WAIT_L(n) asm volatile("s_waitcnt lgkmcnt(" #n ")" ::: "memory")
; template <class Epi, class Sched>
; __device__ __forceinline__ void gemm_phase(LAS unsigned char* lds, const int tid, const char* Abase, const int K, const Sched& S, const Epi& E) {
;     ...
;             const char* a2 = last ? Abase : Abase + (size_t)(t + 2) * kstep; const char* b2 = last ? nB : cB + (size_t)(t + 2) * kstep;
;             const char* a3 = a2 + kstep; const char* b3 = b2 + kstep;
;             unsigned w2[2][2];
;             if (last) { const u32x4 q = *vslot; w2[0][0] = q.x; w2[0][1] = q.y; w2[1][0] = q.z; w2[1][1] = q.w; }
;             else { w2[0][0] = vc[0][0]; w2[0][1] = vc[0][1]; w2[1][0] = vc[1][0]; w2[1][1] = vc[1][1]; }
;             PG8_LDB(B0, 0, 0); PG8_LDB(B1, 0, 1); PG8_SCHED; PG8_LDA(At, 0, 0); PG8_STAGE(PG8_SA(1, 1), a1, vc[1]);
;             PG8_WAIT_V(8); PG8_WAIT_L(0); PG8_BAR; PG8_MMA(0, 0, At, B0); PG8_MMA(0, 1, At, B1); PG8_BAR; PG8_SCHED;
;             PG8_LDA(At, 0, 1); PG8_STAGE(PG8_SB(0, 0), b2, voffB); PG8_STAGE(PG8_SB(0, 1), b2 + hstep, voffB); PG8_STAGE(PG8_SA(0, 0), a2, w2[0]);
;             PG8_WAIT_V(8); PG8_WAIT_L(0); PG8_BAR; PG8_MMA(1, 0, At, B0); PG8_MMA(1, 1, At, B1); PG8_BAR; PG8_SCHED;
	ds_read_b128 v[134:137], v250
	ds_read_b128 v[118:121], v0
	ds_read_b128 v[122:125], v0 offset:1024
	ds_read_b128 v[126:129], v0 offset:2048
	ds_read_b128 v[138:141], v0 offset:3072
	ds_read_b128 v[142:145], v10
	ds_read_b128 v[172:175], v10 offset:1024
	ds_read_b128 v[176:179], v10 offset:2048
	ds_read_b128 v[180:183], v10 offset:3072
	s_mov_b32 m0, s7
	ds_read_b128 v[184:187], v150
	ds_read_b128 v[202:205], v150 offset:1024
	ds_read_b128 v[206:209], v150 offset:2048
	ds_read_b128 v[214:217], v150 offset:3072
	ds_read_b128 v[218:221], v150 offset:4096
	ds_read_b128 v[222:225], v150 offset:5120
	ds_read_b128 v[226:229], v150 offset:6144
	ds_read_b128 v[230:233], v150 offset:7168
	global_load_lds_dwordx4 v4, s[42:43]
	s_mov_b32 m0, s12
	s_nop 0
	global_load_lds_dwordx4 v5, s[42:43]
	s_waitcnt vmcnt(8)
	s_waitcnt lgkmcnt(0)
	s_barrier
	s_setprio 1
	s_waitcnt lgkmcnt(0)
	v_mfma_f32_16x16x32_bf16 v[2:5], v[118:121], v[184:187], v[70:73]
	v_mfma_f32_16x16x32_bf16 v[70:73], v[126:129], v[184:187], v[74:77]
	v_mfma_f32_16x16x32_bf16 v[74:77], v[118:121], v[206:209], v[78:81]
	v_mfma_f32_16x16x32_bf16 v[78:81], v[126:129], v[206:209], v[82:85]
	v_mfma_f32_16x16x32_bf16 v[82:85], v[118:121], v[218:221], v[86:89]
	v_mfma_f32_16x16x32_bf16 v[86:89], v[126:129], v[218:221], v[90:93]
	v_mfma_f32_16x16x32_bf16 v[90:93], v[118:121], v[226:229], v[94:97]
	v_mfma_f32_16x16x32_bf16 v[234:237], v[122:125], v[230:233], v[90:93]
	v_mfma_f32_16x16x32_bf16 v[90:93], v[126:129], v[226:229], v[98:101]
	v_mfma_f32_16x16x32_bf16 v[2:5], v[122:125], v[202:205], v[2:5]
	v_mfma_f32_16x16x32_bf16 v[70:73], v[138:141], v[202:205], v[70:73]
	v_mfma_f32_16x16x32_bf16 v[74:77], v[122:125], v[214:217], v[74:77]
	v_mfma_f32_16x16x32_bf16 v[78:81], v[138:141], v[214:217], v[78:81]
	v_mfma_f32_16x16x32_bf16 v[82:85], v[122:125], v[222:225], v[82:85]
	v_mfma_f32_16x16x32_bf16 v[86:89], v[138:141], v[222:225], v[86:89]
	v_mfma_f32_16x16x32_bf16 v[98:101], v[138:141], v[230:233], v[90:93]
	v_mfma_f32_16x16x32_bf16 v[90:93], v[142:145], v[184:187], v[102:105]
	v_mfma_f32_16x16x32_bf16 v[42:45], v[176:179], v[184:187], v[42:45]
	v_mfma_f32_16x16x32_bf16 v[46:49], v[176:179], v[206:209], v[46:49]
	v_mfma_f32_16x16x32_bf16 v[50:53], v[142:145], v[218:221], v[50:53]
	v_mfma_f32_16x16x32_bf16 v[54:57], v[176:179], v[218:221], v[54:57]
	v_mfma_f32_16x16x32_bf16 v[58:61], v[142:145], v[226:229], v[58:61]
	v_mfma_f32_16x16x32_bf16 v[62:65], v[176:179], v[226:229], v[62:65]
	v_mfma_f32_16x16x32_bf16 v[102:105], v[172:175], v[202:205], v[90:93]
	v_mfma_f32_16x16x32_bf16 v[42:45], v[180:183], v[202:205], v[42:45]
	v_mfma_f32_16x16x32_bf16 v[90:93], v[142:145], v[206:209], v[106:109]
	v_mfma_f32_16x16x32_bf16 v[46:49], v[180:183], v[214:217], v[46:49]
	v_mfma_f32_16x16x32_bf16 v[50:53], v[172:175], v[222:225], v[50:53]
	v_mfma_f32_16x16x32_bf16 v[54:57], v[180:183], v[222:225], v[54:57]
	v_mfma_f32_16x16x32_bf16 v[58:61], v[172:175], v[230:233], v[58:61]
	v_mfma_f32_16x16x32_bf16 v[62:65], v[180:183], v[230:233], v[62:65]
	v_mfma_f32_16x16x32_bf16 v[184:187], v[172:175], v[214:217], v[90:93]
	s_setprio 0
	s_barrier
	s_mov_b32 m0, s65
	v_lshl_add_u64 v[146:147], s[46:47], 0, v[130:131]
	s_add_u32 s12, s46, 0x18000
	ds_read_b128 v[90:93], v150 offset:16384
	ds_read_b128 v[94:97], v150 offset:17408
	ds_read_b128 v[106:109], v150 offset:18432
	ds_read_b128 v[202:205], v150 offset:19456
	ds_read_b128 v[206:209], v150 offset:20480
	ds_read_b128 v[214:217], v150 offset:21504
	ds_read_b128 v[218:221], v150 offset:22528
	ds_read_b128 v[222:225], v150 offset:23552
	global_load_lds_dwordx4 v[146:147], off
	v_lshl_add_u64 v[190:191], s[46:47], 0, v[132:133]
	s_mov_b32 m0, s13
	s_addc_u32 s13, s47, 0
	global_load_lds_dwordx4 v[190:191], off
	v_lshl_add_u64 v[192:193], s[12:13], 0, v[130:131]
	s_mov_b32 m0, s48
	s_nop 0
	global_load_lds_dwordx4 v[192:193], off
	v_lshl_add_u64 v[192:193], s[12:13], 0, v[132:133]
	s_mov_b32 m0, s49
	s_nop 0
	global_load_lds_dwordx4 v[192:193], off
	s_mov_b32 m0, s51
	s_nop 0
	global_load_lds_dwordx4 v134, s[18:19]
	s_mov_b32 m0, s52
	s_nop 0
	global_load_lds_dwordx4 v135, s[18:19]
	s_waitcnt vmcnt(8)
	s_waitcnt lgkmcnt(0)
	s_barrier
	s_setprio 1
	s_waitcnt lgkmcnt(0)
	v_mfma_f32_16x16x32_bf16 v[6:9], v[118:121], v[90:93], v[6:9]
	v_mfma_f32_16x16x32_bf16 v[14:17], v[118:121], v[218:221], v[14:17]
	v_mfma_f32_16x16x32_bf16 v[18:21], v[126:129], v[218:221], v[18:21]
	v_mfma_f32_16x16x32_bf16 v[6:9], v[122:125], v[94:97], v[6:9]
	v_mfma_f32_16x16x32_bf16 v[152:155], v[126:129], v[90:93], v[152:155]
	v_mfma_f32_16x16x32_bf16 v[156:159], v[118:121], v[106:109], v[156:159]
	v_mfma_f32_16x16x32_bf16 v[160:163], v[126:129], v[106:109], v[160:163]
	v_mfma_f32_16x16x32_bf16 v[164:167], v[118:121], v[206:209], v[164:167]
	v_mfma_f32_16x16x32_bf16 v[168:171], v[126:129], v[206:209], v[168:171]
	v_mfma_f32_16x16x32_bf16 v[14:17], v[122:125], v[222:225], v[14:17]
	v_mfma_f32_16x16x32_bf16 v[18:21], v[138:141], v[222:225], v[18:21]
	v_mfma_f32_16x16x32_bf16 v[152:155], v[138:141], v[94:97], v[152:155]
	v_mfma_f32_16x16x32_bf16 v[156:159], v[122:125], v[202:205], v[156:159]
	v_mfma_f32_16x16x32_bf16 v[160:163], v[138:141], v[202:205], v[160:163]
	v_mfma_f32_16x16x32_bf16 v[164:167], v[122:125], v[214:217], v[164:167]
	v_mfma_f32_16x16x32_bf16 v[168:171], v[138:141], v[214:217], v[168:171]
	v_mfma_f32_16x16x32_bf16 v[66:69], v[176:179], v[106:109], v[66:69]
	v_mfma_f32_16x16x32_bf16 v[22:25], v[142:145], v[90:93], v[22:25]
	v_mfma_f32_16x16x32_bf16 v[34:37], v[176:179], v[90:93], v[34:37]
	v_mfma_f32_16x16x32_bf16 v[38:41], v[142:145], v[106:109], v[38:41]
	v_mfma_f32_16x16x32_bf16 v[138:141], v[180:183], v[202:205], v[66:69]
	v_mfma_f32_16x16x32_bf16 v[66:69], v[142:145], v[206:209], v[110:113]
	v_mfma_f32_16x16x32_bf16 v[26:29], v[142:145], v[218:221], v[26:29]
	v_mfma_f32_16x16x32_bf16 v[22:25], v[172:175], v[94:97], v[22:25]
	v_mfma_f32_16x16x32_bf16 v[34:37], v[180:183], v[94:97], v[34:37]
	v_mfma_f32_16x16x32_bf16 v[38:41], v[172:175], v[202:205], v[38:41]
	v_mfma_f32_16x16x32_bf16 v[202:205], v[172:175], v[214:217], v[66:69]
	v_mfma_f32_16x16x32_bf16 v[66:69], v[176:179], v[206:209], v[114:117]
	v_mfma_f32_16x16x32_bf16 v[142:145], v[172:175], v[222:225], v[26:29]
	v_mfma_f32_16x16x32_bf16 v[26:29], v[176:179], v[218:221], v[30:33]
	v_mfma_f32_16x16x32_bf16 v[206:209], v[180:183], v[214:217], v[66:69]
	v_mfma_f32_16x16x32_bf16 v[172:175], v[180:183], v[222:225], v[26:29]
	s_setprio 0
	s_barrier
; #define PG8_STAGE(bufoff, gbase, voff) do { _Pragma("unroll") for (int _i = 0; _i < 2; ++_i) \
;         __builtin_amdgcn_global_load_lds((const unsigned*)((const char*)(gbase) + (voff)[_i]), (LAS unsigned*)(lds + (bufoff) + ldsw + _i * 8192), 16, 0, 0); } while (0)
; #define PG8_LDA(dst, b, h) do { _Pragma("unroll") for (int m = 0; m < 4; ++m) _Pragma("unroll") for (int k = 0; k < 2; ++k) dst[m][k] = *(const LAS bf16x8*)(lds + PG8_SA(b, h) + aoff + m * 2048 + k * 1024); } while (0)
; #define PG8_LDB(dst, b, h) do { _Pragma("unroll") for (int n = 0; n < 2; ++n) _Pragma("unroll") for (int k = 0; k < 2; ++k) dst[n][k] = *(const LAS bf16x8*)(lds + PG8_SB(b, h) + boff + n * 2048 + k * 1024); } while (0)
; #define PG8_MMA(ai, bj, At, Bt) do { __builtin_amdgcn_s_setprio(1); _Pragma("unroll") for (int m = 0; m < 4; ++m) _Pragma("unroll") for (int n = 0; n < 2; ++n) _Pragma("unroll") for (int k = 0; k < 2; ++k) \
;         acc[ai][bj][m][n] = __builtin_amdgcn_mfma_f32_16x16x32_bf16(Bt[n][k], At[m][k], acc[ai][bj][m][n], 0, 0, 0); __builtin_amdgcn_s_setprio(0); } while (0)
; #define PG8_WAIT_V(n) asm volatile("s_waitcnt vmcnt(" #n ")" ::: "memory")
; #define PG8_WAIT_L(n) asm volatile("s_waitcnt lgkmcnt(" #n ")" ::: "memory")
; #define PG8_BAR __builtin_amdgcn_s_barrier()
; #define PG8_SCHED __builtin_amdgcn_sched_barrier(0)
; template <class Epi, class Sched>
; __device__ __forceinline__ void gemm_phase(LAS unsigned char* lds, const int tid, const char* Abase, const int K, const Sched& S, const Epi& E) {
;     ...
;             PG8_LDB(B0, 1, 0); PG8_LDB(B1, 1, 1); PG8_SCHED; PG8_LDA(At, 1, 0); PG8_STAGE(PG8_SA(0, 1), a2, w2[1]);
;             PG8_WAIT_V(8); PG8_WAIT_L(0); PG8_BAR; PG8_MMA(0, 0, At, B0); PG8_MMA(0, 1, At, B1); PG8_BAR; PG8_SCHED;
;             PG8_LDA(At, 1, 1); PG8_STAGE(PG8_SB(1, 0), b3, voffB); PG8_STAGE(PG8_SB(1, 1), b3 + hstep, voffB); PG8_STAGE(PG8_SA(1, 0), a3, w2[0]);
;             PG8_WAIT_V(8); PG8_WAIT_L(0); PG8_BAR; PG8_MMA(1, 0, At, B0); PG8_MMA(1, 1, At, B1); PG8_BAR; PG8_SCHED;
;         }
;         if (wr == 0) PG8_BAR;
	ds_read_b128 v[176:179], v11
	ds_read_b128 v[180:183], v11 offset:1024
	ds_read_b128 v[214:217], v11 offset:2048
	ds_read_b128 v[218:221], v11 offset:3072
	ds_read_b128 v[222:225], v12
	ds_read_b128 v[226:229], v12 offset:1024
	ds_read_b128 v[230:233], v12 offset:2048
	ds_read_b128 v[238:241], v12 offset:3072
	s_mov_b32 m0, s53
	ds_read_b128 v[10:13], v150 offset:32768
	ds_read_b128 v[26:29], v150 offset:33792
	ds_read_b128 v[30:33], v150 offset:34816
	ds_read_b128 v[66:69], v150 offset:35840
	ds_read_b128 v[242:245], v150 offset:36864
	ds_read_b128 v[246:249], v150 offset:37888
	ds_read_b128 v[194:197], v150 offset:38912
	ds_read_b128 v[198:201], v150 offset:39936
	global_load_lds_dwordx4 v136, s[18:19]
	s_mov_b32 m0, s54
	s_nop 0
	global_load_lds_dwordx4 v137, s[18:19]
	s_waitcnt vmcnt(8)
	s_waitcnt lgkmcnt(0)
	s_barrier
	s_setprio 1
	s_waitcnt lgkmcnt(0)
	v_mfma_f32_16x16x32_bf16 v[2:5], v[176:179], v[10:13], v[2:5]
	v_mfma_f32_16x16x32_bf16 v[126:129], v[180:183], v[26:29], v[2:5]
	v_mfma_f32_16x16x32_bf16 v[2:5], v[214:217], v[10:13], v[70:73]
	v_mfma_f32_16x16x32_bf16 v[122:125], v[218:221], v[26:29], v[2:5]
	v_mfma_f32_16x16x32_bf16 v[2:5], v[176:179], v[30:33], v[74:77]
	v_mfma_f32_16x16x32_bf16 v[110:113], v[180:183], v[66:69], v[2:5]
	v_mfma_f32_16x16x32_bf16 v[2:5], v[214:217], v[30:33], v[78:81]
	v_mfma_f32_16x16x32_bf16 v[106:109], v[218:221], v[66:69], v[2:5]
	v_mfma_f32_16x16x32_bf16 v[2:5], v[176:179], v[242:245], v[82:85]
	v_mfma_f32_16x16x32_bf16 v[94:97], v[180:183], v[246:249], v[2:5]
	v_mfma_f32_16x16x32_bf16 v[2:5], v[214:217], v[242:245], v[86:89]
	v_mfma_f32_16x16x32_bf16 v[90:93], v[218:221], v[246:249], v[2:5]
	v_mfma_f32_16x16x32_bf16 v[2:5], v[176:179], v[194:197], v[234:237]
	v_mfma_f32_16x16x32_bf16 v[78:81], v[180:183], v[198:201], v[2:5]
	v_mfma_f32_16x16x32_bf16 v[2:5], v[214:217], v[194:197], v[98:101]
	v_mfma_f32_16x16x32_bf16 v[74:77], v[218:221], v[198:201], v[2:5]
	v_mfma_f32_16x16x32_bf16 v[2:5], v[222:225], v[10:13], v[102:105]
	v_mfma_f32_16x16x32_bf16 v[118:121], v[226:229], v[26:29], v[2:5]
	v_mfma_f32_16x16x32_bf16 v[2:5], v[230:233], v[10:13], v[42:45]
	v_mfma_f32_16x16x32_bf16 v[114:117], v[238:241], v[26:29], v[2:5]
	v_mfma_f32_16x16x32_bf16 v[2:5], v[222:225], v[30:33], v[184:187]
	v_mfma_f32_16x16x32_bf16 v[102:105], v[226:229], v[66:69], v[2:5]
	v_mfma_f32_16x16x32_bf16 v[2:5], v[230:233], v[30:33], v[46:49]
	v_mfma_f32_16x16x32_bf16 v[98:101], v[238:241], v[66:69], v[2:5]
	v_mfma_f32_16x16x32_bf16 v[2:5], v[222:225], v[242:245], v[50:53]
	v_mfma_f32_16x16x32_bf16 v[86:89], v[226:229], v[246:249], v[2:5]
	v_mfma_f32_16x16x32_bf16 v[2:5], v[230:233], v[242:245], v[54:57]
	v_mfma_f32_16x16x32_bf16 v[82:85], v[238:241], v[246:249], v[2:5]
	v_mfma_f32_16x16x32_bf16 v[2:5], v[222:225], v[194:197], v[58:61]
	v_mfma_f32_16x16x32_bf16 v[70:73], v[226:229], v[198:201], v[2:5]
	v_mfma_f32_16x16x32_bf16 v[2:5], v[230:233], v[194:197], v[62:65]
	v_mfma_f32_16x16x32_bf16 v[66:69], v[238:241], v[198:201], v[2:5]
	s_setprio 0
	s_barrier
	s_mov_b32 m0, s67
	v_lshl_add_u64 v[10:11], v[146:147], 0, s[24:25]
	s_add_u32 s12, s46, 0x18080
	s_nop 1
	ds_read_b128 v[2:5], v150 offset:49152
	ds_read_b128 v[50:53], v150 offset:50176
	ds_read_b128 v[184:187], v150 offset:51200
	ds_read_b128 v[194:197], v150 offset:52224
	ds_read_b128 v[198:201], v150 offset:53248
	ds_read_b128 v[234:237], v150 offset:54272
	ds_read_b128 v[242:245], v150 offset:55296
	ds_read_b128 v[246:249], v150 offset:56320
	global_load_lds_dwordx4 v[10:11], off
	v_lshl_add_u64 v[10:11], v[190:191], 0, s[24:25]
	s_mov_b32 m0, s63
	s_addc_u32 s13, s47, 0
	global_load_lds_dwordx4 v[10:11], off
	v_lshl_add_u64 v[10:11], s[12:13], 0, v[130:131]
	s_mov_b32 m0, s64
	s_nop 0
	global_load_lds_dwordx4 v[10:11], off
	v_lshl_add_u64 v[10:11], s[12:13], 0, v[132:133]
	s_mov_b32 m0, s66
	s_nop 0
	global_load_lds_dwordx4 v[10:11], off
	s_mov_b32 m0, s58
	s_nop 0
	global_load_lds_dwordx4 v134, s[30:31]
	s_mov_b32 m0, s59
	s_nop 0
	global_load_lds_dwordx4 v135, s[30:31]
	s_waitcnt vmcnt(8)
	s_waitcnt lgkmcnt(0)
	s_barrier
	s_setprio 1
	s_waitcnt lgkmcnt(0)
	v_mfma_f32_16x16x32_bf16 v[6:9], v[176:179], v[2:5], v[6:9]
	v_mfma_f32_16x16x32_bf16 v[62:65], v[180:183], v[50:53], v[6:9]
	v_mfma_f32_16x16x32_bf16 v[6:9], v[214:217], v[2:5], v[152:155]
	v_mfma_f32_16x16x32_bf16 v[58:61], v[218:221], v[50:53], v[6:9]
	v_mfma_f32_16x16x32_bf16 v[6:9], v[176:179], v[184:187], v[156:159]
	v_mfma_f32_16x16x32_bf16 v[46:49], v[180:183], v[194:197], v[6:9]
	v_mfma_f32_16x16x32_bf16 v[6:9], v[214:217], v[184:187], v[160:163]
	v_mfma_f32_16x16x32_bf16 v[42:45], v[218:221], v[194:197], v[6:9]
	v_mfma_f32_16x16x32_bf16 v[6:9], v[176:179], v[198:201], v[164:167]
	v_mfma_f32_16x16x32_bf16 v[30:33], v[180:183], v[234:237], v[6:9]
	v_mfma_f32_16x16x32_bf16 v[6:9], v[214:217], v[198:201], v[168:171]
	v_mfma_f32_16x16x32_bf16 v[26:29], v[218:221], v[234:237], v[6:9]
	v_mfma_f32_16x16x32_bf16 v[6:9], v[176:179], v[242:245], v[14:17]
	v_mfma_f32_16x16x32_bf16 v[14:17], v[180:183], v[246:249], v[6:9]
	v_mfma_f32_16x16x32_bf16 v[6:9], v[214:217], v[242:245], v[18:21]
	v_mfma_f32_16x16x32_bf16 v[10:13], v[218:221], v[246:249], v[6:9]
	v_mfma_f32_16x16x32_bf16 v[6:9], v[222:225], v[2:5], v[22:25]
	v_mfma_f32_16x16x32_bf16 v[2:5], v[230:233], v[2:5], v[34:37]
	v_mfma_f32_16x16x32_bf16 v[54:57], v[226:229], v[50:53], v[6:9]
	v_mfma_f32_16x16x32_bf16 v[50:53], v[238:241], v[50:53], v[2:5]
	v_mfma_f32_16x16x32_bf16 v[2:5], v[222:225], v[184:187], v[38:41]
	v_mfma_f32_16x16x32_bf16 v[38:41], v[226:229], v[194:197], v[2:5]
	v_mfma_f32_16x16x32_bf16 v[2:5], v[230:233], v[184:187], v[138:141]
	v_mfma_f32_16x16x32_bf16 v[34:37], v[238:241], v[194:197], v[2:5]
	v_mfma_f32_16x16x32_bf16 v[2:5], v[222:225], v[198:201], v[202:205]
	v_mfma_f32_16x16x32_bf16 v[22:25], v[226:229], v[234:237], v[2:5]
	v_mfma_f32_16x16x32_bf16 v[2:5], v[230:233], v[198:201], v[206:209]
	v_mfma_f32_16x16x32_bf16 v[18:21], v[238:241], v[234:237], v[2:5]
	v_mfma_f32_16x16x32_bf16 v[2:5], v[222:225], v[242:245], v[142:145]
	v_mfma_f32_16x16x32_bf16 v[6:9], v[226:229], v[246:249], v[2:5]
	v_mfma_f32_16x16x32_bf16 v[2:5], v[230:233], v[242:245], v[172:175]
	v_mfma_f32_16x16x32_bf16 v[2:5], v[238:241], v[246:249], v[2:5]
	s_setprio 0
	s_barrier
	s_andn2_b64 vcc, exec, s[34:35]
	s_cbranch_vccnz .LBB0_656
	s_barrier

; #define PG8_STAGE(bufoff, gbase, voff) do { _Pragma("unroll") for (int _i = 0; _i < 2; ++_i) \
;         __builtin_amdgcn_global_load_lds((const unsigned*)((const char*)(gbase) + (voff)[_i]), (LAS unsigned*)(lds + (bufoff) + ldsw + _i * 8192), 16, 0, 0); } while (0)
; #define PG8_LDA(dst, b, h) do { _Pragma("unroll") for (int m = 0; m < 4; ++m) _Pragma("unroll") for (int k = 0; k < 2; ++k) dst[m][k] = *(const LAS bf16x8*)(lds + PG8_SA(b, h) + aoff + m * 2048 + k * 1024); } while (0)
; #define PG8_LDB(dst, b, h) do { _Pragma("unroll") for (int n = 0; n < 2; ++n) _Pragma("unroll") for (int k = 0; k < 2; ++k) dst[n][k] = *(const LAS bf16x8*)(lds + PG8_SB(b, h) + boff + n * 2048 + k * 1024); } while (0)
; #define PG8_WAIT_V(n) asm volatile("s_waitcnt vmcnt(" #n ")" ::: "memory")
; template <class Epi, class Sched>
; __device__ __forceinline__ void gemm_phase(LAS unsigned char* lds, const int tid, const char* Abase, const int K, const Sched& S, const Epi& E) {
;     ...
;           if (has_next) { PG8_AOFFS(vn, nxt); nB = S.b_tile(nxt); *vslot = (u32x4){vn[0][0], vn[0][1], vn[1][0], vn[1][1]}; }
;           else *vslot = (u32x4){vc[0][0], vc[0][1], vc[1][0], vc[1][1]}; }
;         for (int t = 0; t < nt; t += 2) {
;             if constexpr (Epi::MID) { if (t == (nt >> 1)) E.mid(acc, ui, wr, fr, lds); }
;             const bool last = (t == nt - 2);
;             const char* a1 = Abase + (size_t)(t + 1) * kstep;
;             const char* a2 = last ? Abase : Abase + (size_t)(t + 2) * kstep; const char* b2 = last ? nB : cB + (size_t)(t + 2) * kstep;
;             const char* a3 = a2 + kstep; const char* b3 = b2 + kstep;
;             unsigned w2[2][2];
;             if (last) { const u32x4 q = *vslot; w2[0][0] = q.x; w2[0][1] = q.y; w2[1][0] = q.z; w2[1][1] = q.w; }
;             else { w2[0][0] = vc[0][0]; w2[0][1] = vc[0][1]; w2[1][0] = vc[1][0]; w2[1][1] = vc[1][1]; }
;             PG8_LDB(B0, 0, 0); PG8_LDB(B1, 0, 1); PG8_SCHED; PG8_LDA(At, 0, 0); PG8_STAGE(PG8_SA(1, 1), a1, vc[1]);
;             PG8_WAIT_V(8); PG8_WAIT_L(0); PG8_BAR; PG8_MMA(0, 0, At, B0); PG8_MMA(0, 1, At, B1); PG8_BAR; PG8_SCHED;
;             PG8_LDA(At, 0, 1); PG8_STAGE(PG8_SB(0, 0), b2, voffB); PG8_STAGE(PG8_SB(0, 1), b2 + hstep, voffB); PG8_STAGE(PG8_SA(0, 0), a2, w2[0]);
;             PG8_WAIT_V(8); PG8_WAIT_L(0); PG8_BAR; PG8_MMA(1, 0, At, B0); PG8_MMA(1, 1, At, B1); PG8_BAR; PG8_SCHED;
.LBB0_711:
	s_add_i32 s53, 0, 0x10000
	s_add_i32 s50, 0, 0x14000
	ds_write_b128 v136, v[6:9]
	v_add_u32_e32 v0, s53, v137
	v_add_u32_e32 v139, s50, v137
	ds_read_b128 v[6:9], v0
	ds_read_b128 v[10:13], v0 offset:1024
	ds_read_b128 v[14:17], v0 offset:2048
	ds_read_b128 v[18:21], v0 offset:3072
	ds_read_b128 v[22:25], v139
	ds_read_b128 v[26:29], v139 offset:1024
	ds_read_b128 v[30:33], v139 offset:2048
	ds_read_b128 v[34:37], v139 offset:3072
	s_add_i32 s35, s7, 0xc000
	s_mov_b32 m0, s35
	s_add_i32 s48, s7, 0xe000
	ds_read_b128 v[38:41], v138
	ds_read_b128 v[42:45], v138 offset:1024
	ds_read_b128 v[46:49], v138 offset:2048
	ds_read_b128 v[50:53], v138 offset:3072
	ds_read_b128 v[54:57], v138 offset:4096
	ds_read_b128 v[58:61], v138 offset:5120
	ds_read_b128 v[62:65], v138 offset:6144
	ds_read_b128 v[66:69], v138 offset:7168
	global_load_lds_dwordx4 v4, s[20:21]
	s_mov_b32 m0, s48
	s_nop 0
	global_load_lds_dwordx4 v5, s[20:21]
	s_waitcnt vmcnt(8)
	s_waitcnt lgkmcnt(0)
	s_barrier
	s_setprio 1
	s_waitcnt lgkmcnt(0)
	v_mfma_f32_16x16x32_bf16 v[70:73], v[6:9], v[38:41], 0
	v_mfma_f32_16x16x32_bf16 v[74:77], v[14:17], v[38:41], 0
	v_mfma_f32_16x16x32_bf16 v[78:81], v[6:9], v[46:49], 0
	v_mfma_f32_16x16x32_bf16 v[82:85], v[14:17], v[46:49], 0
	v_mfma_f32_16x16x32_bf16 v[86:89], v[6:9], v[54:57], 0
	v_mfma_f32_16x16x32_bf16 v[90:93], v[14:17], v[54:57], 0
	v_mfma_f32_16x16x32_bf16 v[94:97], v[6:9], v[62:65], 0
	v_mfma_f32_16x16x32_bf16 v[98:101], v[14:17], v[62:65], 0
	v_mfma_f32_16x16x32_bf16 v[70:73], v[10:13], v[42:45], v[70:73]
	v_mfma_f32_16x16x32_bf16 v[74:77], v[18:21], v[42:45], v[74:77]
	v_mfma_f32_16x16x32_bf16 v[78:81], v[10:13], v[50:53], v[78:81]
	v_mfma_f32_16x16x32_bf16 v[82:85], v[18:21], v[50:53], v[82:85]
	v_mfma_f32_16x16x32_bf16 v[86:89], v[10:13], v[58:61], v[86:89]
	v_mfma_f32_16x16x32_bf16 v[90:93], v[18:21], v[58:61], v[90:93]
	v_mfma_f32_16x16x32_bf16 v[94:97], v[10:13], v[66:69], v[94:97]
	v_mfma_f32_16x16x32_bf16 v[98:101], v[18:21], v[66:69], v[98:101]
	v_mfma_f32_16x16x32_bf16 v[102:105], v[22:25], v[38:41], 0
	v_mfma_f32_16x16x32_bf16 v[38:41], v[30:33], v[38:41], 0
	v_mfma_f32_16x16x32_bf16 v[102:105], v[26:29], v[42:45], v[102:105]
	v_mfma_f32_16x16x32_bf16 v[38:41], v[34:37], v[42:45], v[38:41]
	v_mfma_f32_16x16x32_bf16 v[42:45], v[22:25], v[46:49], 0
	v_mfma_f32_16x16x32_bf16 v[46:49], v[30:33], v[46:49], 0
	v_mfma_f32_16x16x32_bf16 v[42:45], v[26:29], v[50:53], v[42:45]
	v_mfma_f32_16x16x32_bf16 v[46:49], v[34:37], v[50:53], v[46:49]
	v_mfma_f32_16x16x32_bf16 v[50:53], v[22:25], v[54:57], 0
	v_mfma_f32_16x16x32_bf16 v[54:57], v[30:33], v[54:57], 0
	v_mfma_f32_16x16x32_bf16 v[50:53], v[26:29], v[58:61], v[50:53]
	v_mfma_f32_16x16x32_bf16 v[54:57], v[34:37], v[58:61], v[54:57]
	v_mfma_f32_16x16x32_bf16 v[58:61], v[22:25], v[62:65], 0
	v_mfma_f32_16x16x32_bf16 v[62:65], v[30:33], v[62:65], 0
	v_mfma_f32_16x16x32_bf16 v[58:61], v[26:29], v[66:69], v[58:61]
	v_mfma_f32_16x16x32_bf16 v[62:65], v[34:37], v[66:69], v[62:65]
	s_setprio 0
	s_barrier
	v_lshl_add_u64 v[134:135], s[36:37], 0, v[130:131]
	s_mov_b64 s[54:55], 0x100
	s_add_i32 s53, s53, s6
	v_lshl_add_u64 v[144:145], v[134:135], 0, s[54:55]
	s_mov_b32 m0, s53
	v_lshl_add_u64 v[190:191], s[36:37], 0, v[132:133]
	s_add_i32 s49, s53, 0x2000
	ds_read_b128 v[66:69], v138 offset:16384
	ds_read_b128 v[106:109], v138 offset:17408
	ds_read_b128 v[110:113], v138 offset:18432
	ds_read_b128 v[114:117], v138 offset:19456
	ds_read_b128 v[118:121], v138 offset:20480
	ds_read_b128 v[122:125], v138 offset:21504
	ds_read_b128 v[126:129], v138 offset:22528
	ds_read_b128 v[140:143], v138 offset:23552
	global_load_lds_dwordx4 v[144:145], off
	v_lshl_add_u64 v[144:145], v[190:191], 0, s[54:55]
	s_add_u32 s54, s36, 0x10100
	s_mov_b32 m0, s49
	s_addc_u32 s55, s37, 0
	s_add_i32 s50, s50, s6
	global_load_lds_dwordx4 v[144:145], off
	v_lshl_add_u64 v[144:145], s[54:55], 0, v[130:131]
	s_mov_b32 m0, s50
	s_add_i32 s51, s50, 0x2000
	global_load_lds_dwordx4 v[144:145], off
	v_lshl_add_u64 v[144:145], s[54:55], 0, v[132:133]
	s_mov_b32 m0, s51
	s_nop 0
	global_load_lds_dwordx4 v[144:145], off
	s_mov_b32 m0, s7
	s_nop 0
	global_load_lds_dwordx4 v2, s[26:27]
	s_mov_b32 m0, s33
	s_nop 0
	global_load_lds_dwordx4 v3, s[26:27]
	s_waitcnt vmcnt(8)
	s_waitcnt lgkmcnt(0)
	s_barrier
	s_setprio 1
	s_waitcnt lgkmcnt(0)
	v_mfma_f32_16x16x32_bf16 v[144:147], v[6:9], v[66:69], 0
	v_mfma_f32_16x16x32_bf16 v[152:155], v[6:9], v[110:113], 0
	v_mfma_f32_16x16x32_bf16 v[160:163], v[6:9], v[118:121], 0
	v_mfma_f32_16x16x32_bf16 v[6:9], v[6:9], v[126:129], 0
	v_mfma_f32_16x16x32_bf16 v[144:147], v[10:13], v[106:109], v[144:147]
	v_mfma_f32_16x16x32_bf16 v[152:155], v[10:13], v[114:117], v[152:155]
	v_mfma_f32_16x16x32_bf16 v[160:163], v[10:13], v[122:125], v[160:163]
	v_mfma_f32_16x16x32_bf16 v[6:9], v[10:13], v[140:143], v[6:9]
	v_mfma_f32_16x16x32_bf16 v[10:13], v[14:17], v[126:129], 0
	v_mfma_f32_16x16x32_bf16 v[148:151], v[14:17], v[66:69], 0
	v_mfma_f32_16x16x32_bf16 v[156:159], v[14:17], v[110:113], 0
	v_mfma_f32_16x16x32_bf16 v[164:167], v[14:17], v[118:121], 0
	v_mfma_f32_16x16x32_bf16 v[10:13], v[18:21], v[140:143], v[10:13]
	v_mfma_f32_16x16x32_bf16 v[148:151], v[18:21], v[106:109], v[148:151]
	v_mfma_f32_16x16x32_bf16 v[156:159], v[18:21], v[114:117], v[156:159]
	v_mfma_f32_16x16x32_bf16 v[164:167], v[18:21], v[122:125], v[164:167]
	v_mfma_f32_16x16x32_bf16 v[14:17], v[22:25], v[66:69], 0
	v_mfma_f32_16x16x32_bf16 v[18:21], v[30:33], v[66:69], 0
	v_mfma_f32_16x16x32_bf16 v[14:17], v[26:29], v[106:109], v[14:17]
	v_mfma_f32_16x16x32_bf16 v[18:21], v[34:37], v[106:109], v[18:21]
	v_mfma_f32_16x16x32_bf16 v[66:69], v[22:25], v[110:113], 0
	v_mfma_f32_16x16x32_bf16 v[106:109], v[30:33], v[110:113], 0
	v_mfma_f32_16x16x32_bf16 v[110:113], v[22:25], v[118:121], 0
	v_mfma_f32_16x16x32_bf16 v[22:25], v[22:25], v[126:129], 0
	v_mfma_f32_16x16x32_bf16 v[66:69], v[26:29], v[114:117], v[66:69]
	v_mfma_f32_16x16x32_bf16 v[106:109], v[34:37], v[114:117], v[106:109]
	v_mfma_f32_16x16x32_bf16 v[110:113], v[26:29], v[122:125], v[110:113]
	v_mfma_f32_16x16x32_bf16 v[114:117], v[30:33], v[118:121], 0
	v_mfma_f32_16x16x32_bf16 v[22:25], v[26:29], v[140:143], v[22:25]
	v_mfma_f32_16x16x32_bf16 v[26:29], v[30:33], v[126:129], 0
	v_mfma_f32_16x16x32_bf16 v[114:117], v[34:37], v[122:125], v[114:117]
	v_mfma_f32_16x16x32_bf16 v[26:29], v[34:37], v[140:143], v[26:29]
	s_setprio 0
	s_barrier
; #define PG8_STAGE(bufoff, gbase, voff) do { _Pragma("unroll") for (int _i = 0; _i < 2; ++_i) \
;         __builtin_amdgcn_global_load_lds((const unsigned*)((const char*)(gbase) + (voff)[_i]), (LAS unsigned*)(lds + (bufoff) + ldsw + _i * 8192), 16, 0, 0); } while (0)
; #define PG8_LDA(dst, b, h) do { _Pragma("unroll") for (int m = 0; m < 4; ++m) _Pragma("unroll") for (int k = 0; k < 2; ++k) dst[m][k] = *(const LAS bf16x8*)(lds + PG8_SA(b, h) + aoff + m * 2048 + k * 1024); } while (0)
; #define PG8_LDB(dst, b, h) do { _Pragma("unroll") for (int n = 0; n < 2; ++n) _Pragma("unroll") for (int k = 0; k < 2; ++k) dst[n][k] = *(const LAS bf16x8*)(lds + PG8_SB(b, h) + boff + n * 2048 + k * 1024); } while (0)
; #define PG8_MMA(ai, bj, At, Bt) do { __builtin_amdgcn_s_setprio(1); _Pragma("unroll") for (int m = 0; m < 4; ++m) _Pragma("unroll") for (int n = 0; n < 2; ++n) _Pragma("unroll") for (int k = 0; k < 2; ++k) \
;         acc[ai][bj][m][n] = __builtin_amdgcn_mfma_f32_16x16x32_bf16(Bt[n][k], At[m][k], acc[ai][bj][m][n], 0, 0, 0); __builtin_amdgcn_s_setprio(0); } while (0)
; #define PG8_WAIT_V(n) asm volatile("s_waitcnt vmcnt(" #n ")" ::: "memory")
; #define PG8_WAIT_L(n) asm volatile("s_waitcnt lgkmcnt(" #n ")" ::: "memory")
; #define PG8_BAR __builtin_amdgcn_s_barrier()
; #define PG8_SCHED __builtin_amdgcn_sched_barrier(0)
; template <class Epi, class Sched>
; __device__ __forceinline__ void gemm_phase(LAS unsigned char* lds, const int tid, const char* Abase, const int K, const Sched& S, const Epi& E) {
;     ...
;             PG8_LDB(B0, 1, 0); PG8_LDB(B1, 1, 1); PG8_SCHED; PG8_LDA(At, 1, 0); PG8_STAGE(PG8_SA(0, 1), a2, w2[1]);
;             PG8_WAIT_V(8); PG8_WAIT_L(0); PG8_BAR; PG8_MMA(0, 0, At, B0); PG8_MMA(0, 1, At, B1); PG8_BAR; PG8_SCHED;
;             PG8_LDA(At, 1, 1); PG8_STAGE(PG8_SB(1, 0), b3, voffB); PG8_STAGE(PG8_SB(1, 1), b3 + hstep, voffB); PG8_STAGE(PG8_SA(1, 0), a3, w2[0]);
;             PG8_WAIT_V(8); PG8_WAIT_L(0); PG8_BAR; PG8_MMA(1, 0, At, B0); PG8_MMA(1, 1, At, B1); PG8_BAR; PG8_SCHED;
	s_add_i32 s54, 0, 0x18000
	s_add_i32 s55, 0, 0x1c000
	v_add_u32_e32 v189, s54, v137
	v_add_u32_e32 v192, s55, v137
	ds_read_b128 v[30:33], v189
	ds_read_b128 v[34:37], v189 offset:1024
	ds_read_b128 v[118:121], v189 offset:2048
	ds_read_b128 v[122:125], v189 offset:3072
	ds_read_b128 v[126:129], v192
	ds_read_b128 v[140:143], v192 offset:1024
	ds_read_b128 v[168:171], v192 offset:2048
	ds_read_b128 v[172:175], v192 offset:3072
	s_mov_b32 m0, s38
	ds_read_b128 v[176:179], v138 offset:32768
	ds_read_b128 v[180:183], v138 offset:33792
	ds_read_b128 v[184:187], v138 offset:34816
	ds_read_b128 v[194:197], v138 offset:35840
	ds_read_b128 v[198:201], v138 offset:36864
	ds_read_b128 v[202:205], v138 offset:37888
	ds_read_b128 v[206:209], v138 offset:38912
	ds_read_b128 v[214:217], v138 offset:39936
	global_load_lds_dwordx4 v4, s[26:27]
	s_mov_b32 m0, s39
	s_nop 0
	global_load_lds_dwordx4 v5, s[26:27]
	s_waitcnt vmcnt(8)
	s_waitcnt lgkmcnt(0)
	s_barrier
	s_setprio 1
	s_waitcnt lgkmcnt(0)
	v_mfma_f32_16x16x32_bf16 v[70:73], v[30:33], v[176:179], v[70:73]
	v_mfma_f32_16x16x32_bf16 v[74:77], v[118:121], v[176:179], v[74:77]
	v_mfma_f32_16x16x32_bf16 v[78:81], v[30:33], v[184:187], v[78:81]
	v_mfma_f32_16x16x32_bf16 v[82:85], v[118:121], v[184:187], v[82:85]
	v_mfma_f32_16x16x32_bf16 v[86:89], v[30:33], v[198:201], v[86:89]
	v_mfma_f32_16x16x32_bf16 v[90:93], v[118:121], v[198:201], v[90:93]
	v_mfma_f32_16x16x32_bf16 v[94:97], v[30:33], v[206:209], v[94:97]
	v_mfma_f32_16x16x32_bf16 v[98:101], v[118:121], v[206:209], v[98:101]
	v_mfma_f32_16x16x32_bf16 v[70:73], v[34:37], v[180:183], v[70:73]
	v_mfma_f32_16x16x32_bf16 v[74:77], v[122:125], v[180:183], v[74:77]
	v_mfma_f32_16x16x32_bf16 v[78:81], v[34:37], v[194:197], v[78:81]
	v_mfma_f32_16x16x32_bf16 v[82:85], v[122:125], v[194:197], v[82:85]
	v_mfma_f32_16x16x32_bf16 v[86:89], v[34:37], v[202:205], v[86:89]
	v_mfma_f32_16x16x32_bf16 v[90:93], v[122:125], v[202:205], v[90:93]
	v_mfma_f32_16x16x32_bf16 v[94:97], v[34:37], v[214:217], v[94:97]
	v_mfma_f32_16x16x32_bf16 v[98:101], v[122:125], v[214:217], v[98:101]
	v_mfma_f32_16x16x32_bf16 v[102:105], v[126:129], v[176:179], v[102:105]
	v_mfma_f32_16x16x32_bf16 v[38:41], v[168:171], v[176:179], v[38:41]
	v_mfma_f32_16x16x32_bf16 v[42:45], v[126:129], v[184:187], v[42:45]
	v_mfma_f32_16x16x32_bf16 v[46:49], v[168:171], v[184:187], v[46:49]
	v_mfma_f32_16x16x32_bf16 v[50:53], v[126:129], v[198:201], v[50:53]
	v_mfma_f32_16x16x32_bf16 v[54:57], v[168:171], v[198:201], v[54:57]
	v_mfma_f32_16x16x32_bf16 v[58:61], v[126:129], v[206:209], v[58:61]
	v_mfma_f32_16x16x32_bf16 v[62:65], v[168:171], v[206:209], v[62:65]
	v_mfma_f32_16x16x32_bf16 v[102:105], v[140:143], v[180:183], v[102:105]
	v_mfma_f32_16x16x32_bf16 v[38:41], v[172:175], v[180:183], v[38:41]
	v_mfma_f32_16x16x32_bf16 v[42:45], v[140:143], v[194:197], v[42:45]
	v_mfma_f32_16x16x32_bf16 v[46:49], v[172:175], v[194:197], v[46:49]
	v_mfma_f32_16x16x32_bf16 v[50:53], v[140:143], v[202:205], v[50:53]
	v_mfma_f32_16x16x32_bf16 v[54:57], v[172:175], v[202:205], v[54:57]
	v_mfma_f32_16x16x32_bf16 v[58:61], v[140:143], v[214:217], v[58:61]
	v_mfma_f32_16x16x32_bf16 v[62:65], v[172:175], v[214:217], v[62:65]
	s_setprio 0
	s_barrier
	s_mov_b64 s[56:57], 0x180
	s_add_i32 s54, s54, s6
	v_lshl_add_u64 v[134:135], v[134:135], 0, s[56:57]
	s_mov_b32 m0, s54
	s_add_i32 s52, s54, 0x2000
	ds_read_b128 v[176:179], v138 offset:49152
	ds_read_b128 v[180:183], v138 offset:50176
	ds_read_b128 v[184:187], v138 offset:51200
	ds_read_b128 v[194:197], v138 offset:52224
	ds_read_b128 v[198:201], v138 offset:53248
	ds_read_b128 v[202:205], v138 offset:54272
	ds_read_b128 v[206:209], v138 offset:55296
	ds_read_b128 v[214:217], v138 offset:56320
	global_load_lds_dwordx4 v[134:135], off
	v_lshl_add_u64 v[134:135], v[190:191], 0, s[56:57]
	s_add_u32 s56, s36, 0x10180
	s_mov_b32 m0, s52
	s_addc_u32 s57, s37, 0
	s_add_i32 s36, s55, s6
	global_load_lds_dwordx4 v[134:135], off
	v_lshl_add_u64 v[134:135], s[56:57], 0, v[130:131]
	s_mov_b32 m0, s36
	s_add_i32 s37, s36, 0x2000
	global_load_lds_dwordx4 v[134:135], off
	v_lshl_add_u64 v[134:135], s[56:57], 0, v[132:133]
	s_mov_b32 m0, s37
	s_nop 0
	global_load_lds_dwordx4 v[134:135], off
	s_mov_b32 m0, s42
	s_nop 0
	global_load_lds_dwordx4 v2, s[28:29]
	s_mov_b32 m0, s43
	s_nop 0
	global_load_lds_dwordx4 v3, s[28:29]
	s_waitcnt vmcnt(8)
	s_waitcnt lgkmcnt(0)
	s_barrier
	s_setprio 1
	s_waitcnt lgkmcnt(0)
	v_mfma_f32_16x16x32_bf16 v[6:9], v[30:33], v[206:209], v[6:9]
	v_mfma_f32_16x16x32_bf16 v[10:13], v[118:121], v[206:209], v[10:13]
	v_mfma_f32_16x16x32_bf16 v[144:147], v[30:33], v[176:179], v[144:147]
	v_mfma_f32_16x16x32_bf16 v[148:151], v[118:121], v[176:179], v[148:151]
	v_mfma_f32_16x16x32_bf16 v[152:155], v[30:33], v[184:187], v[152:155]
	v_mfma_f32_16x16x32_bf16 v[156:159], v[118:121], v[184:187], v[156:159]
	v_mfma_f32_16x16x32_bf16 v[160:163], v[30:33], v[198:201], v[160:163]
	v_mfma_f32_16x16x32_bf16 v[164:167], v[118:121], v[198:201], v[164:167]
	v_mfma_f32_16x16x32_bf16 v[6:9], v[34:37], v[214:217], v[6:9]
	v_mfma_f32_16x16x32_bf16 v[10:13], v[122:125], v[214:217], v[10:13]
	v_mfma_f32_16x16x32_bf16 v[144:147], v[34:37], v[180:183], v[144:147]
	v_mfma_f32_16x16x32_bf16 v[148:151], v[122:125], v[180:183], v[148:151]
	v_mfma_f32_16x16x32_bf16 v[152:155], v[34:37], v[194:197], v[152:155]
	v_mfma_f32_16x16x32_bf16 v[156:159], v[122:125], v[194:197], v[156:159]
	v_mfma_f32_16x16x32_bf16 v[160:163], v[34:37], v[202:205], v[160:163]
	v_mfma_f32_16x16x32_bf16 v[164:167], v[122:125], v[202:205], v[164:167]
	v_mfma_f32_16x16x32_bf16 v[14:17], v[126:129], v[176:179], v[14:17]
	v_mfma_f32_16x16x32_bf16 v[18:21], v[168:171], v[176:179], v[18:21]
	v_mfma_f32_16x16x32_bf16 v[30:33], v[126:129], v[184:187], v[66:69]
	v_mfma_f32_16x16x32_bf16 v[34:37], v[168:171], v[184:187], v[106:109]
	v_mfma_f32_16x16x32_bf16 v[66:69], v[126:129], v[198:201], v[110:113]
	v_mfma_f32_16x16x32_bf16 v[106:109], v[168:171], v[198:201], v[114:117]
	v_mfma_f32_16x16x32_bf16 v[22:25], v[126:129], v[206:209], v[22:25]
	v_mfma_f32_16x16x32_bf16 v[26:29], v[168:171], v[206:209], v[26:29]
	v_mfma_f32_16x16x32_bf16 v[14:17], v[140:143], v[180:183], v[14:17]
	v_mfma_f32_16x16x32_bf16 v[18:21], v[172:175], v[180:183], v[18:21]
	v_mfma_f32_16x16x32_bf16 v[30:33], v[140:143], v[194:197], v[30:33]
	v_mfma_f32_16x16x32_bf16 v[34:37], v[172:175], v[194:197], v[34:37]
	v_mfma_f32_16x16x32_bf16 v[66:69], v[140:143], v[202:205], v[66:69]
	v_mfma_f32_16x16x32_bf16 v[106:109], v[172:175], v[202:205], v[106:109]
	v_mfma_f32_16x16x32_bf16 v[22:25], v[140:143], v[214:217], v[22:25]
	v_mfma_f32_16x16x32_bf16 v[26:29], v[172:175], v[214:217], v[26:29]
	s_setprio 0
	s_barrier
; #define PG8_STAGE(bufoff, gbase, voff) do { _Pragma("unroll") for (int _i = 0; _i < 2; ++_i) \
;         __builtin_amdgcn_global_load_lds((const unsigned*)((const char*)(gbase) + (voff)[_i]), (LAS unsigned*)(lds + (bufoff) + ldsw + _i * 8192), 16, 0, 0); } while (0)
; #define PG8_LDA(dst, b, h) do { _Pragma("unroll") for (int m = 0; m < 4; ++m) _Pragma("unroll") for (int k = 0; k < 2; ++k) dst[m][k] = *(const LAS bf16x8*)(lds + PG8_SA(b, h) + aoff + m * 2048 + k * 1024); } while (0)
; #define PG8_LDB(dst, b, h) do { _Pragma("unroll") for (int n = 0; n < 2; ++n) _Pragma("unroll") for (int k = 0; k < 2; ++k) dst[n][k] = *(const LAS bf16x8*)(lds + PG8_SB(b, h) + boff + n * 2048 + k * 1024); } while (0)
; #define PG8_MMA(ai, bj, At, Bt) do { __builtin_amdgcn_s_setprio(1); _Pragma("unroll") for (int m = 0; m < 4; ++m) _Pragma("unroll") for (int n = 0; n < 2; ++n) _Pragma("unroll") for (int k = 0; k < 2; ++k) \
;         acc[ai][bj][m][n] = __builtin_amdgcn_mfma_f32_16x16x32_bf16(Bt[n][k], At[m][k], acc[ai][bj][m][n], 0, 0, 0); __builtin_amdgcn_s_setprio(0); } while (0)
; #define PG8_WAIT_V(n) asm volatile("s_waitcnt vmcnt(" #n ")" ::: "memory")
; #define PG8_WAIT_L(n) asm volatile("s_waitcnt lgkmcnt(" #n ")" ::: "memory")
; template <class Epi, class Sched>
; __device__ __forceinline__ void gemm_phase(LAS unsigned char* lds, const int tid, const char* Abase, const int K, const Sched& S, const Epi& E) {
;     ...
;             const char* a2 = last ? Abase : Abase + (size_t)(t + 2) * kstep; const char* b2 = last ? nB : cB + (size_t)(t + 2) * kstep;
;             const char* a3 = a2 + kstep; const char* b3 = b2 + kstep;
;             unsigned w2[2][2];
;             if (last) { const u32x4 q = *vslot; w2[0][0] = q.x; w2[0][1] = q.y; w2[1][0] = q.z; w2[1][1] = q.w; }
;             else { w2[0][0] = vc[0][0]; w2[0][1] = vc[0][1]; w2[1][0] = vc[1][0]; w2[1][1] = vc[1][1]; }
;             PG8_LDB(B0, 0, 0); PG8_LDB(B1, 0, 1); PG8_SCHED; PG8_LDA(At, 0, 0); PG8_STAGE(PG8_SA(1, 1), a1, vc[1]);
;             PG8_WAIT_V(8); PG8_WAIT_L(0); PG8_BAR; PG8_MMA(0, 0, At, B0); PG8_MMA(0, 1, At, B1); PG8_BAR; PG8_SCHED;
;             PG8_LDA(At, 0, 1); PG8_STAGE(PG8_SB(0, 0), b2, voffB); PG8_STAGE(PG8_SB(0, 1), b2 + hstep, voffB); PG8_STAGE(PG8_SA(0, 0), a2, w2[0]);
;             PG8_WAIT_V(8); PG8_WAIT_L(0); PG8_BAR; PG8_MMA(1, 0, At, B0); PG8_MMA(1, 1, At, B1); PG8_BAR; PG8_SCHED;
	ds_read_b128 v[140:143], v136
	ds_read_b128 v[110:113], v0
	ds_read_b128 v[114:117], v0 offset:1024
	ds_read_b128 v[118:121], v0 offset:2048
	ds_read_b128 v[122:125], v0 offset:3072
	ds_read_b128 v[126:129], v139
	ds_read_b128 v[168:171], v139 offset:1024
	ds_read_b128 v[172:175], v139 offset:2048
	ds_read_b128 v[176:179], v139 offset:3072
	s_mov_b32 m0, s35
	ds_read_b128 v[180:183], v138
	ds_read_b128 v[184:187], v138 offset:1024
	ds_read_b128 v[194:197], v138 offset:2048
	ds_read_b128 v[198:201], v138 offset:3072
	ds_read_b128 v[202:205], v138 offset:4096
	ds_read_b128 v[206:209], v138 offset:5120
	ds_read_b128 v[214:217], v138 offset:6144
	ds_read_b128 v[218:221], v138 offset:7168
	global_load_lds_dwordx4 v4, s[28:29]
	s_mov_b32 m0, s48
	s_nop 0
	global_load_lds_dwordx4 v5, s[28:29]
	s_waitcnt vmcnt(8)
	s_waitcnt lgkmcnt(0)
	s_barrier
	s_setprio 1
	s_waitcnt lgkmcnt(0)
	v_mfma_f32_16x16x32_bf16 v[2:5], v[110:113], v[180:183], v[70:73]
	v_mfma_f32_16x16x32_bf16 v[70:73], v[118:121], v[180:183], v[74:77]
	v_mfma_f32_16x16x32_bf16 v[74:77], v[110:113], v[194:197], v[78:81]
	v_mfma_f32_16x16x32_bf16 v[78:81], v[118:121], v[194:197], v[82:85]
	v_mfma_f32_16x16x32_bf16 v[82:85], v[110:113], v[202:205], v[86:89]
	v_mfma_f32_16x16x32_bf16 v[86:89], v[118:121], v[202:205], v[90:93]
	v_mfma_f32_16x16x32_bf16 v[90:93], v[110:113], v[214:217], v[94:97]
	v_mfma_f32_16x16x32_bf16 v[2:5], v[114:117], v[184:187], v[2:5]
	v_mfma_f32_16x16x32_bf16 v[70:73], v[122:125], v[184:187], v[70:73]
	v_mfma_f32_16x16x32_bf16 v[74:77], v[114:117], v[198:201], v[74:77]
	v_mfma_f32_16x16x32_bf16 v[78:81], v[122:125], v[198:201], v[78:81]
	v_mfma_f32_16x16x32_bf16 v[82:85], v[114:117], v[206:209], v[82:85]
	v_mfma_f32_16x16x32_bf16 v[86:89], v[122:125], v[206:209], v[86:89]
	v_mfma_f32_16x16x32_bf16 v[94:97], v[114:117], v[218:221], v[90:93]
	v_mfma_f32_16x16x32_bf16 v[90:93], v[118:121], v[214:217], v[98:101]
	v_mfma_f32_16x16x32_bf16 v[222:225], v[122:125], v[218:221], v[90:93]
	v_mfma_f32_16x16x32_bf16 v[50:53], v[126:129], v[202:205], v[50:53]
	v_mfma_f32_16x16x32_bf16 v[90:93], v[126:129], v[180:183], v[102:105]
	v_mfma_f32_16x16x32_bf16 v[38:41], v[172:175], v[180:183], v[38:41]
	v_mfma_f32_16x16x32_bf16 v[180:183], v[168:171], v[206:209], v[50:53]
	v_mfma_f32_16x16x32_bf16 v[50:53], v[172:175], v[202:205], v[54:57]
	v_mfma_f32_16x16x32_bf16 v[42:45], v[126:129], v[194:197], v[42:45]
	v_mfma_f32_16x16x32_bf16 v[46:49], v[172:175], v[194:197], v[46:49]
	v_mfma_f32_16x16x32_bf16 v[54:57], v[176:179], v[206:209], v[50:53]
	v_mfma_f32_16x16x32_bf16 v[50:53], v[126:129], v[214:217], v[58:61]
	v_mfma_f32_16x16x32_bf16 v[102:105], v[168:171], v[184:187], v[90:93]
	v_mfma_f32_16x16x32_bf16 v[38:41], v[176:179], v[184:187], v[38:41]
	v_mfma_f32_16x16x32_bf16 v[42:45], v[168:171], v[198:201], v[42:45]
	v_mfma_f32_16x16x32_bf16 v[46:49], v[176:179], v[198:201], v[46:49]
	v_mfma_f32_16x16x32_bf16 v[184:187], v[168:171], v[218:221], v[50:53]
	v_mfma_f32_16x16x32_bf16 v[50:53], v[172:175], v[214:217], v[62:65]
	v_mfma_f32_16x16x32_bf16 v[194:197], v[176:179], v[218:221], v[50:53]
	s_setprio 0
	s_barrier
	s_mov_b32 m0, s53
	v_lshl_add_u64 v[134:135], s[12:13], 0, v[130:131]
	s_add_u32 s48, s12, 0x10000
	s_nop 1
	ds_read_b128 v[50:53], v138 offset:16384
	ds_read_b128 v[58:61], v138 offset:17408
	ds_read_b128 v[62:65], v138 offset:18432
	ds_read_b128 v[90:93], v138 offset:19456
	ds_read_b128 v[98:101], v138 offset:20480
	ds_read_b128 v[198:201], v138 offset:21504
	ds_read_b128 v[202:205], v138 offset:22528
	ds_read_b128 v[206:209], v138 offset:23552
	global_load_lds_dwordx4 v[134:135], off
	v_lshl_add_u64 v[250:251], s[12:13], 0, v[132:133]
	s_mov_b32 m0, s49
	s_addc_u32 s49, s13, 0
	global_load_lds_dwordx4 v[250:251], off
	v_lshl_add_u64 v[190:191], s[48:49], 0, v[130:131]
	s_mov_b32 m0, s50
	s_nop 0
	global_load_lds_dwordx4 v[190:191], off
	v_lshl_add_u64 v[190:191], s[48:49], 0, v[132:133]
	s_mov_b32 m0, s51
	s_nop 0
	global_load_lds_dwordx4 v[190:191], off
	s_mov_b32 m0, s7
	s_nop 0
	global_load_lds_dwordx4 v140, s[16:17]
	s_mov_b32 m0, s33
	s_nop 0
	global_load_lds_dwordx4 v141, s[16:17]
	s_waitcnt vmcnt(8)
	s_waitcnt lgkmcnt(0)
	s_barrier
	s_setprio 1
	s_waitcnt lgkmcnt(0)
	v_mfma_f32_16x16x32_bf16 v[6:9], v[110:113], v[202:205], v[6:9]
	v_mfma_f32_16x16x32_bf16 v[144:147], v[110:113], v[50:53], v[144:147]
	v_mfma_f32_16x16x32_bf16 v[148:151], v[118:121], v[50:53], v[148:151]
	v_mfma_f32_16x16x32_bf16 v[152:155], v[110:113], v[62:65], v[152:155]
	v_mfma_f32_16x16x32_bf16 v[156:159], v[118:121], v[62:65], v[156:159]
	v_mfma_f32_16x16x32_bf16 v[160:163], v[110:113], v[98:101], v[160:163]
	v_mfma_f32_16x16x32_bf16 v[164:167], v[118:121], v[98:101], v[164:167]
	v_mfma_f32_16x16x32_bf16 v[6:9], v[114:117], v[206:209], v[6:9]
	v_mfma_f32_16x16x32_bf16 v[10:13], v[118:121], v[202:205], v[10:13]
	v_mfma_f32_16x16x32_bf16 v[144:147], v[114:117], v[58:61], v[144:147]
	v_mfma_f32_16x16x32_bf16 v[148:151], v[122:125], v[58:61], v[148:151]
	v_mfma_f32_16x16x32_bf16 v[152:155], v[114:117], v[90:93], v[152:155]
	v_mfma_f32_16x16x32_bf16 v[156:159], v[122:125], v[90:93], v[156:159]
	v_mfma_f32_16x16x32_bf16 v[160:163], v[114:117], v[198:201], v[160:163]
	v_mfma_f32_16x16x32_bf16 v[164:167], v[122:125], v[198:201], v[164:167]
	v_mfma_f32_16x16x32_bf16 v[214:217], v[122:125], v[206:209], v[10:13]
	v_mfma_f32_16x16x32_bf16 v[10:13], v[126:129], v[50:53], v[14:17]
	v_mfma_f32_16x16x32_bf16 v[14:17], v[168:171], v[58:61], v[10:13]
	v_mfma_f32_16x16x32_bf16 v[10:13], v[172:175], v[50:53], v[18:21]
	v_mfma_f32_16x16x32_bf16 v[218:221], v[176:179], v[58:61], v[10:13]
	v_mfma_f32_16x16x32_bf16 v[10:13], v[126:129], v[62:65], v[30:33]
	v_mfma_f32_16x16x32_bf16 v[30:33], v[168:171], v[90:93], v[10:13]
	v_mfma_f32_16x16x32_bf16 v[10:13], v[172:175], v[62:65], v[34:37]
	v_mfma_f32_16x16x32_bf16 v[226:229], v[176:179], v[90:93], v[10:13]
	v_mfma_f32_16x16x32_bf16 v[10:13], v[126:129], v[98:101], v[66:69]
	v_mfma_f32_16x16x32_bf16 v[230:233], v[168:171], v[198:201], v[10:13]
	v_mfma_f32_16x16x32_bf16 v[10:13], v[172:175], v[98:101], v[106:109]
	v_mfma_f32_16x16x32_bf16 v[198:201], v[176:179], v[198:201], v[10:13]
	v_mfma_f32_16x16x32_bf16 v[10:13], v[126:129], v[202:205], v[22:25]
	v_mfma_f32_16x16x32_bf16 v[168:171], v[168:171], v[206:209], v[10:13]
	v_mfma_f32_16x16x32_bf16 v[10:13], v[172:175], v[202:205], v[26:29]
	v_mfma_f32_16x16x32_bf16 v[172:175], v[176:179], v[206:209], v[10:13]
	s_setprio 0
	s_barrier
; #define PG8_STAGE(bufoff, gbase, voff) do { _Pragma("unroll") for (int _i = 0; _i < 2; ++_i) \
;         __builtin_amdgcn_global_load_lds((const unsigned*)((const char*)(gbase) + (voff)[_i]), (LAS unsigned*)(lds + (bufoff) + ldsw + _i * 8192), 16, 0, 0); } while (0)
; #define PG8_LDA(dst, b, h) do { _Pragma("unroll") for (int m = 0; m < 4; ++m) _Pragma("unroll") for (int k = 0; k < 2; ++k) dst[m][k] = *(const LAS bf16x8*)(lds + PG8_SA(b, h) + aoff + m * 2048 + k * 1024); } while (0)
; #define PG8_LDB(dst, b, h) do { _Pragma("unroll") for (int n = 0; n < 2; ++n) _Pragma("unroll") for (int k = 0; k < 2; ++k) dst[n][k] = *(const LAS bf16x8*)(lds + PG8_SB(b, h) + boff + n * 2048 + k * 1024); } while (0)
; #define PG8_MMA(ai, bj, At, Bt) do { __builtin_amdgcn_s_setprio(1); _Pragma("unroll") for (int m = 0; m < 4; ++m) _Pragma("unroll") for (int n = 0; n < 2; ++n) _Pragma("unroll") for (int k = 0; k < 2; ++k) \
;         acc[ai][bj][m][n] = __builtin_amdgcn_mfma_f32_16x16x32_bf16(Bt[n][k], At[m][k], acc[ai][bj][m][n], 0, 0, 0); __builtin_amdgcn_s_setprio(0); } while (0)
; #define PG8_WAIT_V(n) asm volatile("s_waitcnt vmcnt(" #n ")" ::: "memory")
; #define PG8_WAIT_L(n) asm volatile("s_waitcnt lgkmcnt(" #n ")" ::: "memory")
; #define PG8_BAR __builtin_amdgcn_s_barrier()
; #define PG8_SCHED __builtin_amdgcn_sched_barrier(0)
; template <class Epi, class Sched>
; __device__ __forceinline__ void gemm_phase(LAS unsigned char* lds, const int tid, const char* Abase, const int K, const Sched& S, const Epi& E) {
;     ...
;             PG8_LDB(B0, 1, 0); PG8_LDB(B1, 1, 1); PG8_SCHED; PG8_LDA(At, 1, 0); PG8_STAGE(PG8_SA(0, 1), a2, w2[1]);
;             PG8_WAIT_V(8); PG8_WAIT_L(0); PG8_BAR; PG8_MMA(0, 0, At, B0); PG8_MMA(0, 1, At, B1); PG8_BAR; PG8_SCHED;
;             PG8_LDA(At, 1, 1); PG8_STAGE(PG8_SB(1, 0), b3, voffB); PG8_STAGE(PG8_SB(1, 1), b3 + hstep, voffB); PG8_STAGE(PG8_SA(1, 0), a3, w2[0]);
;             PG8_WAIT_V(8); PG8_WAIT_L(0); PG8_BAR; PG8_MMA(1, 0, At, B0); PG8_MMA(1, 1, At, B1); PG8_BAR; PG8_SCHED;
;         }
;         if (wr == 0) PG8_BAR;
	s_nop 4
	ds_read_b128 v[10:13], v189
	ds_read_b128 v[22:25], v189 offset:1024
	ds_read_b128 v[176:179], v189 offset:2048
	ds_read_b128 v[202:205], v189 offset:3072
	ds_read_b128 v[206:209], v192
	ds_read_b128 v[234:237], v192 offset:1024
	ds_read_b128 v[238:241], v192 offset:2048
	ds_read_b128 v[242:245], v192 offset:3072
	s_mov_b32 m0, s38
	ds_read_b128 v[18:21], v138 offset:32768
	ds_read_b128 v[26:29], v138 offset:33792
	ds_read_b128 v[34:37], v138 offset:34816
	ds_read_b128 v[62:65], v138 offset:35840
	ds_read_b128 v[66:69], v138 offset:36864
	ds_read_b128 v[246:249], v138 offset:37888
	ds_read_b128 v[190:193], v138 offset:38912
	ds_read_b128 v[210:213], v138 offset:39936
	global_load_lds_dwordx4 v142, s[16:17]
	s_mov_b32 m0, s39
	s_nop 0
	global_load_lds_dwordx4 v143, s[16:17]
	s_waitcnt vmcnt(8)
	s_waitcnt lgkmcnt(0)
	s_barrier
	s_setprio 1
	s_waitcnt lgkmcnt(0)
	v_mfma_f32_16x16x32_bf16 v[2:5], v[10:13], v[18:21], v[2:5]
	v_mfma_f32_16x16x32_bf16 v[126:129], v[22:25], v[26:29], v[2:5]
	v_mfma_f32_16x16x32_bf16 v[2:5], v[176:179], v[18:21], v[70:73]
	v_mfma_f32_16x16x32_bf16 v[122:125], v[202:205], v[26:29], v[2:5]
	v_mfma_f32_16x16x32_bf16 v[2:5], v[10:13], v[34:37], v[74:77]
	v_mfma_f32_16x16x32_bf16 v[106:109], v[22:25], v[62:65], v[2:5]
	v_mfma_f32_16x16x32_bf16 v[2:5], v[176:179], v[34:37], v[78:81]
	v_mfma_f32_16x16x32_bf16 v[98:101], v[202:205], v[62:65], v[2:5]
	v_mfma_f32_16x16x32_bf16 v[2:5], v[10:13], v[66:69], v[82:85]
	v_mfma_f32_16x16x32_bf16 v[90:93], v[22:25], v[246:249], v[2:5]
	v_mfma_f32_16x16x32_bf16 v[2:5], v[176:179], v[66:69], v[86:89]
	v_mfma_f32_16x16x32_bf16 v[82:85], v[202:205], v[246:249], v[2:5]
	v_mfma_f32_16x16x32_bf16 v[2:5], v[10:13], v[190:193], v[94:97]
	v_mfma_f32_16x16x32_bf16 v[58:61], v[22:25], v[210:213], v[2:5]
	v_mfma_f32_16x16x32_bf16 v[2:5], v[176:179], v[190:193], v[222:225]
	v_mfma_f32_16x16x32_bf16 v[50:53], v[202:205], v[210:213], v[2:5]
	v_mfma_f32_16x16x32_bf16 v[2:5], v[206:209], v[18:21], v[102:105]
	v_mfma_f32_16x16x32_bf16 v[118:121], v[234:237], v[26:29], v[2:5]
	v_mfma_f32_16x16x32_bf16 v[2:5], v[238:241], v[18:21], v[38:41]
	v_mfma_f32_16x16x32_bf16 v[114:117], v[242:245], v[26:29], v[2:5]
	v_mfma_f32_16x16x32_bf16 v[2:5], v[206:209], v[34:37], v[42:45]
	v_mfma_f32_16x16x32_bf16 v[110:113], v[234:237], v[62:65], v[2:5]
	v_mfma_f32_16x16x32_bf16 v[2:5], v[238:241], v[34:37], v[46:49]
	v_mfma_f32_16x16x32_bf16 v[102:105], v[242:245], v[62:65], v[2:5]
	v_mfma_f32_16x16x32_bf16 v[2:5], v[206:209], v[66:69], v[180:183]
	v_mfma_f32_16x16x32_bf16 v[94:97], v[234:237], v[246:249], v[2:5]
	v_mfma_f32_16x16x32_bf16 v[2:5], v[238:241], v[66:69], v[54:57]
	v_mfma_f32_16x16x32_bf16 v[86:89], v[242:245], v[246:249], v[2:5]
	v_mfma_f32_16x16x32_bf16 v[2:5], v[206:209], v[190:193], v[184:187]
	v_mfma_f32_16x16x32_bf16 v[62:65], v[234:237], v[210:213], v[2:5]
	v_mfma_f32_16x16x32_bf16 v[2:5], v[238:241], v[190:193], v[194:197]
	v_mfma_f32_16x16x32_bf16 v[54:57], v[242:245], v[210:213], v[2:5]
	s_setprio 0
	s_barrier
	s_mov_b32 m0, s54
	s_nop 3
	v_lshl_add_u64 v[2:3], v[134:135], 0, s[24:25]
	s_add_u32 s48, s12, 0x10080
	ds_read_b128 v[38:41], v138 offset:49152
	ds_read_b128 v[46:49], v138 offset:50176
	ds_read_b128 v[180:183], v138 offset:51200
	ds_read_b128 v[184:187], v138 offset:52224
	ds_read_b128 v[190:193], v138 offset:53248
	ds_read_b128 v[194:197], v138 offset:54272
	ds_read_b128 v[210:213], v138 offset:55296
	ds_read_b128 v[222:225], v138 offset:56320
	global_load_lds_dwordx4 v[2:3], off
	v_lshl_add_u64 v[2:3], v[250:251], 0, s[24:25]
	s_mov_b32 m0, s52
	s_addc_u32 s49, s13, 0
	global_load_lds_dwordx4 v[2:3], off
	v_lshl_add_u64 v[2:3], s[48:49], 0, v[130:131]
	s_mov_b32 m0, s36
	s_nop 0
	global_load_lds_dwordx4 v[2:3], off
	v_lshl_add_u64 v[2:3], s[48:49], 0, v[132:133]
	s_mov_b32 m0, s37
	s_nop 0
	global_load_lds_dwordx4 v[2:3], off
	s_mov_b32 m0, s42
	s_nop 0
	global_load_lds_dwordx4 v140, s[20:21]
	s_mov_b32 m0, s43
	s_nop 0
	global_load_lds_dwordx4 v141, s[20:21]
	s_waitcnt vmcnt(8)
	s_waitcnt lgkmcnt(0)
	s_barrier
	s_setprio 1
	s_waitcnt lgkmcnt(0)
	v_mfma_f32_16x16x32_bf16 v[2:5], v[10:13], v[38:41], v[144:147]
	v_mfma_f32_16x16x32_bf16 v[74:77], v[22:25], v[46:49], v[2:5]
	v_mfma_f32_16x16x32_bf16 v[2:5], v[176:179], v[38:41], v[148:151]
	v_mfma_f32_16x16x32_bf16 v[66:69], v[202:205], v[46:49], v[2:5]
	v_mfma_f32_16x16x32_bf16 v[2:5], v[10:13], v[180:183], v[152:155]
	v_mfma_f32_16x16x32_bf16 v[42:45], v[22:25], v[184:187], v[2:5]
	v_mfma_f32_16x16x32_bf16 v[2:5], v[176:179], v[180:183], v[156:159]
	v_mfma_f32_16x16x32_bf16 v[34:37], v[202:205], v[184:187], v[2:5]
	v_mfma_f32_16x16x32_bf16 v[2:5], v[10:13], v[190:193], v[160:163]
	v_mfma_f32_16x16x32_bf16 v[26:29], v[22:25], v[194:197], v[2:5]
	v_mfma_f32_16x16x32_bf16 v[2:5], v[176:179], v[190:193], v[164:167]
	v_mfma_f32_16x16x32_bf16 v[18:21], v[202:205], v[194:197], v[2:5]
	v_mfma_f32_16x16x32_bf16 v[2:5], v[10:13], v[210:213], v[6:9]
	v_mfma_f32_16x16x32_bf16 v[10:13], v[22:25], v[222:225], v[2:5]
	v_mfma_f32_16x16x32_bf16 v[2:5], v[176:179], v[210:213], v[214:217]
	v_mfma_f32_16x16x32_bf16 v[2:5], v[202:205], v[222:225], v[2:5]
	v_mfma_f32_16x16x32_bf16 v[6:9], v[206:209], v[38:41], v[14:17]
	v_mfma_f32_16x16x32_bf16 v[78:81], v[234:237], v[46:49], v[6:9]
	v_mfma_f32_16x16x32_bf16 v[6:9], v[238:241], v[38:41], v[218:221]
	v_mfma_f32_16x16x32_bf16 v[70:73], v[242:245], v[46:49], v[6:9]
	v_mfma_f32_16x16x32_bf16 v[6:9], v[206:209], v[180:183], v[30:33]
	v_mfma_f32_16x16x32_bf16 v[46:49], v[234:237], v[184:187], v[6:9]
	v_mfma_f32_16x16x32_bf16 v[6:9], v[238:241], v[180:183], v[226:229]
	v_mfma_f32_16x16x32_bf16 v[38:41], v[242:245], v[184:187], v[6:9]
	v_mfma_f32_16x16x32_bf16 v[6:9], v[206:209], v[190:193], v[230:233]
	v_mfma_f32_16x16x32_bf16 v[30:33], v[234:237], v[194:197], v[6:9]
	v_mfma_f32_16x16x32_bf16 v[6:9], v[238:241], v[190:193], v[198:201]
	v_mfma_f32_16x16x32_bf16 v[22:25], v[242:245], v[194:197], v[6:9]
	v_mfma_f32_16x16x32_bf16 v[6:9], v[206:209], v[210:213], v[168:171]
	v_mfma_f32_16x16x32_bf16 v[14:17], v[234:237], v[222:225], v[6:9]
	v_mfma_f32_16x16x32_bf16 v[6:9], v[238:241], v[210:213], v[172:175]
	v_mfma_f32_16x16x32_bf16 v[6:9], v[242:245], v[222:225], v[6:9]
	s_setprio 0
	s_barrier
	s_andn2_b64 vcc, exec, s[22:23]
	s_cbranch_vccnz .LBB0_713
	s_barrier

; #define PG8_STAGE(bufoff, gbase, voff) do { _Pragma("unroll") for (int _i = 0; _i < 2; ++_i) \
;         __builtin_amdgcn_global_load_lds((const unsigned*)((const char*)(gbase) + (voff)[_i]), (LAS unsigned*)(lds + (bufoff) + ldsw + _i * 8192), 16, 0, 0); } while (0)
; #define PG8_LDA(dst, b, h) do { _Pragma("unroll") for (int m = 0; m < 4; ++m) _Pragma("unroll") for (int k = 0; k < 2; ++k) dst[m][k] = *(const LAS bf16x8*)(lds + PG8_SA(b, h) + aoff + m * 2048 + k * 1024); } while (0)
; #define PG8_LDB(dst, b, h) do { _Pragma("unroll") for (int n = 0; n < 2; ++n) _Pragma("unroll") for (int k = 0; k < 2; ++k) dst[n][k] = *(const LAS bf16x8*)(lds + PG8_SB(b, h) + boff + n * 2048 + k * 1024); } while (0)
; #define PG8_MMA(ai, bj, At, Bt) do { __builtin_amdgcn_s_setprio(1); _Pragma("unroll") for (int m = 0; m < 4; ++m) _Pragma("unroll") for (int n = 0; n < 2; ++n) _Pragma("unroll") for (int k = 0; k < 2; ++k) \
;         acc[ai][bj][m][n] = __builtin_amdgcn_mfma_f32_16x16x32_bf16(Bt[n][k], At[m][k], acc[ai][bj][m][n], 0, 0, 0); __builtin_amdgcn_s_setprio(0); } while (0)
; #define PG8_BAR __builtin_amdgcn_s_barrier()
; template <class Epi, class Sched>
; __device__ __forceinline__ void gemm_phase(LAS unsigned char* lds, const int tid, const char* Abase, const int K, const Sched& S, const Epi& E) {
;     ...
;             const bool last = (t == nt - 2);
;             const char* a1 = Abase + (size_t)(t + 1) * kstep;
;             const char* a2 = last ? Abase : Abase + (size_t)(t + 2) * kstep; const char* b2 = last ? nB : cB + (size_t)(t + 2) * kstep;
;             const char* a3 = a2 + kstep; const char* b3 = b2 + kstep;
;             unsigned w2[2][2];
;             if (last) { const u32x4 q = *vslot; w2[0][0] = q.x; w2[0][1] = q.y; w2[1][0] = q.z; w2[1][1] = q.w; }
;             else { w2[0][0] = vc[0][0]; w2[0][1] = vc[0][1]; w2[1][0] = vc[1][0]; w2[1][1] = vc[1][1]; }
;             PG8_LDB(B0, 0, 0); PG8_LDB(B1, 0, 1); PG8_SCHED; PG8_LDA(At, 0, 0); PG8_STAGE(PG8_SA(1, 1), a1, vc[1]);
;             PG8_WAIT_V(8); PG8_WAIT_L(0); PG8_BAR; PG8_MMA(0, 0, At, B0); PG8_MMA(0, 1, At, B1); PG8_BAR; PG8_SCHED;
;             PG8_LDA(At, 0, 1); PG8_STAGE(PG8_SB(0, 0), b2, voffB); PG8_STAGE(PG8_SB(0, 1), b2 + hstep, voffB); PG8_STAGE(PG8_SA(0, 0), a2, w2[0]);
;             PG8_WAIT_V(8); PG8_WAIT_L(0); PG8_BAR; PG8_MMA(1, 0, At, B0); PG8_MMA(1, 1, At, B1); PG8_BAR; PG8_SCHED;
.LBB0_954:
	s_add_u32 s46, s74, s14
	s_addc_u32 s47, s75, s15
	s_add_u32 s62, s46, 0x22800100
	s_addc_u32 s63, s47, 0
	s_and_b64 s[46:47], s[42:43], exec
	s_cselect_b32 s47, s19, s63
	s_cselect_b32 s46, s18, s62
	s_add_u32 s62, s39, s14
	s_addc_u32 s63, s60, s15
	s_and_b64 s[42:43], s[42:43], exec
	s_cselect_b32 s43, s41, s63
	s_cselect_b32 s42, s40, s62
	s_add_i32 s62, 0, 0x10000
	v_add_u32_e32 v145, s62, v171
	s_add_i32 s64, 0, 0x14000
	ds_read_b128 v[148:151], v145
	ds_read_b128 v[158:161], v145 offset:1024
	ds_read_b128 v[162:165], v145 offset:2048
	ds_read_b128 v[166:169], v145 offset:3072
	v_add_u32_e32 v145, s64, v171
	ds_read_b128 v[176:179], v145
	ds_read_b128 v[180:183], v145 offset:1024
	ds_read_b128 v[184:187], v145 offset:2048
	ds_read_b128 v[190:193], v145 offset:3072
	v_lshl_add_u64 v[152:153], v[138:139], 0, s[14:15]
	s_add_i32 m0, s49, 0xc000
	ds_read_b128 v[194:197], v174
	ds_read_b128 v[198:201], v174 offset:1024
	ds_read_b128 v[202:205], v174 offset:2048
	ds_read_b128 v[206:209], v174 offset:3072
	ds_read_b128 v[210:213], v174 offset:4096
	ds_read_b128 v[214:217], v174 offset:5120
	ds_read_b128 v[218:221], v174 offset:6144
	ds_read_b128 v[222:225], v174 offset:7168
	global_load_lds_dwordx4 v[152:153], off
	v_lshl_add_u64 v[152:153], v[136:137], 0, s[14:15]
	s_add_i32 m0, s49, 0xe000
	s_nop 0
	global_load_lds_dwordx4 v[152:153], off
	s_waitcnt vmcnt(8)
	s_waitcnt lgkmcnt(0)
	s_barrier
	s_setprio 1
	s_waitcnt lgkmcnt(0)
	v_mfma_f32_16x16x32_bf16 v[126:129], v[148:151], v[194:197], v[126:129]
	v_mfma_f32_16x16x32_bf16 v[122:125], v[162:165], v[194:197], v[122:125]
	v_mfma_f32_16x16x32_bf16 v[110:113], v[148:151], v[202:205], v[110:113]
	v_mfma_f32_16x16x32_bf16 v[106:109], v[162:165], v[202:205], v[106:109]
	v_mfma_f32_16x16x32_bf16 v[94:97], v[148:151], v[210:213], v[94:97]
	v_mfma_f32_16x16x32_bf16 v[90:93], v[162:165], v[210:213], v[90:93]
	v_mfma_f32_16x16x32_bf16 v[78:81], v[148:151], v[218:221], v[78:81]
	v_mfma_f32_16x16x32_bf16 v[74:77], v[162:165], v[218:221], v[74:77]
	v_mfma_f32_16x16x32_bf16 v[126:129], v[158:161], v[198:201], v[126:129]
	v_mfma_f32_16x16x32_bf16 v[122:125], v[166:169], v[198:201], v[122:125]
	v_mfma_f32_16x16x32_bf16 v[110:113], v[158:161], v[206:209], v[110:113]
	v_mfma_f32_16x16x32_bf16 v[106:109], v[166:169], v[206:209], v[106:109]
	v_mfma_f32_16x16x32_bf16 v[94:97], v[158:161], v[214:217], v[94:97]
	v_mfma_f32_16x16x32_bf16 v[90:93], v[166:169], v[214:217], v[90:93]
	v_mfma_f32_16x16x32_bf16 v[78:81], v[158:161], v[222:225], v[78:81]
	v_mfma_f32_16x16x32_bf16 v[74:77], v[166:169], v[222:225], v[74:77]
	v_mfma_f32_16x16x32_bf16 v[118:121], v[176:179], v[194:197], v[118:121]
	v_mfma_f32_16x16x32_bf16 v[114:117], v[184:187], v[194:197], v[114:117]
	v_mfma_f32_16x16x32_bf16 v[102:105], v[176:179], v[202:205], v[102:105]
	v_mfma_f32_16x16x32_bf16 v[98:101], v[184:187], v[202:205], v[98:101]
	v_mfma_f32_16x16x32_bf16 v[86:89], v[176:179], v[210:213], v[86:89]
	v_mfma_f32_16x16x32_bf16 v[82:85], v[184:187], v[210:213], v[82:85]
	v_mfma_f32_16x16x32_bf16 v[70:73], v[176:179], v[218:221], v[70:73]
	v_mfma_f32_16x16x32_bf16 v[66:69], v[184:187], v[218:221], v[66:69]
	v_mfma_f32_16x16x32_bf16 v[118:121], v[180:183], v[198:201], v[118:121]
	v_mfma_f32_16x16x32_bf16 v[114:117], v[190:193], v[198:201], v[114:117]
	v_mfma_f32_16x16x32_bf16 v[102:105], v[180:183], v[206:209], v[102:105]
	v_mfma_f32_16x16x32_bf16 v[98:101], v[190:193], v[206:209], v[98:101]
	v_mfma_f32_16x16x32_bf16 v[86:89], v[180:183], v[214:217], v[86:89]
	v_mfma_f32_16x16x32_bf16 v[82:85], v[190:193], v[214:217], v[82:85]
	v_mfma_f32_16x16x32_bf16 v[70:73], v[180:183], v[222:225], v[70:73]
	v_mfma_f32_16x16x32_bf16 v[66:69], v[190:193], v[222:225], v[66:69]
	s_setprio 0
	s_barrier
	s_add_i32 s62, s62, s48
	v_lshl_add_u64 v[152:153], s[42:43], 0, v[154:155]
	s_mov_b32 m0, s62
	ds_read_b128 v[194:197], v174 offset:16384
	ds_read_b128 v[198:201], v174 offset:17408
	ds_read_b128 v[202:205], v174 offset:18432
	ds_read_b128 v[206:209], v174 offset:19456
	ds_read_b128 v[210:213], v174 offset:20480
	ds_read_b128 v[214:217], v174 offset:21504
	ds_read_b128 v[218:221], v174 offset:22528
	ds_read_b128 v[222:225], v174 offset:23552
	global_load_lds_dwordx4 v[152:153], off
	s_add_i32 m0, s62, 0x2000
	s_add_u32 s62, s42, 0x40000
	v_lshl_add_u64 v[226:227], s[42:43], 0, v[156:157]
	s_addc_u32 s63, s43, 0
	s_add_i32 s64, s64, s48
	global_load_lds_dwordx4 v[226:227], off
	v_lshl_add_u64 v[228:229], s[62:63], 0, v[154:155]
	s_mov_b32 m0, s64
	v_mov_b32_e32 v145, v1
	global_load_lds_dwordx4 v[228:229], off
	v_lshl_add_u64 v[228:229], s[62:63], 0, v[156:157]
	s_add_i32 m0, s64, 0x2000
	s_nop 0
	global_load_lds_dwordx4 v[228:229], off
	s_mov_b32 m0, s49
	v_lshl_add_u64 v[228:229], s[46:47], 0, v[0:1]
	global_load_lds_dwordx4 v0, s[46:47]
	s_mov_b32 m0, s50
	s_nop 0
	global_load_lds_dwordx4 v144, s[46:47]
	s_waitcnt vmcnt(8)
	s_waitcnt lgkmcnt(0)
	v_lshl_add_u64 v[144:145], s[46:47], 0, v[144:145]
	s_barrier
; #define PG8_STAGE(bufoff, gbase, voff) do { _Pragma("unroll") for (int _i = 0; _i < 2; ++_i) \
;         __builtin_amdgcn_global_load_lds((const unsigned*)((const char*)(gbase) + (voff)[_i]), (LAS unsigned*)(lds + (bufoff) + ldsw + _i * 8192), 16, 0, 0); } while (0)
; #define PG8_LDA(dst, b, h) do { _Pragma("unroll") for (int m = 0; m < 4; ++m) _Pragma("unroll") for (int k = 0; k < 2; ++k) dst[m][k] = *(const LAS bf16x8*)(lds + PG8_SA(b, h) + aoff + m * 2048 + k * 1024); } while (0)
; #define PG8_LDB(dst, b, h) do { _Pragma("unroll") for (int n = 0; n < 2; ++n) _Pragma("unroll") for (int k = 0; k < 2; ++k) dst[n][k] = *(const LAS bf16x8*)(lds + PG8_SB(b, h) + boff + n * 2048 + k * 1024); } while (0)
; #define PG8_MMA(ai, bj, At, Bt) do { __builtin_amdgcn_s_setprio(1); _Pragma("unroll") for (int m = 0; m < 4; ++m) _Pragma("unroll") for (int n = 0; n < 2; ++n) _Pragma("unroll") for (int k = 0; k < 2; ++k) \
;         acc[ai][bj][m][n] = __builtin_amdgcn_mfma_f32_16x16x32_bf16(Bt[n][k], At[m][k], acc[ai][bj][m][n], 0, 0, 0); __builtin_amdgcn_s_setprio(0); } while (0)
; #define PG8_WAIT_V(n) asm volatile("s_waitcnt vmcnt(" #n ")" ::: "memory")
; #define PG8_WAIT_L(n) asm volatile("s_waitcnt lgkmcnt(" #n ")" ::: "memory")
; #define PG8_BAR __builtin_amdgcn_s_barrier()
; #define PG8_SCHED __builtin_amdgcn_sched_barrier(0)
; template <class Epi, class Sched>
; __device__ __forceinline__ void gemm_phase(LAS unsigned char* lds, const int tid, const char* Abase, const int K, const Sched& S, const Epi& E) {
;     ...
;             PG8_WAIT_V(8); PG8_WAIT_L(0); PG8_BAR; PG8_MMA(1, 0, At, B0); PG8_MMA(1, 1, At, B1); PG8_BAR; PG8_SCHED;
;             PG8_LDB(B0, 1, 0); PG8_LDB(B1, 1, 1); PG8_SCHED; PG8_LDA(At, 1, 0); PG8_STAGE(PG8_SA(0, 1), a2, w2[1]);
;             PG8_WAIT_V(8); PG8_WAIT_L(0); PG8_BAR; PG8_MMA(0, 0, At, B0); PG8_MMA(0, 1, At, B1); PG8_BAR; PG8_SCHED;
;             PG8_LDA(At, 1, 1); PG8_STAGE(PG8_SB(1, 0), b3, voffB); PG8_STAGE(PG8_SB(1, 1), b3 + hstep, voffB); PG8_STAGE(PG8_SA(1, 0), a3, w2[0]);
	s_setprio 1
	s_waitcnt lgkmcnt(0)
	v_mfma_f32_16x16x32_bf16 v[62:65], v[148:151], v[194:197], v[62:65]
	v_mfma_f32_16x16x32_bf16 v[58:61], v[162:165], v[194:197], v[58:61]
	v_mfma_f32_16x16x32_bf16 v[46:49], v[148:151], v[202:205], v[46:49]
	v_mfma_f32_16x16x32_bf16 v[42:45], v[162:165], v[202:205], v[42:45]
	v_mfma_f32_16x16x32_bf16 v[30:33], v[148:151], v[210:213], v[30:33]
	v_mfma_f32_16x16x32_bf16 v[26:29], v[162:165], v[210:213], v[26:29]
	v_mfma_f32_16x16x32_bf16 v[14:17], v[148:151], v[218:221], v[14:17]
	v_mfma_f32_16x16x32_bf16 v[10:13], v[162:165], v[218:221], v[10:13]
	v_mfma_f32_16x16x32_bf16 v[62:65], v[158:161], v[198:201], v[62:65]
	v_mfma_f32_16x16x32_bf16 v[58:61], v[166:169], v[198:201], v[58:61]
	v_mfma_f32_16x16x32_bf16 v[46:49], v[158:161], v[206:209], v[46:49]
	v_mfma_f32_16x16x32_bf16 v[42:45], v[166:169], v[206:209], v[42:45]
	v_mfma_f32_16x16x32_bf16 v[30:33], v[158:161], v[214:217], v[30:33]
	v_mfma_f32_16x16x32_bf16 v[26:29], v[166:169], v[214:217], v[26:29]
	v_mfma_f32_16x16x32_bf16 v[14:17], v[158:161], v[222:225], v[14:17]
	v_mfma_f32_16x16x32_bf16 v[10:13], v[166:169], v[222:225], v[10:13]
	v_mfma_f32_16x16x32_bf16 v[54:57], v[176:179], v[194:197], v[54:57]
	v_mfma_f32_16x16x32_bf16 v[50:53], v[184:187], v[194:197], v[50:53]
	v_mfma_f32_16x16x32_bf16 v[38:41], v[176:179], v[202:205], v[38:41]
	v_mfma_f32_16x16x32_bf16 v[34:37], v[184:187], v[202:205], v[34:37]
	v_mfma_f32_16x16x32_bf16 v[22:25], v[176:179], v[210:213], v[22:25]
	v_mfma_f32_16x16x32_bf16 v[18:21], v[184:187], v[210:213], v[18:21]
	v_mfma_f32_16x16x32_bf16 v[6:9], v[176:179], v[218:221], v[6:9]
	v_mfma_f32_16x16x32_bf16 v[2:5], v[184:187], v[218:221], v[2:5]
	v_mfma_f32_16x16x32_bf16 v[54:57], v[180:183], v[198:201], v[54:57]
	v_mfma_f32_16x16x32_bf16 v[50:53], v[190:193], v[198:201], v[50:53]
	v_mfma_f32_16x16x32_bf16 v[38:41], v[180:183], v[206:209], v[38:41]
	v_mfma_f32_16x16x32_bf16 v[34:37], v[190:193], v[206:209], v[34:37]
	v_mfma_f32_16x16x32_bf16 v[22:25], v[180:183], v[214:217], v[22:25]
	v_mfma_f32_16x16x32_bf16 v[18:21], v[190:193], v[214:217], v[18:21]
	v_mfma_f32_16x16x32_bf16 v[6:9], v[180:183], v[222:225], v[6:9]
	v_mfma_f32_16x16x32_bf16 v[2:5], v[190:193], v[222:225], v[2:5]
	s_setprio 0
	s_barrier
	s_add_i32 s62, 0, 0x18000
	v_add_u32_e32 v0, s62, v171
	s_add_i32 s63, 0, 0x1c000
	ds_read_b128 v[148:151], v0
	ds_read_b128 v[158:161], v0 offset:1024
	ds_read_b128 v[162:165], v0 offset:2048
	ds_read_b128 v[166:169], v0 offset:3072
	v_add_u32_e32 v0, s63, v171
	ds_read_b128 v[176:179], v0
	ds_read_b128 v[180:183], v0 offset:1024
	ds_read_b128 v[184:187], v0 offset:2048
	ds_read_b128 v[190:193], v0 offset:3072
	s_mov_b32 m0, s51
	v_lshl_add_u64 v[142:143], s[46:47], 0, v[142:143]
	ds_read_b128 v[194:197], v174 offset:32768
	ds_read_b128 v[198:201], v174 offset:33792
	ds_read_b128 v[202:205], v174 offset:34816
	ds_read_b128 v[206:209], v174 offset:35840
	ds_read_b128 v[210:213], v174 offset:36864
	ds_read_b128 v[214:217], v174 offset:37888
	ds_read_b128 v[218:221], v174 offset:38912
	ds_read_b128 v[222:225], v174 offset:39936
	global_load_lds_dwordx4 v[142:143], off
	v_lshl_add_u64 v[140:141], s[46:47], 0, v[140:141]
	s_mov_b32 m0, s52
	s_nop 0
	global_load_lds_dwordx4 v[140:141], off
	s_waitcnt vmcnt(8)
	s_waitcnt lgkmcnt(0)
	s_barrier
	s_setprio 1
	s_waitcnt lgkmcnt(0)
	v_mfma_f32_16x16x32_bf16 v[126:129], v[148:151], v[194:197], v[126:129]
	v_mfma_f32_16x16x32_bf16 v[122:125], v[162:165], v[194:197], v[122:125]
	v_mfma_f32_16x16x32_bf16 v[110:113], v[148:151], v[202:205], v[110:113]
	v_mfma_f32_16x16x32_bf16 v[106:109], v[162:165], v[202:205], v[106:109]
	v_mfma_f32_16x16x32_bf16 v[94:97], v[148:151], v[210:213], v[94:97]
	v_mfma_f32_16x16x32_bf16 v[90:93], v[162:165], v[210:213], v[90:93]
	v_mfma_f32_16x16x32_bf16 v[78:81], v[148:151], v[218:221], v[78:81]
	v_mfma_f32_16x16x32_bf16 v[74:77], v[162:165], v[218:221], v[74:77]
	v_mfma_f32_16x16x32_bf16 v[126:129], v[158:161], v[198:201], v[126:129]
	v_mfma_f32_16x16x32_bf16 v[122:125], v[166:169], v[198:201], v[122:125]
	v_mfma_f32_16x16x32_bf16 v[110:113], v[158:161], v[206:209], v[110:113]
	v_mfma_f32_16x16x32_bf16 v[106:109], v[166:169], v[206:209], v[106:109]
	v_mfma_f32_16x16x32_bf16 v[94:97], v[158:161], v[214:217], v[94:97]
	v_mfma_f32_16x16x32_bf16 v[90:93], v[166:169], v[214:217], v[90:93]
	v_mfma_f32_16x16x32_bf16 v[78:81], v[158:161], v[222:225], v[78:81]
	v_mfma_f32_16x16x32_bf16 v[74:77], v[166:169], v[222:225], v[74:77]
	v_mfma_f32_16x16x32_bf16 v[118:121], v[176:179], v[194:197], v[118:121]
	v_mfma_f32_16x16x32_bf16 v[114:117], v[184:187], v[194:197], v[114:117]
	v_mfma_f32_16x16x32_bf16 v[102:105], v[176:179], v[202:205], v[102:105]
	v_mfma_f32_16x16x32_bf16 v[98:101], v[184:187], v[202:205], v[98:101]
	v_mfma_f32_16x16x32_bf16 v[86:89], v[176:179], v[210:213], v[86:89]
	v_mfma_f32_16x16x32_bf16 v[82:85], v[184:187], v[210:213], v[82:85]
	v_mfma_f32_16x16x32_bf16 v[70:73], v[176:179], v[218:221], v[70:73]
	v_mfma_f32_16x16x32_bf16 v[66:69], v[184:187], v[218:221], v[66:69]
	v_mfma_f32_16x16x32_bf16 v[118:121], v[180:183], v[198:201], v[118:121]
	v_mfma_f32_16x16x32_bf16 v[114:117], v[190:193], v[198:201], v[114:117]
	v_mfma_f32_16x16x32_bf16 v[102:105], v[180:183], v[206:209], v[102:105]
	v_mfma_f32_16x16x32_bf16 v[98:101], v[190:193], v[206:209], v[98:101]
	v_mfma_f32_16x16x32_bf16 v[86:89], v[180:183], v[214:217], v[86:89]
	v_mfma_f32_16x16x32_bf16 v[82:85], v[190:193], v[214:217], v[82:85]
	v_mfma_f32_16x16x32_bf16 v[70:73], v[180:183], v[222:225], v[70:73]
	v_mfma_f32_16x16x32_bf16 v[66:69], v[190:193], v[222:225], v[66:69]
	s_setprio 0
	s_barrier
; #define PG8_STAGE(bufoff, gbase, voff) do { _Pragma("unroll") for (int _i = 0; _i < 2; ++_i) \
;         __builtin_amdgcn_global_load_lds((const unsigned*)((const char*)(gbase) + (voff)[_i]), (LAS unsigned*)(lds + (bufoff) + ldsw + _i * 8192), 16, 0, 0); } while (0)
; #define PG8_LDA(dst, b, h) do { _Pragma("unroll") for (int m = 0; m < 4; ++m) _Pragma("unroll") for (int k = 0; k < 2; ++k) dst[m][k] = *(const LAS bf16x8*)(lds + PG8_SA(b, h) + aoff + m * 2048 + k * 1024); } while (0)
; #define PG8_MMA(ai, bj, At, Bt) do { __builtin_amdgcn_s_setprio(1); _Pragma("unroll") for (int m = 0; m < 4; ++m) _Pragma("unroll") for (int n = 0; n < 2; ++n) _Pragma("unroll") for (int k = 0; k < 2; ++k) \
;         acc[ai][bj][m][n] = __builtin_amdgcn_mfma_f32_16x16x32_bf16(Bt[n][k], At[m][k], acc[ai][bj][m][n], 0, 0, 0); __builtin_amdgcn_s_setprio(0); } while (0)
; #define PG8_WAIT_V(n) asm volatile("s_waitcnt vmcnt(" #n ")" ::: "memory")
; #define PG8_WAIT_L(n) asm volatile("s_waitcnt lgkmcnt(" #n ")" ::: "memory")
; #define PG8_BAR __builtin_amdgcn_s_barrier()
; #define PG8_SCHED __builtin_amdgcn_sched_barrier(0)
; template <class Epi, class Sched>
; __device__ __forceinline__ void gemm_phase(LAS unsigned char* lds, const int tid, const char* Abase, const int K, const Sched& S, const Epi& E) {
;     ...
;             PG8_LDA(At, 1, 1); PG8_STAGE(PG8_SB(1, 0), b3, voffB); PG8_STAGE(PG8_SB(1, 1), b3 + hstep, voffB); PG8_STAGE(PG8_SA(1, 0), a3, w2[0]);
;             PG8_WAIT_V(8); PG8_WAIT_L(0); PG8_BAR; PG8_MMA(1, 0, At, B0); PG8_MMA(1, 1, At, B1); PG8_BAR; PG8_SCHED;
;         }
	s_add_i32 s46, s62, s48
	v_lshl_add_u64 v[152:153], v[152:153], 0, s[24:25]
	s_mov_b32 m0, s46
	ds_read_b128 v[140:143], v174 offset:49152
	ds_read_b128 v[194:197], v174 offset:50176
	ds_read_b128 v[198:201], v174 offset:51200
	ds_read_b128 v[202:205], v174 offset:52224
	ds_read_b128 v[206:209], v174 offset:53248
	ds_read_b128 v[210:213], v174 offset:54272
	ds_read_b128 v[214:217], v174 offset:55296
	ds_read_b128 v[218:221], v174 offset:56320
	global_load_lds_dwordx4 v[152:153], off
	s_add_i32 m0, s46, 0x2000
	s_add_u32 s42, s42, 0x40080
	v_lshl_add_u64 v[152:153], v[226:227], 0, s[24:25]
	s_addc_u32 s43, s43, 0
	s_add_i32 s46, s63, s48
	global_load_lds_dwordx4 v[152:153], off
	v_lshl_add_u64 v[152:153], s[42:43], 0, v[154:155]
	s_mov_b32 m0, s46
	v_lshl_add_u64 v[144:145], v[144:145], 0, s[24:25]
	global_load_lds_dwordx4 v[152:153], off
	v_lshl_add_u64 v[152:153], s[42:43], 0, v[156:157]
	s_add_i32 m0, s46, 0x2000
	s_nop 0
	global_load_lds_dwordx4 v[152:153], off
	v_lshl_add_u64 v[152:153], v[228:229], 0, s[24:25]
	s_mov_b32 m0, s54
	s_nop 0
	global_load_lds_dwordx4 v[152:153], off
	s_mov_b32 m0, s55
	s_nop 0
	global_load_lds_dwordx4 v[144:145], off
	s_waitcnt vmcnt(8)
	s_waitcnt lgkmcnt(0)
	s_barrier
	s_setprio 1
	s_waitcnt lgkmcnt(0)
	v_mfma_f32_16x16x32_bf16 v[62:65], v[148:151], v[140:143], v[62:65]
	v_mfma_f32_16x16x32_bf16 v[58:61], v[162:165], v[140:143], v[58:61]
	v_mfma_f32_16x16x32_bf16 v[46:49], v[148:151], v[198:201], v[46:49]
	v_mfma_f32_16x16x32_bf16 v[42:45], v[162:165], v[198:201], v[42:45]
	v_mfma_f32_16x16x32_bf16 v[30:33], v[148:151], v[206:209], v[30:33]
	v_mfma_f32_16x16x32_bf16 v[26:29], v[162:165], v[206:209], v[26:29]
	v_mfma_f32_16x16x32_bf16 v[14:17], v[148:151], v[214:217], v[14:17]
	v_mfma_f32_16x16x32_bf16 v[10:13], v[162:165], v[214:217], v[10:13]
	v_mfma_f32_16x16x32_bf16 v[62:65], v[158:161], v[194:197], v[62:65]
	v_mfma_f32_16x16x32_bf16 v[58:61], v[166:169], v[194:197], v[58:61]
	v_mfma_f32_16x16x32_bf16 v[46:49], v[158:161], v[202:205], v[46:49]
	v_mfma_f32_16x16x32_bf16 v[42:45], v[166:169], v[202:205], v[42:45]
	v_mfma_f32_16x16x32_bf16 v[30:33], v[158:161], v[210:213], v[30:33]
	v_mfma_f32_16x16x32_bf16 v[26:29], v[166:169], v[210:213], v[26:29]
	v_mfma_f32_16x16x32_bf16 v[14:17], v[158:161], v[218:221], v[14:17]
	v_mfma_f32_16x16x32_bf16 v[10:13], v[166:169], v[218:221], v[10:13]
	v_mfma_f32_16x16x32_bf16 v[54:57], v[176:179], v[140:143], v[54:57]
	v_mfma_f32_16x16x32_bf16 v[50:53], v[184:187], v[140:143], v[50:53]
	v_mfma_f32_16x16x32_bf16 v[38:41], v[176:179], v[198:201], v[38:41]
	v_mfma_f32_16x16x32_bf16 v[34:37], v[184:187], v[198:201], v[34:37]
	v_mfma_f32_16x16x32_bf16 v[22:25], v[176:179], v[206:209], v[22:25]
	v_mfma_f32_16x16x32_bf16 v[18:21], v[184:187], v[206:209], v[18:21]
	v_mfma_f32_16x16x32_bf16 v[6:9], v[176:179], v[214:217], v[6:9]
	v_mfma_f32_16x16x32_bf16 v[2:5], v[184:187], v[214:217], v[2:5]
	v_mfma_f32_16x16x32_bf16 v[54:57], v[180:183], v[194:197], v[54:57]
	v_mfma_f32_16x16x32_bf16 v[50:53], v[190:193], v[194:197], v[50:53]
	v_mfma_f32_16x16x32_bf16 v[38:41], v[180:183], v[202:205], v[38:41]
	v_mfma_f32_16x16x32_bf16 v[34:37], v[190:193], v[202:205], v[34:37]
	v_mfma_f32_16x16x32_bf16 v[22:25], v[180:183], v[210:213], v[22:25]
	v_mfma_f32_16x16x32_bf16 v[18:21], v[190:193], v[210:213], v[18:21]
	v_mfma_f32_16x16x32_bf16 v[6:9], v[180:183], v[218:221], v[6:9]
	v_mfma_f32_16x16x32_bf16 v[2:5], v[190:193], v[218:221], v[2:5]
	s_setprio 0
	s_barrier
	s_add_i32 s61, s61, 2
	s_add_u32 s14, s14, 0x100
	s_addc_u32 s15, s15, 0
	s_cmp_gt_u32 s61, 13
	s_cbranch_scc1 .LBB0_959

; #define PG8_STAGE(bufoff, gbase, voff) do { _Pragma("unroll") for (int _i = 0; _i < 2; ++_i) \
;         __builtin_amdgcn_global_load_lds((const unsigned*)((const char*)(gbase) + (voff)[_i]), (LAS unsigned*)(lds + (bufoff) + ldsw + _i * 8192), 16, 0, 0); } while (0)
; #define PG8_LDA(dst, b, h) do { _Pragma("unroll") for (int m = 0; m < 4; ++m) _Pragma("unroll") for (int k = 0; k < 2; ++k) dst[m][k] = *(const LAS bf16x8*)(lds + PG8_SA(b, h) + aoff + m * 2048 + k * 1024); } while (0)
; #define PG8_LDB(dst, b, h) do { _Pragma("unroll") for (int n = 0; n < 2; ++n) _Pragma("unroll") for (int k = 0; k < 2; ++k) dst[n][k] = *(const LAS bf16x8*)(lds + PG8_SB(b, h) + boff + n * 2048 + k * 1024); } while (0)
; #define PG8_MMA(ai, bj, At, Bt) do { __builtin_amdgcn_s_setprio(1); _Pragma("unroll") for (int m = 0; m < 4; ++m) _Pragma("unroll") for (int n = 0; n < 2; ++n) _Pragma("unroll") for (int k = 0; k < 2; ++k) \
;         acc[ai][bj][m][n] = __builtin_amdgcn_mfma_f32_16x16x32_bf16(Bt[n][k], At[m][k], acc[ai][bj][m][n], 0, 0, 0); __builtin_amdgcn_s_setprio(0); } while (0)
; #define PG8_BAR __builtin_amdgcn_s_barrier()
; template <class Epi, class Sched>
; __device__ __forceinline__ void gemm_phase(LAS unsigned char* lds, const int tid, const char* Abase, const int K, const Sched& S, const Epi& E) {
;     ...
;             const bool last = (t == nt - 2);
;             const char* a1 = Abase + (size_t)(t + 1) * kstep;
;             const char* a2 = last ? Abase : Abase + (size_t)(t + 2) * kstep; const char* b2 = last ? nB : cB + (size_t)(t + 2) * kstep;
;             const char* a3 = a2 + kstep; const char* b3 = b2 + kstep;
;             unsigned w2[2][2];
;             if (last) { const u32x4 q = *vslot; w2[0][0] = q.x; w2[0][1] = q.y; w2[1][0] = q.z; w2[1][1] = q.w; }
;             else { w2[0][0] = vc[0][0]; w2[0][1] = vc[0][1]; w2[1][0] = vc[1][0]; w2[1][1] = vc[1][1]; }
;             PG8_LDB(B0, 0, 0); PG8_LDB(B1, 0, 1); PG8_SCHED; PG8_LDA(At, 0, 0); PG8_STAGE(PG8_SA(1, 1), a1, vc[1]);
;             PG8_WAIT_V(8); PG8_WAIT_L(0); PG8_BAR; PG8_MMA(0, 0, At, B0); PG8_MMA(0, 1, At, B1); PG8_BAR; PG8_SCHED;
;             PG8_LDA(At, 0, 1); PG8_STAGE(PG8_SB(0, 0), b2, voffB); PG8_STAGE(PG8_SB(0, 1), b2 + hstep, voffB); PG8_STAGE(PG8_SA(0, 0), a2, w2[0]);
;             PG8_WAIT_V(8); PG8_WAIT_L(0); PG8_BAR; PG8_MMA(1, 0, At, B0); PG8_MMA(1, 1, At, B1); PG8_BAR; PG8_SCHED;
.LBB0_1186:
	s_add_u32 s6, s74, s40
	s_addc_u32 s7, s75, s41
	s_add_u32 s44, s6, 0xee00100
	s_addc_u32 s45, s7, 0
	s_and_b64 s[6:7], s[42:43], exec
	s_cselect_b32 s45, s19, s45
	s_cselect_b32 s44, s18, s44
	s_add_u32 s59, s31, s40
	s_addc_u32 s60, s35, s41
	s_and_b64 s[6:7], s[42:43], exec
	s_cselect_b32 s43, s39, s60
	s_cselect_b32 s42, s38, s59
	s_add_i32 s6, 0, 0x10000
	v_add_u32_e32 v151, s6, v155
	s_add_i32 s59, 0, 0x14000
	ds_read_b128 v[160:163], v151
	ds_read_b128 v[164:167], v151 offset:1024
	ds_read_b128 v[168:171], v151 offset:2048
	ds_read_b128 v[172:175], v151 offset:3072
	v_add_u32_e32 v151, s59, v155
	ds_read_b128 v[176:179], v151
	ds_read_b128 v[180:183], v151 offset:1024
	ds_read_b128 v[184:187], v151 offset:2048
	ds_read_b128 v[190:193], v151 offset:3072
	v_lshl_add_u64 v[226:227], v[144:145], 0, s[40:41]
	s_add_i32 m0, s49, 0xc000
	ds_read_b128 v[194:197], v156
	ds_read_b128 v[198:201], v156 offset:1024
	ds_read_b128 v[202:205], v156 offset:2048
	ds_read_b128 v[206:209], v156 offset:3072
	ds_read_b128 v[210:213], v156 offset:4096
	ds_read_b128 v[214:217], v156 offset:5120
	ds_read_b128 v[218:221], v156 offset:6144
	ds_read_b128 v[222:225], v156 offset:7168
	global_load_lds_dwordx4 v[226:227], off
	v_lshl_add_u64 v[226:227], v[142:143], 0, s[40:41]
	s_add_i32 m0, s49, 0xe000
	s_nop 0
	global_load_lds_dwordx4 v[226:227], off
	s_waitcnt vmcnt(8)
	s_waitcnt lgkmcnt(0)
	s_barrier
	s_setprio 1
	s_waitcnt lgkmcnt(0)
	v_mfma_f32_16x16x32_bf16 v[130:133], v[160:163], v[194:197], v[130:133]
	v_mfma_f32_16x16x32_bf16 v[126:129], v[168:171], v[194:197], v[126:129]
	v_mfma_f32_16x16x32_bf16 v[122:125], v[160:163], v[202:205], v[122:125]
	v_mfma_f32_16x16x32_bf16 v[118:121], v[168:171], v[202:205], v[118:121]
	v_mfma_f32_16x16x32_bf16 v[114:117], v[160:163], v[210:213], v[114:117]
	v_mfma_f32_16x16x32_bf16 v[110:113], v[168:171], v[210:213], v[110:113]
	v_mfma_f32_16x16x32_bf16 v[106:109], v[160:163], v[218:221], v[106:109]
	v_mfma_f32_16x16x32_bf16 v[102:105], v[168:171], v[218:221], v[102:105]
	v_mfma_f32_16x16x32_bf16 v[130:133], v[164:167], v[198:201], v[130:133]
	v_mfma_f32_16x16x32_bf16 v[126:129], v[172:175], v[198:201], v[126:129]
	v_mfma_f32_16x16x32_bf16 v[122:125], v[164:167], v[206:209], v[122:125]
	v_mfma_f32_16x16x32_bf16 v[118:121], v[172:175], v[206:209], v[118:121]
	v_mfma_f32_16x16x32_bf16 v[114:117], v[164:167], v[214:217], v[114:117]
	v_mfma_f32_16x16x32_bf16 v[110:113], v[172:175], v[214:217], v[110:113]
	v_mfma_f32_16x16x32_bf16 v[106:109], v[164:167], v[222:225], v[106:109]
	v_mfma_f32_16x16x32_bf16 v[102:105], v[172:175], v[222:225], v[102:105]
	v_mfma_f32_16x16x32_bf16 v[98:101], v[176:179], v[194:197], v[98:101]
	v_mfma_f32_16x16x32_bf16 v[94:97], v[184:187], v[194:197], v[94:97]
	v_mfma_f32_16x16x32_bf16 v[90:93], v[176:179], v[202:205], v[90:93]
	v_mfma_f32_16x16x32_bf16 v[86:89], v[184:187], v[202:205], v[86:89]
	v_mfma_f32_16x16x32_bf16 v[82:85], v[176:179], v[210:213], v[82:85]
	v_mfma_f32_16x16x32_bf16 v[78:81], v[184:187], v[210:213], v[78:81]
	v_mfma_f32_16x16x32_bf16 v[74:77], v[176:179], v[218:221], v[74:77]
	v_mfma_f32_16x16x32_bf16 v[70:73], v[184:187], v[218:221], v[70:73]
	v_mfma_f32_16x16x32_bf16 v[98:101], v[180:183], v[198:201], v[98:101]
	v_mfma_f32_16x16x32_bf16 v[94:97], v[190:193], v[198:201], v[94:97]
	v_mfma_f32_16x16x32_bf16 v[90:93], v[180:183], v[206:209], v[90:93]
	v_mfma_f32_16x16x32_bf16 v[86:89], v[190:193], v[206:209], v[86:89]
	v_mfma_f32_16x16x32_bf16 v[82:85], v[180:183], v[214:217], v[82:85]
	v_mfma_f32_16x16x32_bf16 v[78:81], v[190:193], v[214:217], v[78:81]
	v_mfma_f32_16x16x32_bf16 v[74:77], v[180:183], v[222:225], v[74:77]
	v_mfma_f32_16x16x32_bf16 v[70:73], v[190:193], v[222:225], v[70:73]
	s_setprio 0
	s_barrier
	s_add_i32 s6, s6, s48
	v_lshl_add_u64 v[226:227], s[42:43], 0, v[138:139]
	s_mov_b32 m0, s6
	ds_read_b128 v[194:197], v156 offset:16384
	ds_read_b128 v[198:201], v156 offset:17408
	ds_read_b128 v[202:205], v156 offset:18432
	ds_read_b128 v[206:209], v156 offset:19456
	ds_read_b128 v[210:213], v156 offset:20480
	ds_read_b128 v[214:217], v156 offset:21504
	ds_read_b128 v[218:221], v156 offset:22528
	ds_read_b128 v[222:225], v156 offset:23552
	global_load_lds_dwordx4 v[226:227], off
	s_add_i32 m0, s6, 0x2000
	s_add_u32 s6, s42, 0x40000
	v_lshl_add_u64 v[228:229], s[42:43], 0, v[140:141]
	s_addc_u32 s7, s43, 0
	s_add_i32 s59, s59, s48
	global_load_lds_dwordx4 v[228:229], off
	v_lshl_add_u64 v[230:231], s[6:7], 0, v[138:139]
	s_mov_b32 m0, s59
	v_mov_b32_e32 v151, v1
	global_load_lds_dwordx4 v[230:231], off
	v_lshl_add_u64 v[230:231], s[6:7], 0, v[140:141]
	s_add_i32 m0, s59, 0x2000
	s_nop 0
	global_load_lds_dwordx4 v[230:231], off
	s_mov_b32 m0, s49
	v_lshl_add_u64 v[230:231], s[44:45], 0, v[0:1]
	global_load_lds_dwordx4 v0, s[44:45]
	s_mov_b32 m0, s50
	s_nop 0
	global_load_lds_dwordx4 v150, s[44:45]
	s_waitcnt vmcnt(8)
	s_waitcnt lgkmcnt(0)
	v_lshl_add_u64 v[150:151], s[44:45], 0, v[150:151]
	s_barrier
; #define PG8_STAGE(bufoff, gbase, voff) do { _Pragma("unroll") for (int _i = 0; _i < 2; ++_i) \
;         __builtin_amdgcn_global_load_lds((const unsigned*)((const char*)(gbase) + (voff)[_i]), (LAS unsigned*)(lds + (bufoff) + ldsw + _i * 8192), 16, 0, 0); } while (0)
; #define PG8_LDA(dst, b, h) do { _Pragma("unroll") for (int m = 0; m < 4; ++m) _Pragma("unroll") for (int k = 0; k < 2; ++k) dst[m][k] = *(const LAS bf16x8*)(lds + PG8_SA(b, h) + aoff + m * 2048 + k * 1024); } while (0)
; #define PG8_LDB(dst, b, h) do { _Pragma("unroll") for (int n = 0; n < 2; ++n) _Pragma("unroll") for (int k = 0; k < 2; ++k) dst[n][k] = *(const LAS bf16x8*)(lds + PG8_SB(b, h) + boff + n * 2048 + k * 1024); } while (0)
; #define PG8_MMA(ai, bj, At, Bt) do { __builtin_amdgcn_s_setprio(1); _Pragma("unroll") for (int m = 0; m < 4; ++m) _Pragma("unroll") for (int n = 0; n < 2; ++n) _Pragma("unroll") for (int k = 0; k < 2; ++k) \
;         acc[ai][bj][m][n] = __builtin_amdgcn_mfma_f32_16x16x32_bf16(Bt[n][k], At[m][k], acc[ai][bj][m][n], 0, 0, 0); __builtin_amdgcn_s_setprio(0); } while (0)
; #define PG8_WAIT_V(n) asm volatile("s_waitcnt vmcnt(" #n ")" ::: "memory")
; #define PG8_WAIT_L(n) asm volatile("s_waitcnt lgkmcnt(" #n ")" ::: "memory")
; #define PG8_BAR __builtin_amdgcn_s_barrier()
; #define PG8_SCHED __builtin_amdgcn_sched_barrier(0)
; template <class Epi, class Sched>
; __device__ __forceinline__ void gemm_phase(LAS unsigned char* lds, const int tid, const char* Abase, const int K, const Sched& S, const Epi& E) {
;     ...
;             PG8_WAIT_V(8); PG8_WAIT_L(0); PG8_BAR; PG8_MMA(1, 0, At, B0); PG8_MMA(1, 1, At, B1); PG8_BAR; PG8_SCHED;
;             PG8_LDB(B0, 1, 0); PG8_LDB(B1, 1, 1); PG8_SCHED; PG8_LDA(At, 1, 0); PG8_STAGE(PG8_SA(0, 1), a2, w2[1]);
;             PG8_WAIT_V(8); PG8_WAIT_L(0); PG8_BAR; PG8_MMA(0, 0, At, B0); PG8_MMA(0, 1, At, B1); PG8_BAR; PG8_SCHED;
;             PG8_LDA(At, 1, 1); PG8_STAGE(PG8_SB(1, 0), b3, voffB); PG8_STAGE(PG8_SB(1, 1), b3 + hstep, voffB); PG8_STAGE(PG8_SA(1, 0), a3, w2[0]);
	s_setprio 1
	s_waitcnt lgkmcnt(0)
	v_mfma_f32_16x16x32_bf16 v[54:57], v[160:163], v[194:197], v[54:57]
	v_mfma_f32_16x16x32_bf16 v[50:53], v[168:171], v[194:197], v[50:53]
	v_mfma_f32_16x16x32_bf16 v[46:49], v[160:163], v[202:205], v[46:49]
	v_mfma_f32_16x16x32_bf16 v[42:45], v[168:171], v[202:205], v[42:45]
	v_mfma_f32_16x16x32_bf16 v[38:41], v[160:163], v[210:213], v[38:41]
	v_mfma_f32_16x16x32_bf16 v[34:37], v[168:171], v[210:213], v[34:37]
	v_mfma_f32_16x16x32_bf16 v[30:33], v[160:163], v[218:221], v[30:33]
	v_mfma_f32_16x16x32_bf16 v[26:29], v[168:171], v[218:221], v[26:29]
	v_mfma_f32_16x16x32_bf16 v[54:57], v[164:167], v[198:201], v[54:57]
	v_mfma_f32_16x16x32_bf16 v[50:53], v[172:175], v[198:201], v[50:53]
	v_mfma_f32_16x16x32_bf16 v[46:49], v[164:167], v[206:209], v[46:49]
	v_mfma_f32_16x16x32_bf16 v[42:45], v[172:175], v[206:209], v[42:45]
	v_mfma_f32_16x16x32_bf16 v[38:41], v[164:167], v[214:217], v[38:41]
	v_mfma_f32_16x16x32_bf16 v[34:37], v[172:175], v[214:217], v[34:37]
	v_mfma_f32_16x16x32_bf16 v[30:33], v[164:167], v[222:225], v[30:33]
	v_mfma_f32_16x16x32_bf16 v[26:29], v[172:175], v[222:225], v[26:29]
	v_mfma_f32_16x16x32_bf16 v[22:25], v[176:179], v[194:197], v[22:25]
	v_mfma_f32_16x16x32_bf16 v[18:21], v[184:187], v[194:197], v[18:21]
	v_mfma_f32_16x16x32_bf16 v[14:17], v[176:179], v[202:205], v[14:17]
	v_mfma_f32_16x16x32_bf16 v[6:9], v[184:187], v[202:205], v[6:9]
	v_mfma_f32_16x16x32_bf16 v[58:61], v[176:179], v[210:213], v[58:61]
	v_mfma_f32_16x16x32_bf16 v[62:65], v[184:187], v[210:213], v[62:65]
	v_mfma_f32_16x16x32_bf16 v[66:69], v[176:179], v[218:221], v[66:69]
	v_mfma_f32_16x16x32_bf16 v[10:13], v[184:187], v[218:221], v[10:13]
	v_mfma_f32_16x16x32_bf16 v[22:25], v[180:183], v[198:201], v[22:25]
	v_mfma_f32_16x16x32_bf16 v[18:21], v[190:193], v[198:201], v[18:21]
	v_mfma_f32_16x16x32_bf16 v[14:17], v[180:183], v[206:209], v[14:17]
	v_mfma_f32_16x16x32_bf16 v[6:9], v[190:193], v[206:209], v[6:9]
	v_mfma_f32_16x16x32_bf16 v[58:61], v[180:183], v[214:217], v[58:61]
	v_mfma_f32_16x16x32_bf16 v[62:65], v[190:193], v[214:217], v[62:65]
	v_mfma_f32_16x16x32_bf16 v[66:69], v[180:183], v[222:225], v[66:69]
	v_mfma_f32_16x16x32_bf16 v[10:13], v[190:193], v[222:225], v[10:13]
	s_setprio 0
	s_barrier
	s_add_i32 s6, 0, 0x18000
	v_add_u32_e32 v0, s6, v155
	s_add_i32 s59, 0, 0x1c000
	ds_read_b128 v[160:163], v0
	ds_read_b128 v[164:167], v0 offset:1024
	ds_read_b128 v[168:171], v0 offset:2048
	ds_read_b128 v[172:175], v0 offset:3072
	v_add_u32_e32 v0, s59, v155
	ds_read_b128 v[176:179], v0
	ds_read_b128 v[180:183], v0 offset:1024
	ds_read_b128 v[184:187], v0 offset:2048
	ds_read_b128 v[190:193], v0 offset:3072
	s_mov_b32 m0, s51
	v_lshl_add_u64 v[148:149], s[44:45], 0, v[148:149]
	ds_read_b128 v[194:197], v156 offset:32768
	ds_read_b128 v[198:201], v156 offset:33792
	ds_read_b128 v[202:205], v156 offset:34816
	ds_read_b128 v[206:209], v156 offset:35840
	ds_read_b128 v[210:213], v156 offset:36864
	ds_read_b128 v[214:217], v156 offset:37888
	ds_read_b128 v[218:221], v156 offset:38912
	ds_read_b128 v[222:225], v156 offset:39936
	global_load_lds_dwordx4 v[148:149], off
	v_lshl_add_u64 v[146:147], s[44:45], 0, v[146:147]
	s_mov_b32 m0, s52
	s_nop 0
	global_load_lds_dwordx4 v[146:147], off
	s_waitcnt vmcnt(8)
	s_waitcnt lgkmcnt(0)
	s_barrier
	s_setprio 1
	s_waitcnt lgkmcnt(0)
	v_mfma_f32_16x16x32_bf16 v[130:133], v[160:163], v[194:197], v[130:133]
	v_mfma_f32_16x16x32_bf16 v[126:129], v[168:171], v[194:197], v[126:129]
	v_mfma_f32_16x16x32_bf16 v[122:125], v[160:163], v[202:205], v[122:125]
	v_mfma_f32_16x16x32_bf16 v[118:121], v[168:171], v[202:205], v[118:121]
	v_mfma_f32_16x16x32_bf16 v[114:117], v[160:163], v[210:213], v[114:117]
	v_mfma_f32_16x16x32_bf16 v[110:113], v[168:171], v[210:213], v[110:113]
	v_mfma_f32_16x16x32_bf16 v[106:109], v[160:163], v[218:221], v[106:109]
	v_mfma_f32_16x16x32_bf16 v[102:105], v[168:171], v[218:221], v[102:105]
	v_mfma_f32_16x16x32_bf16 v[130:133], v[164:167], v[198:201], v[130:133]
	v_mfma_f32_16x16x32_bf16 v[126:129], v[172:175], v[198:201], v[126:129]
	v_mfma_f32_16x16x32_bf16 v[122:125], v[164:167], v[206:209], v[122:125]
	v_mfma_f32_16x16x32_bf16 v[118:121], v[172:175], v[206:209], v[118:121]
	v_mfma_f32_16x16x32_bf16 v[114:117], v[164:167], v[214:217], v[114:117]
	v_mfma_f32_16x16x32_bf16 v[110:113], v[172:175], v[214:217], v[110:113]
	v_mfma_f32_16x16x32_bf16 v[106:109], v[164:167], v[222:225], v[106:109]
	v_mfma_f32_16x16x32_bf16 v[102:105], v[172:175], v[222:225], v[102:105]
	v_mfma_f32_16x16x32_bf16 v[98:101], v[176:179], v[194:197], v[98:101]
	v_mfma_f32_16x16x32_bf16 v[94:97], v[184:187], v[194:197], v[94:97]
	v_mfma_f32_16x16x32_bf16 v[90:93], v[176:179], v[202:205], v[90:93]
	v_mfma_f32_16x16x32_bf16 v[86:89], v[184:187], v[202:205], v[86:89]
	v_mfma_f32_16x16x32_bf16 v[82:85], v[176:179], v[210:213], v[82:85]
	v_mfma_f32_16x16x32_bf16 v[78:81], v[184:187], v[210:213], v[78:81]
	v_mfma_f32_16x16x32_bf16 v[74:77], v[176:179], v[218:221], v[74:77]
	v_mfma_f32_16x16x32_bf16 v[70:73], v[184:187], v[218:221], v[70:73]
	v_mfma_f32_16x16x32_bf16 v[98:101], v[180:183], v[198:201], v[98:101]
	v_mfma_f32_16x16x32_bf16 v[94:97], v[190:193], v[198:201], v[94:97]
	v_mfma_f32_16x16x32_bf16 v[90:93], v[180:183], v[206:209], v[90:93]
	v_mfma_f32_16x16x32_bf16 v[86:89], v[190:193], v[206:209], v[86:89]
	v_mfma_f32_16x16x32_bf16 v[82:85], v[180:183], v[214:217], v[82:85]
	v_mfma_f32_16x16x32_bf16 v[78:81], v[190:193], v[214:217], v[78:81]
	v_mfma_f32_16x16x32_bf16 v[74:77], v[180:183], v[222:225], v[74:77]
	v_mfma_f32_16x16x32_bf16 v[70:73], v[190:193], v[222:225], v[70:73]
	s_setprio 0
	s_barrier
; #define PG8_STAGE(bufoff, gbase, voff) do { _Pragma("unroll") for (int _i = 0; _i < 2; ++_i) \
;         __builtin_amdgcn_global_load_lds((const unsigned*)((const char*)(gbase) + (voff)[_i]), (LAS unsigned*)(lds + (bufoff) + ldsw + _i * 8192), 16, 0, 0); } while (0)
; #define PG8_LDA(dst, b, h) do { _Pragma("unroll") for (int m = 0; m < 4; ++m) _Pragma("unroll") for (int k = 0; k < 2; ++k) dst[m][k] = *(const LAS bf16x8*)(lds + PG8_SA(b, h) + aoff + m * 2048 + k * 1024); } while (0)
; #define PG8_MMA(ai, bj, At, Bt) do { __builtin_amdgcn_s_setprio(1); _Pragma("unroll") for (int m = 0; m < 4; ++m) _Pragma("unroll") for (int n = 0; n < 2; ++n) _Pragma("unroll") for (int k = 0; k < 2; ++k) \
;         acc[ai][bj][m][n] = __builtin_amdgcn_mfma_f32_16x16x32_bf16(Bt[n][k], At[m][k], acc[ai][bj][m][n], 0, 0, 0); __builtin_amdgcn_s_setprio(0); } while (0)
; #define PG8_WAIT_V(n) asm volatile("s_waitcnt vmcnt(" #n ")" ::: "memory")
; #define PG8_WAIT_L(n) asm volatile("s_waitcnt lgkmcnt(" #n ")" ::: "memory")
; #define PG8_BAR __builtin_amdgcn_s_barrier()
; #define PG8_SCHED __builtin_amdgcn_sched_barrier(0)
; template <class Epi, class Sched>
; __device__ __forceinline__ void gemm_phase(LAS unsigned char* lds, const int tid, const char* Abase, const int K, const Sched& S, const Epi& E) {
;     ...
;             PG8_LDA(At, 1, 1); PG8_STAGE(PG8_SB(1, 0), b3, voffB); PG8_STAGE(PG8_SB(1, 1), b3 + hstep, voffB); PG8_STAGE(PG8_SA(1, 0), a3, w2[0]);
;             PG8_WAIT_V(8); PG8_WAIT_L(0); PG8_BAR; PG8_MMA(1, 0, At, B0); PG8_MMA(1, 1, At, B1); PG8_BAR; PG8_SCHED;
;         }
	s_add_i32 s6, s6, s48
	v_lshl_add_u64 v[222:223], v[226:227], 0, s[24:25]
	s_mov_b32 m0, s6
	ds_read_b128 v[146:149], v156 offset:49152
	ds_read_b128 v[194:197], v156 offset:50176
	ds_read_b128 v[198:201], v156 offset:51200
	ds_read_b128 v[202:205], v156 offset:52224
	ds_read_b128 v[206:209], v156 offset:53248
	ds_read_b128 v[210:213], v156 offset:54272
	ds_read_b128 v[214:217], v156 offset:55296
	ds_read_b128 v[218:221], v156 offset:56320
	global_load_lds_dwordx4 v[222:223], off
	s_add_i32 m0, s6, 0x2000
	s_add_u32 s6, s42, 0x40080
	v_lshl_add_u64 v[222:223], v[228:229], 0, s[24:25]
	s_addc_u32 s7, s43, 0
	s_add_i32 s42, s59, s48
	global_load_lds_dwordx4 v[222:223], off
	v_lshl_add_u64 v[222:223], s[6:7], 0, v[138:139]
	s_mov_b32 m0, s42
	v_lshl_add_u64 v[150:151], v[150:151], 0, s[24:25]
	global_load_lds_dwordx4 v[222:223], off
	v_lshl_add_u64 v[222:223], s[6:7], 0, v[140:141]
	s_add_i32 m0, s42, 0x2000
	s_nop 0
	global_load_lds_dwordx4 v[222:223], off
	v_lshl_add_u64 v[222:223], v[230:231], 0, s[24:25]
	s_mov_b32 m0, s55
	s_nop 0
	global_load_lds_dwordx4 v[222:223], off
	s_mov_b32 m0, s56
	s_nop 0
	global_load_lds_dwordx4 v[150:151], off
	s_waitcnt vmcnt(8)
	s_waitcnt lgkmcnt(0)
	s_barrier
	s_setprio 1
	s_waitcnt lgkmcnt(0)
	v_mfma_f32_16x16x32_bf16 v[54:57], v[160:163], v[146:149], v[54:57]
	v_mfma_f32_16x16x32_bf16 v[50:53], v[168:171], v[146:149], v[50:53]
	v_mfma_f32_16x16x32_bf16 v[46:49], v[160:163], v[198:201], v[46:49]
	v_mfma_f32_16x16x32_bf16 v[42:45], v[168:171], v[198:201], v[42:45]
	v_mfma_f32_16x16x32_bf16 v[38:41], v[160:163], v[206:209], v[38:41]
	v_mfma_f32_16x16x32_bf16 v[34:37], v[168:171], v[206:209], v[34:37]
	v_mfma_f32_16x16x32_bf16 v[30:33], v[160:163], v[214:217], v[30:33]
	v_mfma_f32_16x16x32_bf16 v[26:29], v[168:171], v[214:217], v[26:29]
	v_mfma_f32_16x16x32_bf16 v[54:57], v[164:167], v[194:197], v[54:57]
	v_mfma_f32_16x16x32_bf16 v[50:53], v[172:175], v[194:197], v[50:53]
	v_mfma_f32_16x16x32_bf16 v[46:49], v[164:167], v[202:205], v[46:49]
	v_mfma_f32_16x16x32_bf16 v[42:45], v[172:175], v[202:205], v[42:45]
	v_mfma_f32_16x16x32_bf16 v[38:41], v[164:167], v[210:213], v[38:41]
	v_mfma_f32_16x16x32_bf16 v[34:37], v[172:175], v[210:213], v[34:37]
	v_mfma_f32_16x16x32_bf16 v[30:33], v[164:167], v[218:221], v[30:33]
	v_mfma_f32_16x16x32_bf16 v[26:29], v[172:175], v[218:221], v[26:29]
	v_mfma_f32_16x16x32_bf16 v[22:25], v[176:179], v[146:149], v[22:25]
	v_mfma_f32_16x16x32_bf16 v[18:21], v[184:187], v[146:149], v[18:21]
	v_mfma_f32_16x16x32_bf16 v[14:17], v[176:179], v[198:201], v[14:17]
	v_mfma_f32_16x16x32_bf16 v[6:9], v[184:187], v[198:201], v[6:9]
	v_mfma_f32_16x16x32_bf16 v[58:61], v[176:179], v[206:209], v[58:61]
	v_mfma_f32_16x16x32_bf16 v[62:65], v[184:187], v[206:209], v[62:65]
	v_mfma_f32_16x16x32_bf16 v[66:69], v[176:179], v[214:217], v[66:69]
	v_mfma_f32_16x16x32_bf16 v[10:13], v[184:187], v[214:217], v[10:13]
	v_mfma_f32_16x16x32_bf16 v[22:25], v[180:183], v[194:197], v[22:25]
	v_mfma_f32_16x16x32_bf16 v[18:21], v[190:193], v[194:197], v[18:21]
	v_mfma_f32_16x16x32_bf16 v[14:17], v[180:183], v[202:205], v[14:17]
	v_mfma_f32_16x16x32_bf16 v[6:9], v[190:193], v[202:205], v[6:9]
	v_mfma_f32_16x16x32_bf16 v[58:61], v[180:183], v[210:213], v[58:61]
	v_mfma_f32_16x16x32_bf16 v[62:65], v[190:193], v[210:213], v[62:65]
	v_mfma_f32_16x16x32_bf16 v[66:69], v[180:183], v[218:221], v[66:69]
	v_mfma_f32_16x16x32_bf16 v[10:13], v[190:193], v[218:221], v[10:13]
	s_setprio 0
	s_barrier
	s_add_i32 s3, s3, 2
	s_add_u32 s40, s40, 0x100
	s_addc_u32 s41, s41, 0
	s_cmp_gt_u32 s3, 13
	s_cbranch_scc1 .LBB0_1189

; #define PG8_STAGE(bufoff, gbase, voff) do { _Pragma("unroll") for (int _i = 0; _i < 2; ++_i) \
;         __builtin_amdgcn_global_load_lds((const unsigned*)((const char*)(gbase) + (voff)[_i]), (LAS unsigned*)(lds + (bufoff) + ldsw + _i * 8192), 16, 0, 0); } while (0)
; #define PG8_LDA(dst, b, h) do { _Pragma("unroll") for (int m = 0; m < 4; ++m) _Pragma("unroll") for (int k = 0; k < 2; ++k) dst[m][k] = *(const LAS bf16x8*)(lds + PG8_SA(b, h) + aoff + m * 2048 + k * 1024); } while (0)
; #define PG8_LDB(dst, b, h) do { _Pragma("unroll") for (int n = 0; n < 2; ++n) _Pragma("unroll") for (int k = 0; k < 2; ++k) dst[n][k] = *(const LAS bf16x8*)(lds + PG8_SB(b, h) + boff + n * 2048 + k * 1024); } while (0)
; #define PG8_WAIT_V(n) asm volatile("s_waitcnt vmcnt(" #n ")" ::: "memory")
; template <class Epi, class Sched>
; __device__ __forceinline__ void gemm_phase(LAS unsigned char* lds, const int tid, const char* Abase, const int K, const Sched& S, const Epi& E) {
;     ...
;           if (has_next) { PG8_AOFFS(vn, nxt); nB = S.b_tile(nxt); *vslot = (u32x4){vn[0][0], vn[0][1], vn[1][0], vn[1][1]}; }
;           else *vslot = (u32x4){vc[0][0], vc[0][1], vc[1][0], vc[1][1]}; }
;         for (int t = 0; t < nt; t += 2) {
;             if constexpr (Epi::MID) { if (t == (nt >> 1)) E.mid(acc, ui, wr, fr, lds); }
;             const bool last = (t == nt - 2);
;             const char* a1 = Abase + (size_t)(t + 1) * kstep;
;             const char* a2 = last ? Abase : Abase + (size_t)(t + 2) * kstep; const char* b2 = last ? nB : cB + (size_t)(t + 2) * kstep;
;             const char* a3 = a2 + kstep; const char* b3 = b2 + kstep;
;             unsigned w2[2][2];
;             if (last) { const u32x4 q = *vslot; w2[0][0] = q.x; w2[0][1] = q.y; w2[1][0] = q.z; w2[1][1] = q.w; }
;             else { w2[0][0] = vc[0][0]; w2[0][1] = vc[0][1]; w2[1][0] = vc[1][0]; w2[1][1] = vc[1][1]; }
;             PG8_LDB(B0, 0, 0); PG8_LDB(B1, 0, 1); PG8_SCHED; PG8_LDA(At, 0, 0); PG8_STAGE(PG8_SA(1, 1), a1, vc[1]);
;             PG8_WAIT_V(8); PG8_WAIT_L(0); PG8_BAR; PG8_MMA(0, 0, At, B0); PG8_MMA(0, 1, At, B1); PG8_BAR; PG8_SCHED;
;             PG8_LDA(At, 0, 1); PG8_STAGE(PG8_SB(0, 0), b2, voffB); PG8_STAGE(PG8_SB(0, 1), b2 + hstep, voffB); PG8_STAGE(PG8_SA(0, 0), a2, w2[0]);
;             PG8_WAIT_V(8); PG8_WAIT_L(0); PG8_BAR; PG8_MMA(1, 0, At, B0); PG8_MMA(1, 1, At, B1); PG8_BAR; PG8_SCHED;
.LBB0_1229:
	s_add_i32 s54, 0, 0x10000
	s_add_i32 s51, 0, 0x14000
	ds_write_b128 v132, v[6:9]
	v_add_u32_e32 v135, s54, v133
	v_add_u32_e32 v189, s51, v133
	ds_read_b128 v[6:9], v135
	ds_read_b128 v[10:13], v135 offset:1024
	ds_read_b128 v[14:17], v135 offset:2048
	ds_read_b128 v[18:21], v135 offset:3072
	ds_read_b128 v[22:25], v189
	ds_read_b128 v[26:29], v189 offset:1024
	ds_read_b128 v[30:33], v189 offset:2048
	ds_read_b128 v[34:37], v189 offset:3072
	v_mov_b32_e32 v252, 1
	s_add_i32 s35, s7, 0xc000
	s_mov_b32 m0, s35
	s_add_i32 s49, s7, 0xe000
	ds_read_b128 v[38:41], v134
	ds_read_b128 v[42:45], v134 offset:1024
	ds_read_b128 v[46:49], v134 offset:2048
	ds_read_b128 v[50:53], v134 offset:3072
	ds_read_b128 v[54:57], v134 offset:4096
	ds_read_b128 v[58:61], v134 offset:5120
	ds_read_b128 v[62:65], v134 offset:6144
	ds_read_b128 v[66:69], v134 offset:7168
	global_load_lds_dwordx4 v4, s[20:21]
	s_mov_b32 m0, s49
	s_nop 0
	global_load_lds_dwordx4 v5, s[20:21]
	s_waitcnt vmcnt(8)
	s_waitcnt lgkmcnt(0)
	s_barrier
	s_setprio 1
	s_waitcnt lgkmcnt(0)
	v_mfma_f32_16x16x32_bf16 v[70:73], v[6:9], v[38:41], 0
	v_mfma_f32_16x16x32_bf16 v[74:77], v[14:17], v[38:41], 0
	v_mfma_f32_16x16x32_bf16 v[78:81], v[6:9], v[46:49], 0
	v_mfma_f32_16x16x32_bf16 v[82:85], v[14:17], v[46:49], 0
	v_mfma_f32_16x16x32_bf16 v[86:89], v[6:9], v[54:57], 0
	v_mfma_f32_16x16x32_bf16 v[90:93], v[14:17], v[54:57], 0
	v_mfma_f32_16x16x32_bf16 v[94:97], v[6:9], v[62:65], 0
	v_mfma_f32_16x16x32_bf16 v[98:101], v[14:17], v[62:65], 0
	v_mfma_f32_16x16x32_bf16 v[70:73], v[10:13], v[42:45], v[70:73]
	v_mfma_f32_16x16x32_bf16 v[74:77], v[18:21], v[42:45], v[74:77]
	v_mfma_f32_16x16x32_bf16 v[78:81], v[10:13], v[50:53], v[78:81]
	v_mfma_f32_16x16x32_bf16 v[82:85], v[18:21], v[50:53], v[82:85]
	v_mfma_f32_16x16x32_bf16 v[86:89], v[10:13], v[58:61], v[86:89]
	v_mfma_f32_16x16x32_bf16 v[90:93], v[18:21], v[58:61], v[90:93]
	v_mfma_f32_16x16x32_bf16 v[94:97], v[10:13], v[66:69], v[94:97]
	v_mfma_f32_16x16x32_bf16 v[98:101], v[18:21], v[66:69], v[98:101]
	v_mfma_f32_16x16x32_bf16 v[102:105], v[22:25], v[38:41], 0
	v_mfma_f32_16x16x32_bf16 v[38:41], v[30:33], v[38:41], 0
	v_mfma_f32_16x16x32_bf16 v[102:105], v[26:29], v[42:45], v[102:105]
	v_mfma_f32_16x16x32_bf16 v[38:41], v[34:37], v[42:45], v[38:41]
	v_mfma_f32_16x16x32_bf16 v[42:45], v[22:25], v[46:49], 0
	v_mfma_f32_16x16x32_bf16 v[46:49], v[30:33], v[46:49], 0
	v_mfma_f32_16x16x32_bf16 v[42:45], v[26:29], v[50:53], v[42:45]
	v_mfma_f32_16x16x32_bf16 v[46:49], v[34:37], v[50:53], v[46:49]
	v_mfma_f32_16x16x32_bf16 v[50:53], v[22:25], v[54:57], 0
	v_mfma_f32_16x16x32_bf16 v[54:57], v[30:33], v[54:57], 0
	v_mfma_f32_16x16x32_bf16 v[50:53], v[26:29], v[58:61], v[50:53]
	v_mfma_f32_16x16x32_bf16 v[54:57], v[34:37], v[58:61], v[54:57]
	v_mfma_f32_16x16x32_bf16 v[58:61], v[22:25], v[62:65], 0
	v_mfma_f32_16x16x32_bf16 v[62:65], v[30:33], v[62:65], 0
	v_mfma_f32_16x16x32_bf16 v[58:61], v[26:29], v[66:69], v[58:61]
	v_mfma_f32_16x16x32_bf16 v[62:65], v[34:37], v[66:69], v[62:65]
	s_setprio 0
	s_barrier
	v_lshl_add_u64 v[206:207], s[36:37], 0, v[0:1]
	s_mov_b64 s[52:53], 0x100
	s_add_i32 s54, s54, s6
	v_lshl_add_u64 v[140:141], v[206:207], 0, s[52:53]
	s_mov_b32 m0, s54
	v_lshl_add_u64 v[208:209], s[36:37], 0, v[130:131]
	s_add_i32 s50, s54, 0x2000
	ds_read_b128 v[66:69], v134 offset:16384
	ds_read_b128 v[106:109], v134 offset:17408
	ds_read_b128 v[110:113], v134 offset:18432
	ds_read_b128 v[114:117], v134 offset:19456
	ds_read_b128 v[118:121], v134 offset:20480
	ds_read_b128 v[122:125], v134 offset:21504
	ds_read_b128 v[126:129], v134 offset:22528
	ds_read_b128 v[136:139], v134 offset:23552
	global_load_lds_dwordx4 v[140:141], off
	v_lshl_add_u64 v[140:141], v[208:209], 0, s[52:53]
	s_add_u32 s52, s36, 0x10100
	s_mov_b32 m0, s50
	s_addc_u32 s53, s37, 0
	s_add_i32 s51, s51, s6
	global_load_lds_dwordx4 v[140:141], off
	v_lshl_add_u64 v[140:141], s[52:53], 0, v[0:1]
	s_mov_b32 m0, s51
	s_nop 0
	global_load_lds_dwordx4 v[140:141], off
	v_lshl_add_u64 v[140:141], s[52:53], 0, v[130:131]
	s_add_i32 s52, s51, 0x2000
	s_mov_b32 m0, s52
	s_nop 0
	global_load_lds_dwordx4 v[140:141], off
	s_mov_b32 m0, s7
	s_nop 0
	global_load_lds_dwordx4 v2, s[26:27]
	s_mov_b32 m0, s33
	s_nop 0
	global_load_lds_dwordx4 v3, s[26:27]
	s_waitcnt vmcnt(8)
	s_waitcnt lgkmcnt(0)
	s_barrier
	s_setprio 1
	s_waitcnt lgkmcnt(0)
	v_mfma_f32_16x16x32_bf16 v[140:143], v[6:9], v[66:69], 0
	v_mfma_f32_16x16x32_bf16 v[148:151], v[6:9], v[110:113], 0
	v_mfma_f32_16x16x32_bf16 v[156:159], v[6:9], v[118:121], 0
	v_mfma_f32_16x16x32_bf16 v[6:9], v[6:9], v[126:129], 0
	v_mfma_f32_16x16x32_bf16 v[140:143], v[10:13], v[106:109], v[140:143]
	v_mfma_f32_16x16x32_bf16 v[148:151], v[10:13], v[114:117], v[148:151]
	v_mfma_f32_16x16x32_bf16 v[156:159], v[10:13], v[122:125], v[156:159]
	v_mfma_f32_16x16x32_bf16 v[6:9], v[10:13], v[136:139], v[6:9]
	v_mfma_f32_16x16x32_bf16 v[10:13], v[14:17], v[126:129], 0
	v_mfma_f32_16x16x32_bf16 v[144:147], v[14:17], v[66:69], 0
	v_mfma_f32_16x16x32_bf16 v[152:155], v[14:17], v[110:113], 0
	v_mfma_f32_16x16x32_bf16 v[160:163], v[14:17], v[118:121], 0
	v_mfma_f32_16x16x32_bf16 v[10:13], v[18:21], v[136:139], v[10:13]
	v_mfma_f32_16x16x32_bf16 v[144:147], v[18:21], v[106:109], v[144:147]
	v_mfma_f32_16x16x32_bf16 v[152:155], v[18:21], v[114:117], v[152:155]
	v_mfma_f32_16x16x32_bf16 v[160:163], v[18:21], v[122:125], v[160:163]
	v_mfma_f32_16x16x32_bf16 v[14:17], v[22:25], v[66:69], 0
	v_mfma_f32_16x16x32_bf16 v[18:21], v[30:33], v[66:69], 0
	v_mfma_f32_16x16x32_bf16 v[14:17], v[26:29], v[106:109], v[14:17]
	v_mfma_f32_16x16x32_bf16 v[18:21], v[34:37], v[106:109], v[18:21]
	v_mfma_f32_16x16x32_bf16 v[66:69], v[22:25], v[110:113], 0
	v_mfma_f32_16x16x32_bf16 v[106:109], v[30:33], v[110:113], 0
	v_mfma_f32_16x16x32_bf16 v[110:113], v[22:25], v[118:121], 0
	v_mfma_f32_16x16x32_bf16 v[22:25], v[22:25], v[126:129], 0
	v_mfma_f32_16x16x32_bf16 v[66:69], v[26:29], v[114:117], v[66:69]
	v_mfma_f32_16x16x32_bf16 v[106:109], v[34:37], v[114:117], v[106:109]
	v_mfma_f32_16x16x32_bf16 v[110:113], v[26:29], v[122:125], v[110:113]
	v_mfma_f32_16x16x32_bf16 v[114:117], v[30:33], v[118:121], 0
	v_mfma_f32_16x16x32_bf16 v[22:25], v[26:29], v[136:139], v[22:25]
	v_mfma_f32_16x16x32_bf16 v[26:29], v[30:33], v[126:129], 0
	v_mfma_f32_16x16x32_bf16 v[114:117], v[34:37], v[122:125], v[114:117]
	v_mfma_f32_16x16x32_bf16 v[26:29], v[34:37], v[136:139], v[26:29]
	s_setprio 0
	s_barrier
; #define PG8_STAGE(bufoff, gbase, voff) do { _Pragma("unroll") for (int _i = 0; _i < 2; ++_i) \
;         __builtin_amdgcn_global_load_lds((const unsigned*)((const char*)(gbase) + (voff)[_i]), (LAS unsigned*)(lds + (bufoff) + ldsw + _i * 8192), 16, 0, 0); } while (0)
; #define PG8_LDA(dst, b, h) do { _Pragma("unroll") for (int m = 0; m < 4; ++m) _Pragma("unroll") for (int k = 0; k < 2; ++k) dst[m][k] = *(const LAS bf16x8*)(lds + PG8_SA(b, h) + aoff + m * 2048 + k * 1024); } while (0)
; #define PG8_LDB(dst, b, h) do { _Pragma("unroll") for (int n = 0; n < 2; ++n) _Pragma("unroll") for (int k = 0; k < 2; ++k) dst[n][k] = *(const LAS bf16x8*)(lds + PG8_SB(b, h) + boff + n * 2048 + k * 1024); } while (0)
; #define PG8_MMA(ai, bj, At, Bt) do { __builtin_amdgcn_s_setprio(1); _Pragma("unroll") for (int m = 0; m < 4; ++m) _Pragma("unroll") for (int n = 0; n < 2; ++n) _Pragma("unroll") for (int k = 0; k < 2; ++k) \
;         acc[ai][bj][m][n] = __builtin_amdgcn_mfma_f32_16x16x32_bf16(Bt[n][k], At[m][k], acc[ai][bj][m][n], 0, 0, 0); __builtin_amdgcn_s_setprio(0); } while (0)
; #define PG8_WAIT_V(n) asm volatile("s_waitcnt vmcnt(" #n ")" ::: "memory")
; #define PG8_WAIT_L(n) asm volatile("s_waitcnt lgkmcnt(" #n ")" ::: "memory")
; #define PG8_BAR __builtin_amdgcn_s_barrier()
; #define PG8_SCHED __builtin_amdgcn_sched_barrier(0)
; template <class Epi, class Sched>
; __device__ __forceinline__ void gemm_phase(LAS unsigned char* lds, const int tid, const char* Abase, const int K, const Sched& S, const Epi& E) {
;     ...
;             PG8_LDB(B0, 1, 0); PG8_LDB(B1, 1, 1); PG8_SCHED; PG8_LDA(At, 1, 0); PG8_STAGE(PG8_SA(0, 1), a2, w2[1]);
;             PG8_WAIT_V(8); PG8_WAIT_L(0); PG8_BAR; PG8_MMA(0, 0, At, B0); PG8_MMA(0, 1, At, B1); PG8_BAR; PG8_SCHED;
;             PG8_LDA(At, 1, 1); PG8_STAGE(PG8_SB(1, 0), b3, voffB); PG8_STAGE(PG8_SB(1, 1), b3 + hstep, voffB); PG8_STAGE(PG8_SA(1, 0), a3, w2[0]);
;             PG8_WAIT_V(8); PG8_WAIT_L(0); PG8_BAR; PG8_MMA(1, 0, At, B0); PG8_MMA(1, 1, At, B1); PG8_BAR; PG8_SCHED;
	s_add_i32 s55, 0, 0x18000
	s_add_i32 s58, 0, 0x1c000
	v_add_u32_e32 v214, s55, v133
	v_add_u32_e32 v222, s58, v133
	ds_read_b128 v[30:33], v214
	ds_read_b128 v[34:37], v214 offset:1024
	ds_read_b128 v[118:121], v214 offset:2048
	ds_read_b128 v[122:125], v214 offset:3072
	ds_read_b128 v[126:129], v222
	ds_read_b128 v[136:139], v222 offset:1024
	ds_read_b128 v[164:167], v222 offset:2048
	ds_read_b128 v[168:171], v222 offset:3072
	s_mov_b32 m0, s38
	ds_read_b128 v[172:175], v134 offset:32768
	ds_read_b128 v[176:179], v134 offset:33792
	ds_read_b128 v[180:183], v134 offset:34816
	ds_read_b128 v[184:187], v134 offset:35840
	ds_read_b128 v[190:193], v134 offset:36864
	ds_read_b128 v[194:197], v134 offset:37888
	ds_read_b128 v[198:201], v134 offset:38912
	ds_read_b128 v[202:205], v134 offset:39936
	global_load_lds_dwordx4 v4, s[26:27]
	s_mov_b32 m0, s39
	s_nop 0
	global_load_lds_dwordx4 v5, s[26:27]
	s_waitcnt vmcnt(8)
	s_waitcnt lgkmcnt(0)
	s_barrier
	s_setprio 1
	s_waitcnt lgkmcnt(0)
	v_mfma_f32_16x16x32_bf16 v[70:73], v[30:33], v[172:175], v[70:73]
	v_mfma_f32_16x16x32_bf16 v[74:77], v[118:121], v[172:175], v[74:77]
	v_mfma_f32_16x16x32_bf16 v[78:81], v[30:33], v[180:183], v[78:81]
	v_mfma_f32_16x16x32_bf16 v[82:85], v[118:121], v[180:183], v[82:85]
	v_mfma_f32_16x16x32_bf16 v[86:89], v[30:33], v[190:193], v[86:89]
	v_mfma_f32_16x16x32_bf16 v[90:93], v[118:121], v[190:193], v[90:93]
	v_mfma_f32_16x16x32_bf16 v[94:97], v[30:33], v[198:201], v[94:97]
	v_mfma_f32_16x16x32_bf16 v[98:101], v[118:121], v[198:201], v[98:101]
	v_mfma_f32_16x16x32_bf16 v[70:73], v[34:37], v[176:179], v[70:73]
	v_mfma_f32_16x16x32_bf16 v[74:77], v[122:125], v[176:179], v[74:77]
	v_mfma_f32_16x16x32_bf16 v[78:81], v[34:37], v[184:187], v[78:81]
	v_mfma_f32_16x16x32_bf16 v[82:85], v[122:125], v[184:187], v[82:85]
	v_mfma_f32_16x16x32_bf16 v[86:89], v[34:37], v[194:197], v[86:89]
	v_mfma_f32_16x16x32_bf16 v[90:93], v[122:125], v[194:197], v[90:93]
	v_mfma_f32_16x16x32_bf16 v[94:97], v[34:37], v[202:205], v[94:97]
	v_mfma_f32_16x16x32_bf16 v[98:101], v[122:125], v[202:205], v[98:101]
	v_mfma_f32_16x16x32_bf16 v[102:105], v[126:129], v[172:175], v[102:105]
	v_mfma_f32_16x16x32_bf16 v[38:41], v[164:167], v[172:175], v[38:41]
	v_mfma_f32_16x16x32_bf16 v[42:45], v[126:129], v[180:183], v[42:45]
	v_mfma_f32_16x16x32_bf16 v[46:49], v[164:167], v[180:183], v[46:49]
	v_mfma_f32_16x16x32_bf16 v[50:53], v[126:129], v[190:193], v[50:53]
	v_mfma_f32_16x16x32_bf16 v[54:57], v[164:167], v[190:193], v[54:57]
	v_mfma_f32_16x16x32_bf16 v[58:61], v[126:129], v[198:201], v[58:61]
	v_mfma_f32_16x16x32_bf16 v[62:65], v[164:167], v[198:201], v[62:65]
	v_mfma_f32_16x16x32_bf16 v[102:105], v[136:139], v[176:179], v[102:105]
	v_mfma_f32_16x16x32_bf16 v[38:41], v[168:171], v[176:179], v[38:41]
	v_mfma_f32_16x16x32_bf16 v[42:45], v[136:139], v[184:187], v[42:45]
	v_mfma_f32_16x16x32_bf16 v[46:49], v[168:171], v[184:187], v[46:49]
	v_mfma_f32_16x16x32_bf16 v[50:53], v[136:139], v[194:197], v[50:53]
	v_mfma_f32_16x16x32_bf16 v[54:57], v[168:171], v[194:197], v[54:57]
	v_mfma_f32_16x16x32_bf16 v[58:61], v[136:139], v[202:205], v[58:61]
	v_mfma_f32_16x16x32_bf16 v[62:65], v[168:171], v[202:205], v[62:65]
	s_setprio 0
	s_barrier
	s_mov_b64 s[56:57], 0x180
	s_add_i32 s55, s55, s6
	v_lshl_add_u64 v[206:207], v[206:207], 0, s[56:57]
	s_mov_b32 m0, s55
	s_add_i32 s53, s55, 0x2000
	ds_read_b128 v[172:175], v134 offset:49152
	ds_read_b128 v[176:179], v134 offset:50176
	ds_read_b128 v[180:183], v134 offset:51200
	ds_read_b128 v[184:187], v134 offset:52224
	ds_read_b128 v[190:193], v134 offset:53248
	ds_read_b128 v[194:197], v134 offset:54272
	ds_read_b128 v[198:201], v134 offset:55296
	ds_read_b128 v[202:205], v134 offset:56320
	global_load_lds_dwordx4 v[206:207], off
	v_lshl_add_u64 v[206:207], v[208:209], 0, s[56:57]
	s_add_u32 s56, s36, 0x10180
	s_mov_b32 m0, s53
	s_addc_u32 s57, s37, 0
	s_add_i32 s36, s58, s6
	global_load_lds_dwordx4 v[206:207], off
	v_lshl_add_u64 v[206:207], s[56:57], 0, v[0:1]
	s_mov_b32 m0, s36
	s_add_i32 s37, s36, 0x2000
	global_load_lds_dwordx4 v[206:207], off
	v_lshl_add_u64 v[206:207], s[56:57], 0, v[130:131]
	s_mov_b32 m0, s37
	s_nop 0
	global_load_lds_dwordx4 v[206:207], off
	s_mov_b32 m0, s42
	s_nop 0
	global_load_lds_dwordx4 v2, s[28:29]
	s_mov_b32 m0, s43
	s_nop 0
	global_load_lds_dwordx4 v3, s[28:29]
	s_waitcnt vmcnt(8)
	s_waitcnt lgkmcnt(0)
	s_barrier
	s_setprio 1
	s_waitcnt lgkmcnt(0)
	v_mfma_f32_16x16x32_bf16 v[6:9], v[30:33], v[198:201], v[6:9]
	v_mfma_f32_16x16x32_bf16 v[10:13], v[118:121], v[198:201], v[10:13]
	v_mfma_f32_16x16x32_bf16 v[140:143], v[30:33], v[172:175], v[140:143]
	v_mfma_f32_16x16x32_bf16 v[144:147], v[118:121], v[172:175], v[144:147]
	v_mfma_f32_16x16x32_bf16 v[148:151], v[30:33], v[180:183], v[148:151]
	v_mfma_f32_16x16x32_bf16 v[152:155], v[118:121], v[180:183], v[152:155]
	v_mfma_f32_16x16x32_bf16 v[156:159], v[30:33], v[190:193], v[156:159]
	v_mfma_f32_16x16x32_bf16 v[160:163], v[118:121], v[190:193], v[160:163]
	v_mfma_f32_16x16x32_bf16 v[6:9], v[34:37], v[202:205], v[6:9]
	v_mfma_f32_16x16x32_bf16 v[10:13], v[122:125], v[202:205], v[10:13]
	v_mfma_f32_16x16x32_bf16 v[140:143], v[34:37], v[176:179], v[140:143]
	v_mfma_f32_16x16x32_bf16 v[144:147], v[122:125], v[176:179], v[144:147]
	v_mfma_f32_16x16x32_bf16 v[148:151], v[34:37], v[184:187], v[148:151]
	v_mfma_f32_16x16x32_bf16 v[152:155], v[122:125], v[184:187], v[152:155]
	v_mfma_f32_16x16x32_bf16 v[156:159], v[34:37], v[194:197], v[156:159]
	v_mfma_f32_16x16x32_bf16 v[160:163], v[122:125], v[194:197], v[160:163]
	v_mfma_f32_16x16x32_bf16 v[14:17], v[126:129], v[172:175], v[14:17]
	v_mfma_f32_16x16x32_bf16 v[18:21], v[164:167], v[172:175], v[18:21]
	v_mfma_f32_16x16x32_bf16 v[30:33], v[126:129], v[180:183], v[66:69]
	v_mfma_f32_16x16x32_bf16 v[34:37], v[164:167], v[180:183], v[106:109]
	v_mfma_f32_16x16x32_bf16 v[66:69], v[126:129], v[190:193], v[110:113]
	v_mfma_f32_16x16x32_bf16 v[106:109], v[164:167], v[190:193], v[114:117]
	v_mfma_f32_16x16x32_bf16 v[22:25], v[126:129], v[198:201], v[22:25]
	v_mfma_f32_16x16x32_bf16 v[26:29], v[164:167], v[198:201], v[26:29]
	v_mfma_f32_16x16x32_bf16 v[14:17], v[136:139], v[176:179], v[14:17]
	v_mfma_f32_16x16x32_bf16 v[18:21], v[168:171], v[176:179], v[18:21]
	v_mfma_f32_16x16x32_bf16 v[30:33], v[136:139], v[184:187], v[30:33]
	v_mfma_f32_16x16x32_bf16 v[34:37], v[168:171], v[184:187], v[34:37]
	v_mfma_f32_16x16x32_bf16 v[66:69], v[136:139], v[194:197], v[66:69]
	v_mfma_f32_16x16x32_bf16 v[106:109], v[168:171], v[194:197], v[106:109]
	v_mfma_f32_16x16x32_bf16 v[22:25], v[136:139], v[202:205], v[22:25]
	v_mfma_f32_16x16x32_bf16 v[26:29], v[168:171], v[202:205], v[26:29]
	s_setprio 0
	s_barrier
; #define PG8_STAGE(bufoff, gbase, voff) do { _Pragma("unroll") for (int _i = 0; _i < 2; ++_i) \
;         __builtin_amdgcn_global_load_lds((const unsigned*)((const char*)(gbase) + (voff)[_i]), (LAS unsigned*)(lds + (bufoff) + ldsw + _i * 8192), 16, 0, 0); } while (0)
; #define PG8_LDA(dst, b, h) do { _Pragma("unroll") for (int m = 0; m < 4; ++m) _Pragma("unroll") for (int k = 0; k < 2; ++k) dst[m][k] = *(const LAS bf16x8*)(lds + PG8_SA(b, h) + aoff + m * 2048 + k * 1024); } while (0)
; #define PG8_LDB(dst, b, h) do { _Pragma("unroll") for (int n = 0; n < 2; ++n) _Pragma("unroll") for (int k = 0; k < 2; ++k) dst[n][k] = *(const LAS bf16x8*)(lds + PG8_SB(b, h) + boff + n * 2048 + k * 1024); } while (0)
; #define PG8_MMA(ai, bj, At, Bt) do { __builtin_amdgcn_s_setprio(1); _Pragma("unroll") for (int m = 0; m < 4; ++m) _Pragma("unroll") for (int n = 0; n < 2; ++n) _Pragma("unroll") for (int k = 0; k < 2; ++k) \
;         acc[ai][bj][m][n] = __builtin_amdgcn_mfma_f32_16x16x32_bf16(Bt[n][k], At[m][k], acc[ai][bj][m][n], 0, 0, 0); __builtin_amdgcn_s_setprio(0); } while (0)
; #define PG8_WAIT_V(n) asm volatile("s_waitcnt vmcnt(" #n ")" ::: "memory")
; #define PG8_WAIT_L(n) asm volatile("s_waitcnt lgkmcnt(" #n ")" ::: "memory")
; #define PG8_BAR __builtin_amdgcn_s_barrier()
; #define PG8_SCHED __builtin_amdgcn_sched_barrier(0)
; template <class Epi, class Sched>
; __device__ __forceinline__ void gemm_phase(LAS unsigned char* lds, const int tid, const char* Abase, const int K, const Sched& S, const Epi& E) {
;     ...
;             PG8_LDB(B0, 0, 0); PG8_LDB(B1, 0, 1); PG8_SCHED; PG8_LDA(At, 0, 0); PG8_STAGE(PG8_SA(1, 1), a1, vc[1]);
;             PG8_WAIT_V(8); PG8_WAIT_L(0); PG8_BAR; PG8_MMA(0, 0, At, B0); PG8_MMA(0, 1, At, B1); PG8_BAR; PG8_SCHED;
;             PG8_LDA(At, 0, 1); PG8_STAGE(PG8_SB(0, 0), b2, voffB); PG8_STAGE(PG8_SB(0, 1), b2 + hstep, voffB); PG8_STAGE(PG8_SA(0, 0), a2, w2[0]);
;             PG8_WAIT_V(8); PG8_WAIT_L(0); PG8_BAR; PG8_MMA(1, 0, At, B0); PG8_MMA(1, 1, At, B1); PG8_BAR; PG8_SCHED;
	ds_read_b128 v[136:139], v132
	ds_read_b128 v[110:113], v135
	ds_read_b128 v[114:117], v135 offset:1024
	ds_read_b128 v[118:121], v135 offset:2048
	ds_read_b128 v[122:125], v135 offset:3072
	ds_read_b128 v[126:129], v189
	ds_read_b128 v[164:167], v189 offset:1024
	ds_read_b128 v[168:171], v189 offset:2048
	ds_read_b128 v[172:175], v189 offset:3072
	s_mov_b32 m0, s35
	ds_read_b128 v[176:179], v134
	ds_read_b128 v[180:183], v134 offset:1024
	ds_read_b128 v[184:187], v134 offset:2048
	ds_read_b128 v[190:193], v134 offset:3072
	ds_read_b128 v[194:197], v134 offset:4096
	ds_read_b128 v[198:201], v134 offset:5120
	ds_read_b128 v[202:205], v134 offset:6144
	ds_read_b128 v[206:209], v134 offset:7168
	global_load_lds_dwordx4 v4, s[28:29]
	s_mov_b32 m0, s49
	s_nop 0
	global_load_lds_dwordx4 v5, s[28:29]
	s_waitcnt vmcnt(8)
	s_waitcnt lgkmcnt(0)
	s_barrier
	s_setprio 1
	s_waitcnt lgkmcnt(0)
	v_mfma_f32_16x16x32_bf16 v[2:5], v[110:113], v[176:179], v[70:73]
	v_mfma_f32_16x16x32_bf16 v[70:73], v[118:121], v[176:179], v[74:77]
	v_mfma_f32_16x16x32_bf16 v[74:77], v[110:113], v[184:187], v[78:81]
	v_mfma_f32_16x16x32_bf16 v[78:81], v[118:121], v[184:187], v[82:85]
	v_mfma_f32_16x16x32_bf16 v[82:85], v[110:113], v[194:197], v[86:89]
	v_mfma_f32_16x16x32_bf16 v[86:89], v[118:121], v[194:197], v[90:93]
	v_mfma_f32_16x16x32_bf16 v[90:93], v[110:113], v[202:205], v[94:97]
	v_mfma_f32_16x16x32_bf16 v[94:97], v[118:121], v[202:205], v[98:101]
	v_mfma_f32_16x16x32_bf16 v[2:5], v[114:117], v[180:183], v[2:5]
	v_mfma_f32_16x16x32_bf16 v[70:73], v[122:125], v[180:183], v[70:73]
	v_mfma_f32_16x16x32_bf16 v[74:77], v[114:117], v[190:193], v[74:77]
	v_mfma_f32_16x16x32_bf16 v[78:81], v[122:125], v[190:193], v[78:81]
	v_mfma_f32_16x16x32_bf16 v[82:85], v[114:117], v[198:201], v[82:85]
	v_mfma_f32_16x16x32_bf16 v[86:89], v[122:125], v[198:201], v[86:89]
	v_mfma_f32_16x16x32_bf16 v[90:93], v[114:117], v[206:209], v[90:93]
	v_mfma_f32_16x16x32_bf16 v[94:97], v[122:125], v[206:209], v[94:97]
	v_mfma_f32_16x16x32_bf16 v[38:41], v[168:171], v[176:179], v[38:41]
	v_mfma_f32_16x16x32_bf16 v[98:101], v[126:129], v[176:179], v[102:105]
	v_mfma_f32_16x16x32_bf16 v[176:179], v[172:175], v[180:183], v[38:41]
	v_mfma_f32_16x16x32_bf16 v[38:41], v[126:129], v[184:187], v[42:45]
	v_mfma_f32_16x16x32_bf16 v[42:45], v[164:167], v[190:193], v[38:41]
	v_mfma_f32_16x16x32_bf16 v[38:41], v[168:171], v[184:187], v[46:49]
	v_mfma_f32_16x16x32_bf16 v[46:49], v[172:175], v[190:193], v[38:41]
	v_mfma_f32_16x16x32_bf16 v[38:41], v[126:129], v[194:197], v[50:53]
	v_mfma_f32_16x16x32_bf16 v[50:53], v[164:167], v[198:201], v[38:41]
	v_mfma_f32_16x16x32_bf16 v[38:41], v[168:171], v[194:197], v[54:57]
	v_mfma_f32_16x16x32_bf16 v[54:57], v[172:175], v[198:201], v[38:41]
	v_mfma_f32_16x16x32_bf16 v[38:41], v[126:129], v[202:205], v[58:61]
	v_mfma_f32_16x16x32_bf16 v[58:61], v[164:167], v[206:209], v[38:41]
	v_mfma_f32_16x16x32_bf16 v[38:41], v[168:171], v[202:205], v[62:65]
	v_mfma_f32_16x16x32_bf16 v[62:65], v[172:175], v[206:209], v[38:41]
	v_mfma_f32_16x16x32_bf16 v[210:213], v[164:167], v[180:183], v[98:101]
	s_setprio 0
	s_barrier
	s_mov_b32 m0, s54
	v_lshl_add_u64 v[246:247], s[12:13], 0, v[0:1]
	s_add_u32 s56, s12, 0x10000
	s_nop 0
	ds_read_b128 v[38:41], v134 offset:16384
	ds_read_b128 v[98:101], v134 offset:17408
	ds_read_b128 v[102:105], v134 offset:18432
	ds_read_b128 v[180:183], v134 offset:19456
	ds_read_b128 v[184:187], v134 offset:20480
	ds_read_b128 v[190:193], v134 offset:21504
	ds_read_b128 v[194:197], v134 offset:22528
	ds_read_b128 v[198:201], v134 offset:23552
	global_load_lds_dwordx4 v[246:247], off
	v_lshl_add_u64 v[248:249], s[12:13], 0, v[130:131]
	s_mov_b32 m0, s50
	s_addc_u32 s57, s13, 0
	global_load_lds_dwordx4 v[248:249], off
	v_lshl_add_u64 v[202:203], s[56:57], 0, v[0:1]
	s_mov_b32 m0, s51
	s_nop 0
	global_load_lds_dwordx4 v[202:203], off
	v_lshl_add_u64 v[202:203], s[56:57], 0, v[130:131]
	s_mov_b32 m0, s52
	s_nop 0
	global_load_lds_dwordx4 v[202:203], off
	s_mov_b32 m0, s7
	s_nop 0
	global_load_lds_dwordx4 v136, s[14:15]
	s_mov_b32 m0, s33
	s_nop 0
	global_load_lds_dwordx4 v137, s[14:15]
	s_waitcnt vmcnt(8)
	s_waitcnt lgkmcnt(0)
	s_barrier
	s_setprio 1
	s_waitcnt lgkmcnt(0)
	v_mfma_f32_16x16x32_bf16 v[6:9], v[110:113], v[194:197], v[6:9]
	v_mfma_f32_16x16x32_bf16 v[10:13], v[118:121], v[194:197], v[10:13]
	v_mfma_f32_16x16x32_bf16 v[140:143], v[110:113], v[38:41], v[140:143]
	v_mfma_f32_16x16x32_bf16 v[144:147], v[118:121], v[38:41], v[144:147]
	v_mfma_f32_16x16x32_bf16 v[148:151], v[110:113], v[102:105], v[148:151]
	v_mfma_f32_16x16x32_bf16 v[152:155], v[118:121], v[102:105], v[152:155]
	v_mfma_f32_16x16x32_bf16 v[156:159], v[110:113], v[184:187], v[156:159]
	v_mfma_f32_16x16x32_bf16 v[160:163], v[118:121], v[184:187], v[160:163]
	v_mfma_f32_16x16x32_bf16 v[6:9], v[114:117], v[198:201], v[6:9]
	v_mfma_f32_16x16x32_bf16 v[10:13], v[122:125], v[198:201], v[10:13]
	v_mfma_f32_16x16x32_bf16 v[140:143], v[114:117], v[98:101], v[140:143]
	v_mfma_f32_16x16x32_bf16 v[144:147], v[122:125], v[98:101], v[144:147]
	v_mfma_f32_16x16x32_bf16 v[148:151], v[114:117], v[180:183], v[148:151]
	v_mfma_f32_16x16x32_bf16 v[152:155], v[122:125], v[180:183], v[152:155]
	v_mfma_f32_16x16x32_bf16 v[156:159], v[114:117], v[190:193], v[156:159]
	v_mfma_f32_16x16x32_bf16 v[160:163], v[122:125], v[190:193], v[160:163]
	v_mfma_f32_16x16x32_bf16 v[18:21], v[168:171], v[38:41], v[18:21]
	v_mfma_f32_16x16x32_bf16 v[202:205], v[172:175], v[98:101], v[18:21]
	v_mfma_f32_16x16x32_bf16 v[18:21], v[126:129], v[102:105], v[30:33]
	v_mfma_f32_16x16x32_bf16 v[30:33], v[164:167], v[180:183], v[18:21]
	v_mfma_f32_16x16x32_bf16 v[18:21], v[168:171], v[102:105], v[34:37]
	v_mfma_f32_16x16x32_bf16 v[180:183], v[172:175], v[180:183], v[18:21]
	v_mfma_f32_16x16x32_bf16 v[18:21], v[126:129], v[184:187], v[66:69]
	v_mfma_f32_16x16x32_bf16 v[206:209], v[164:167], v[190:193], v[18:21]
	v_mfma_f32_16x16x32_bf16 v[18:21], v[168:171], v[184:187], v[106:109]
	v_mfma_f32_16x16x32_bf16 v[14:17], v[126:129], v[38:41], v[14:17]
	v_mfma_f32_16x16x32_bf16 v[184:187], v[172:175], v[190:193], v[18:21]
	v_mfma_f32_16x16x32_bf16 v[18:21], v[126:129], v[194:197], v[22:25]
	v_mfma_f32_16x16x32_bf16 v[14:17], v[164:167], v[98:101], v[14:17]
	v_mfma_f32_16x16x32_bf16 v[164:167], v[164:167], v[198:201], v[18:21]
	v_mfma_f32_16x16x32_bf16 v[18:21], v[168:171], v[194:197], v[26:29]
	v_mfma_f32_16x16x32_bf16 v[168:171], v[172:175], v[198:201], v[18:21]
	s_setprio 0
	s_barrier
; #define PG8_STAGE(bufoff, gbase, voff) do { _Pragma("unroll") for (int _i = 0; _i < 2; ++_i) \
;         __builtin_amdgcn_global_load_lds((const unsigned*)((const char*)(gbase) + (voff)[_i]), (LAS unsigned*)(lds + (bufoff) + ldsw + _i * 8192), 16, 0, 0); } while (0)
; #define PG8_LDA(dst, b, h) do { _Pragma("unroll") for (int m = 0; m < 4; ++m) _Pragma("unroll") for (int k = 0; k < 2; ++k) dst[m][k] = *(const LAS bf16x8*)(lds + PG8_SA(b, h) + aoff + m * 2048 + k * 1024); } while (0)
; #define PG8_LDB(dst, b, h) do { _Pragma("unroll") for (int n = 0; n < 2; ++n) _Pragma("unroll") for (int k = 0; k < 2; ++k) dst[n][k] = *(const LAS bf16x8*)(lds + PG8_SB(b, h) + boff + n * 2048 + k * 1024); } while (0)
; #define PG8_MMA(ai, bj, At, Bt) do { __builtin_amdgcn_s_setprio(1); _Pragma("unroll") for (int m = 0; m < 4; ++m) _Pragma("unroll") for (int n = 0; n < 2; ++n) _Pragma("unroll") for (int k = 0; k < 2; ++k) \
;         acc[ai][bj][m][n] = __builtin_amdgcn_mfma_f32_16x16x32_bf16(Bt[n][k], At[m][k], acc[ai][bj][m][n], 0, 0, 0); __builtin_amdgcn_s_setprio(0); } while (0)
; #define PG8_WAIT_V(n) asm volatile("s_waitcnt vmcnt(" #n ")" ::: "memory")
; #define PG8_WAIT_L(n) asm volatile("s_waitcnt lgkmcnt(" #n ")" ::: "memory")
; #define PG8_BAR __builtin_amdgcn_s_barrier()
; #define PG8_SCHED __builtin_amdgcn_sched_barrier(0)
; template <class Epi, class Sched>
; __device__ __forceinline__ void gemm_phase(LAS unsigned char* lds, const int tid, const char* Abase, const int K, const Sched& S, const Epi& E) {
;     ...
;             PG8_LDB(B0, 1, 0); PG8_LDB(B1, 1, 1); PG8_SCHED; PG8_LDA(At, 1, 0); PG8_STAGE(PG8_SA(0, 1), a2, w2[1]);
;             PG8_WAIT_V(8); PG8_WAIT_L(0); PG8_BAR; PG8_MMA(0, 0, At, B0); PG8_MMA(0, 1, At, B1); PG8_BAR; PG8_SCHED;
;             PG8_LDA(At, 1, 1); PG8_STAGE(PG8_SB(1, 0), b3, voffB); PG8_STAGE(PG8_SB(1, 1), b3 + hstep, voffB); PG8_STAGE(PG8_SA(1, 0), a3, w2[0]);
;             PG8_WAIT_V(8); PG8_WAIT_L(0); PG8_BAR; PG8_MMA(1, 0, At, B0); PG8_MMA(1, 1, At, B1); PG8_BAR; PG8_SCHED;
;         }
;         if (wr == 0) PG8_BAR;
	ds_read_b128 v[26:29], v214
	ds_read_b128 v[172:175], v214 offset:1024
	ds_read_b128 v[190:193], v214 offset:2048
	ds_read_b128 v[194:197], v214 offset:3072
	ds_read_b128 v[198:201], v222
	ds_read_b128 v[214:217], v222 offset:1024
	ds_read_b128 v[218:221], v222 offset:2048
	ds_read_b128 v[222:225], v222 offset:3072
	s_mov_b32 m0, s38
	ds_read_b128 v[18:21], v134 offset:32768
	ds_read_b128 v[22:25], v134 offset:33792
	ds_read_b128 v[110:113], v134 offset:34816
	ds_read_b128 v[226:229], v134 offset:35840
	ds_read_b128 v[230:233], v134 offset:36864
	ds_read_b128 v[234:237], v134 offset:37888
	ds_read_b128 v[238:241], v134 offset:38912
	ds_read_b128 v[242:245], v134 offset:39936
	global_load_lds_dwordx4 v138, s[14:15]
	s_mov_b32 m0, s39
	s_nop 0
	global_load_lds_dwordx4 v139, s[14:15]
	s_waitcnt vmcnt(8)
	s_waitcnt lgkmcnt(0)
	s_barrier
	s_setprio 1
	s_waitcnt lgkmcnt(0)
	v_mfma_f32_16x16x32_bf16 v[2:5], v[26:29], v[18:21], v[2:5]
	v_mfma_f32_16x16x32_bf16 v[114:117], v[172:175], v[22:25], v[2:5]
	v_mfma_f32_16x16x32_bf16 v[2:5], v[190:193], v[18:21], v[70:73]
	v_mfma_f32_16x16x32_bf16 v[118:121], v[194:197], v[22:25], v[2:5]
	v_mfma_f32_16x16x32_bf16 v[2:5], v[26:29], v[110:113], v[74:77]
	v_mfma_f32_16x16x32_bf16 v[98:101], v[172:175], v[226:229], v[2:5]
	v_mfma_f32_16x16x32_bf16 v[2:5], v[190:193], v[110:113], v[78:81]
	v_mfma_f32_16x16x32_bf16 v[102:105], v[194:197], v[226:229], v[2:5]
	v_mfma_f32_16x16x32_bf16 v[2:5], v[26:29], v[230:233], v[82:85]
	v_mfma_f32_16x16x32_bf16 v[66:69], v[172:175], v[234:237], v[2:5]
	v_mfma_f32_16x16x32_bf16 v[2:5], v[190:193], v[230:233], v[86:89]
	v_mfma_f32_16x16x32_bf16 v[70:73], v[194:197], v[234:237], v[2:5]
	v_mfma_f32_16x16x32_bf16 v[2:5], v[26:29], v[238:241], v[90:93]
	v_mfma_f32_16x16x32_bf16 v[34:37], v[172:175], v[242:245], v[2:5]
	v_mfma_f32_16x16x32_bf16 v[2:5], v[190:193], v[238:241], v[94:97]
	v_mfma_f32_16x16x32_bf16 v[38:41], v[194:197], v[242:245], v[2:5]
	v_mfma_f32_16x16x32_bf16 v[2:5], v[198:201], v[18:21], v[210:213]
	v_mfma_f32_16x16x32_bf16 v[122:125], v[214:217], v[22:25], v[2:5]
	v_mfma_f32_16x16x32_bf16 v[2:5], v[218:221], v[18:21], v[176:179]
	v_mfma_f32_16x16x32_bf16 v[126:129], v[222:225], v[22:25], v[2:5]
	v_mfma_f32_16x16x32_bf16 v[2:5], v[198:201], v[110:113], v[42:45]
	v_mfma_f32_16x16x32_bf16 v[106:109], v[214:217], v[226:229], v[2:5]
	v_mfma_f32_16x16x32_bf16 v[2:5], v[218:221], v[110:113], v[46:49]
	v_mfma_f32_16x16x32_bf16 v[110:113], v[222:225], v[226:229], v[2:5]
	v_mfma_f32_16x16x32_bf16 v[2:5], v[198:201], v[230:233], v[50:53]
	v_mfma_f32_16x16x32_bf16 v[74:77], v[214:217], v[234:237], v[2:5]
	v_mfma_f32_16x16x32_bf16 v[2:5], v[218:221], v[230:233], v[54:57]
	v_mfma_f32_16x16x32_bf16 v[78:81], v[222:225], v[234:237], v[2:5]
	v_mfma_f32_16x16x32_bf16 v[2:5], v[198:201], v[238:241], v[58:61]
	v_mfma_f32_16x16x32_bf16 v[42:45], v[214:217], v[242:245], v[2:5]
	v_mfma_f32_16x16x32_bf16 v[2:5], v[218:221], v[238:241], v[62:65]
	v_mfma_f32_16x16x32_bf16 v[46:49], v[222:225], v[242:245], v[2:5]
	s_setprio 0
	s_barrier
	s_mov_b32 m0, s55
	s_nop 3
	v_lshl_add_u64 v[2:3], v[246:247], 0, s[24:25]
	s_add_u32 s50, s12, 0x10080
	ds_read_b128 v[58:61], v134 offset:49152
	ds_read_b128 v[62:65], v134 offset:50176
	ds_read_b128 v[176:179], v134 offset:51200
	ds_read_b128 v[210:213], v134 offset:52224
	ds_read_b128 v[226:229], v134 offset:53248
	ds_read_b128 v[230:233], v134 offset:54272
	ds_read_b128 v[234:237], v134 offset:55296
	ds_read_b128 v[238:241], v134 offset:56320
	global_load_lds_dwordx4 v[2:3], off
	v_lshl_add_u64 v[2:3], v[248:249], 0, s[24:25]
	s_mov_b32 m0, s53
	s_addc_u32 s51, s13, 0
	global_load_lds_dwordx4 v[2:3], off
	v_lshl_add_u64 v[2:3], s[50:51], 0, v[0:1]
	s_mov_b32 m0, s36
	s_nop 0
	global_load_lds_dwordx4 v[2:3], off
	v_lshl_add_u64 v[2:3], s[50:51], 0, v[130:131]
	s_mov_b32 m0, s37
	s_nop 0
	global_load_lds_dwordx4 v[2:3], off
	s_mov_b32 m0, s42
	s_nop 0
	global_load_lds_dwordx4 v136, s[20:21]
	s_mov_b32 m0, s43
	s_nop 0
	global_load_lds_dwordx4 v137, s[20:21]
	s_waitcnt vmcnt(8)
	s_waitcnt lgkmcnt(0)
	s_barrier
	s_setprio 1
	s_waitcnt lgkmcnt(0)
	v_mfma_f32_16x16x32_bf16 v[2:5], v[26:29], v[58:61], v[140:143]
	v_mfma_f32_16x16x32_bf16 v[82:85], v[172:175], v[62:65], v[2:5]
	v_mfma_f32_16x16x32_bf16 v[2:5], v[190:193], v[58:61], v[144:147]
	v_mfma_f32_16x16x32_bf16 v[86:89], v[194:197], v[62:65], v[2:5]
	v_mfma_f32_16x16x32_bf16 v[2:5], v[26:29], v[176:179], v[148:151]
	v_mfma_f32_16x16x32_bf16 v[50:53], v[172:175], v[210:213], v[2:5]
	v_mfma_f32_16x16x32_bf16 v[2:5], v[190:193], v[176:179], v[152:155]
	v_mfma_f32_16x16x32_bf16 v[54:57], v[194:197], v[210:213], v[2:5]
	v_mfma_f32_16x16x32_bf16 v[2:5], v[26:29], v[226:229], v[156:159]
	v_mfma_f32_16x16x32_bf16 v[18:21], v[172:175], v[230:233], v[2:5]
	v_mfma_f32_16x16x32_bf16 v[2:5], v[190:193], v[226:229], v[160:163]
	v_mfma_f32_16x16x32_bf16 v[22:25], v[194:197], v[230:233], v[2:5]
	v_mfma_f32_16x16x32_bf16 v[2:5], v[26:29], v[234:237], v[6:9]
	v_mfma_f32_16x16x32_bf16 v[6:9], v[190:193], v[234:237], v[10:13]
	v_mfma_f32_16x16x32_bf16 v[2:5], v[172:175], v[238:241], v[2:5]
	v_mfma_f32_16x16x32_bf16 v[6:9], v[194:197], v[238:241], v[6:9]
	v_mfma_f32_16x16x32_bf16 v[10:13], v[198:201], v[58:61], v[14:17]
	v_mfma_f32_16x16x32_bf16 v[90:93], v[214:217], v[62:65], v[10:13]
	v_mfma_f32_16x16x32_bf16 v[10:13], v[218:221], v[58:61], v[202:205]
	v_mfma_f32_16x16x32_bf16 v[94:97], v[222:225], v[62:65], v[10:13]
	v_mfma_f32_16x16x32_bf16 v[10:13], v[198:201], v[176:179], v[30:33]
	v_mfma_f32_16x16x32_bf16 v[58:61], v[214:217], v[210:213], v[10:13]
	v_mfma_f32_16x16x32_bf16 v[10:13], v[218:221], v[176:179], v[180:183]
	v_mfma_f32_16x16x32_bf16 v[62:65], v[222:225], v[210:213], v[10:13]
	v_mfma_f32_16x16x32_bf16 v[10:13], v[198:201], v[226:229], v[206:209]
	v_mfma_f32_16x16x32_bf16 v[26:29], v[214:217], v[230:233], v[10:13]
	v_mfma_f32_16x16x32_bf16 v[10:13], v[218:221], v[226:229], v[184:187]
	v_mfma_f32_16x16x32_bf16 v[30:33], v[222:225], v[230:233], v[10:13]
	v_mfma_f32_16x16x32_bf16 v[10:13], v[198:201], v[234:237], v[164:167]
	v_mfma_f32_16x16x32_bf16 v[14:17], v[218:221], v[234:237], v[168:171]
	v_mfma_f32_16x16x32_bf16 v[10:13], v[214:217], v[238:241], v[10:13]
	v_mfma_f32_16x16x32_bf16 v[14:17], v[222:225], v[238:241], v[14:17]
	s_setprio 0
	s_barrier
	s_andn2_b64 vcc, exec, s[22:23]
	s_cbranch_vccnz .LBB0_1231
	s_barrier

; #define PG8_STAGE(bufoff, gbase, voff) do { _Pragma("unroll") for (int _i = 0; _i < 2; ++_i) \
;         __builtin_amdgcn_global_load_lds((const unsigned*)((const char*)(gbase) + (voff)[_i]), (LAS unsigned*)(lds + (bufoff) + ldsw + _i * 8192), 16, 0, 0); } while (0)
; #define PG8_LDA(dst, b, h) do { _Pragma("unroll") for (int m = 0; m < 4; ++m) _Pragma("unroll") for (int k = 0; k < 2; ++k) dst[m][k] = *(const LAS bf16x8*)(lds + PG8_SA(b, h) + aoff + m * 2048 + k * 1024); } while (0)
; #define PG8_LDB(dst, b, h) do { _Pragma("unroll") for (int n = 0; n < 2; ++n) _Pragma("unroll") for (int k = 0; k < 2; ++k) dst[n][k] = *(const LAS bf16x8*)(lds + PG8_SB(b, h) + boff + n * 2048 + k * 1024); } while (0)
; #define PG8_WAIT_V(n) asm volatile("s_waitcnt vmcnt(" #n ")" ::: "memory")
; template <class Epi, class Sched>
; __device__ __forceinline__ void gemm_phase(LAS unsigned char* lds, const int tid, const char* Abase, const int K, const Sched& S, const Epi& E) {
;     ...
;           if (has_next) { PG8_AOFFS(vn, nxt); nB = S.b_tile(nxt); *vslot = (u32x4){vn[0][0], vn[0][1], vn[1][0], vn[1][1]}; }
;           else *vslot = (u32x4){vc[0][0], vc[0][1], vc[1][0], vc[1][1]}; }
;         for (int t = 0; t < nt; t += 2) {
;             if constexpr (Epi::MID) { if (t == (nt >> 1)) E.mid(acc, ui, wr, fr, lds); }
;             const bool last = (t == nt - 2);
;             const char* a1 = Abase + (size_t)(t + 1) * kstep;
;             const char* a2 = last ? Abase : Abase + (size_t)(t + 2) * kstep; const char* b2 = last ? nB : cB + (size_t)(t + 2) * kstep;
;             const char* a3 = a2 + kstep; const char* b3 = b2 + kstep;
;             unsigned w2[2][2];
;             if (last) { const u32x4 q = *vslot; w2[0][0] = q.x; w2[0][1] = q.y; w2[1][0] = q.z; w2[1][1] = q.w; }
;             else { w2[0][0] = vc[0][0]; w2[0][1] = vc[0][1]; w2[1][0] = vc[1][0]; w2[1][1] = vc[1][1]; }
;             PG8_LDB(B0, 0, 0); PG8_LDB(B1, 0, 1); PG8_SCHED; PG8_LDA(At, 0, 0); PG8_STAGE(PG8_SA(1, 1), a1, vc[1]);
;             PG8_WAIT_V(8); PG8_WAIT_L(0); PG8_BAR; PG8_MMA(0, 0, At, B0); PG8_MMA(0, 1, At, B1); PG8_BAR; PG8_SCHED;
;             PG8_LDA(At, 0, 1); PG8_STAGE(PG8_SB(0, 0), b2, voffB); PG8_STAGE(PG8_SB(0, 1), b2 + hstep, voffB); PG8_STAGE(PG8_SA(0, 0), a2, w2[0]);
;             PG8_WAIT_V(8); PG8_WAIT_L(0); PG8_BAR; PG8_MMA(1, 0, At, B0); PG8_MMA(1, 1, At, B1); PG8_BAR; PG8_SCHED;
.LBB0_1251:
	s_add_i32 s52, 0, 0x10000
	s_add_i32 s49, 0, 0x14000
	ds_write_b128 v132, v[6:9]
	v_add_u32_e32 v135, s52, v133
	v_add_u32_e32 v189, s49, v133
	ds_read_b128 v[6:9], v135
	ds_read_b128 v[10:13], v135 offset:1024
	ds_read_b128 v[14:17], v135 offset:2048
	ds_read_b128 v[18:21], v135 offset:3072
	ds_read_b128 v[22:25], v189
	ds_read_b128 v[26:29], v189 offset:1024
	ds_read_b128 v[30:33], v189 offset:2048
	ds_read_b128 v[34:37], v189 offset:3072
	v_mov_b32_e32 v252, 1
	s_add_i32 s35, s7, 0xc000
	s_mov_b32 m0, s35
	s_add_i32 s47, s7, 0xe000
	ds_read_b128 v[38:41], v134
	ds_read_b128 v[42:45], v134 offset:1024
	ds_read_b128 v[46:49], v134 offset:2048
	ds_read_b128 v[50:53], v134 offset:3072
	ds_read_b128 v[54:57], v134 offset:4096
	ds_read_b128 v[58:61], v134 offset:5120
	ds_read_b128 v[62:65], v134 offset:6144
	ds_read_b128 v[66:69], v134 offset:7168
	global_load_lds_dwordx4 v4, s[20:21]
	s_mov_b32 m0, s47
	s_nop 0
	global_load_lds_dwordx4 v5, s[20:21]
	s_waitcnt vmcnt(8)
	s_waitcnt lgkmcnt(0)
	s_barrier
	s_setprio 1
	s_waitcnt lgkmcnt(0)
	v_mfma_f32_16x16x32_bf16 v[70:73], v[6:9], v[38:41], 0
	v_mfma_f32_16x16x32_bf16 v[74:77], v[14:17], v[38:41], 0
	v_mfma_f32_16x16x32_bf16 v[78:81], v[6:9], v[46:49], 0
	v_mfma_f32_16x16x32_bf16 v[82:85], v[14:17], v[46:49], 0
	v_mfma_f32_16x16x32_bf16 v[86:89], v[6:9], v[54:57], 0
	v_mfma_f32_16x16x32_bf16 v[90:93], v[14:17], v[54:57], 0
	v_mfma_f32_16x16x32_bf16 v[94:97], v[6:9], v[62:65], 0
	v_mfma_f32_16x16x32_bf16 v[98:101], v[14:17], v[62:65], 0
	v_mfma_f32_16x16x32_bf16 v[70:73], v[10:13], v[42:45], v[70:73]
	v_mfma_f32_16x16x32_bf16 v[74:77], v[18:21], v[42:45], v[74:77]
	v_mfma_f32_16x16x32_bf16 v[78:81], v[10:13], v[50:53], v[78:81]
	v_mfma_f32_16x16x32_bf16 v[82:85], v[18:21], v[50:53], v[82:85]
	v_mfma_f32_16x16x32_bf16 v[86:89], v[10:13], v[58:61], v[86:89]
	v_mfma_f32_16x16x32_bf16 v[90:93], v[18:21], v[58:61], v[90:93]
	v_mfma_f32_16x16x32_bf16 v[94:97], v[10:13], v[66:69], v[94:97]
	v_mfma_f32_16x16x32_bf16 v[98:101], v[18:21], v[66:69], v[98:101]
	v_mfma_f32_16x16x32_bf16 v[102:105], v[22:25], v[38:41], 0
	v_mfma_f32_16x16x32_bf16 v[38:41], v[30:33], v[38:41], 0
	v_mfma_f32_16x16x32_bf16 v[102:105], v[26:29], v[42:45], v[102:105]
	v_mfma_f32_16x16x32_bf16 v[38:41], v[34:37], v[42:45], v[38:41]
	v_mfma_f32_16x16x32_bf16 v[42:45], v[22:25], v[46:49], 0
	v_mfma_f32_16x16x32_bf16 v[46:49], v[30:33], v[46:49], 0
	v_mfma_f32_16x16x32_bf16 v[42:45], v[26:29], v[50:53], v[42:45]
	v_mfma_f32_16x16x32_bf16 v[46:49], v[34:37], v[50:53], v[46:49]
	v_mfma_f32_16x16x32_bf16 v[50:53], v[22:25], v[54:57], 0
	v_mfma_f32_16x16x32_bf16 v[54:57], v[30:33], v[54:57], 0
	v_mfma_f32_16x16x32_bf16 v[50:53], v[26:29], v[58:61], v[50:53]
	v_mfma_f32_16x16x32_bf16 v[54:57], v[34:37], v[58:61], v[54:57]
	v_mfma_f32_16x16x32_bf16 v[58:61], v[22:25], v[62:65], 0
	v_mfma_f32_16x16x32_bf16 v[62:65], v[30:33], v[62:65], 0
	v_mfma_f32_16x16x32_bf16 v[58:61], v[26:29], v[66:69], v[58:61]
	v_mfma_f32_16x16x32_bf16 v[62:65], v[34:37], v[66:69], v[62:65]
	s_setprio 0
	s_barrier
	v_lshl_add_u64 v[206:207], s[36:37], 0, v[0:1]
	s_mov_b64 s[50:51], 0x100
	s_add_i32 s52, s52, s6
	v_lshl_add_u64 v[140:141], v[206:207], 0, s[50:51]
	s_mov_b32 m0, s52
	v_lshl_add_u64 v[208:209], s[36:37], 0, v[130:131]
	s_add_i32 s48, s52, 0x2000
	ds_read_b128 v[66:69], v134 offset:16384
	ds_read_b128 v[106:109], v134 offset:17408
	ds_read_b128 v[110:113], v134 offset:18432
	ds_read_b128 v[114:117], v134 offset:19456
	ds_read_b128 v[118:121], v134 offset:20480
	ds_read_b128 v[122:125], v134 offset:21504
	ds_read_b128 v[126:129], v134 offset:22528
	ds_read_b128 v[136:139], v134 offset:23552
	global_load_lds_dwordx4 v[140:141], off
	v_lshl_add_u64 v[140:141], v[208:209], 0, s[50:51]
	s_add_u32 s50, s36, 0x10100
	s_mov_b32 m0, s48
	s_addc_u32 s51, s37, 0
	s_add_i32 s49, s49, s6
	global_load_lds_dwordx4 v[140:141], off
	v_lshl_add_u64 v[140:141], s[50:51], 0, v[0:1]
	s_mov_b32 m0, s49
	s_nop 0
	global_load_lds_dwordx4 v[140:141], off
	v_lshl_add_u64 v[140:141], s[50:51], 0, v[130:131]
	s_add_i32 s50, s49, 0x2000
	s_mov_b32 m0, s50
	s_nop 0
	global_load_lds_dwordx4 v[140:141], off
	s_mov_b32 m0, s7
	s_nop 0
	global_load_lds_dwordx4 v2, s[26:27]
	s_mov_b32 m0, s33
	s_nop 0
	global_load_lds_dwordx4 v3, s[26:27]
	s_waitcnt vmcnt(8)
	s_waitcnt lgkmcnt(0)
	s_barrier
	s_setprio 1
	s_waitcnt lgkmcnt(0)
	v_mfma_f32_16x16x32_bf16 v[140:143], v[6:9], v[66:69], 0
	v_mfma_f32_16x16x32_bf16 v[148:151], v[6:9], v[110:113], 0
	v_mfma_f32_16x16x32_bf16 v[156:159], v[6:9], v[118:121], 0
	v_mfma_f32_16x16x32_bf16 v[6:9], v[6:9], v[126:129], 0
	v_mfma_f32_16x16x32_bf16 v[140:143], v[10:13], v[106:109], v[140:143]
	v_mfma_f32_16x16x32_bf16 v[148:151], v[10:13], v[114:117], v[148:151]
	v_mfma_f32_16x16x32_bf16 v[156:159], v[10:13], v[122:125], v[156:159]
	v_mfma_f32_16x16x32_bf16 v[6:9], v[10:13], v[136:139], v[6:9]
	v_mfma_f32_16x16x32_bf16 v[10:13], v[14:17], v[126:129], 0
	v_mfma_f32_16x16x32_bf16 v[144:147], v[14:17], v[66:69], 0
	v_mfma_f32_16x16x32_bf16 v[152:155], v[14:17], v[110:113], 0
	v_mfma_f32_16x16x32_bf16 v[160:163], v[14:17], v[118:121], 0
	v_mfma_f32_16x16x32_bf16 v[10:13], v[18:21], v[136:139], v[10:13]
	v_mfma_f32_16x16x32_bf16 v[144:147], v[18:21], v[106:109], v[144:147]
	v_mfma_f32_16x16x32_bf16 v[152:155], v[18:21], v[114:117], v[152:155]
	v_mfma_f32_16x16x32_bf16 v[160:163], v[18:21], v[122:125], v[160:163]
	v_mfma_f32_16x16x32_bf16 v[14:17], v[22:25], v[66:69], 0
	v_mfma_f32_16x16x32_bf16 v[18:21], v[30:33], v[66:69], 0
	v_mfma_f32_16x16x32_bf16 v[14:17], v[26:29], v[106:109], v[14:17]
	v_mfma_f32_16x16x32_bf16 v[18:21], v[34:37], v[106:109], v[18:21]
	v_mfma_f32_16x16x32_bf16 v[66:69], v[22:25], v[110:113], 0
	v_mfma_f32_16x16x32_bf16 v[106:109], v[30:33], v[110:113], 0
	v_mfma_f32_16x16x32_bf16 v[110:113], v[22:25], v[118:121], 0
	v_mfma_f32_16x16x32_bf16 v[22:25], v[22:25], v[126:129], 0
	v_mfma_f32_16x16x32_bf16 v[66:69], v[26:29], v[114:117], v[66:69]
	v_mfma_f32_16x16x32_bf16 v[106:109], v[34:37], v[114:117], v[106:109]
	v_mfma_f32_16x16x32_bf16 v[110:113], v[26:29], v[122:125], v[110:113]
	v_mfma_f32_16x16x32_bf16 v[114:117], v[30:33], v[118:121], 0
	v_mfma_f32_16x16x32_bf16 v[22:25], v[26:29], v[136:139], v[22:25]
	v_mfma_f32_16x16x32_bf16 v[26:29], v[30:33], v[126:129], 0
	v_mfma_f32_16x16x32_bf16 v[114:117], v[34:37], v[122:125], v[114:117]
	v_mfma_f32_16x16x32_bf16 v[26:29], v[34:37], v[136:139], v[26:29]
	s_setprio 0
	s_barrier
; #define PG8_STAGE(bufoff, gbase, voff) do { _Pragma("unroll") for (int _i = 0; _i < 2; ++_i) \
;         __builtin_amdgcn_global_load_lds((const unsigned*)((const char*)(gbase) + (voff)[_i]), (LAS unsigned*)(lds + (bufoff) + ldsw + _i * 8192), 16, 0, 0); } while (0)
; #define PG8_LDA(dst, b, h) do { _Pragma("unroll") for (int m = 0; m < 4; ++m) _Pragma("unroll") for (int k = 0; k < 2; ++k) dst[m][k] = *(const LAS bf16x8*)(lds + PG8_SA(b, h) + aoff + m * 2048 + k * 1024); } while (0)
; #define PG8_LDB(dst, b, h) do { _Pragma("unroll") for (int n = 0; n < 2; ++n) _Pragma("unroll") for (int k = 0; k < 2; ++k) dst[n][k] = *(const LAS bf16x8*)(lds + PG8_SB(b, h) + boff + n * 2048 + k * 1024); } while (0)
; #define PG8_MMA(ai, bj, At, Bt) do { __builtin_amdgcn_s_setprio(1); _Pragma("unroll") for (int m = 0; m < 4; ++m) _Pragma("unroll") for (int n = 0; n < 2; ++n) _Pragma("unroll") for (int k = 0; k < 2; ++k) \
;         acc[ai][bj][m][n] = __builtin_amdgcn_mfma_f32_16x16x32_bf16(Bt[n][k], At[m][k], acc[ai][bj][m][n], 0, 0, 0); __builtin_amdgcn_s_setprio(0); } while (0)
; #define PG8_WAIT_V(n) asm volatile("s_waitcnt vmcnt(" #n ")" ::: "memory")
; #define PG8_WAIT_L(n) asm volatile("s_waitcnt lgkmcnt(" #n ")" ::: "memory")
; #define PG8_BAR __builtin_amdgcn_s_barrier()
; #define PG8_SCHED __builtin_amdgcn_sched_barrier(0)
; template <class Epi, class Sched>
; __device__ __forceinline__ void gemm_phase(LAS unsigned char* lds, const int tid, const char* Abase, const int K, const Sched& S, const Epi& E) {
;     ...
;             PG8_LDB(B0, 1, 0); PG8_LDB(B1, 1, 1); PG8_SCHED; PG8_LDA(At, 1, 0); PG8_STAGE(PG8_SA(0, 1), a2, w2[1]);
;             PG8_WAIT_V(8); PG8_WAIT_L(0); PG8_BAR; PG8_MMA(0, 0, At, B0); PG8_MMA(0, 1, At, B1); PG8_BAR; PG8_SCHED;
;             PG8_LDA(At, 1, 1); PG8_STAGE(PG8_SB(1, 0), b3, voffB); PG8_STAGE(PG8_SB(1, 1), b3 + hstep, voffB); PG8_STAGE(PG8_SA(1, 0), a3, w2[0]);
;             PG8_WAIT_V(8); PG8_WAIT_L(0); PG8_BAR; PG8_MMA(1, 0, At, B0); PG8_MMA(1, 1, At, B1); PG8_BAR; PG8_SCHED;
	s_add_i32 s53, 0, 0x18000
	s_add_i32 s56, 0, 0x1c000
	v_add_u32_e32 v214, s53, v133
	v_add_u32_e32 v222, s56, v133
	ds_read_b128 v[30:33], v214
	ds_read_b128 v[34:37], v214 offset:1024
	ds_read_b128 v[118:121], v214 offset:2048
	ds_read_b128 v[122:125], v214 offset:3072
	ds_read_b128 v[126:129], v222
	ds_read_b128 v[136:139], v222 offset:1024
	ds_read_b128 v[164:167], v222 offset:2048
	ds_read_b128 v[168:171], v222 offset:3072
	s_mov_b32 m0, s38
	ds_read_b128 v[172:175], v134 offset:32768
	ds_read_b128 v[176:179], v134 offset:33792
	ds_read_b128 v[180:183], v134 offset:34816
	ds_read_b128 v[184:187], v134 offset:35840
	ds_read_b128 v[190:193], v134 offset:36864
	ds_read_b128 v[194:197], v134 offset:37888
	ds_read_b128 v[198:201], v134 offset:38912
	ds_read_b128 v[202:205], v134 offset:39936
	global_load_lds_dwordx4 v4, s[26:27]
	s_mov_b32 m0, s39
	s_nop 0
	global_load_lds_dwordx4 v5, s[26:27]
	s_waitcnt vmcnt(8)
	s_waitcnt lgkmcnt(0)
	s_barrier
	s_setprio 1
	s_waitcnt lgkmcnt(0)
	v_mfma_f32_16x16x32_bf16 v[70:73], v[30:33], v[172:175], v[70:73]
	v_mfma_f32_16x16x32_bf16 v[74:77], v[118:121], v[172:175], v[74:77]
	v_mfma_f32_16x16x32_bf16 v[78:81], v[30:33], v[180:183], v[78:81]
	v_mfma_f32_16x16x32_bf16 v[82:85], v[118:121], v[180:183], v[82:85]
	v_mfma_f32_16x16x32_bf16 v[86:89], v[30:33], v[190:193], v[86:89]
	v_mfma_f32_16x16x32_bf16 v[90:93], v[118:121], v[190:193], v[90:93]
	v_mfma_f32_16x16x32_bf16 v[94:97], v[30:33], v[198:201], v[94:97]
	v_mfma_f32_16x16x32_bf16 v[98:101], v[118:121], v[198:201], v[98:101]
	v_mfma_f32_16x16x32_bf16 v[70:73], v[34:37], v[176:179], v[70:73]
	v_mfma_f32_16x16x32_bf16 v[74:77], v[122:125], v[176:179], v[74:77]
	v_mfma_f32_16x16x32_bf16 v[78:81], v[34:37], v[184:187], v[78:81]
	v_mfma_f32_16x16x32_bf16 v[82:85], v[122:125], v[184:187], v[82:85]
	v_mfma_f32_16x16x32_bf16 v[86:89], v[34:37], v[194:197], v[86:89]
	v_mfma_f32_16x16x32_bf16 v[90:93], v[122:125], v[194:197], v[90:93]
	v_mfma_f32_16x16x32_bf16 v[94:97], v[34:37], v[202:205], v[94:97]
	v_mfma_f32_16x16x32_bf16 v[98:101], v[122:125], v[202:205], v[98:101]
	v_mfma_f32_16x16x32_bf16 v[102:105], v[126:129], v[172:175], v[102:105]
	v_mfma_f32_16x16x32_bf16 v[38:41], v[164:167], v[172:175], v[38:41]
	v_mfma_f32_16x16x32_bf16 v[42:45], v[126:129], v[180:183], v[42:45]
	v_mfma_f32_16x16x32_bf16 v[46:49], v[164:167], v[180:183], v[46:49]
	v_mfma_f32_16x16x32_bf16 v[50:53], v[126:129], v[190:193], v[50:53]
	v_mfma_f32_16x16x32_bf16 v[54:57], v[164:167], v[190:193], v[54:57]
	v_mfma_f32_16x16x32_bf16 v[58:61], v[126:129], v[198:201], v[58:61]
	v_mfma_f32_16x16x32_bf16 v[62:65], v[164:167], v[198:201], v[62:65]
	v_mfma_f32_16x16x32_bf16 v[102:105], v[136:139], v[176:179], v[102:105]
	v_mfma_f32_16x16x32_bf16 v[38:41], v[168:171], v[176:179], v[38:41]
	v_mfma_f32_16x16x32_bf16 v[42:45], v[136:139], v[184:187], v[42:45]
	v_mfma_f32_16x16x32_bf16 v[46:49], v[168:171], v[184:187], v[46:49]
	v_mfma_f32_16x16x32_bf16 v[50:53], v[136:139], v[194:197], v[50:53]
	v_mfma_f32_16x16x32_bf16 v[54:57], v[168:171], v[194:197], v[54:57]
	v_mfma_f32_16x16x32_bf16 v[58:61], v[136:139], v[202:205], v[58:61]
	v_mfma_f32_16x16x32_bf16 v[62:65], v[168:171], v[202:205], v[62:65]
	s_setprio 0
	s_barrier
	s_mov_b64 s[54:55], 0x180
	s_add_i32 s53, s53, s6
	v_lshl_add_u64 v[206:207], v[206:207], 0, s[54:55]
	s_mov_b32 m0, s53
	s_add_i32 s51, s53, 0x2000
	ds_read_b128 v[172:175], v134 offset:49152
	ds_read_b128 v[176:179], v134 offset:50176
	ds_read_b128 v[180:183], v134 offset:51200
	ds_read_b128 v[184:187], v134 offset:52224
	ds_read_b128 v[190:193], v134 offset:53248
	ds_read_b128 v[194:197], v134 offset:54272
	ds_read_b128 v[198:201], v134 offset:55296
	ds_read_b128 v[202:205], v134 offset:56320
	global_load_lds_dwordx4 v[206:207], off
	v_lshl_add_u64 v[206:207], v[208:209], 0, s[54:55]
	s_add_u32 s54, s36, 0x10180
	s_mov_b32 m0, s51
	s_addc_u32 s55, s37, 0
	s_add_i32 s36, s56, s6
	global_load_lds_dwordx4 v[206:207], off
	v_lshl_add_u64 v[206:207], s[54:55], 0, v[0:1]
	s_mov_b32 m0, s36
	s_add_i32 s37, s36, 0x2000
	global_load_lds_dwordx4 v[206:207], off
	v_lshl_add_u64 v[206:207], s[54:55], 0, v[130:131]
	s_mov_b32 m0, s37
	s_nop 0
	global_load_lds_dwordx4 v[206:207], off
	s_mov_b32 m0, s42
	s_nop 0
	global_load_lds_dwordx4 v2, s[28:29]
	s_mov_b32 m0, s43
	s_nop 0
	global_load_lds_dwordx4 v3, s[28:29]
	s_waitcnt vmcnt(8)
	s_waitcnt lgkmcnt(0)
	s_barrier
	s_setprio 1
	s_waitcnt lgkmcnt(0)
	v_mfma_f32_16x16x32_bf16 v[6:9], v[30:33], v[198:201], v[6:9]
	v_mfma_f32_16x16x32_bf16 v[10:13], v[118:121], v[198:201], v[10:13]
	v_mfma_f32_16x16x32_bf16 v[140:143], v[30:33], v[172:175], v[140:143]
	v_mfma_f32_16x16x32_bf16 v[144:147], v[118:121], v[172:175], v[144:147]
	v_mfma_f32_16x16x32_bf16 v[148:151], v[30:33], v[180:183], v[148:151]
	v_mfma_f32_16x16x32_bf16 v[152:155], v[118:121], v[180:183], v[152:155]
	v_mfma_f32_16x16x32_bf16 v[156:159], v[30:33], v[190:193], v[156:159]
	v_mfma_f32_16x16x32_bf16 v[160:163], v[118:121], v[190:193], v[160:163]
	v_mfma_f32_16x16x32_bf16 v[6:9], v[34:37], v[202:205], v[6:9]
	v_mfma_f32_16x16x32_bf16 v[10:13], v[122:125], v[202:205], v[10:13]
	v_mfma_f32_16x16x32_bf16 v[140:143], v[34:37], v[176:179], v[140:143]
	v_mfma_f32_16x16x32_bf16 v[144:147], v[122:125], v[176:179], v[144:147]
	v_mfma_f32_16x16x32_bf16 v[148:151], v[34:37], v[184:187], v[148:151]
	v_mfma_f32_16x16x32_bf16 v[152:155], v[122:125], v[184:187], v[152:155]
	v_mfma_f32_16x16x32_bf16 v[156:159], v[34:37], v[194:197], v[156:159]
	v_mfma_f32_16x16x32_bf16 v[160:163], v[122:125], v[194:197], v[160:163]
	v_mfma_f32_16x16x32_bf16 v[14:17], v[126:129], v[172:175], v[14:17]
	v_mfma_f32_16x16x32_bf16 v[18:21], v[164:167], v[172:175], v[18:21]
	v_mfma_f32_16x16x32_bf16 v[30:33], v[126:129], v[180:183], v[66:69]
	v_mfma_f32_16x16x32_bf16 v[34:37], v[164:167], v[180:183], v[106:109]
	v_mfma_f32_16x16x32_bf16 v[66:69], v[126:129], v[190:193], v[110:113]
	v_mfma_f32_16x16x32_bf16 v[106:109], v[164:167], v[190:193], v[114:117]
	v_mfma_f32_16x16x32_bf16 v[22:25], v[126:129], v[198:201], v[22:25]
	v_mfma_f32_16x16x32_bf16 v[26:29], v[164:167], v[198:201], v[26:29]
	v_mfma_f32_16x16x32_bf16 v[14:17], v[136:139], v[176:179], v[14:17]
	v_mfma_f32_16x16x32_bf16 v[18:21], v[168:171], v[176:179], v[18:21]
	v_mfma_f32_16x16x32_bf16 v[30:33], v[136:139], v[184:187], v[30:33]
	v_mfma_f32_16x16x32_bf16 v[34:37], v[168:171], v[184:187], v[34:37]
	v_mfma_f32_16x16x32_bf16 v[66:69], v[136:139], v[194:197], v[66:69]
	v_mfma_f32_16x16x32_bf16 v[106:109], v[168:171], v[194:197], v[106:109]
	v_mfma_f32_16x16x32_bf16 v[22:25], v[136:139], v[202:205], v[22:25]
	v_mfma_f32_16x16x32_bf16 v[26:29], v[168:171], v[202:205], v[26:29]
	s_setprio 0
	s_barrier
; #define PG8_STAGE(bufoff, gbase, voff) do { _Pragma("unroll") for (int _i = 0; _i < 2; ++_i) \
;         __builtin_amdgcn_global_load_lds((const unsigned*)((const char*)(gbase) + (voff)[_i]), (LAS unsigned*)(lds + (bufoff) + ldsw + _i * 8192), 16, 0, 0); } while (0)
; #define PG8_LDA(dst, b, h) do { _Pragma("unroll") for (int m = 0; m < 4; ++m) _Pragma("unroll") for (int k = 0; k < 2; ++k) dst[m][k] = *(const LAS bf16x8*)(lds + PG8_SA(b, h) + aoff + m * 2048 + k * 1024); } while (0)
; #define PG8_LDB(dst, b, h) do { _Pragma("unroll") for (int n = 0; n < 2; ++n) _Pragma("unroll") for (int k = 0; k < 2; ++k) dst[n][k] = *(const LAS bf16x8*)(lds + PG8_SB(b, h) + boff + n * 2048 + k * 1024); } while (0)
; #define PG8_MMA(ai, bj, At, Bt) do { __builtin_amdgcn_s_setprio(1); _Pragma("unroll") for (int m = 0; m < 4; ++m) _Pragma("unroll") for (int n = 0; n < 2; ++n) _Pragma("unroll") for (int k = 0; k < 2; ++k) \
;         acc[ai][bj][m][n] = __builtin_amdgcn_mfma_f32_16x16x32_bf16(Bt[n][k], At[m][k], acc[ai][bj][m][n], 0, 0, 0); __builtin_amdgcn_s_setprio(0); } while (0)
; #define PG8_WAIT_V(n) asm volatile("s_waitcnt vmcnt(" #n ")" ::: "memory")
; #define PG8_WAIT_L(n) asm volatile("s_waitcnt lgkmcnt(" #n ")" ::: "memory")
; #define PG8_BAR __builtin_amdgcn_s_barrier()
; #define PG8_SCHED __builtin_amdgcn_sched_barrier(0)
; template <class Epi, class Sched>
; __device__ __forceinline__ void gemm_phase(LAS unsigned char* lds, const int tid, const char* Abase, const int K, const Sched& S, const Epi& E) {
;     ...
;             PG8_LDB(B0, 0, 0); PG8_LDB(B1, 0, 1); PG8_SCHED; PG8_LDA(At, 0, 0); PG8_STAGE(PG8_SA(1, 1), a1, vc[1]);
;             PG8_WAIT_V(8); PG8_WAIT_L(0); PG8_BAR; PG8_MMA(0, 0, At, B0); PG8_MMA(0, 1, At, B1); PG8_BAR; PG8_SCHED;
;             PG8_LDA(At, 0, 1); PG8_STAGE(PG8_SB(0, 0), b2, voffB); PG8_STAGE(PG8_SB(0, 1), b2 + hstep, voffB); PG8_STAGE(PG8_SA(0, 0), a2, w2[0]);
;             PG8_WAIT_V(8); PG8_WAIT_L(0); PG8_BAR; PG8_MMA(1, 0, At, B0); PG8_MMA(1, 1, At, B1); PG8_BAR; PG8_SCHED;
	ds_read_b128 v[136:139], v132
	ds_read_b128 v[110:113], v135
	ds_read_b128 v[114:117], v135 offset:1024
	ds_read_b128 v[118:121], v135 offset:2048
	ds_read_b128 v[122:125], v135 offset:3072
	ds_read_b128 v[126:129], v189
	ds_read_b128 v[164:167], v189 offset:1024
	ds_read_b128 v[168:171], v189 offset:2048
	ds_read_b128 v[172:175], v189 offset:3072
	s_mov_b32 m0, s35
	ds_read_b128 v[176:179], v134
	ds_read_b128 v[180:183], v134 offset:1024
	ds_read_b128 v[184:187], v134 offset:2048
	ds_read_b128 v[190:193], v134 offset:3072
	ds_read_b128 v[194:197], v134 offset:4096
	ds_read_b128 v[198:201], v134 offset:5120
	ds_read_b128 v[202:205], v134 offset:6144
	ds_read_b128 v[206:209], v134 offset:7168
	global_load_lds_dwordx4 v4, s[28:29]
	s_mov_b32 m0, s47
	s_nop 0
	global_load_lds_dwordx4 v5, s[28:29]
	s_waitcnt vmcnt(8)
	s_waitcnt lgkmcnt(0)
	s_barrier
	s_setprio 1
	s_waitcnt lgkmcnt(0)
	v_mfma_f32_16x16x32_bf16 v[2:5], v[110:113], v[176:179], v[70:73]
	v_mfma_f32_16x16x32_bf16 v[70:73], v[118:121], v[176:179], v[74:77]
	v_mfma_f32_16x16x32_bf16 v[74:77], v[110:113], v[184:187], v[78:81]
	v_mfma_f32_16x16x32_bf16 v[78:81], v[118:121], v[184:187], v[82:85]
	v_mfma_f32_16x16x32_bf16 v[82:85], v[110:113], v[194:197], v[86:89]
	v_mfma_f32_16x16x32_bf16 v[86:89], v[118:121], v[194:197], v[90:93]
	v_mfma_f32_16x16x32_bf16 v[90:93], v[110:113], v[202:205], v[94:97]
	v_mfma_f32_16x16x32_bf16 v[94:97], v[118:121], v[202:205], v[98:101]
	v_mfma_f32_16x16x32_bf16 v[2:5], v[114:117], v[180:183], v[2:5]
	v_mfma_f32_16x16x32_bf16 v[70:73], v[122:125], v[180:183], v[70:73]
	v_mfma_f32_16x16x32_bf16 v[74:77], v[114:117], v[190:193], v[74:77]
	v_mfma_f32_16x16x32_bf16 v[78:81], v[122:125], v[190:193], v[78:81]
	v_mfma_f32_16x16x32_bf16 v[82:85], v[114:117], v[198:201], v[82:85]
	v_mfma_f32_16x16x32_bf16 v[86:89], v[122:125], v[198:201], v[86:89]
	v_mfma_f32_16x16x32_bf16 v[90:93], v[114:117], v[206:209], v[90:93]
	v_mfma_f32_16x16x32_bf16 v[94:97], v[122:125], v[206:209], v[94:97]
	v_mfma_f32_16x16x32_bf16 v[38:41], v[168:171], v[176:179], v[38:41]
	v_mfma_f32_16x16x32_bf16 v[98:101], v[126:129], v[176:179], v[102:105]
	v_mfma_f32_16x16x32_bf16 v[176:179], v[172:175], v[180:183], v[38:41]
	v_mfma_f32_16x16x32_bf16 v[38:41], v[126:129], v[184:187], v[42:45]
	v_mfma_f32_16x16x32_bf16 v[42:45], v[164:167], v[190:193], v[38:41]
	v_mfma_f32_16x16x32_bf16 v[38:41], v[168:171], v[184:187], v[46:49]
	v_mfma_f32_16x16x32_bf16 v[46:49], v[172:175], v[190:193], v[38:41]
	v_mfma_f32_16x16x32_bf16 v[38:41], v[126:129], v[194:197], v[50:53]
	v_mfma_f32_16x16x32_bf16 v[50:53], v[164:167], v[198:201], v[38:41]
	v_mfma_f32_16x16x32_bf16 v[38:41], v[168:171], v[194:197], v[54:57]
	v_mfma_f32_16x16x32_bf16 v[54:57], v[172:175], v[198:201], v[38:41]
	v_mfma_f32_16x16x32_bf16 v[38:41], v[126:129], v[202:205], v[58:61]
	v_mfma_f32_16x16x32_bf16 v[58:61], v[164:167], v[206:209], v[38:41]
	v_mfma_f32_16x16x32_bf16 v[38:41], v[168:171], v[202:205], v[62:65]
	v_mfma_f32_16x16x32_bf16 v[62:65], v[172:175], v[206:209], v[38:41]
	v_mfma_f32_16x16x32_bf16 v[210:213], v[164:167], v[180:183], v[98:101]
	s_setprio 0
	s_barrier
	s_mov_b32 m0, s52
	v_lshl_add_u64 v[246:247], s[12:13], 0, v[0:1]
	s_add_u32 s54, s12, 0x10000
	s_nop 0
	ds_read_b128 v[38:41], v134 offset:16384
	ds_read_b128 v[98:101], v134 offset:17408
	ds_read_b128 v[102:105], v134 offset:18432
	ds_read_b128 v[180:183], v134 offset:19456
	ds_read_b128 v[184:187], v134 offset:20480
	ds_read_b128 v[190:193], v134 offset:21504
	ds_read_b128 v[194:197], v134 offset:22528
	ds_read_b128 v[198:201], v134 offset:23552
	global_load_lds_dwordx4 v[246:247], off
	v_lshl_add_u64 v[248:249], s[12:13], 0, v[130:131]
	s_mov_b32 m0, s48
	s_addc_u32 s55, s13, 0
	global_load_lds_dwordx4 v[248:249], off
	v_lshl_add_u64 v[202:203], s[54:55], 0, v[0:1]
	s_mov_b32 m0, s49
	s_nop 0
	global_load_lds_dwordx4 v[202:203], off
	v_lshl_add_u64 v[202:203], s[54:55], 0, v[130:131]
	s_mov_b32 m0, s50
	s_nop 0
	global_load_lds_dwordx4 v[202:203], off
	s_mov_b32 m0, s7
	s_nop 0
	global_load_lds_dwordx4 v136, s[14:15]
	s_mov_b32 m0, s33
	s_nop 0
	global_load_lds_dwordx4 v137, s[14:15]
	s_waitcnt vmcnt(8)
	s_waitcnt lgkmcnt(0)
	s_barrier
	s_setprio 1
	s_waitcnt lgkmcnt(0)
	v_mfma_f32_16x16x32_bf16 v[6:9], v[110:113], v[194:197], v[6:9]
	v_mfma_f32_16x16x32_bf16 v[10:13], v[118:121], v[194:197], v[10:13]
	v_mfma_f32_16x16x32_bf16 v[140:143], v[110:113], v[38:41], v[140:143]
	v_mfma_f32_16x16x32_bf16 v[144:147], v[118:121], v[38:41], v[144:147]
	v_mfma_f32_16x16x32_bf16 v[148:151], v[110:113], v[102:105], v[148:151]
	v_mfma_f32_16x16x32_bf16 v[152:155], v[118:121], v[102:105], v[152:155]
	v_mfma_f32_16x16x32_bf16 v[156:159], v[110:113], v[184:187], v[156:159]
	v_mfma_f32_16x16x32_bf16 v[160:163], v[118:121], v[184:187], v[160:163]
	v_mfma_f32_16x16x32_bf16 v[6:9], v[114:117], v[198:201], v[6:9]
	v_mfma_f32_16x16x32_bf16 v[10:13], v[122:125], v[198:201], v[10:13]
	v_mfma_f32_16x16x32_bf16 v[140:143], v[114:117], v[98:101], v[140:143]
	v_mfma_f32_16x16x32_bf16 v[144:147], v[122:125], v[98:101], v[144:147]
	v_mfma_f32_16x16x32_bf16 v[148:151], v[114:117], v[180:183], v[148:151]
	v_mfma_f32_16x16x32_bf16 v[152:155], v[122:125], v[180:183], v[152:155]
	v_mfma_f32_16x16x32_bf16 v[156:159], v[114:117], v[190:193], v[156:159]
	v_mfma_f32_16x16x32_bf16 v[160:163], v[122:125], v[190:193], v[160:163]
	v_mfma_f32_16x16x32_bf16 v[18:21], v[168:171], v[38:41], v[18:21]
	v_mfma_f32_16x16x32_bf16 v[202:205], v[172:175], v[98:101], v[18:21]
	v_mfma_f32_16x16x32_bf16 v[18:21], v[126:129], v[102:105], v[30:33]
	v_mfma_f32_16x16x32_bf16 v[30:33], v[164:167], v[180:183], v[18:21]
	v_mfma_f32_16x16x32_bf16 v[18:21], v[168:171], v[102:105], v[34:37]
	v_mfma_f32_16x16x32_bf16 v[180:183], v[172:175], v[180:183], v[18:21]
	v_mfma_f32_16x16x32_bf16 v[18:21], v[126:129], v[184:187], v[66:69]
	v_mfma_f32_16x16x32_bf16 v[206:209], v[164:167], v[190:193], v[18:21]
	v_mfma_f32_16x16x32_bf16 v[18:21], v[168:171], v[184:187], v[106:109]
	v_mfma_f32_16x16x32_bf16 v[14:17], v[126:129], v[38:41], v[14:17]
	v_mfma_f32_16x16x32_bf16 v[184:187], v[172:175], v[190:193], v[18:21]
	v_mfma_f32_16x16x32_bf16 v[18:21], v[126:129], v[194:197], v[22:25]
	v_mfma_f32_16x16x32_bf16 v[14:17], v[164:167], v[98:101], v[14:17]
	v_mfma_f32_16x16x32_bf16 v[164:167], v[164:167], v[198:201], v[18:21]
	v_mfma_f32_16x16x32_bf16 v[18:21], v[168:171], v[194:197], v[26:29]
	v_mfma_f32_16x16x32_bf16 v[168:171], v[172:175], v[198:201], v[18:21]
	s_setprio 0
	s_barrier
; #define PG8_STAGE(bufoff, gbase, voff) do { _Pragma("unroll") for (int _i = 0; _i < 2; ++_i) \
;         __builtin_amdgcn_global_load_lds((const unsigned*)((const char*)(gbase) + (voff)[_i]), (LAS unsigned*)(lds + (bufoff) + ldsw + _i * 8192), 16, 0, 0); } while (0)
; #define PG8_LDA(dst, b, h) do { _Pragma("unroll") for (int m = 0; m < 4; ++m) _Pragma("unroll") for (int k = 0; k < 2; ++k) dst[m][k] = *(const LAS bf16x8*)(lds + PG8_SA(b, h) + aoff + m * 2048 + k * 1024); } while (0)
; #define PG8_LDB(dst, b, h) do { _Pragma("unroll") for (int n = 0; n < 2; ++n) _Pragma("unroll") for (int k = 0; k < 2; ++k) dst[n][k] = *(const LAS bf16x8*)(lds + PG8_SB(b, h) + boff + n * 2048 + k * 1024); } while (0)
; #define PG8_MMA(ai, bj, At, Bt) do { __builtin_amdgcn_s_setprio(1); _Pragma("unroll") for (int m = 0; m < 4; ++m) _Pragma("unroll") for (int n = 0; n < 2; ++n) _Pragma("unroll") for (int k = 0; k < 2; ++k) \
;         acc[ai][bj][m][n] = __builtin_amdgcn_mfma_f32_16x16x32_bf16(Bt[n][k], At[m][k], acc[ai][bj][m][n], 0, 0, 0); __builtin_amdgcn_s_setprio(0); } while (0)
; #define PG8_WAIT_V(n) asm volatile("s_waitcnt vmcnt(" #n ")" ::: "memory")
; #define PG8_WAIT_L(n) asm volatile("s_waitcnt lgkmcnt(" #n ")" ::: "memory")
; #define PG8_BAR __builtin_amdgcn_s_barrier()
; #define PG8_SCHED __builtin_amdgcn_sched_barrier(0)
; template <class Epi, class Sched>
; __device__ __forceinline__ void gemm_phase(LAS unsigned char* lds, const int tid, const char* Abase, const int K, const Sched& S, const Epi& E) {
;     ...
;             PG8_LDB(B0, 1, 0); PG8_LDB(B1, 1, 1); PG8_SCHED; PG8_LDA(At, 1, 0); PG8_STAGE(PG8_SA(0, 1), a2, w2[1]);
;             PG8_WAIT_V(8); PG8_WAIT_L(0); PG8_BAR; PG8_MMA(0, 0, At, B0); PG8_MMA(0, 1, At, B1); PG8_BAR; PG8_SCHED;
;             PG8_LDA(At, 1, 1); PG8_STAGE(PG8_SB(1, 0), b3, voffB); PG8_STAGE(PG8_SB(1, 1), b3 + hstep, voffB); PG8_STAGE(PG8_SA(1, 0), a3, w2[0]);
;             PG8_WAIT_V(8); PG8_WAIT_L(0); PG8_BAR; PG8_MMA(1, 0, At, B0); PG8_MMA(1, 1, At, B1); PG8_BAR; PG8_SCHED;
;         }
;         if (wr == 0) PG8_BAR;
	ds_read_b128 v[26:29], v214
	ds_read_b128 v[172:175], v214 offset:1024
	ds_read_b128 v[190:193], v214 offset:2048
	ds_read_b128 v[194:197], v214 offset:3072
	ds_read_b128 v[198:201], v222
	ds_read_b128 v[214:217], v222 offset:1024
	ds_read_b128 v[218:221], v222 offset:2048
	ds_read_b128 v[222:225], v222 offset:3072
	s_mov_b32 m0, s38
	ds_read_b128 v[18:21], v134 offset:32768
	ds_read_b128 v[22:25], v134 offset:33792
	ds_read_b128 v[110:113], v134 offset:34816
	ds_read_b128 v[226:229], v134 offset:35840
	ds_read_b128 v[230:233], v134 offset:36864
	ds_read_b128 v[234:237], v134 offset:37888
	ds_read_b128 v[238:241], v134 offset:38912
	ds_read_b128 v[242:245], v134 offset:39936
	global_load_lds_dwordx4 v138, s[14:15]
	s_mov_b32 m0, s39
	s_nop 0
	global_load_lds_dwordx4 v139, s[14:15]
	s_waitcnt vmcnt(8)
	s_waitcnt lgkmcnt(0)
	s_barrier
	s_setprio 1
	s_waitcnt lgkmcnt(0)
	v_mfma_f32_16x16x32_bf16 v[2:5], v[26:29], v[18:21], v[2:5]
	v_mfma_f32_16x16x32_bf16 v[114:117], v[172:175], v[22:25], v[2:5]
	v_mfma_f32_16x16x32_bf16 v[2:5], v[190:193], v[18:21], v[70:73]
	v_mfma_f32_16x16x32_bf16 v[118:121], v[194:197], v[22:25], v[2:5]
	v_mfma_f32_16x16x32_bf16 v[2:5], v[26:29], v[110:113], v[74:77]
	v_mfma_f32_16x16x32_bf16 v[98:101], v[172:175], v[226:229], v[2:5]
	v_mfma_f32_16x16x32_bf16 v[2:5], v[190:193], v[110:113], v[78:81]
	v_mfma_f32_16x16x32_bf16 v[102:105], v[194:197], v[226:229], v[2:5]
	v_mfma_f32_16x16x32_bf16 v[2:5], v[26:29], v[230:233], v[82:85]
	v_mfma_f32_16x16x32_bf16 v[66:69], v[172:175], v[234:237], v[2:5]
	v_mfma_f32_16x16x32_bf16 v[2:5], v[190:193], v[230:233], v[86:89]
	v_mfma_f32_16x16x32_bf16 v[70:73], v[194:197], v[234:237], v[2:5]
	v_mfma_f32_16x16x32_bf16 v[2:5], v[26:29], v[238:241], v[90:93]
	v_mfma_f32_16x16x32_bf16 v[34:37], v[172:175], v[242:245], v[2:5]
	v_mfma_f32_16x16x32_bf16 v[2:5], v[190:193], v[238:241], v[94:97]
	v_mfma_f32_16x16x32_bf16 v[38:41], v[194:197], v[242:245], v[2:5]
	v_mfma_f32_16x16x32_bf16 v[2:5], v[198:201], v[18:21], v[210:213]
	v_mfma_f32_16x16x32_bf16 v[122:125], v[214:217], v[22:25], v[2:5]
	v_mfma_f32_16x16x32_bf16 v[2:5], v[218:221], v[18:21], v[176:179]
	v_mfma_f32_16x16x32_bf16 v[126:129], v[222:225], v[22:25], v[2:5]
	v_mfma_f32_16x16x32_bf16 v[2:5], v[198:201], v[110:113], v[42:45]
	v_mfma_f32_16x16x32_bf16 v[106:109], v[214:217], v[226:229], v[2:5]
	v_mfma_f32_16x16x32_bf16 v[2:5], v[218:221], v[110:113], v[46:49]
	v_mfma_f32_16x16x32_bf16 v[110:113], v[222:225], v[226:229], v[2:5]
	v_mfma_f32_16x16x32_bf16 v[2:5], v[198:201], v[230:233], v[50:53]
	v_mfma_f32_16x16x32_bf16 v[74:77], v[214:217], v[234:237], v[2:5]
	v_mfma_f32_16x16x32_bf16 v[2:5], v[218:221], v[230:233], v[54:57]
	v_mfma_f32_16x16x32_bf16 v[78:81], v[222:225], v[234:237], v[2:5]
	v_mfma_f32_16x16x32_bf16 v[2:5], v[198:201], v[238:241], v[58:61]
	v_mfma_f32_16x16x32_bf16 v[42:45], v[214:217], v[242:245], v[2:5]
	v_mfma_f32_16x16x32_bf16 v[2:5], v[218:221], v[238:241], v[62:65]
	v_mfma_f32_16x16x32_bf16 v[46:49], v[222:225], v[242:245], v[2:5]
	s_setprio 0
	s_barrier
	s_mov_b32 m0, s53
	s_nop 3
	v_lshl_add_u64 v[2:3], v[246:247], 0, s[24:25]
	s_add_u32 s48, s12, 0x10080
	ds_read_b128 v[58:61], v134 offset:49152
	ds_read_b128 v[62:65], v134 offset:50176
	ds_read_b128 v[176:179], v134 offset:51200
	ds_read_b128 v[210:213], v134 offset:52224
	ds_read_b128 v[226:229], v134 offset:53248
	ds_read_b128 v[230:233], v134 offset:54272
	ds_read_b128 v[234:237], v134 offset:55296
	ds_read_b128 v[238:241], v134 offset:56320
	global_load_lds_dwordx4 v[2:3], off
	v_lshl_add_u64 v[2:3], v[248:249], 0, s[24:25]
	s_mov_b32 m0, s51
	s_addc_u32 s49, s13, 0
	global_load_lds_dwordx4 v[2:3], off
	v_lshl_add_u64 v[2:3], s[48:49], 0, v[0:1]
	s_mov_b32 m0, s36
	s_nop 0
	global_load_lds_dwordx4 v[2:3], off
	v_lshl_add_u64 v[2:3], s[48:49], 0, v[130:131]
	s_mov_b32 m0, s37
	s_nop 0
	global_load_lds_dwordx4 v[2:3], off
	s_mov_b32 m0, s42
	s_nop 0
	global_load_lds_dwordx4 v136, s[20:21]
	s_mov_b32 m0, s43
	s_nop 0
	global_load_lds_dwordx4 v137, s[20:21]
	s_waitcnt vmcnt(8)
	s_waitcnt lgkmcnt(0)
	s_barrier
	s_setprio 1
	s_waitcnt lgkmcnt(0)
	v_mfma_f32_16x16x32_bf16 v[2:5], v[26:29], v[58:61], v[140:143]
	v_mfma_f32_16x16x32_bf16 v[82:85], v[172:175], v[62:65], v[2:5]
	v_mfma_f32_16x16x32_bf16 v[2:5], v[190:193], v[58:61], v[144:147]
	v_mfma_f32_16x16x32_bf16 v[86:89], v[194:197], v[62:65], v[2:5]
	v_mfma_f32_16x16x32_bf16 v[2:5], v[26:29], v[176:179], v[148:151]
	v_mfma_f32_16x16x32_bf16 v[50:53], v[172:175], v[210:213], v[2:5]
	v_mfma_f32_16x16x32_bf16 v[2:5], v[190:193], v[176:179], v[152:155]
	v_mfma_f32_16x16x32_bf16 v[54:57], v[194:197], v[210:213], v[2:5]
	v_mfma_f32_16x16x32_bf16 v[2:5], v[26:29], v[226:229], v[156:159]
	v_mfma_f32_16x16x32_bf16 v[18:21], v[172:175], v[230:233], v[2:5]
	v_mfma_f32_16x16x32_bf16 v[2:5], v[190:193], v[226:229], v[160:163]
	v_mfma_f32_16x16x32_bf16 v[22:25], v[194:197], v[230:233], v[2:5]
	v_mfma_f32_16x16x32_bf16 v[2:5], v[26:29], v[234:237], v[6:9]
	v_mfma_f32_16x16x32_bf16 v[6:9], v[190:193], v[234:237], v[10:13]
	v_mfma_f32_16x16x32_bf16 v[2:5], v[172:175], v[238:241], v[2:5]
	v_mfma_f32_16x16x32_bf16 v[6:9], v[194:197], v[238:241], v[6:9]
	v_mfma_f32_16x16x32_bf16 v[10:13], v[198:201], v[58:61], v[14:17]
	v_mfma_f32_16x16x32_bf16 v[90:93], v[214:217], v[62:65], v[10:13]
	v_mfma_f32_16x16x32_bf16 v[10:13], v[218:221], v[58:61], v[202:205]
	v_mfma_f32_16x16x32_bf16 v[94:97], v[222:225], v[62:65], v[10:13]
	v_mfma_f32_16x16x32_bf16 v[10:13], v[198:201], v[176:179], v[30:33]
	v_mfma_f32_16x16x32_bf16 v[58:61], v[214:217], v[210:213], v[10:13]
	v_mfma_f32_16x16x32_bf16 v[10:13], v[218:221], v[176:179], v[180:183]
	v_mfma_f32_16x16x32_bf16 v[62:65], v[222:225], v[210:213], v[10:13]
	v_mfma_f32_16x16x32_bf16 v[10:13], v[198:201], v[226:229], v[206:209]
	v_mfma_f32_16x16x32_bf16 v[26:29], v[214:217], v[230:233], v[10:13]
	v_mfma_f32_16x16x32_bf16 v[10:13], v[218:221], v[226:229], v[184:187]
	v_mfma_f32_16x16x32_bf16 v[30:33], v[222:225], v[230:233], v[10:13]
	v_mfma_f32_16x16x32_bf16 v[10:13], v[198:201], v[234:237], v[164:167]
	v_mfma_f32_16x16x32_bf16 v[14:17], v[218:221], v[234:237], v[168:171]
	v_mfma_f32_16x16x32_bf16 v[10:13], v[214:217], v[238:241], v[10:13]
	v_mfma_f32_16x16x32_bf16 v[14:17], v[222:225], v[238:241], v[14:17]
	s_setprio 0
	s_barrier
	s_andn2_b64 vcc, exec, s[22:23]
	s_cbranch_vccnz .LBB0_1253
	s_barrier

; #define PG8_STAGE(bufoff, gbase, voff) do { _Pragma("unroll") for (int _i = 0; _i < 2; ++_i) \
;         __builtin_amdgcn_global_load_lds((const unsigned*)((const char*)(gbase) + (voff)[_i]), (LAS unsigned*)(lds + (bufoff) + ldsw + _i * 8192), 16, 0, 0); } while (0)
; #define PG8_LDA(dst, b, h) do { _Pragma("unroll") for (int m = 0; m < 4; ++m) _Pragma("unroll") for (int k = 0; k < 2; ++k) dst[m][k] = *(const LAS bf16x8*)(lds + PG8_SA(b, h) + aoff + m * 2048 + k * 1024); } while (0)
; #define PG8_LDB(dst, b, h) do { _Pragma("unroll") for (int n = 0; n < 2; ++n) _Pragma("unroll") for (int k = 0; k < 2; ++k) dst[n][k] = *(const LAS bf16x8*)(lds + PG8_SB(b, h) + boff + n * 2048 + k * 1024); } while (0)
; #define PG8_WAIT_V(n) asm volatile("s_waitcnt vmcnt(" #n ")" ::: "memory")
; template <class Epi, class Sched>
; __device__ __forceinline__ void gemm_phase(LAS unsigned char* lds, const int tid, const char* Abase, const int K, const Sched& S, const Epi& E) {
;     ...
;           if (has_next) { PG8_AOFFS(vn, nxt); nB = S.b_tile(nxt); *vslot = (u32x4){vn[0][0], vn[0][1], vn[1][0], vn[1][1]}; }
;           else *vslot = (u32x4){vc[0][0], vc[0][1], vc[1][0], vc[1][1]}; }
;         for (int t = 0; t < nt; t += 2) {
;             if constexpr (Epi::MID) { if (t == (nt >> 1)) E.mid(acc, ui, wr, fr, lds); }
;             const bool last = (t == nt - 2);
;             const char* a1 = Abase + (size_t)(t + 1) * kstep;
;             const char* a2 = last ? Abase : Abase + (size_t)(t + 2) * kstep; const char* b2 = last ? nB : cB + (size_t)(t + 2) * kstep;
;             const char* a3 = a2 + kstep; const char* b3 = b2 + kstep;
;             unsigned w2[2][2];
;             if (last) { const u32x4 q = *vslot; w2[0][0] = q.x; w2[0][1] = q.y; w2[1][0] = q.z; w2[1][1] = q.w; }
;             else { w2[0][0] = vc[0][0]; w2[0][1] = vc[0][1]; w2[1][0] = vc[1][0]; w2[1][1] = vc[1][1]; }
;             PG8_LDB(B0, 0, 0); PG8_LDB(B1, 0, 1); PG8_SCHED; PG8_LDA(At, 0, 0); PG8_STAGE(PG8_SA(1, 1), a1, vc[1]);
;             PG8_WAIT_V(8); PG8_WAIT_L(0); PG8_BAR; PG8_MMA(0, 0, At, B0); PG8_MMA(0, 1, At, B1); PG8_BAR; PG8_SCHED;
;             PG8_LDA(At, 0, 1); PG8_STAGE(PG8_SB(0, 0), b2, voffB); PG8_STAGE(PG8_SB(0, 1), b2 + hstep, voffB); PG8_STAGE(PG8_SA(0, 0), a2, w2[0]);
;             PG8_WAIT_V(8); PG8_WAIT_L(0); PG8_BAR; PG8_MMA(1, 0, At, B0); PG8_MMA(1, 1, At, B1); PG8_BAR; PG8_SCHED;
.LBB0_1347:
	s_add_i32 s56, 0, 0x10000
	s_add_i32 s53, 0, 0x14000
	ds_write_b128 v135, v[6:9]
	v_add_u32_e32 v189, s56, v136
	v_add_u32_e32 v212, s53, v136
	ds_read_b128 v[6:9], v189
	ds_read_b128 v[10:13], v189 offset:1024
	ds_read_b128 v[14:17], v189 offset:2048
	ds_read_b128 v[18:21], v189 offset:3072
	ds_read_b128 v[22:25], v212
	ds_read_b128 v[26:29], v212 offset:1024
	ds_read_b128 v[30:33], v212 offset:2048
	ds_read_b128 v[34:37], v212 offset:3072
	v_mov_b32_e32 v250, 1
	s_add_i32 s35, s7, 0xc000
	s_mov_b32 m0, s35
	s_add_i32 s39, s7, 0xe000
	ds_read_b128 v[38:41], v137
	ds_read_b128 v[42:45], v137 offset:1024
	ds_read_b128 v[46:49], v137 offset:2048
	ds_read_b128 v[50:53], v137 offset:3072
	ds_read_b128 v[54:57], v137 offset:4096
	ds_read_b128 v[58:61], v137 offset:5120
	ds_read_b128 v[62:65], v137 offset:6144
	ds_read_b128 v[66:69], v137 offset:7168
	global_load_lds_dwordx4 v4, s[22:23]
	s_mov_b32 m0, s39
	s_nop 0
	global_load_lds_dwordx4 v5, s[22:23]
	s_waitcnt vmcnt(8)
	s_waitcnt lgkmcnt(0)
	s_barrier
	s_setprio 1
	s_waitcnt lgkmcnt(0)
	v_mfma_f32_16x16x32_bf16 v[70:73], v[6:9], v[38:41], 0
	v_mfma_f32_16x16x32_bf16 v[74:77], v[14:17], v[38:41], 0
	v_mfma_f32_16x16x32_bf16 v[78:81], v[6:9], v[46:49], 0
	v_mfma_f32_16x16x32_bf16 v[82:85], v[14:17], v[46:49], 0
	v_mfma_f32_16x16x32_bf16 v[86:89], v[6:9], v[54:57], 0
	v_mfma_f32_16x16x32_bf16 v[90:93], v[14:17], v[54:57], 0
	v_mfma_f32_16x16x32_bf16 v[94:97], v[6:9], v[62:65], 0
	v_mfma_f32_16x16x32_bf16 v[98:101], v[14:17], v[62:65], 0
	v_mfma_f32_16x16x32_bf16 v[70:73], v[10:13], v[42:45], v[70:73]
	v_mfma_f32_16x16x32_bf16 v[74:77], v[18:21], v[42:45], v[74:77]
	v_mfma_f32_16x16x32_bf16 v[78:81], v[10:13], v[50:53], v[78:81]
	v_mfma_f32_16x16x32_bf16 v[82:85], v[18:21], v[50:53], v[82:85]
	v_mfma_f32_16x16x32_bf16 v[86:89], v[10:13], v[58:61], v[86:89]
	v_mfma_f32_16x16x32_bf16 v[90:93], v[18:21], v[58:61], v[90:93]
	v_mfma_f32_16x16x32_bf16 v[94:97], v[10:13], v[66:69], v[94:97]
	v_mfma_f32_16x16x32_bf16 v[98:101], v[18:21], v[66:69], v[98:101]
	v_mfma_f32_16x16x32_bf16 v[102:105], v[22:25], v[38:41], 0
	v_mfma_f32_16x16x32_bf16 v[38:41], v[30:33], v[38:41], 0
	v_mfma_f32_16x16x32_bf16 v[102:105], v[26:29], v[42:45], v[102:105]
	v_mfma_f32_16x16x32_bf16 v[38:41], v[34:37], v[42:45], v[38:41]
	v_mfma_f32_16x16x32_bf16 v[42:45], v[22:25], v[46:49], 0
	v_mfma_f32_16x16x32_bf16 v[46:49], v[30:33], v[46:49], 0
	v_mfma_f32_16x16x32_bf16 v[42:45], v[26:29], v[50:53], v[42:45]
	v_mfma_f32_16x16x32_bf16 v[46:49], v[34:37], v[50:53], v[46:49]
	v_mfma_f32_16x16x32_bf16 v[50:53], v[22:25], v[54:57], 0
	v_mfma_f32_16x16x32_bf16 v[54:57], v[30:33], v[54:57], 0
	v_mfma_f32_16x16x32_bf16 v[50:53], v[26:29], v[58:61], v[50:53]
	v_mfma_f32_16x16x32_bf16 v[54:57], v[34:37], v[58:61], v[54:57]
	v_mfma_f32_16x16x32_bf16 v[58:61], v[22:25], v[62:65], 0
	v_mfma_f32_16x16x32_bf16 v[62:65], v[30:33], v[62:65], 0
	v_mfma_f32_16x16x32_bf16 v[58:61], v[26:29], v[66:69], v[58:61]
	v_mfma_f32_16x16x32_bf16 v[62:65], v[34:37], v[66:69], v[62:65]
	s_setprio 0
	s_barrier
	v_lshl_add_u64 v[132:133], s[42:43], 0, v[0:1]
	s_mov_b64 s[54:55], 0x100
	s_add_i32 s56, s56, s6
	v_lshl_add_u64 v[144:145], v[132:133], 0, s[54:55]
	s_mov_b32 m0, s56
	v_lshl_add_u64 v[210:211], s[42:43], 0, v[130:131]
	s_add_i32 s52, s56, 0x2000
	ds_read_b128 v[66:69], v137 offset:16384
	ds_read_b128 v[106:109], v137 offset:17408
	ds_read_b128 v[110:113], v137 offset:18432
	ds_read_b128 v[114:117], v137 offset:19456
	ds_read_b128 v[118:121], v137 offset:20480
	ds_read_b128 v[122:125], v137 offset:21504
	ds_read_b128 v[126:129], v137 offset:22528
	ds_read_b128 v[140:143], v137 offset:23552
	global_load_lds_dwordx4 v[144:145], off
	v_lshl_add_u64 v[144:145], v[210:211], 0, s[54:55]
	s_add_u32 s54, s42, 0x10100
	s_mov_b32 m0, s52
	s_addc_u32 s55, s43, 0
	s_add_i32 s53, s53, s6
	global_load_lds_dwordx4 v[144:145], off
	v_lshl_add_u64 v[144:145], s[54:55], 0, v[0:1]
	s_mov_b32 m0, s53
	s_nop 0
	global_load_lds_dwordx4 v[144:145], off
	v_lshl_add_u64 v[144:145], s[54:55], 0, v[130:131]
	s_add_i32 s54, s53, 0x2000
	s_mov_b32 m0, s54
	s_nop 0
	global_load_lds_dwordx4 v[144:145], off
	s_mov_b32 m0, s7
	s_nop 0
	global_load_lds_dwordx4 v2, s[28:29]
	s_mov_b32 m0, s33
	s_nop 0
	global_load_lds_dwordx4 v3, s[28:29]
	s_waitcnt vmcnt(8)
	s_waitcnt lgkmcnt(0)
	s_barrier
	s_setprio 1
	s_waitcnt lgkmcnt(0)
	v_mfma_f32_16x16x32_bf16 v[144:147], v[6:9], v[66:69], 0
	v_mfma_f32_16x16x32_bf16 v[152:155], v[6:9], v[110:113], 0
	v_mfma_f32_16x16x32_bf16 v[160:163], v[6:9], v[118:121], 0
	v_mfma_f32_16x16x32_bf16 v[6:9], v[6:9], v[126:129], 0
	v_mfma_f32_16x16x32_bf16 v[144:147], v[10:13], v[106:109], v[144:147]
	v_mfma_f32_16x16x32_bf16 v[152:155], v[10:13], v[114:117], v[152:155]
	v_mfma_f32_16x16x32_bf16 v[160:163], v[10:13], v[122:125], v[160:163]
	v_mfma_f32_16x16x32_bf16 v[6:9], v[10:13], v[140:143], v[6:9]
	v_mfma_f32_16x16x32_bf16 v[10:13], v[14:17], v[126:129], 0
	v_mfma_f32_16x16x32_bf16 v[148:151], v[14:17], v[66:69], 0
	v_mfma_f32_16x16x32_bf16 v[156:159], v[14:17], v[110:113], 0
	v_mfma_f32_16x16x32_bf16 v[164:167], v[14:17], v[118:121], 0
	v_mfma_f32_16x16x32_bf16 v[10:13], v[18:21], v[140:143], v[10:13]
	v_mfma_f32_16x16x32_bf16 v[148:151], v[18:21], v[106:109], v[148:151]
	v_mfma_f32_16x16x32_bf16 v[156:159], v[18:21], v[114:117], v[156:159]
	v_mfma_f32_16x16x32_bf16 v[164:167], v[18:21], v[122:125], v[164:167]
	v_mfma_f32_16x16x32_bf16 v[14:17], v[22:25], v[66:69], 0
	v_mfma_f32_16x16x32_bf16 v[18:21], v[30:33], v[66:69], 0
	v_mfma_f32_16x16x32_bf16 v[14:17], v[26:29], v[106:109], v[14:17]
	v_mfma_f32_16x16x32_bf16 v[18:21], v[34:37], v[106:109], v[18:21]
	v_mfma_f32_16x16x32_bf16 v[66:69], v[22:25], v[110:113], 0
	v_mfma_f32_16x16x32_bf16 v[106:109], v[30:33], v[110:113], 0
	v_mfma_f32_16x16x32_bf16 v[110:113], v[22:25], v[118:121], 0
	v_mfma_f32_16x16x32_bf16 v[22:25], v[22:25], v[126:129], 0
	v_mfma_f32_16x16x32_bf16 v[66:69], v[26:29], v[114:117], v[66:69]
	v_mfma_f32_16x16x32_bf16 v[106:109], v[34:37], v[114:117], v[106:109]
	v_mfma_f32_16x16x32_bf16 v[110:113], v[26:29], v[122:125], v[110:113]
	v_mfma_f32_16x16x32_bf16 v[114:117], v[30:33], v[118:121], 0
	v_mfma_f32_16x16x32_bf16 v[22:25], v[26:29], v[140:143], v[22:25]
	v_mfma_f32_16x16x32_bf16 v[26:29], v[30:33], v[126:129], 0
	v_mfma_f32_16x16x32_bf16 v[114:117], v[34:37], v[122:125], v[114:117]
	v_mfma_f32_16x16x32_bf16 v[26:29], v[34:37], v[140:143], v[26:29]
	s_setprio 0
	s_barrier
; #define PG8_STAGE(bufoff, gbase, voff) do { _Pragma("unroll") for (int _i = 0; _i < 2; ++_i) \
;         __builtin_amdgcn_global_load_lds((const unsigned*)((const char*)(gbase) + (voff)[_i]), (LAS unsigned*)(lds + (bufoff) + ldsw + _i * 8192), 16, 0, 0); } while (0)
; #define PG8_LDA(dst, b, h) do { _Pragma("unroll") for (int m = 0; m < 4; ++m) _Pragma("unroll") for (int k = 0; k < 2; ++k) dst[m][k] = *(const LAS bf16x8*)(lds + PG8_SA(b, h) + aoff + m * 2048 + k * 1024); } while (0)
; #define PG8_LDB(dst, b, h) do { _Pragma("unroll") for (int n = 0; n < 2; ++n) _Pragma("unroll") for (int k = 0; k < 2; ++k) dst[n][k] = *(const LAS bf16x8*)(lds + PG8_SB(b, h) + boff + n * 2048 + k * 1024); } while (0)
; #define PG8_MMA(ai, bj, At, Bt) do { __builtin_amdgcn_s_setprio(1); _Pragma("unroll") for (int m = 0; m < 4; ++m) _Pragma("unroll") for (int n = 0; n < 2; ++n) _Pragma("unroll") for (int k = 0; k < 2; ++k) \
;         acc[ai][bj][m][n] = __builtin_amdgcn_mfma_f32_16x16x32_bf16(Bt[n][k], At[m][k], acc[ai][bj][m][n], 0, 0, 0); __builtin_amdgcn_s_setprio(0); } while (0)
; #define PG8_WAIT_V(n) asm volatile("s_waitcnt vmcnt(" #n ")" ::: "memory")
; #define PG8_WAIT_L(n) asm volatile("s_waitcnt lgkmcnt(" #n ")" ::: "memory")
; #define PG8_BAR __builtin_amdgcn_s_barrier()
; #define PG8_SCHED __builtin_amdgcn_sched_barrier(0)
; template <class Epi, class Sched>
; __device__ __forceinline__ void gemm_phase(LAS unsigned char* lds, const int tid, const char* Abase, const int K, const Sched& S, const Epi& E) {
;     ...
;             PG8_LDB(B0, 1, 0); PG8_LDB(B1, 1, 1); PG8_SCHED; PG8_LDA(At, 1, 0); PG8_STAGE(PG8_SA(0, 1), a2, w2[1]);
;             PG8_WAIT_V(8); PG8_WAIT_L(0); PG8_BAR; PG8_MMA(0, 0, At, B0); PG8_MMA(0, 1, At, B1); PG8_BAR; PG8_SCHED;
;             PG8_LDA(At, 1, 1); PG8_STAGE(PG8_SB(1, 0), b3, voffB); PG8_STAGE(PG8_SB(1, 1), b3 + hstep, voffB); PG8_STAGE(PG8_SA(1, 0), a3, w2[0]);
;             PG8_WAIT_V(8); PG8_WAIT_L(0); PG8_BAR; PG8_MMA(1, 0, At, B0); PG8_MMA(1, 1, At, B1); PG8_BAR; PG8_SCHED;
	s_add_i32 s57, 0, 0x18000
	s_add_i32 s60, 0, 0x1c000
	v_add_u32_e32 v218, s57, v136
	v_add_u32_e32 v219, s60, v136
	ds_read_b128 v[30:33], v218
	ds_read_b128 v[34:37], v218 offset:1024
	ds_read_b128 v[118:121], v218 offset:2048
	ds_read_b128 v[122:125], v218 offset:3072
	ds_read_b128 v[126:129], v219
	ds_read_b128 v[140:143], v219 offset:1024
	ds_read_b128 v[168:171], v219 offset:2048
	ds_read_b128 v[172:175], v219 offset:3072
	s_mov_b32 m0, s44
	ds_read_b128 v[176:179], v137 offset:32768
	ds_read_b128 v[180:183], v137 offset:33792
	ds_read_b128 v[184:187], v137 offset:34816
	ds_read_b128 v[190:193], v137 offset:35840
	ds_read_b128 v[194:197], v137 offset:36864
	ds_read_b128 v[198:201], v137 offset:37888
	ds_read_b128 v[202:205], v137 offset:38912
	ds_read_b128 v[206:209], v137 offset:39936
	global_load_lds_dwordx4 v4, s[28:29]
	s_mov_b32 m0, s45
	s_nop 0
	global_load_lds_dwordx4 v5, s[28:29]
	s_waitcnt vmcnt(8)
	s_waitcnt lgkmcnt(0)
	s_barrier
	s_setprio 1
	s_waitcnt lgkmcnt(0)
	v_mfma_f32_16x16x32_bf16 v[70:73], v[30:33], v[176:179], v[70:73]
	v_mfma_f32_16x16x32_bf16 v[74:77], v[118:121], v[176:179], v[74:77]
	v_mfma_f32_16x16x32_bf16 v[78:81], v[30:33], v[184:187], v[78:81]
	v_mfma_f32_16x16x32_bf16 v[82:85], v[118:121], v[184:187], v[82:85]
	v_mfma_f32_16x16x32_bf16 v[86:89], v[30:33], v[194:197], v[86:89]
	v_mfma_f32_16x16x32_bf16 v[90:93], v[118:121], v[194:197], v[90:93]
	v_mfma_f32_16x16x32_bf16 v[94:97], v[30:33], v[202:205], v[94:97]
	v_mfma_f32_16x16x32_bf16 v[98:101], v[118:121], v[202:205], v[98:101]
	v_mfma_f32_16x16x32_bf16 v[70:73], v[34:37], v[180:183], v[70:73]
	v_mfma_f32_16x16x32_bf16 v[74:77], v[122:125], v[180:183], v[74:77]
	v_mfma_f32_16x16x32_bf16 v[78:81], v[34:37], v[190:193], v[78:81]
	v_mfma_f32_16x16x32_bf16 v[82:85], v[122:125], v[190:193], v[82:85]
	v_mfma_f32_16x16x32_bf16 v[86:89], v[34:37], v[198:201], v[86:89]
	v_mfma_f32_16x16x32_bf16 v[90:93], v[122:125], v[198:201], v[90:93]
	v_mfma_f32_16x16x32_bf16 v[94:97], v[34:37], v[206:209], v[94:97]
	v_mfma_f32_16x16x32_bf16 v[98:101], v[122:125], v[206:209], v[98:101]
	v_mfma_f32_16x16x32_bf16 v[102:105], v[126:129], v[176:179], v[102:105]
	v_mfma_f32_16x16x32_bf16 v[38:41], v[168:171], v[176:179], v[38:41]
	v_mfma_f32_16x16x32_bf16 v[42:45], v[126:129], v[184:187], v[42:45]
	v_mfma_f32_16x16x32_bf16 v[46:49], v[168:171], v[184:187], v[46:49]
	v_mfma_f32_16x16x32_bf16 v[50:53], v[126:129], v[194:197], v[50:53]
	v_mfma_f32_16x16x32_bf16 v[54:57], v[168:171], v[194:197], v[54:57]
	v_mfma_f32_16x16x32_bf16 v[58:61], v[126:129], v[202:205], v[58:61]
	v_mfma_f32_16x16x32_bf16 v[62:65], v[168:171], v[202:205], v[62:65]
	v_mfma_f32_16x16x32_bf16 v[102:105], v[140:143], v[180:183], v[102:105]
	v_mfma_f32_16x16x32_bf16 v[38:41], v[172:175], v[180:183], v[38:41]
	v_mfma_f32_16x16x32_bf16 v[42:45], v[140:143], v[190:193], v[42:45]
	v_mfma_f32_16x16x32_bf16 v[46:49], v[172:175], v[190:193], v[46:49]
	v_mfma_f32_16x16x32_bf16 v[50:53], v[140:143], v[198:201], v[50:53]
	v_mfma_f32_16x16x32_bf16 v[54:57], v[172:175], v[198:201], v[54:57]
	v_mfma_f32_16x16x32_bf16 v[58:61], v[140:143], v[206:209], v[58:61]
	v_mfma_f32_16x16x32_bf16 v[62:65], v[172:175], v[206:209], v[62:65]
	s_setprio 0
	s_barrier
	s_mov_b64 s[58:59], 0x180
	s_add_i32 s57, s57, s6
	v_lshl_add_u64 v[132:133], v[132:133], 0, s[58:59]
	s_mov_b32 m0, s57
	s_add_i32 s55, s57, 0x2000
	ds_read_b128 v[176:179], v137 offset:49152
	ds_read_b128 v[180:183], v137 offset:50176
	ds_read_b128 v[184:187], v137 offset:51200
	ds_read_b128 v[190:193], v137 offset:52224
	ds_read_b128 v[194:197], v137 offset:53248
	ds_read_b128 v[198:201], v137 offset:54272
	ds_read_b128 v[202:205], v137 offset:55296
	ds_read_b128 v[206:209], v137 offset:56320
	global_load_lds_dwordx4 v[132:133], off
	v_lshl_add_u64 v[132:133], v[210:211], 0, s[58:59]
	s_add_u32 s58, s42, 0x10180
	s_mov_b32 m0, s55
	s_addc_u32 s59, s43, 0
	s_add_i32 s42, s60, s6
	global_load_lds_dwordx4 v[132:133], off
	v_lshl_add_u64 v[132:133], s[58:59], 0, v[0:1]
	s_mov_b32 m0, s42
	s_add_i32 s43, s42, 0x2000
	global_load_lds_dwordx4 v[132:133], off
	v_lshl_add_u64 v[132:133], s[58:59], 0, v[130:131]
	s_mov_b32 m0, s43
	s_nop 0
	global_load_lds_dwordx4 v[132:133], off
	s_mov_b32 m0, s48
	s_nop 0
	global_load_lds_dwordx4 v2, s[30:31]
	s_mov_b32 m0, s49
	s_nop 0
	global_load_lds_dwordx4 v3, s[30:31]
	s_waitcnt vmcnt(8)
	s_waitcnt lgkmcnt(0)
	s_barrier
	s_setprio 1
	s_waitcnt lgkmcnt(0)
	v_mfma_f32_16x16x32_bf16 v[6:9], v[30:33], v[202:205], v[6:9]
	v_mfma_f32_16x16x32_bf16 v[10:13], v[118:121], v[202:205], v[10:13]
	v_mfma_f32_16x16x32_bf16 v[144:147], v[30:33], v[176:179], v[144:147]
	v_mfma_f32_16x16x32_bf16 v[148:151], v[118:121], v[176:179], v[148:151]
	v_mfma_f32_16x16x32_bf16 v[152:155], v[30:33], v[184:187], v[152:155]
	v_mfma_f32_16x16x32_bf16 v[156:159], v[118:121], v[184:187], v[156:159]
	v_mfma_f32_16x16x32_bf16 v[160:163], v[30:33], v[194:197], v[160:163]
	v_mfma_f32_16x16x32_bf16 v[164:167], v[118:121], v[194:197], v[164:167]
	v_mfma_f32_16x16x32_bf16 v[6:9], v[34:37], v[206:209], v[6:9]
	v_mfma_f32_16x16x32_bf16 v[10:13], v[122:125], v[206:209], v[10:13]
	v_mfma_f32_16x16x32_bf16 v[144:147], v[34:37], v[180:183], v[144:147]
	v_mfma_f32_16x16x32_bf16 v[148:151], v[122:125], v[180:183], v[148:151]
	v_mfma_f32_16x16x32_bf16 v[152:155], v[34:37], v[190:193], v[152:155]
	v_mfma_f32_16x16x32_bf16 v[156:159], v[122:125], v[190:193], v[156:159]
	v_mfma_f32_16x16x32_bf16 v[160:163], v[34:37], v[198:201], v[160:163]
	v_mfma_f32_16x16x32_bf16 v[164:167], v[122:125], v[198:201], v[164:167]
	v_mfma_f32_16x16x32_bf16 v[14:17], v[126:129], v[176:179], v[14:17]
	v_mfma_f32_16x16x32_bf16 v[18:21], v[168:171], v[176:179], v[18:21]
	v_mfma_f32_16x16x32_bf16 v[30:33], v[126:129], v[184:187], v[66:69]
	v_mfma_f32_16x16x32_bf16 v[34:37], v[168:171], v[184:187], v[106:109]
	v_mfma_f32_16x16x32_bf16 v[66:69], v[126:129], v[194:197], v[110:113]
	v_mfma_f32_16x16x32_bf16 v[106:109], v[168:171], v[194:197], v[114:117]
	v_mfma_f32_16x16x32_bf16 v[22:25], v[126:129], v[202:205], v[22:25]
	v_mfma_f32_16x16x32_bf16 v[26:29], v[168:171], v[202:205], v[26:29]
	v_mfma_f32_16x16x32_bf16 v[14:17], v[140:143], v[180:183], v[14:17]
	v_mfma_f32_16x16x32_bf16 v[18:21], v[172:175], v[180:183], v[18:21]
	v_mfma_f32_16x16x32_bf16 v[30:33], v[140:143], v[190:193], v[30:33]
	v_mfma_f32_16x16x32_bf16 v[34:37], v[172:175], v[190:193], v[34:37]
	v_mfma_f32_16x16x32_bf16 v[66:69], v[140:143], v[198:201], v[66:69]
	v_mfma_f32_16x16x32_bf16 v[106:109], v[172:175], v[198:201], v[106:109]
	v_mfma_f32_16x16x32_bf16 v[22:25], v[140:143], v[206:209], v[22:25]
	v_mfma_f32_16x16x32_bf16 v[26:29], v[172:175], v[206:209], v[26:29]
	s_setprio 0
	s_barrier
; #define PG8_STAGE(bufoff, gbase, voff) do { _Pragma("unroll") for (int _i = 0; _i < 2; ++_i) \
;         __builtin_amdgcn_global_load_lds((const unsigned*)((const char*)(gbase) + (voff)[_i]), (LAS unsigned*)(lds + (bufoff) + ldsw + _i * 8192), 16, 0, 0); } while (0)
; #define PG8_LDA(dst, b, h) do { _Pragma("unroll") for (int m = 0; m < 4; ++m) _Pragma("unroll") for (int k = 0; k < 2; ++k) dst[m][k] = *(const LAS bf16x8*)(lds + PG8_SA(b, h) + aoff + m * 2048 + k * 1024); } while (0)
; #define PG8_LDB(dst, b, h) do { _Pragma("unroll") for (int n = 0; n < 2; ++n) _Pragma("unroll") for (int k = 0; k < 2; ++k) dst[n][k] = *(const LAS bf16x8*)(lds + PG8_SB(b, h) + boff + n * 2048 + k * 1024); } while (0)
; #define PG8_MMA(ai, bj, At, Bt) do { __builtin_amdgcn_s_setprio(1); _Pragma("unroll") for (int m = 0; m < 4; ++m) _Pragma("unroll") for (int n = 0; n < 2; ++n) _Pragma("unroll") for (int k = 0; k < 2; ++k) \
;         acc[ai][bj][m][n] = __builtin_amdgcn_mfma_f32_16x16x32_bf16(Bt[n][k], At[m][k], acc[ai][bj][m][n], 0, 0, 0); __builtin_amdgcn_s_setprio(0); } while (0)
; #define PG8_WAIT_V(n) asm volatile("s_waitcnt vmcnt(" #n ")" ::: "memory")
; #define PG8_WAIT_L(n) asm volatile("s_waitcnt lgkmcnt(" #n ")" ::: "memory")
; #define PG8_BAR __builtin_amdgcn_s_barrier()
; #define PG8_SCHED __builtin_amdgcn_sched_barrier(0)
; template <class Epi, class Sched>
; __device__ __forceinline__ void gemm_phase(LAS unsigned char* lds, const int tid, const char* Abase, const int K, const Sched& S, const Epi& E) {
;     ...
;             PG8_LDB(B0, 0, 0); PG8_LDB(B1, 0, 1); PG8_SCHED; PG8_LDA(At, 0, 0); PG8_STAGE(PG8_SA(1, 1), a1, vc[1]);
;             PG8_WAIT_V(8); PG8_WAIT_L(0); PG8_BAR; PG8_MMA(0, 0, At, B0); PG8_MMA(0, 1, At, B1); PG8_BAR; PG8_SCHED;
;             PG8_LDA(At, 0, 1); PG8_STAGE(PG8_SB(0, 0), b2, voffB); PG8_STAGE(PG8_SB(0, 1), b2 + hstep, voffB); PG8_STAGE(PG8_SA(0, 0), a2, w2[0]);
;             PG8_WAIT_V(8); PG8_WAIT_L(0); PG8_BAR; PG8_MMA(1, 0, At, B0); PG8_MMA(1, 1, At, B1); PG8_BAR; PG8_SCHED;
	ds_read_b128 v[140:143], v135
	ds_read_b128 v[110:113], v189
	ds_read_b128 v[114:117], v189 offset:1024
	ds_read_b128 v[118:121], v189 offset:2048
	ds_read_b128 v[122:125], v189 offset:3072
	ds_read_b128 v[126:129], v212
	ds_read_b128 v[168:171], v212 offset:1024
	ds_read_b128 v[172:175], v212 offset:2048
	ds_read_b128 v[176:179], v212 offset:3072
	s_mov_b32 m0, s35
	ds_read_b128 v[180:183], v137
	ds_read_b128 v[184:187], v137 offset:1024
	ds_read_b128 v[190:193], v137 offset:2048
	ds_read_b128 v[194:197], v137 offset:3072
	ds_read_b128 v[198:201], v137 offset:4096
	ds_read_b128 v[202:205], v137 offset:5120
	ds_read_b128 v[206:209], v137 offset:6144
	ds_read_b128 v[210:213], v137 offset:7168
	global_load_lds_dwordx4 v4, s[30:31]
	s_mov_b32 m0, s39
	s_nop 0
	global_load_lds_dwordx4 v5, s[30:31]
	s_waitcnt vmcnt(8)
	s_waitcnt lgkmcnt(0)
	s_barrier
	s_setprio 1
	s_waitcnt lgkmcnt(0)
	v_mfma_f32_16x16x32_bf16 v[2:5], v[110:113], v[180:183], v[70:73]
	v_mfma_f32_16x16x32_bf16 v[70:73], v[118:121], v[180:183], v[74:77]
	v_mfma_f32_16x16x32_bf16 v[74:77], v[110:113], v[190:193], v[78:81]
	v_mfma_f32_16x16x32_bf16 v[78:81], v[118:121], v[190:193], v[82:85]
	v_mfma_f32_16x16x32_bf16 v[82:85], v[110:113], v[198:201], v[86:89]
	v_mfma_f32_16x16x32_bf16 v[86:89], v[118:121], v[198:201], v[90:93]
	v_mfma_f32_16x16x32_bf16 v[90:93], v[110:113], v[206:209], v[94:97]
	v_mfma_f32_16x16x32_bf16 v[214:217], v[114:117], v[210:213], v[90:93]
	v_mfma_f32_16x16x32_bf16 v[90:93], v[118:121], v[206:209], v[98:101]
	v_mfma_f32_16x16x32_bf16 v[2:5], v[114:117], v[184:187], v[2:5]
	v_mfma_f32_16x16x32_bf16 v[70:73], v[122:125], v[184:187], v[70:73]
	v_mfma_f32_16x16x32_bf16 v[74:77], v[114:117], v[194:197], v[74:77]
	v_mfma_f32_16x16x32_bf16 v[78:81], v[122:125], v[194:197], v[78:81]
	v_mfma_f32_16x16x32_bf16 v[82:85], v[114:117], v[202:205], v[82:85]
	v_mfma_f32_16x16x32_bf16 v[86:89], v[122:125], v[202:205], v[86:89]
	v_mfma_f32_16x16x32_bf16 v[98:101], v[122:125], v[210:213], v[90:93]
	v_mfma_f32_16x16x32_bf16 v[58:61], v[126:129], v[206:209], v[58:61]
	v_mfma_f32_16x16x32_bf16 v[90:93], v[126:129], v[180:183], v[102:105]
	v_mfma_f32_16x16x32_bf16 v[38:41], v[172:175], v[180:183], v[38:41]
	v_mfma_f32_16x16x32_bf16 v[42:45], v[126:129], v[190:193], v[42:45]
	v_mfma_f32_16x16x32_bf16 v[46:49], v[172:175], v[190:193], v[46:49]
	v_mfma_f32_16x16x32_bf16 v[50:53], v[126:129], v[198:201], v[50:53]
	v_mfma_f32_16x16x32_bf16 v[54:57], v[172:175], v[198:201], v[54:57]
	v_mfma_f32_16x16x32_bf16 v[180:183], v[168:171], v[210:213], v[58:61]
	v_mfma_f32_16x16x32_bf16 v[58:61], v[172:175], v[206:209], v[62:65]
	v_mfma_f32_16x16x32_bf16 v[102:105], v[168:171], v[184:187], v[90:93]
	v_mfma_f32_16x16x32_bf16 v[38:41], v[176:179], v[184:187], v[38:41]
	v_mfma_f32_16x16x32_bf16 v[42:45], v[168:171], v[194:197], v[42:45]
	v_mfma_f32_16x16x32_bf16 v[46:49], v[176:179], v[194:197], v[46:49]
	v_mfma_f32_16x16x32_bf16 v[50:53], v[168:171], v[202:205], v[50:53]
	v_mfma_f32_16x16x32_bf16 v[54:57], v[176:179], v[202:205], v[54:57]
	v_mfma_f32_16x16x32_bf16 v[62:65], v[176:179], v[210:213], v[58:61]
	s_setprio 0
	s_barrier
	s_mov_b32 m0, s56
	v_lshl_add_u64 v[132:133], s[40:41], 0, v[0:1]
	s_add_u32 s58, s40, 0x10000
	ds_read_b128 v[58:61], v137 offset:16384
	ds_read_b128 v[90:93], v137 offset:17408
	ds_read_b128 v[94:97], v137 offset:18432
	ds_read_b128 v[184:187], v137 offset:19456
	ds_read_b128 v[190:193], v137 offset:20480
	ds_read_b128 v[194:197], v137 offset:21504
	ds_read_b128 v[198:201], v137 offset:22528
	ds_read_b128 v[202:205], v137 offset:23552
	global_load_lds_dwordx4 v[132:133], off
	v_lshl_add_u64 v[246:247], s[40:41], 0, v[130:131]
	s_mov_b32 m0, s52
	s_addc_u32 s59, s41, 0
	global_load_lds_dwordx4 v[246:247], off
	v_lshl_add_u64 v[206:207], s[58:59], 0, v[0:1]
	s_mov_b32 m0, s53
	s_nop 0
	global_load_lds_dwordx4 v[206:207], off
	v_lshl_add_u64 v[206:207], s[58:59], 0, v[130:131]
	s_mov_b32 m0, s54
	s_nop 0
	global_load_lds_dwordx4 v[206:207], off
	s_mov_b32 m0, s7
	s_nop 0
	global_load_lds_dwordx4 v140, s[16:17]
	s_mov_b32 m0, s33
	s_nop 0
	global_load_lds_dwordx4 v141, s[16:17]
	s_waitcnt vmcnt(8)
	s_waitcnt lgkmcnt(0)
	s_barrier
	s_setprio 1
	s_waitcnt lgkmcnt(0)
	v_mfma_f32_16x16x32_bf16 v[6:9], v[110:113], v[198:201], v[6:9]
	v_mfma_f32_16x16x32_bf16 v[10:13], v[118:121], v[198:201], v[10:13]
	v_mfma_f32_16x16x32_bf16 v[144:147], v[110:113], v[58:61], v[144:147]
	v_mfma_f32_16x16x32_bf16 v[148:151], v[118:121], v[58:61], v[148:151]
	v_mfma_f32_16x16x32_bf16 v[152:155], v[110:113], v[94:97], v[152:155]
	v_mfma_f32_16x16x32_bf16 v[156:159], v[118:121], v[94:97], v[156:159]
	v_mfma_f32_16x16x32_bf16 v[160:163], v[110:113], v[190:193], v[160:163]
	v_mfma_f32_16x16x32_bf16 v[164:167], v[118:121], v[190:193], v[164:167]
	v_mfma_f32_16x16x32_bf16 v[6:9], v[114:117], v[202:205], v[6:9]
	v_mfma_f32_16x16x32_bf16 v[10:13], v[122:125], v[202:205], v[10:13]
	v_mfma_f32_16x16x32_bf16 v[144:147], v[114:117], v[90:93], v[144:147]
	v_mfma_f32_16x16x32_bf16 v[148:151], v[122:125], v[90:93], v[148:151]
	v_mfma_f32_16x16x32_bf16 v[152:155], v[114:117], v[184:187], v[152:155]
	v_mfma_f32_16x16x32_bf16 v[156:159], v[122:125], v[184:187], v[156:159]
	v_mfma_f32_16x16x32_bf16 v[160:163], v[114:117], v[194:197], v[160:163]
	v_mfma_f32_16x16x32_bf16 v[164:167], v[122:125], v[194:197], v[164:167]
	v_mfma_f32_16x16x32_bf16 v[14:17], v[126:129], v[58:61], v[14:17]
	v_mfma_f32_16x16x32_bf16 v[206:209], v[168:171], v[90:93], v[14:17]
	v_mfma_f32_16x16x32_bf16 v[14:17], v[172:175], v[58:61], v[18:21]
	v_mfma_f32_16x16x32_bf16 v[18:21], v[176:179], v[90:93], v[14:17]
	v_mfma_f32_16x16x32_bf16 v[14:17], v[126:129], v[94:97], v[30:33]
	v_mfma_f32_16x16x32_bf16 v[210:213], v[168:171], v[184:187], v[14:17]
	v_mfma_f32_16x16x32_bf16 v[14:17], v[172:175], v[94:97], v[34:37]
	v_mfma_f32_16x16x32_bf16 v[34:37], v[176:179], v[184:187], v[14:17]
	v_mfma_f32_16x16x32_bf16 v[14:17], v[126:129], v[190:193], v[66:69]
	v_mfma_f32_16x16x32_bf16 v[184:187], v[168:171], v[194:197], v[14:17]
	v_mfma_f32_16x16x32_bf16 v[14:17], v[172:175], v[190:193], v[106:109]
	v_mfma_f32_16x16x32_bf16 v[190:193], v[176:179], v[194:197], v[14:17]
	v_mfma_f32_16x16x32_bf16 v[14:17], v[126:129], v[198:201], v[22:25]
	v_mfma_f32_16x16x32_bf16 v[168:171], v[168:171], v[202:205], v[14:17]
	v_mfma_f32_16x16x32_bf16 v[14:17], v[172:175], v[198:201], v[26:29]
	v_mfma_f32_16x16x32_bf16 v[172:175], v[176:179], v[202:205], v[14:17]
	s_setprio 0
	s_barrier
; #define PG8_STAGE(bufoff, gbase, voff) do { _Pragma("unroll") for (int _i = 0; _i < 2; ++_i) \
;         __builtin_amdgcn_global_load_lds((const unsigned*)((const char*)(gbase) + (voff)[_i]), (LAS unsigned*)(lds + (bufoff) + ldsw + _i * 8192), 16, 0, 0); } while (0)
; #define PG8_LDA(dst, b, h) do { _Pragma("unroll") for (int m = 0; m < 4; ++m) _Pragma("unroll") for (int k = 0; k < 2; ++k) dst[m][k] = *(const LAS bf16x8*)(lds + PG8_SA(b, h) + aoff + m * 2048 + k * 1024); } while (0)
; #define PG8_LDB(dst, b, h) do { _Pragma("unroll") for (int n = 0; n < 2; ++n) _Pragma("unroll") for (int k = 0; k < 2; ++k) dst[n][k] = *(const LAS bf16x8*)(lds + PG8_SB(b, h) + boff + n * 2048 + k * 1024); } while (0)
; #define PG8_MMA(ai, bj, At, Bt) do { __builtin_amdgcn_s_setprio(1); _Pragma("unroll") for (int m = 0; m < 4; ++m) _Pragma("unroll") for (int n = 0; n < 2; ++n) _Pragma("unroll") for (int k = 0; k < 2; ++k) \
;         acc[ai][bj][m][n] = __builtin_amdgcn_mfma_f32_16x16x32_bf16(Bt[n][k], At[m][k], acc[ai][bj][m][n], 0, 0, 0); __builtin_amdgcn_s_setprio(0); } while (0)
; #define PG8_WAIT_V(n) asm volatile("s_waitcnt vmcnt(" #n ")" ::: "memory")
; #define PG8_WAIT_L(n) asm volatile("s_waitcnt lgkmcnt(" #n ")" ::: "memory")
; #define PG8_BAR __builtin_amdgcn_s_barrier()
; #define PG8_SCHED __builtin_amdgcn_sched_barrier(0)
; template <class Epi, class Sched>
; __device__ __forceinline__ void gemm_phase(LAS unsigned char* lds, const int tid, const char* Abase, const int K, const Sched& S, const Epi& E) {
;     ...
;             PG8_LDB(B0, 1, 0); PG8_LDB(B1, 1, 1); PG8_SCHED; PG8_LDA(At, 1, 0); PG8_STAGE(PG8_SA(0, 1), a2, w2[1]);
;             PG8_WAIT_V(8); PG8_WAIT_L(0); PG8_BAR; PG8_MMA(0, 0, At, B0); PG8_MMA(0, 1, At, B1); PG8_BAR; PG8_SCHED;
;             PG8_LDA(At, 1, 1); PG8_STAGE(PG8_SB(1, 0), b3, voffB); PG8_STAGE(PG8_SB(1, 1), b3 + hstep, voffB); PG8_STAGE(PG8_SA(1, 0), a3, w2[0]);
;             PG8_WAIT_V(8); PG8_WAIT_L(0); PG8_BAR; PG8_MMA(1, 0, At, B0); PG8_MMA(1, 1, At, B1); PG8_BAR; PG8_SCHED;
;         }
;         if (wr == 0) PG8_BAR;
	s_nop 4
	ds_read_b128 v[14:17], v218
	ds_read_b128 v[22:25], v218 offset:1024
	ds_read_b128 v[66:69], v218 offset:2048
	ds_read_b128 v[176:179], v218 offset:3072
	ds_read_b128 v[194:197], v219
	ds_read_b128 v[198:201], v219 offset:1024
	ds_read_b128 v[202:205], v219 offset:2048
	ds_read_b128 v[218:221], v219 offset:3072
	s_mov_b32 m0, s44
	ds_read_b128 v[26:29], v137 offset:32768
	ds_read_b128 v[30:33], v137 offset:33792
	ds_read_b128 v[222:225], v137 offset:34816
	ds_read_b128 v[226:229], v137 offset:35840
	ds_read_b128 v[230:233], v137 offset:36864
	ds_read_b128 v[234:237], v137 offset:37888
	ds_read_b128 v[238:241], v137 offset:38912
	ds_read_b128 v[242:245], v137 offset:39936
	global_load_lds_dwordx4 v142, s[16:17]
	s_mov_b32 m0, s45
	s_nop 0
	global_load_lds_dwordx4 v143, s[16:17]
	s_waitcnt vmcnt(8)
	s_waitcnt lgkmcnt(0)
	s_barrier
	s_setprio 1
	s_waitcnt lgkmcnt(0)
	v_mfma_f32_16x16x32_bf16 v[2:5], v[14:17], v[26:29], v[2:5]
	v_mfma_f32_16x16x32_bf16 v[126:129], v[22:25], v[30:33], v[2:5]
	v_mfma_f32_16x16x32_bf16 v[2:5], v[66:69], v[26:29], v[70:73]
	v_mfma_f32_16x16x32_bf16 v[122:125], v[176:179], v[30:33], v[2:5]
	v_mfma_f32_16x16x32_bf16 v[2:5], v[14:17], v[222:225], v[74:77]
	v_mfma_f32_16x16x32_bf16 v[110:113], v[22:25], v[226:229], v[2:5]
	v_mfma_f32_16x16x32_bf16 v[2:5], v[66:69], v[222:225], v[78:81]
	v_mfma_f32_16x16x32_bf16 v[106:109], v[176:179], v[226:229], v[2:5]
	v_mfma_f32_16x16x32_bf16 v[2:5], v[14:17], v[230:233], v[82:85]
	v_mfma_f32_16x16x32_bf16 v[94:97], v[22:25], v[234:237], v[2:5]
	v_mfma_f32_16x16x32_bf16 v[2:5], v[66:69], v[230:233], v[86:89]
	v_mfma_f32_16x16x32_bf16 v[90:93], v[176:179], v[234:237], v[2:5]
	v_mfma_f32_16x16x32_bf16 v[2:5], v[14:17], v[238:241], v[214:217]
	v_mfma_f32_16x16x32_bf16 v[70:73], v[22:25], v[242:245], v[2:5]
	v_mfma_f32_16x16x32_bf16 v[2:5], v[66:69], v[238:241], v[98:101]
	v_mfma_f32_16x16x32_bf16 v[58:61], v[176:179], v[242:245], v[2:5]
	v_mfma_f32_16x16x32_bf16 v[2:5], v[194:197], v[26:29], v[102:105]
	v_mfma_f32_16x16x32_bf16 v[118:121], v[198:201], v[30:33], v[2:5]
	v_mfma_f32_16x16x32_bf16 v[2:5], v[202:205], v[26:29], v[38:41]
	v_mfma_f32_16x16x32_bf16 v[114:117], v[218:221], v[30:33], v[2:5]
	v_mfma_f32_16x16x32_bf16 v[2:5], v[194:197], v[222:225], v[42:45]
	v_mfma_f32_16x16x32_bf16 v[102:105], v[198:201], v[226:229], v[2:5]
	v_mfma_f32_16x16x32_bf16 v[2:5], v[202:205], v[222:225], v[46:49]
	v_mfma_f32_16x16x32_bf16 v[98:101], v[218:221], v[226:229], v[2:5]
	v_mfma_f32_16x16x32_bf16 v[2:5], v[194:197], v[230:233], v[50:53]
	v_mfma_f32_16x16x32_bf16 v[86:89], v[198:201], v[234:237], v[2:5]
	v_mfma_f32_16x16x32_bf16 v[2:5], v[202:205], v[230:233], v[54:57]
	v_mfma_f32_16x16x32_bf16 v[82:85], v[218:221], v[234:237], v[2:5]
	v_mfma_f32_16x16x32_bf16 v[2:5], v[194:197], v[238:241], v[180:183]
	v_mfma_f32_16x16x32_bf16 v[54:57], v[198:201], v[242:245], v[2:5]
	v_mfma_f32_16x16x32_bf16 v[2:5], v[202:205], v[238:241], v[62:65]
	v_mfma_f32_16x16x32_bf16 v[50:53], v[218:221], v[242:245], v[2:5]
	s_setprio 0
	s_barrier
	s_mov_b32 m0, s57
	v_lshl_add_u64 v[26:27], v[132:133], 0, s[24:25]
	s_add_u32 s52, s40, 0x10080
	s_nop 1
	ds_read_b128 v[2:5], v137 offset:49152
	ds_read_b128 v[38:41], v137 offset:50176
	ds_read_b128 v[180:183], v137 offset:51200
	ds_read_b128 v[214:217], v137 offset:52224
	ds_read_b128 v[222:225], v137 offset:53248
	ds_read_b128 v[226:229], v137 offset:54272
	ds_read_b128 v[230:233], v137 offset:55296
	ds_read_b128 v[234:237], v137 offset:56320
	global_load_lds_dwordx4 v[26:27], off
	v_lshl_add_u64 v[26:27], v[246:247], 0, s[24:25]
	s_mov_b32 m0, s55
	s_addc_u32 s53, s41, 0
	global_load_lds_dwordx4 v[26:27], off
	v_lshl_add_u64 v[26:27], s[52:53], 0, v[0:1]
	s_mov_b32 m0, s42
	s_nop 0
	global_load_lds_dwordx4 v[26:27], off
	v_lshl_add_u64 v[26:27], s[52:53], 0, v[130:131]
	s_mov_b32 m0, s43
	s_nop 0
	global_load_lds_dwordx4 v[26:27], off
	s_mov_b32 m0, s48
	s_nop 0
	global_load_lds_dwordx4 v140, s[22:23]
	s_mov_b32 m0, s49
	s_nop 0
	global_load_lds_dwordx4 v141, s[22:23]
	s_waitcnt vmcnt(8)
	s_waitcnt lgkmcnt(0)
	s_barrier
	s_setprio 1
	s_waitcnt lgkmcnt(0)
	v_mfma_f32_16x16x32_bf16 v[26:29], v[14:17], v[2:5], v[144:147]
	v_mfma_f32_16x16x32_bf16 v[78:81], v[22:25], v[38:41], v[26:29]
	v_mfma_f32_16x16x32_bf16 v[26:29], v[66:69], v[2:5], v[148:151]
	v_mfma_f32_16x16x32_bf16 v[74:77], v[176:179], v[38:41], v[26:29]
	v_mfma_f32_16x16x32_bf16 v[26:29], v[14:17], v[180:183], v[152:155]
	v_mfma_f32_16x16x32_bf16 v[46:49], v[22:25], v[214:217], v[26:29]
	v_mfma_f32_16x16x32_bf16 v[26:29], v[66:69], v[180:183], v[156:159]
	v_mfma_f32_16x16x32_bf16 v[42:45], v[176:179], v[214:217], v[26:29]
	v_mfma_f32_16x16x32_bf16 v[26:29], v[14:17], v[222:225], v[160:163]
	v_mfma_f32_16x16x32_bf16 v[6:9], v[14:17], v[230:233], v[6:9]
	v_mfma_f32_16x16x32_bf16 v[30:33], v[22:25], v[226:229], v[26:29]
	v_mfma_f32_16x16x32_bf16 v[26:29], v[66:69], v[222:225], v[164:167]
	v_mfma_f32_16x16x32_bf16 v[14:17], v[22:25], v[234:237], v[6:9]
	v_mfma_f32_16x16x32_bf16 v[6:9], v[66:69], v[230:233], v[10:13]
	v_mfma_f32_16x16x32_bf16 v[26:29], v[176:179], v[226:229], v[26:29]
	v_mfma_f32_16x16x32_bf16 v[10:13], v[176:179], v[234:237], v[6:9]
	v_mfma_f32_16x16x32_bf16 v[6:9], v[194:197], v[2:5], v[206:209]
	v_mfma_f32_16x16x32_bf16 v[2:5], v[202:205], v[2:5], v[18:21]
	v_mfma_f32_16x16x32_bf16 v[62:65], v[218:221], v[38:41], v[2:5]
	v_mfma_f32_16x16x32_bf16 v[2:5], v[194:197], v[180:183], v[210:213]
	v_mfma_f32_16x16x32_bf16 v[66:69], v[198:201], v[38:41], v[6:9]
	v_mfma_f32_16x16x32_bf16 v[38:41], v[198:201], v[214:217], v[2:5]
	v_mfma_f32_16x16x32_bf16 v[2:5], v[202:205], v[180:183], v[34:37]
	v_mfma_f32_16x16x32_bf16 v[34:37], v[218:221], v[214:217], v[2:5]
	v_mfma_f32_16x16x32_bf16 v[2:5], v[194:197], v[222:225], v[184:187]
	v_mfma_f32_16x16x32_bf16 v[22:25], v[198:201], v[226:229], v[2:5]
	v_mfma_f32_16x16x32_bf16 v[2:5], v[202:205], v[222:225], v[190:193]
	v_mfma_f32_16x16x32_bf16 v[18:21], v[218:221], v[226:229], v[2:5]
	v_mfma_f32_16x16x32_bf16 v[2:5], v[194:197], v[230:233], v[168:171]
	v_mfma_f32_16x16x32_bf16 v[6:9], v[198:201], v[234:237], v[2:5]
	v_mfma_f32_16x16x32_bf16 v[2:5], v[202:205], v[230:233], v[172:175]
	v_mfma_f32_16x16x32_bf16 v[2:5], v[218:221], v[234:237], v[2:5]
	s_setprio 0
	s_barrier
	s_andn2_b64 vcc, exec, s[26:27]
	s_cbranch_vccnz .LBB0_1349
	s_barrier

; #define PG8_STAGE(bufoff, gbase, voff) do { _Pragma("unroll") for (int _i = 0; _i < 2; ++_i) \
;         __builtin_amdgcn_global_load_lds((const unsigned*)((const char*)(gbase) + (voff)[_i]), (LAS unsigned*)(lds + (bufoff) + ldsw + _i * 8192), 16, 0, 0); } while (0)
; #define PG8_LDA(dst, b, h) do { _Pragma("unroll") for (int m = 0; m < 4; ++m) _Pragma("unroll") for (int k = 0; k < 2; ++k) dst[m][k] = *(const LAS bf16x8*)(lds + PG8_SA(b, h) + aoff + m * 2048 + k * 1024); } while (0)
; #define PG8_LDB(dst, b, h) do { _Pragma("unroll") for (int n = 0; n < 2; ++n) _Pragma("unroll") for (int k = 0; k < 2; ++k) dst[n][k] = *(const LAS bf16x8*)(lds + PG8_SB(b, h) + boff + n * 2048 + k * 1024); } while (0)
; #define PG8_MMA(ai, bj, At, Bt) do { __builtin_amdgcn_s_setprio(1); _Pragma("unroll") for (int m = 0; m < 4; ++m) _Pragma("unroll") for (int n = 0; n < 2; ++n) _Pragma("unroll") for (int k = 0; k < 2; ++k) \
;         acc[ai][bj][m][n] = __builtin_amdgcn_mfma_f32_16x16x32_bf16(Bt[n][k], At[m][k], acc[ai][bj][m][n], 0, 0, 0); __builtin_amdgcn_s_setprio(0); } while (0)
; #define PG8_BAR __builtin_amdgcn_s_barrier()
; template <class Epi, class Sched>
; __device__ __forceinline__ void gemm_phase(LAS unsigned char* lds, const int tid, const char* Abase, const int K, const Sched& S, const Epi& E) {
;     ...
;             const bool last = (t == nt - 2);
;             const char* a1 = Abase + (size_t)(t + 1) * kstep;
;             const char* a2 = last ? Abase : Abase + (size_t)(t + 2) * kstep; const char* b2 = last ? nB : cB + (size_t)(t + 2) * kstep;
;             const char* a3 = a2 + kstep; const char* b3 = b2 + kstep;
;             unsigned w2[2][2];
;             if (last) { const u32x4 q = *vslot; w2[0][0] = q.x; w2[0][1] = q.y; w2[1][0] = q.z; w2[1][1] = q.w; }
;             else { w2[0][0] = vc[0][0]; w2[0][1] = vc[0][1]; w2[1][0] = vc[1][0]; w2[1][1] = vc[1][1]; }
;             PG8_LDB(B0, 0, 0); PG8_LDB(B1, 0, 1); PG8_SCHED; PG8_LDA(At, 0, 0); PG8_STAGE(PG8_SA(1, 1), a1, vc[1]);
;             PG8_WAIT_V(8); PG8_WAIT_L(0); PG8_BAR; PG8_MMA(0, 0, At, B0); PG8_MMA(0, 1, At, B1); PG8_BAR; PG8_SCHED;
;             PG8_LDA(At, 0, 1); PG8_STAGE(PG8_SB(0, 0), b2, voffB); PG8_STAGE(PG8_SB(0, 1), b2 + hstep, voffB); PG8_STAGE(PG8_SA(0, 0), a2, w2[0]);
;             PG8_WAIT_V(8); PG8_WAIT_L(0); PG8_BAR; PG8_MMA(1, 0, At, B0); PG8_MMA(1, 1, At, B1); PG8_BAR; PG8_SCHED;
.LBB0_1491:
	s_add_u32 s42, s38, 0x80
	s_addc_u32 s43, s39, 0
	s_and_b64 s[40:41], s[40:41], exec
	s_cselect_b32 s43, s17, s43
	s_cselect_b32 s42, s16, s42
	s_cselect_b32 s41, s13, s55
	s_cselect_b32 s40, s12, s37
	s_add_i32 s57, 0, 0x10000
	v_add_u32_e32 v133, s57, v214
	s_add_i32 s60, 0, 0x14000
	ds_read_b128 v[134:137], v133
	ds_read_b128 v[146:149], v133 offset:1024
	ds_read_b128 v[150:153], v133 offset:2048
	ds_read_b128 v[154:157], v133 offset:3072
	v_add_u32_e32 v133, s60, v214
	ds_read_b128 v[158:161], v133
	ds_read_b128 v[162:165], v133 offset:1024
	ds_read_b128 v[166:169], v133 offset:2048
	ds_read_b128 v[170:173], v133 offset:3072
	v_lshl_add_u64 v[212:213], s[38:39], 0, v[96:97]
	s_add_i32 m0, s45, 0xc000
	ds_read_b128 v[174:177], v215
	ds_read_b128 v[178:181], v215 offset:1024
	ds_read_b128 v[182:185], v215 offset:2048
	ds_read_b128 v[190:193], v215 offset:3072
	ds_read_b128 v[194:197], v215 offset:4096
	ds_read_b128 v[198:201], v215 offset:5120
	ds_read_b128 v[204:207], v215 offset:6144
	ds_read_b128 v[208:211], v215 offset:7168
	global_load_lds_dwordx4 v[212:213], off
	v_lshl_add_u64 v[212:213], s[38:39], 0, v[118:119]
	s_add_i32 m0, s45, 0xe000
	s_nop 0
	global_load_lds_dwordx4 v[212:213], off
	s_waitcnt vmcnt(8)
	s_waitcnt lgkmcnt(0)
	s_barrier
	s_setprio 1
	s_waitcnt lgkmcnt(0)
	v_mfma_f32_16x16x32_bf16 v[142:145], v[134:137], v[174:177], v[142:145]
	v_mfma_f32_16x16x32_bf16 v[138:141], v[150:153], v[174:177], v[138:141]
	v_mfma_f32_16x16x32_bf16 v[114:117], v[134:137], v[182:185], v[114:117]
	v_mfma_f32_16x16x32_bf16 v[110:113], v[150:153], v[182:185], v[110:113]
	v_mfma_f32_16x16x32_bf16 v[98:101], v[134:137], v[194:197], v[98:101]
	v_mfma_f32_16x16x32_bf16 v[90:93], v[150:153], v[194:197], v[90:93]
	v_mfma_f32_16x16x32_bf16 v[78:81], v[134:137], v[204:207], v[78:81]
	v_mfma_f32_16x16x32_bf16 v[74:77], v[150:153], v[204:207], v[74:77]
	v_mfma_f32_16x16x32_bf16 v[142:145], v[146:149], v[178:181], v[142:145]
	v_mfma_f32_16x16x32_bf16 v[138:141], v[154:157], v[178:181], v[138:141]
	v_mfma_f32_16x16x32_bf16 v[114:117], v[146:149], v[190:193], v[114:117]
	v_mfma_f32_16x16x32_bf16 v[110:113], v[154:157], v[190:193], v[110:113]
	v_mfma_f32_16x16x32_bf16 v[98:101], v[146:149], v[198:201], v[98:101]
	v_mfma_f32_16x16x32_bf16 v[90:93], v[154:157], v[198:201], v[90:93]
	v_mfma_f32_16x16x32_bf16 v[78:81], v[146:149], v[208:211], v[78:81]
	v_mfma_f32_16x16x32_bf16 v[74:77], v[154:157], v[208:211], v[74:77]
	v_mfma_f32_16x16x32_bf16 v[126:129], v[158:161], v[174:177], v[126:129]
	v_mfma_f32_16x16x32_bf16 v[122:125], v[166:169], v[174:177], v[122:125]
	v_mfma_f32_16x16x32_bf16 v[106:109], v[158:161], v[182:185], v[106:109]
	v_mfma_f32_16x16x32_bf16 v[102:105], v[166:169], v[182:185], v[102:105]
	v_mfma_f32_16x16x32_bf16 v[86:89], v[158:161], v[194:197], v[86:89]
	v_mfma_f32_16x16x32_bf16 v[82:85], v[166:169], v[194:197], v[82:85]
	v_mfma_f32_16x16x32_bf16 v[70:73], v[158:161], v[204:207], v[70:73]
	v_mfma_f32_16x16x32_bf16 v[66:69], v[166:169], v[204:207], v[66:69]
	v_mfma_f32_16x16x32_bf16 v[126:129], v[162:165], v[178:181], v[126:129]
	v_mfma_f32_16x16x32_bf16 v[122:125], v[170:173], v[178:181], v[122:125]
	v_mfma_f32_16x16x32_bf16 v[106:109], v[162:165], v[190:193], v[106:109]
	v_mfma_f32_16x16x32_bf16 v[102:105], v[170:173], v[190:193], v[102:105]
	v_mfma_f32_16x16x32_bf16 v[86:89], v[162:165], v[198:201], v[86:89]
	v_mfma_f32_16x16x32_bf16 v[82:85], v[170:173], v[198:201], v[82:85]
	v_mfma_f32_16x16x32_bf16 v[70:73], v[162:165], v[208:211], v[70:73]
	v_mfma_f32_16x16x32_bf16 v[66:69], v[170:173], v[208:211], v[66:69]
	s_setprio 0
	s_barrier
	s_add_i32 s57, s57, s44
	v_lshl_add_u64 v[212:213], s[40:41], 0, v[186:187]
	s_mov_b32 m0, s57
	ds_read_b128 v[174:177], v215 offset:16384
	ds_read_b128 v[178:181], v215 offset:17408
	ds_read_b128 v[182:185], v215 offset:18432
	ds_read_b128 v[190:193], v215 offset:19456
	ds_read_b128 v[194:197], v215 offset:20480
	ds_read_b128 v[198:201], v215 offset:21504
	ds_read_b128 v[204:207], v215 offset:22528
	ds_read_b128 v[208:211], v215 offset:23552
	global_load_lds_dwordx4 v[212:213], off
	s_add_i32 m0, s57, 0x2000
	s_add_u32 s58, s40, 0x40000
	v_lshl_add_u64 v[216:217], s[40:41], 0, v[202:203]
	s_addc_u32 s59, s41, 0
	s_add_i32 s57, s60, s44
	global_load_lds_dwordx4 v[216:217], off
	v_lshl_add_u64 v[218:219], s[58:59], 0, v[186:187]
	s_mov_b32 m0, s57
	v_mov_b32_e32 v133, v1
	global_load_lds_dwordx4 v[218:219], off
	v_lshl_add_u64 v[218:219], s[58:59], 0, v[202:203]
	s_add_i32 m0, s57, 0x2000
	v_lshl_add_u64 v[220:221], s[42:43], 0, v[132:133]
	global_load_lds_dwordx4 v[218:219], off
	s_mov_b32 m0, s45
	v_lshl_add_u64 v[218:219], s[42:43], 0, v[0:1]
	global_load_lds_dwordx4 v0, s[42:43]
	s_mov_b32 m0, s46
	s_nop 0
	global_load_lds_dwordx4 v132, s[42:43]
	s_waitcnt vmcnt(8)
	s_waitcnt lgkmcnt(0)
	s_barrier
; #define PG8_STAGE(bufoff, gbase, voff) do { _Pragma("unroll") for (int _i = 0; _i < 2; ++_i) \
;         __builtin_amdgcn_global_load_lds((const unsigned*)((const char*)(gbase) + (voff)[_i]), (LAS unsigned*)(lds + (bufoff) + ldsw + _i * 8192), 16, 0, 0); } while (0)
; #define PG8_LDA(dst, b, h) do { _Pragma("unroll") for (int m = 0; m < 4; ++m) _Pragma("unroll") for (int k = 0; k < 2; ++k) dst[m][k] = *(const LAS bf16x8*)(lds + PG8_SA(b, h) + aoff + m * 2048 + k * 1024); } while (0)
; #define PG8_LDB(dst, b, h) do { _Pragma("unroll") for (int n = 0; n < 2; ++n) _Pragma("unroll") for (int k = 0; k < 2; ++k) dst[n][k] = *(const LAS bf16x8*)(lds + PG8_SB(b, h) + boff + n * 2048 + k * 1024); } while (0)
; #define PG8_MMA(ai, bj, At, Bt) do { __builtin_amdgcn_s_setprio(1); _Pragma("unroll") for (int m = 0; m < 4; ++m) _Pragma("unroll") for (int n = 0; n < 2; ++n) _Pragma("unroll") for (int k = 0; k < 2; ++k) \
;         acc[ai][bj][m][n] = __builtin_amdgcn_mfma_f32_16x16x32_bf16(Bt[n][k], At[m][k], acc[ai][bj][m][n], 0, 0, 0); __builtin_amdgcn_s_setprio(0); } while (0)
; #define PG8_WAIT_V(n) asm volatile("s_waitcnt vmcnt(" #n ")" ::: "memory")
; #define PG8_WAIT_L(n) asm volatile("s_waitcnt lgkmcnt(" #n ")" ::: "memory")
; #define PG8_BAR __builtin_amdgcn_s_barrier()
; #define PG8_SCHED __builtin_amdgcn_sched_barrier(0)
; template <class Epi, class Sched>
; __device__ __forceinline__ void gemm_phase(LAS unsigned char* lds, const int tid, const char* Abase, const int K, const Sched& S, const Epi& E) {
;     ...
;             PG8_WAIT_V(8); PG8_WAIT_L(0); PG8_BAR; PG8_MMA(1, 0, At, B0); PG8_MMA(1, 1, At, B1); PG8_BAR; PG8_SCHED;
;             PG8_LDB(B0, 1, 0); PG8_LDB(B1, 1, 1); PG8_SCHED; PG8_LDA(At, 1, 0); PG8_STAGE(PG8_SA(0, 1), a2, w2[1]);
;             PG8_WAIT_V(8); PG8_WAIT_L(0); PG8_BAR; PG8_MMA(0, 0, At, B0); PG8_MMA(0, 1, At, B1); PG8_BAR; PG8_SCHED;
;             PG8_LDA(At, 1, 1); PG8_STAGE(PG8_SB(1, 0), b3, voffB); PG8_STAGE(PG8_SB(1, 1), b3 + hstep, voffB); PG8_STAGE(PG8_SA(1, 0), a3, w2[0]);
	s_setprio 1
	s_waitcnt lgkmcnt(0)
	v_mfma_f32_16x16x32_bf16 v[62:65], v[134:137], v[174:177], v[62:65]
	v_mfma_f32_16x16x32_bf16 v[58:61], v[150:153], v[174:177], v[58:61]
	v_mfma_f32_16x16x32_bf16 v[46:49], v[134:137], v[182:185], v[46:49]
	v_mfma_f32_16x16x32_bf16 v[42:45], v[150:153], v[182:185], v[42:45]
	v_mfma_f32_16x16x32_bf16 v[30:33], v[134:137], v[194:197], v[30:33]
	v_mfma_f32_16x16x32_bf16 v[26:29], v[150:153], v[194:197], v[26:29]
	v_mfma_f32_16x16x32_bf16 v[14:17], v[134:137], v[204:207], v[14:17]
	v_mfma_f32_16x16x32_bf16 v[10:13], v[150:153], v[204:207], v[10:13]
	v_mfma_f32_16x16x32_bf16 v[62:65], v[146:149], v[178:181], v[62:65]
	v_mfma_f32_16x16x32_bf16 v[58:61], v[154:157], v[178:181], v[58:61]
	v_mfma_f32_16x16x32_bf16 v[46:49], v[146:149], v[190:193], v[46:49]
	v_mfma_f32_16x16x32_bf16 v[42:45], v[154:157], v[190:193], v[42:45]
	v_mfma_f32_16x16x32_bf16 v[30:33], v[146:149], v[198:201], v[30:33]
	v_mfma_f32_16x16x32_bf16 v[26:29], v[154:157], v[198:201], v[26:29]
	v_mfma_f32_16x16x32_bf16 v[14:17], v[146:149], v[208:211], v[14:17]
	v_mfma_f32_16x16x32_bf16 v[10:13], v[154:157], v[208:211], v[10:13]
	v_mfma_f32_16x16x32_bf16 v[54:57], v[158:161], v[174:177], v[54:57]
	v_mfma_f32_16x16x32_bf16 v[50:53], v[166:169], v[174:177], v[50:53]
	v_mfma_f32_16x16x32_bf16 v[38:41], v[158:161], v[182:185], v[38:41]
	v_mfma_f32_16x16x32_bf16 v[34:37], v[166:169], v[182:185], v[34:37]
	v_mfma_f32_16x16x32_bf16 v[22:25], v[158:161], v[194:197], v[22:25]
	v_mfma_f32_16x16x32_bf16 v[18:21], v[166:169], v[194:197], v[18:21]
	v_mfma_f32_16x16x32_bf16 v[6:9], v[158:161], v[204:207], v[6:9]
	v_mfma_f32_16x16x32_bf16 v[2:5], v[166:169], v[204:207], v[2:5]
	v_mfma_f32_16x16x32_bf16 v[54:57], v[162:165], v[178:181], v[54:57]
	v_mfma_f32_16x16x32_bf16 v[50:53], v[170:173], v[178:181], v[50:53]
	v_mfma_f32_16x16x32_bf16 v[38:41], v[162:165], v[190:193], v[38:41]
	v_mfma_f32_16x16x32_bf16 v[34:37], v[170:173], v[190:193], v[34:37]
	v_mfma_f32_16x16x32_bf16 v[22:25], v[162:165], v[198:201], v[22:25]
	v_mfma_f32_16x16x32_bf16 v[18:21], v[170:173], v[198:201], v[18:21]
	v_mfma_f32_16x16x32_bf16 v[6:9], v[162:165], v[208:211], v[6:9]
	v_mfma_f32_16x16x32_bf16 v[2:5], v[170:173], v[208:211], v[2:5]
	s_setprio 0
	s_barrier
	s_add_i32 s57, 0, 0x18000
	v_add_u32_e32 v0, s57, v214
	s_add_i32 s58, 0, 0x1c000
	ds_read_b128 v[132:135], v0
	ds_read_b128 v[146:149], v0 offset:1024
	ds_read_b128 v[150:153], v0 offset:2048
	ds_read_b128 v[154:157], v0 offset:3072
	v_add_u32_e32 v0, s58, v214
	ds_read_b128 v[158:161], v0
	ds_read_b128 v[162:165], v0 offset:1024
	ds_read_b128 v[166:169], v0 offset:2048
	ds_read_b128 v[170:173], v0 offset:3072
	s_mov_b32 m0, s47
	v_lshl_add_u64 v[130:131], s[42:43], 0, v[130:131]
	ds_read_b128 v[174:177], v215 offset:32768
	ds_read_b128 v[178:181], v215 offset:33792
	ds_read_b128 v[182:185], v215 offset:34816
	ds_read_b128 v[190:193], v215 offset:35840
	ds_read_b128 v[194:197], v215 offset:36864
	ds_read_b128 v[198:201], v215 offset:37888
	ds_read_b128 v[204:207], v215 offset:38912
	ds_read_b128 v[208:211], v215 offset:39936
	global_load_lds_dwordx4 v[130:131], off
	v_lshl_add_u64 v[120:121], s[42:43], 0, v[120:121]
	s_mov_b32 m0, s48
	s_nop 0
	global_load_lds_dwordx4 v[120:121], off
	s_waitcnt vmcnt(8)
	s_waitcnt lgkmcnt(0)
	s_barrier
	s_setprio 1
	s_waitcnt lgkmcnt(0)
	v_mfma_f32_16x16x32_bf16 v[142:145], v[132:135], v[174:177], v[142:145]
	v_mfma_f32_16x16x32_bf16 v[136:139], v[150:153], v[174:177], v[138:141]
	v_mfma_f32_16x16x32_bf16 v[114:117], v[132:135], v[182:185], v[114:117]
	v_mfma_f32_16x16x32_bf16 v[110:113], v[150:153], v[182:185], v[110:113]
	v_mfma_f32_16x16x32_bf16 v[98:101], v[132:135], v[194:197], v[98:101]
	v_mfma_f32_16x16x32_bf16 v[90:93], v[150:153], v[194:197], v[90:93]
	v_mfma_f32_16x16x32_bf16 v[78:81], v[132:135], v[204:207], v[78:81]
	v_mfma_f32_16x16x32_bf16 v[74:77], v[150:153], v[204:207], v[74:77]
	v_mfma_f32_16x16x32_bf16 v[142:145], v[146:149], v[178:181], v[142:145]
	v_mfma_f32_16x16x32_bf16 v[138:141], v[154:157], v[178:181], v[136:139]
	v_mfma_f32_16x16x32_bf16 v[114:117], v[146:149], v[190:193], v[114:117]
	v_mfma_f32_16x16x32_bf16 v[110:113], v[154:157], v[190:193], v[110:113]
	v_mfma_f32_16x16x32_bf16 v[98:101], v[146:149], v[198:201], v[98:101]
	v_mfma_f32_16x16x32_bf16 v[90:93], v[154:157], v[198:201], v[90:93]
	v_mfma_f32_16x16x32_bf16 v[78:81], v[146:149], v[208:211], v[78:81]
	v_mfma_f32_16x16x32_bf16 v[74:77], v[154:157], v[208:211], v[74:77]
	v_mfma_f32_16x16x32_bf16 v[126:129], v[158:161], v[174:177], v[126:129]
	v_mfma_f32_16x16x32_bf16 v[120:123], v[166:169], v[174:177], v[122:125]
	v_mfma_f32_16x16x32_bf16 v[106:109], v[158:161], v[182:185], v[106:109]
	v_mfma_f32_16x16x32_bf16 v[102:105], v[166:169], v[182:185], v[102:105]
	v_mfma_f32_16x16x32_bf16 v[86:89], v[158:161], v[194:197], v[86:89]
	v_mfma_f32_16x16x32_bf16 v[82:85], v[166:169], v[194:197], v[82:85]
	v_mfma_f32_16x16x32_bf16 v[70:73], v[158:161], v[204:207], v[70:73]
	v_mfma_f32_16x16x32_bf16 v[66:69], v[166:169], v[204:207], v[66:69]
	v_mfma_f32_16x16x32_bf16 v[126:129], v[162:165], v[178:181], v[126:129]
	v_mfma_f32_16x16x32_bf16 v[122:125], v[170:173], v[178:181], v[120:123]
	v_mfma_f32_16x16x32_bf16 v[106:109], v[162:165], v[190:193], v[106:109]
	v_mfma_f32_16x16x32_bf16 v[102:105], v[170:173], v[190:193], v[102:105]
	v_mfma_f32_16x16x32_bf16 v[86:89], v[162:165], v[198:201], v[86:89]
	v_mfma_f32_16x16x32_bf16 v[82:85], v[170:173], v[198:201], v[82:85]
	v_mfma_f32_16x16x32_bf16 v[70:73], v[162:165], v[208:211], v[70:73]
	v_mfma_f32_16x16x32_bf16 v[66:69], v[170:173], v[208:211], v[66:69]
	s_setprio 0
	s_barrier
; #define PG8_STAGE(bufoff, gbase, voff) do { _Pragma("unroll") for (int _i = 0; _i < 2; ++_i) \
;         __builtin_amdgcn_global_load_lds((const unsigned*)((const char*)(gbase) + (voff)[_i]), (LAS unsigned*)(lds + (bufoff) + ldsw + _i * 8192), 16, 0, 0); } while (0)
; #define PG8_LDA(dst, b, h) do { _Pragma("unroll") for (int m = 0; m < 4; ++m) _Pragma("unroll") for (int k = 0; k < 2; ++k) dst[m][k] = *(const LAS bf16x8*)(lds + PG8_SA(b, h) + aoff + m * 2048 + k * 1024); } while (0)
; #define PG8_MMA(ai, bj, At, Bt) do { __builtin_amdgcn_s_setprio(1); _Pragma("unroll") for (int m = 0; m < 4; ++m) _Pragma("unroll") for (int n = 0; n < 2; ++n) _Pragma("unroll") for (int k = 0; k < 2; ++k) \
;         acc[ai][bj][m][n] = __builtin_amdgcn_mfma_f32_16x16x32_bf16(Bt[n][k], At[m][k], acc[ai][bj][m][n], 0, 0, 0); __builtin_amdgcn_s_setprio(0); } while (0)
; #define PG8_WAIT_V(n) asm volatile("s_waitcnt vmcnt(" #n ")" ::: "memory")
; #define PG8_WAIT_L(n) asm volatile("s_waitcnt lgkmcnt(" #n ")" ::: "memory")
; #define PG8_BAR __builtin_amdgcn_s_barrier()
; #define PG8_SCHED __builtin_amdgcn_sched_barrier(0)
; template <class Epi, class Sched>
; __device__ __forceinline__ void gemm_phase(LAS unsigned char* lds, const int tid, const char* Abase, const int K, const Sched& S, const Epi& E) {
;     ...
;         for (int t = 0; t < nt; t += 2) {
;     ...
;             PG8_LDA(At, 1, 1); PG8_STAGE(PG8_SB(1, 0), b3, voffB); PG8_STAGE(PG8_SB(1, 1), b3 + hstep, voffB); PG8_STAGE(PG8_SA(1, 0), a3, w2[0]);
;             PG8_WAIT_V(8); PG8_WAIT_L(0); PG8_BAR; PG8_MMA(1, 0, At, B0); PG8_MMA(1, 1, At, B1); PG8_BAR; PG8_SCHED;
;         }
	s_add_i32 s42, s57, s44
	v_lshl_add_u64 v[120:121], v[212:213], 0, s[24:25]
	s_mov_b32 m0, s42
	ds_read_b128 v[174:177], v215 offset:49152
	ds_read_b128 v[178:181], v215 offset:50176
	ds_read_b128 v[182:185], v215 offset:51200
	ds_read_b128 v[190:193], v215 offset:52224
	ds_read_b128 v[194:197], v215 offset:53248
	ds_read_b128 v[198:201], v215 offset:54272
	ds_read_b128 v[204:207], v215 offset:55296
	ds_read_b128 v[208:211], v215 offset:56320
	global_load_lds_dwordx4 v[120:121], off
	s_add_i32 m0, s42, 0x2000
	s_add_u32 s40, s40, 0x40080
	v_lshl_add_u64 v[120:121], v[216:217], 0, s[24:25]
	s_addc_u32 s41, s41, 0
	s_add_i32 s42, s58, s44
	global_load_lds_dwordx4 v[120:121], off
	v_lshl_add_u64 v[120:121], s[40:41], 0, v[186:187]
	s_mov_b32 m0, s42
	s_nop 0
	global_load_lds_dwordx4 v[120:121], off
	v_lshl_add_u64 v[120:121], s[40:41], 0, v[202:203]
	s_add_i32 m0, s42, 0x2000
	s_nop 0
	global_load_lds_dwordx4 v[120:121], off
	v_lshl_add_u64 v[120:121], v[218:219], 0, s[24:25]
	s_mov_b32 m0, s51
	s_nop 0
	global_load_lds_dwordx4 v[120:121], off
	v_lshl_add_u64 v[120:121], v[220:221], 0, s[24:25]
	s_mov_b32 m0, s52
	s_nop 0
	global_load_lds_dwordx4 v[120:121], off
	s_waitcnt vmcnt(8)
	s_waitcnt lgkmcnt(0)
	s_barrier
	s_setprio 1
	s_waitcnt lgkmcnt(0)
	v_mfma_f32_16x16x32_bf16 v[62:65], v[132:135], v[174:177], v[62:65]
	v_mfma_f32_16x16x32_bf16 v[58:61], v[150:153], v[174:177], v[58:61]
	v_mfma_f32_16x16x32_bf16 v[46:49], v[132:135], v[182:185], v[46:49]
	v_mfma_f32_16x16x32_bf16 v[42:45], v[150:153], v[182:185], v[42:45]
	v_mfma_f32_16x16x32_bf16 v[30:33], v[132:135], v[194:197], v[30:33]
	v_mfma_f32_16x16x32_bf16 v[26:29], v[150:153], v[194:197], v[26:29]
	v_mfma_f32_16x16x32_bf16 v[14:17], v[132:135], v[204:207], v[14:17]
	v_mfma_f32_16x16x32_bf16 v[10:13], v[150:153], v[204:207], v[10:13]
	v_mfma_f32_16x16x32_bf16 v[62:65], v[146:149], v[178:181], v[62:65]
	v_mfma_f32_16x16x32_bf16 v[58:61], v[154:157], v[178:181], v[58:61]
	v_mfma_f32_16x16x32_bf16 v[46:49], v[146:149], v[190:193], v[46:49]
	v_mfma_f32_16x16x32_bf16 v[42:45], v[154:157], v[190:193], v[42:45]
	v_mfma_f32_16x16x32_bf16 v[30:33], v[146:149], v[198:201], v[30:33]
	v_mfma_f32_16x16x32_bf16 v[26:29], v[154:157], v[198:201], v[26:29]
	v_mfma_f32_16x16x32_bf16 v[14:17], v[146:149], v[208:211], v[14:17]
	v_mfma_f32_16x16x32_bf16 v[10:13], v[154:157], v[208:211], v[10:13]
	v_mfma_f32_16x16x32_bf16 v[54:57], v[158:161], v[174:177], v[54:57]
	v_mfma_f32_16x16x32_bf16 v[50:53], v[166:169], v[174:177], v[50:53]
	v_mfma_f32_16x16x32_bf16 v[38:41], v[158:161], v[182:185], v[38:41]
	v_mfma_f32_16x16x32_bf16 v[34:37], v[166:169], v[182:185], v[34:37]
	v_mfma_f32_16x16x32_bf16 v[22:25], v[158:161], v[194:197], v[22:25]
	v_mfma_f32_16x16x32_bf16 v[18:21], v[166:169], v[194:197], v[18:21]
	v_mfma_f32_16x16x32_bf16 v[6:9], v[158:161], v[204:207], v[6:9]
	v_mfma_f32_16x16x32_bf16 v[2:5], v[166:169], v[204:207], v[2:5]
	v_mfma_f32_16x16x32_bf16 v[54:57], v[162:165], v[178:181], v[54:57]
	v_mfma_f32_16x16x32_bf16 v[50:53], v[170:173], v[178:181], v[50:53]
	v_mfma_f32_16x16x32_bf16 v[38:41], v[162:165], v[190:193], v[38:41]
	v_mfma_f32_16x16x32_bf16 v[34:37], v[170:173], v[190:193], v[34:37]
	v_mfma_f32_16x16x32_bf16 v[22:25], v[162:165], v[198:201], v[22:25]
	v_mfma_f32_16x16x32_bf16 v[18:21], v[170:173], v[198:201], v[18:21]
	v_mfma_f32_16x16x32_bf16 v[6:9], v[162:165], v[208:211], v[6:9]
	v_mfma_f32_16x16x32_bf16 v[2:5], v[170:173], v[208:211], v[2:5]
	s_setprio 0
	s_barrier
	s_add_i32 s56, s56, 2
	s_add_u32 s37, s37, 0x100
	s_addc_u32 s55, s55, 0
	s_add_u32 s38, s38, 0x100
	s_addc_u32 s39, s39, 0
	s_cmp_gt_u32 s56, 13
	s_cbranch_scc1 .LBB0_1494
